# GEMM phases: static priority raise for the trailing half-workgroup instead of per-MFMA-block setprio toggling (on v11)
# baseline (speedup 1.0000x reference)
; #define REPLOOP(id) for (int rep_ = 0; rep_ < NREP(id); ++rep_)
; __global__ void __launch_bounds__(512, 2) fwd(Params p) {
;     ...
;     for (int l = 0; l < 2; ++l) {
;         const int pb = 2 + NPH_LAYER * l;
;         const float* mod = (const float*)(ws + WS_MOD) + (size_t)l * 5 * 12288;
;         if (PSEL(2) && IN(pb + 0)) REPLOOP(2) {
.LBB0_206:
	s_setprio 0
	s_mov_b32 s4, s2
	v_writelane_b32 v252, s4, 5
	s_mul_i32 s2, s2, 13
	v_writelane_b32 v255, s2, 56
	v_writelane_b32 v252, s5, 6
	s_add_i32 s4, s2, 2
	s_cmp_le_i32 s86, s4
	s_cselect_b64 s[2:3], -1, 0
	s_cmp_lt_i32 s4, s87
	s_cselect_b64 s[12:13], -1, 0
	s_and_b64 s[2:3], s[2:3], s[12:13]
	s_mov_b64 s[0:1], -1
	s_and_b64 vcc, exec, s[2:3]
	s_cbranch_vccnz .LBB0_208
	v_readlane_b32 s0, v252, 5
	v_readlane_b32 s1, v252, 6
	s_mul_i32 s0, s0, 13
	s_add_i32 s4, s0, 3
	s_mov_b64 s[0:1], 0

; #define PG8_GOFF(u, o) do { _Pragma("unroll") for (int _h = 0; _h < 2; ++_h) _Pragma("unroll") for (int _i = 0; _i < 2; ++_i) { const int _r = (u).pm * 256 + _h * 128 + gR[_i]; \
;         const int _tok = _r < nvalid ? rowtok[(u).pb * EROWS + _r] : 0; (o)[_h][_i] = (unsigned)(_tok * g.lda + gCc[_i]) * 2u; } } while (0)
; #define PG8_STAGE(bufoff, gbase, voff) do { _Pragma("unroll") for (int _i = 0; _i < 2; ++_i) \
;         __builtin_amdgcn_global_load_lds((const unsigned*)((const char*)(gbase) + (voff)[_i]), (LAS unsigned*)(lds + (bufoff) + ldsw + _i * 8192), 16, 0, 0); } while (0)
; #define PG8_STAGE_A(bufoff, kptr, half, VO) do { if constexpr (GATHER) { _Pragma("unroll") for (int _i = 0; _i < 2; ++_i) \
;         __builtin_amdgcn_global_load_lds((const unsigned*)((const char*)(kptr) + (VO)[half][_i]), (LAS unsigned*)(lds + (bufoff) + ldsw + _i * 8192), 16, 0, 0); } \
;         else { PG8_STAGE(bufoff, (kptr) + (half) * hstepA, voffA); } } while (0)
; #define PG8_BAR __builtin_amdgcn_s_barrier()
;     ...
;     for (int i = 0; i < 2; ++i) { int R, C; stage_rc(tid * 16 + i * 8192, R, C); const int Rb = Epi::PERM ? ((R & ~31) + perm32(R & 31)) : R;
;         voffA[i] = (unsigned)(R * g.lda + C) * 2u; voffB[i] = (unsigned)(Rb * g.ldb + C) * 2u; gR[i] = R; gCc[i] = C; }
;     unsigned gC[2][2], gN[2][2];
;     ...
;     const size_t kstep = (size_t)(BK * 2);
;     const size_t hstepA = (size_t)HALF * g.lda * 2, hstepB = (size_t)HALF * g.ldb * 2;
;     const unsigned ldsw = (unsigned)wid * 1024u;
;     const int aoff = lds_byte(wr * 64 + fr, fq * 8), boff = lds_byte(wc * 32 + fr, fq * 8);
;     ...
;     Unit cur, nxt; int ui = 0;
;     if (!S.next(0, cur)) return;
;     f32x4 acc[2][2][4][2];
; #pragma unroll
;     for (int a = 0; a < 2; ++a)
; #pragma unroll
;         for (int b = 0; b < 2; ++b)
; #pragma unroll
;             for (int m = 0; m < 4; ++m)
; #pragma unroll
;                 for (int n = 0; n < 2; ++n) acc[a][b][m][n] = (f32x4){0.f, 0.f, 0.f, 0.f};
;     bf16x8 At[4][2], B0[2][2], B1[2][2];
;     const char* cA = cur.a; const char* cB = cur.b;
;     if constexpr (GATHER) { PG8_GOFF(cur, gC); }
;     if constexpr (SP2) {
;         PG8_STAGE(PG8_SB(0, 0), cB, voffB); PG8_STAGE(PG8_SB(0, 1), cB + hstepB, voffB); PG8_STAGE_A(PG8_SA(0, 0), cA, 0, gC); PG8_STAGE_A(PG8_SA(0, 1), cA, 1, gC);
;         if (wr == 1) PG8_BAR;
.LBB0_212:
	s_andn2_b64 vcc, exec, s[12:13]
	s_cbranch_vccnz .LBB0_231
	v_ashrrev_i32_e32 v3, 31, v10
	v_lshrrev_b32_e32 v3, 26, v3
	v_add_u32_e32 v3, v10, v3
	v_ashrrev_i32_e32 v11, 6, v3
	v_bfe_i32 v3, v10, 27, 1
	v_lshlrev_b32_e32 v2, 4, v10
	v_lshrrev_b32_e32 v3, 22, v3
	v_add_u32_e32 v3, v2, v3
	v_and_b32_e32 v3, 0xfffffc00, v3
	v_sub_u32_e32 v3, v2, v3
	v_lshrrev_b32_e32 v4, 4, v3
	v_bitop3_b32 v4, v4, v3, 32 bitop3:0x6c
	v_ashrrev_i32_e32 v3, 31, v3
	v_lshrrev_b32_e32 v3, 26, v3
	v_add_u32_e32 v3, v4, v3
	v_ashrrev_i32_e32 v12, 6, v3
	v_lshlrev_b32_e32 v5, 3, v11
	v_mul_i32_i24_e32 v6, 64, v12
	v_and_b32_e32 v5, -16, v5
	v_sub_u32_e32 v4, v4, v6
	v_add_u32_e32 v3, v12, v5
	v_lshlrev_b32_e32 v5, 5, v11
	v_ashrrev_i16_sdwa v4, v245, sext(v4) dst_sel:DWORD dst_unused:UNUSED_PAD src0_sel:DWORD src1_sel:BYTE_0
	v_and_b32_e32 v5, 32, v5
	v_bfe_i32 v13, v4, 0, 16
	v_and_b32_e32 v7, 3, v12
	s_mov_b32 s12, 0xfffe0
	v_add_lshl_u32 v5, v5, v13, 1
	v_add_u32_e32 v2, 0x2000, v2
	v_lshlrev_b32_e32 v4, 1, v3
	v_lshrrev_b32_e32 v6, 2, v3
	v_and_or_b32 v7, v3, s12, v7
	v_lshl_add_u32 v130, v3, 12, v5
	v_ashrrev_i32_e32 v3, 31, v2
	v_lshrrev_b32_e32 v3, 22, v3
	v_add_u32_e32 v3, v2, v3
	v_ashrrev_i32_e32 v14, 10, v3
	v_mul_i32_i24_e32 v3, 0x400, v14
	v_sub_u32_e32 v2, v2, v3
	v_and_b32_e32 v4, 24, v4
	v_and_b32_e32 v6, 4, v6
	v_lshrrev_b32_e32 v3, 4, v2
	v_or3_b32 v4, v7, v6, v4
	v_bitop3_b32 v2, v3, v2, 32 bitop3:0x6c
	v_lshl_add_u32 v132, v4, 12, v5
	v_ashrrev_i32_e32 v4, 31, v2
	v_lshrrev_b32_e32 v4, 26, v4
	v_lshlrev_b32_e32 v3, 3, v14
	v_add_u32_e32 v4, v2, v4
	v_and_b32_e32 v3, -16, v3
	v_ashrrev_i32_e32 v15, 6, v4
	v_add_u32_e32 v3, v15, v3
	v_and_b32_e32 v6, 3, v15
	s_ashr_i32 s15, s4, 6
	s_ashr_i32 s14, s4, 8
	v_and_or_b32 v6, v3, s12, v6
	s_lshl_b32 s12, s15, 10
	s_lshl_b64 s[2:3], s[2:3], 20
	v_readlane_b32 s16, v252, 24
	v_and_b32_e32 v4, 0xc0, v4
	v_readlane_b32 s17, v252, 25
	s_add_u32 s24, s16, s2
	v_sub_u32_e32 v2, v2, v4
	s_addc_u32 s25, s17, s3
	v_readlane_b32 s2, v252, 26
	v_ashrrev_i16_sdwa v2, v245, sext(v2) dst_sel:DWORD dst_unused:UNUSED_PAD src0_sel:DWORD src1_sel:BYTE_0
	s_add_u32 s0, s2, s0
	v_readlane_b32 s2, v252, 27
	v_lshlrev_b32_e32 v5, 5, v14
	v_bfe_i32 v16, v2, 0, 16
	v_lshlrev_b32_e32 v2, 1, v3
	v_lshrrev_b32_e32 v4, 2, v3
	s_addc_u32 s1, s2, s1
	s_add_i32 s13, s12, 0
	v_and_b32_e32 v5, 32, v5
	v_and_b32_e32 v2, 24, v2
	v_and_b32_e32 v4, 4, v4
	s_add_i32 m0, s13, 0x10000
	v_or3_b32 v2, v6, v4, v2
	v_add_lshl_u32 v4, v5, v16, 1
	global_load_lds_dwordx4 v132, s[0:1]
	s_add_i32 m0, s13, 0x12000
	v_lshl_add_u32 v136, v2, 12, v4
	s_add_u32 s2, s0, 0x80000
	global_load_lds_dwordx4 v136, s[0:1]
	s_addc_u32 s3, s1, 0
	s_add_i32 m0, s13, 0x14000
	s_add_i32 s26, s13, 0x2000
	global_load_lds_dwordx4 v132, s[2:3]
	s_add_i32 m0, s13, 0x16000
	v_lshl_add_u32 v134, v3, 12, v4
	global_load_lds_dwordx4 v136, s[2:3]
	s_mov_b32 m0, s13
	s_add_u32 s2, s24, 0x80000
	global_load_lds_dwordx4 v130, s[24:25]
	s_mov_b32 m0, s26
	s_addc_u32 s3, s25, 0
	s_add_i32 s27, s13, 0x4000
	global_load_lds_dwordx4 v134, s[24:25]
	s_mov_b32 m0, s27
	s_add_i32 s48, s13, 0x6000
	global_load_lds_dwordx4 v130, s[2:3]
	s_mov_b32 m0, s48
	v_mov_b32_e32 v133, v207
	global_load_lds_dwordx4 v134, s[2:3]
	v_mov_b32_e32 v137, v207
	v_mov_b32_e32 v131, v207
	v_mov_b32_e32 v135, v207
	s_cmp_eq_u32 s14, 1
	v_lshl_add_u64 v[8:9], s[0:1], 0, v[132:133]
	v_lshl_add_u64 v[6:7], s[0:1], 0, v[136:137]
	v_lshl_add_u64 v[2:3], s[24:25], 0, v[130:131]
	s_cselect_b64 s[2:3], -1, 0
	s_cmp_lg_u32 s14, 1
	v_lshl_add_u64 v[4:5], s[24:25], 0, v[134:135]
	s_cbranch_scc1 .LBB0_215
	s_barrier
	s_setprio 1

; #define PG8_STAGE(bufoff, gbase, voff) do { _Pragma("unroll") for (int _i = 0; _i < 2; ++_i) \
;         __builtin_amdgcn_global_load_lds((const unsigned*)((const char*)(gbase) + (voff)[_i]), (LAS unsigned*)(lds + (bufoff) + ldsw + _i * 8192), 16, 0, 0); } while (0)
; #define PG8_STAGE_A(bufoff, kptr, half, VO) do { if constexpr (GATHER) { _Pragma("unroll") for (int _i = 0; _i < 2; ++_i) \
;         __builtin_amdgcn_global_load_lds((const unsigned*)((const char*)(kptr) + (VO)[half][_i]), (LAS unsigned*)(lds + (bufoff) + ldsw + _i * 8192), 16, 0, 0); } \
;         else { PG8_STAGE(bufoff, (kptr) + (half) * hstepA, voffA); } } while (0)
; #define PG8_LDA(dst, b, h) do { _Pragma("unroll") for (int m = 0; m < 4; ++m) _Pragma("unroll") for (int k = 0; k < 2; ++k) dst[m][k] = *(const LAS bf16x8*)(lds + PG8_SA(b, h) + aoff + m * 2048 + k * 1024); } while (0)
; #define PG8_LDB(dst, b, h) do { _Pragma("unroll") for (int n = 0; n < 2; ++n) _Pragma("unroll") for (int k = 0; k < 2; ++k) dst[n][k] = *(const LAS bf16x8*)(lds + PG8_SB(b, h) + boff + n * 2048 + k * 1024); } while (0)
; #define PG8_MMA(ai, bj, At, Bt) do { __builtin_amdgcn_s_setprio(1); _Pragma("unroll") for (int m = 0; m < 4; ++m) _Pragma("unroll") for (int n = 0; n < 2; ++n) _Pragma("unroll") for (int k = 0; k < 2; ++k) \
;         acc[ai][bj][m][n] = __builtin_amdgcn_mfma_f32_16x16x32_bf16(Bt[n][k], At[m][k], acc[ai][bj][m][n], 0, 0, 0); __builtin_amdgcn_s_setprio(0); } while (0)
; #define PG8_WAIT_V(n) asm volatile("s_waitcnt vmcnt(" #n ")" ::: "memory")
; #define PG8_WAIT_L(n) asm volatile("s_waitcnt lgkmcnt(" #n ")" ::: "memory")
; #define PG8_BAR __builtin_amdgcn_s_barrier()
; #define PG8_SCHED __builtin_amdgcn_sched_barrier(0)
;     ...
;             PG8_LDB(B0, 0, 0); PG8_LDB(B1, 0, 1); PG8_SCHED; PG8_LDA(At, 0, 0); PG8_STAGE_A(PG8_SA(1, 1), a1, 1, gC);
;             PG8_WAIT_V(8); PG8_WAIT_L(0); PG8_BAR; PG8_MMA(0, 0, At, B0); PG8_MMA(0, 1, At, B1); PG8_BAR; PG8_SCHED;
;             PG8_LDA(At, 0, 1); PG8_STAGE(PG8_SB(0, 0), b2, voffB); PG8_STAGE(PG8_SB(0, 1), b2 + hstepB, voffB); PG8_STAGE_A(PG8_SA(0, 0), a2, 0, g2);
;             PG8_WAIT_V(8); PG8_WAIT_L(0); PG8_BAR; PG8_MMA(1, 0, At, B0); PG8_MMA(1, 1, At, B1); PG8_BAR; PG8_SCHED;
.LBB0_224:
	s_add_u32 s0, s24, 0xfff80080
	s_addc_u32 s1, s25, -1
	s_add_i32 s20, 0, 0x10000
	s_cmp_eq_u32 s19, 28
	s_cselect_b32 s31, s4, s1
	s_cselect_b32 s30, s14, s0
	s_cselect_b32 s1, s15, s18
	s_cselect_b32 s0, s16, s17
	s_add_i32 s22, 0, 0x14000
	v_add_u32_e32 v160, s20, v143
	v_add_u32_e32 v176, s22, v143
	ds_read_b128 v[148:151], v160
	ds_read_b128 v[152:155], v160 offset:1024
	ds_read_b128 v[156:159], v160 offset:2048
	ds_read_b128 v[160:163], v160 offset:3072
	ds_read_b128 v[164:167], v176
	ds_read_b128 v[168:171], v176 offset:1024
	ds_read_b128 v[172:175], v176 offset:2048
	ds_read_b128 v[176:179], v176 offset:3072
	v_lshl_add_u64 v[204:205], s[24:25], 0, v[138:139]
	s_add_i32 m0, s13, 0xc000
	ds_read_b128 v[180:183], v147
	ds_read_b128 v[184:187], v147 offset:1024
	ds_read_b128 v[188:191], v147 offset:2048
	ds_read_b128 v[192:195], v147 offset:3072
	ds_read_b128 v[196:199], v147 offset:4096
	ds_read_b128 v[200:203], v147 offset:5120
	ds_read_b128 v[216:219], v147 offset:6144
	ds_read_b128 v[220:223], v147 offset:7168
	global_load_lds_dwordx4 v[204:205], off
	v_lshl_add_u64 v[204:205], s[24:25], 0, v[140:141]
	s_add_i32 m0, s13, 0xe000
	s_nop 0
	global_load_lds_dwordx4 v[204:205], off
	s_waitcnt vmcnt(8)
	s_waitcnt lgkmcnt(0)
	s_barrier
	s_waitcnt lgkmcnt(0)
	v_mfma_f32_16x16x32_bf16 v[126:129], v[148:151], v[180:183], v[126:129]
	v_mfma_f32_16x16x32_bf16 v[122:125], v[156:159], v[180:183], v[122:125]
	v_mfma_f32_16x16x32_bf16 v[118:121], v[148:151], v[188:191], v[118:121]
	v_mfma_f32_16x16x32_bf16 v[114:117], v[156:159], v[188:191], v[114:117]
	v_mfma_f32_16x16x32_bf16 v[102:105], v[148:151], v[196:199], v[102:105]
	v_mfma_f32_16x16x32_bf16 v[98:101], v[156:159], v[196:199], v[98:101]
	v_mfma_f32_16x16x32_bf16 v[86:89], v[148:151], v[216:219], v[86:89]
	v_mfma_f32_16x16x32_bf16 v[82:85], v[156:159], v[216:219], v[82:85]
	v_mfma_f32_16x16x32_bf16 v[126:129], v[152:155], v[184:187], v[126:129]
	v_mfma_f32_16x16x32_bf16 v[122:125], v[160:163], v[184:187], v[122:125]
	v_mfma_f32_16x16x32_bf16 v[118:121], v[152:155], v[192:195], v[118:121]
	v_mfma_f32_16x16x32_bf16 v[114:117], v[160:163], v[192:195], v[114:117]
	v_mfma_f32_16x16x32_bf16 v[102:105], v[152:155], v[200:203], v[102:105]
	v_mfma_f32_16x16x32_bf16 v[98:101], v[160:163], v[200:203], v[98:101]
	v_mfma_f32_16x16x32_bf16 v[86:89], v[152:155], v[220:223], v[86:89]
	v_mfma_f32_16x16x32_bf16 v[82:85], v[160:163], v[220:223], v[82:85]
	v_mfma_f32_16x16x32_bf16 v[110:113], v[164:167], v[180:183], v[110:113]
	v_mfma_f32_16x16x32_bf16 v[106:109], v[172:175], v[180:183], v[106:109]
	v_mfma_f32_16x16x32_bf16 v[94:97], v[164:167], v[188:191], v[94:97]
	v_mfma_f32_16x16x32_bf16 v[90:93], v[172:175], v[188:191], v[90:93]
	v_mfma_f32_16x16x32_bf16 v[78:81], v[164:167], v[196:199], v[78:81]
	v_mfma_f32_16x16x32_bf16 v[74:77], v[172:175], v[196:199], v[74:77]
	v_mfma_f32_16x16x32_bf16 v[70:73], v[164:167], v[216:219], v[70:73]
	v_mfma_f32_16x16x32_bf16 v[66:69], v[172:175], v[216:219], v[66:69]
	v_mfma_f32_16x16x32_bf16 v[110:113], v[168:171], v[184:187], v[110:113]
	v_mfma_f32_16x16x32_bf16 v[106:109], v[176:179], v[184:187], v[106:109]
	v_mfma_f32_16x16x32_bf16 v[94:97], v[168:171], v[192:195], v[94:97]
	v_mfma_f32_16x16x32_bf16 v[90:93], v[176:179], v[192:195], v[90:93]
	v_mfma_f32_16x16x32_bf16 v[78:81], v[168:171], v[200:203], v[78:81]
	v_mfma_f32_16x16x32_bf16 v[74:77], v[176:179], v[200:203], v[74:77]
	v_mfma_f32_16x16x32_bf16 v[70:73], v[168:171], v[220:223], v[70:73]
	v_mfma_f32_16x16x32_bf16 v[66:69], v[176:179], v[220:223], v[66:69]
	s_barrier
	s_add_i32 s20, s20, s12
	v_lshl_add_u64 v[204:205], s[0:1], 0, v[132:133]
	s_mov_b32 m0, s20
	ds_read_b128 v[180:183], v147 offset:16384
	ds_read_b128 v[184:187], v147 offset:17408
	ds_read_b128 v[188:191], v147 offset:18432
	ds_read_b128 v[192:195], v147 offset:19456
	ds_read_b128 v[196:199], v147 offset:20480
	ds_read_b128 v[200:203], v147 offset:21504
	ds_read_b128 v[216:219], v147 offset:22528
	ds_read_b128 v[220:223], v147 offset:23552
	global_load_lds_dwordx4 v[204:205], off
	s_add_i32 m0, s20, 0x2000
	s_add_u32 s20, s0, 0x80000
	v_lshl_add_u64 v[208:209], s[0:1], 0, v[136:137]
	s_addc_u32 s21, s1, 0
	s_add_i32 s22, s22, s12
	global_load_lds_dwordx4 v[208:209], off
	v_lshl_add_u64 v[210:211], s[20:21], 0, v[132:133]
	s_mov_b32 m0, s22
	v_lshl_add_u64 v[212:213], s[30:31], 0, v[134:135]
	global_load_lds_dwordx4 v[210:211], off
	v_lshl_add_u64 v[210:211], s[20:21], 0, v[136:137]
	s_add_i32 m0, s22, 0x2000
	s_nop 0
	global_load_lds_dwordx4 v[210:211], off
	v_lshl_add_u64 v[210:211], s[30:31], 0, v[130:131]
	s_mov_b32 m0, s13
	s_nop 0
	global_load_lds_dwordx4 v[210:211], off
	s_mov_b32 m0, s26
	s_nop 0
	global_load_lds_dwordx4 v[212:213], off
	s_waitcnt vmcnt(8)
	s_waitcnt lgkmcnt(0)
	s_barrier
; #define PG8_STAGE_A(bufoff, kptr, half, VO) do { if constexpr (GATHER) { _Pragma("unroll") for (int _i = 0; _i < 2; ++_i) \
;         __builtin_amdgcn_global_load_lds((const unsigned*)((const char*)(kptr) + (VO)[half][_i]), (LAS unsigned*)(lds + (bufoff) + ldsw + _i * 8192), 16, 0, 0); } \
;         else { PG8_STAGE(bufoff, (kptr) + (half) * hstepA, voffA); } } while (0)
; #define PG8_LDA(dst, b, h) do { _Pragma("unroll") for (int m = 0; m < 4; ++m) _Pragma("unroll") for (int k = 0; k < 2; ++k) dst[m][k] = *(const LAS bf16x8*)(lds + PG8_SA(b, h) + aoff + m * 2048 + k * 1024); } while (0)
; #define PG8_LDB(dst, b, h) do { _Pragma("unroll") for (int n = 0; n < 2; ++n) _Pragma("unroll") for (int k = 0; k < 2; ++k) dst[n][k] = *(const LAS bf16x8*)(lds + PG8_SB(b, h) + boff + n * 2048 + k * 1024); } while (0)
; #define PG8_MMA(ai, bj, At, Bt) do { __builtin_amdgcn_s_setprio(1); _Pragma("unroll") for (int m = 0; m < 4; ++m) _Pragma("unroll") for (int n = 0; n < 2; ++n) _Pragma("unroll") for (int k = 0; k < 2; ++k) \
;         acc[ai][bj][m][n] = __builtin_amdgcn_mfma_f32_16x16x32_bf16(Bt[n][k], At[m][k], acc[ai][bj][m][n], 0, 0, 0); __builtin_amdgcn_s_setprio(0); } while (0)
; #define PG8_WAIT_V(n) asm volatile("s_waitcnt vmcnt(" #n ")" ::: "memory")
; #define PG8_WAIT_L(n) asm volatile("s_waitcnt lgkmcnt(" #n ")" ::: "memory")
; #define PG8_BAR __builtin_amdgcn_s_barrier()
; #define PG8_SCHED __builtin_amdgcn_sched_barrier(0)
;     ...
;             PG8_WAIT_V(8); PG8_WAIT_L(0); PG8_BAR; PG8_MMA(1, 0, At, B0); PG8_MMA(1, 1, At, B1); PG8_BAR; PG8_SCHED;
;             PG8_LDB(B0, 1, 0); PG8_LDB(B1, 1, 1); PG8_SCHED; PG8_LDA(At, 1, 0); PG8_STAGE_A(PG8_SA(0, 1), a2, 1, g2);
;             PG8_WAIT_V(8); PG8_WAIT_L(0); PG8_BAR; PG8_MMA(0, 0, At, B0); PG8_MMA(0, 1, At, B1); PG8_BAR; PG8_SCHED;
	s_waitcnt lgkmcnt(0)
	v_mfma_f32_16x16x32_bf16 v[62:65], v[148:151], v[180:183], v[62:65]
	v_mfma_f32_16x16x32_bf16 v[58:61], v[156:159], v[180:183], v[58:61]
	v_mfma_f32_16x16x32_bf16 v[54:57], v[148:151], v[188:191], v[54:57]
	v_mfma_f32_16x16x32_bf16 v[50:53], v[156:159], v[188:191], v[50:53]
	v_mfma_f32_16x16x32_bf16 v[38:41], v[148:151], v[196:199], v[38:41]
	v_mfma_f32_16x16x32_bf16 v[34:37], v[156:159], v[196:199], v[34:37]
	v_mfma_f32_16x16x32_bf16 v[22:25], v[148:151], v[216:219], v[22:25]
	v_mfma_f32_16x16x32_bf16 v[18:21], v[156:159], v[216:219], v[18:21]
	v_mfma_f32_16x16x32_bf16 v[62:65], v[152:155], v[184:187], v[62:65]
	v_mfma_f32_16x16x32_bf16 v[58:61], v[160:163], v[184:187], v[58:61]
	v_mfma_f32_16x16x32_bf16 v[54:57], v[152:155], v[192:195], v[54:57]
	v_mfma_f32_16x16x32_bf16 v[50:53], v[160:163], v[192:195], v[50:53]
	v_mfma_f32_16x16x32_bf16 v[38:41], v[152:155], v[200:203], v[38:41]
	v_mfma_f32_16x16x32_bf16 v[34:37], v[160:163], v[200:203], v[34:37]
	v_mfma_f32_16x16x32_bf16 v[22:25], v[152:155], v[220:223], v[22:25]
	v_mfma_f32_16x16x32_bf16 v[18:21], v[160:163], v[220:223], v[18:21]
	v_mfma_f32_16x16x32_bf16 v[46:49], v[164:167], v[180:183], v[46:49]
	v_mfma_f32_16x16x32_bf16 v[42:45], v[172:175], v[180:183], v[42:45]
	v_mfma_f32_16x16x32_bf16 v[30:33], v[164:167], v[188:191], v[30:33]
	v_mfma_f32_16x16x32_bf16 v[26:29], v[172:175], v[188:191], v[26:29]
	v_mfma_f32_16x16x32_bf16 v[14:17], v[164:167], v[196:199], v[14:17]
	v_mfma_f32_16x16x32_bf16 v[10:13], v[172:175], v[196:199], v[10:13]
	v_mfma_f32_16x16x32_bf16 v[6:9], v[164:167], v[216:219], v[6:9]
	v_mfma_f32_16x16x32_bf16 v[2:5], v[172:175], v[216:219], v[2:5]
	v_mfma_f32_16x16x32_bf16 v[46:49], v[168:171], v[184:187], v[46:49]
	v_mfma_f32_16x16x32_bf16 v[42:45], v[176:179], v[184:187], v[42:45]
	v_mfma_f32_16x16x32_bf16 v[30:33], v[168:171], v[192:195], v[30:33]
	v_mfma_f32_16x16x32_bf16 v[26:29], v[176:179], v[192:195], v[26:29]
	v_mfma_f32_16x16x32_bf16 v[14:17], v[168:171], v[200:203], v[14:17]
	v_mfma_f32_16x16x32_bf16 v[10:13], v[176:179], v[200:203], v[10:13]
	v_mfma_f32_16x16x32_bf16 v[6:9], v[168:171], v[220:223], v[6:9]
	v_mfma_f32_16x16x32_bf16 v[2:5], v[176:179], v[220:223], v[2:5]
	s_barrier
	s_add_i32 s22, 0, 0x18000
	s_add_i32 s23, 0, 0x1c000
	v_add_u32_e32 v160, s22, v143
	v_add_u32_e32 v176, s23, v143
	ds_read_b128 v[148:151], v160
	ds_read_b128 v[152:155], v160 offset:1024
	ds_read_b128 v[156:159], v160 offset:2048
	ds_read_b128 v[160:163], v160 offset:3072
	ds_read_b128 v[164:167], v176
	ds_read_b128 v[168:171], v176 offset:1024
	ds_read_b128 v[172:175], v176 offset:2048
	ds_read_b128 v[176:179], v176 offset:3072
	s_add_u32 s20, s30, 0x80000
	s_addc_u32 s21, s31, 0
	s_mov_b32 m0, s27
	v_lshl_add_u64 v[224:225], s[20:21], 0, v[130:131]
	ds_read_b128 v[180:183], v147 offset:32768
	ds_read_b128 v[184:187], v147 offset:33792
	ds_read_b128 v[188:191], v147 offset:34816
	ds_read_b128 v[192:195], v147 offset:35840
	ds_read_b128 v[196:199], v147 offset:36864
	ds_read_b128 v[200:203], v147 offset:37888
	ds_read_b128 v[216:219], v147 offset:38912
	ds_read_b128 v[220:223], v147 offset:39936
	global_load_lds_dwordx4 v[224:225], off
	v_lshl_add_u64 v[224:225], s[20:21], 0, v[134:135]
	s_mov_b32 m0, s48
	s_nop 0
	global_load_lds_dwordx4 v[224:225], off
	s_waitcnt vmcnt(8)
	s_waitcnt lgkmcnt(0)
	s_barrier
	s_waitcnt lgkmcnt(0)
	v_mfma_f32_16x16x32_bf16 v[126:129], v[148:151], v[180:183], v[126:129]
	v_mfma_f32_16x16x32_bf16 v[122:125], v[156:159], v[180:183], v[122:125]
	v_mfma_f32_16x16x32_bf16 v[118:121], v[148:151], v[188:191], v[118:121]
	v_mfma_f32_16x16x32_bf16 v[114:117], v[156:159], v[188:191], v[114:117]
	v_mfma_f32_16x16x32_bf16 v[102:105], v[148:151], v[196:199], v[102:105]
	v_mfma_f32_16x16x32_bf16 v[98:101], v[156:159], v[196:199], v[98:101]
	v_mfma_f32_16x16x32_bf16 v[86:89], v[148:151], v[216:219], v[86:89]
	v_mfma_f32_16x16x32_bf16 v[82:85], v[156:159], v[216:219], v[82:85]
	v_mfma_f32_16x16x32_bf16 v[126:129], v[152:155], v[184:187], v[126:129]
	v_mfma_f32_16x16x32_bf16 v[122:125], v[160:163], v[184:187], v[122:125]
	v_mfma_f32_16x16x32_bf16 v[118:121], v[152:155], v[192:195], v[118:121]
	v_mfma_f32_16x16x32_bf16 v[114:117], v[160:163], v[192:195], v[114:117]
	v_mfma_f32_16x16x32_bf16 v[102:105], v[152:155], v[200:203], v[102:105]
	v_mfma_f32_16x16x32_bf16 v[98:101], v[160:163], v[200:203], v[98:101]
	v_mfma_f32_16x16x32_bf16 v[86:89], v[152:155], v[220:223], v[86:89]
	v_mfma_f32_16x16x32_bf16 v[82:85], v[160:163], v[220:223], v[82:85]
	v_mfma_f32_16x16x32_bf16 v[110:113], v[164:167], v[180:183], v[110:113]
	v_mfma_f32_16x16x32_bf16 v[106:109], v[172:175], v[180:183], v[106:109]
	v_mfma_f32_16x16x32_bf16 v[94:97], v[164:167], v[188:191], v[94:97]
	v_mfma_f32_16x16x32_bf16 v[90:93], v[172:175], v[188:191], v[90:93]
	v_mfma_f32_16x16x32_bf16 v[78:81], v[164:167], v[196:199], v[78:81]
	v_mfma_f32_16x16x32_bf16 v[74:77], v[172:175], v[196:199], v[74:77]
	v_mfma_f32_16x16x32_bf16 v[70:73], v[164:167], v[216:219], v[70:73]
	v_mfma_f32_16x16x32_bf16 v[66:69], v[172:175], v[216:219], v[66:69]
	v_mfma_f32_16x16x32_bf16 v[110:113], v[168:171], v[184:187], v[110:113]
	v_mfma_f32_16x16x32_bf16 v[106:109], v[176:179], v[184:187], v[106:109]
	v_mfma_f32_16x16x32_bf16 v[94:97], v[168:171], v[192:195], v[94:97]
	v_mfma_f32_16x16x32_bf16 v[90:93], v[176:179], v[192:195], v[90:93]
	v_mfma_f32_16x16x32_bf16 v[78:81], v[168:171], v[200:203], v[78:81]
	v_mfma_f32_16x16x32_bf16 v[74:77], v[176:179], v[200:203], v[74:77]
	v_mfma_f32_16x16x32_bf16 v[70:73], v[168:171], v[220:223], v[70:73]
	v_mfma_f32_16x16x32_bf16 v[66:69], v[176:179], v[220:223], v[66:69]
	s_barrier
; #define PG8_STAGE(bufoff, gbase, voff) do { _Pragma("unroll") for (int _i = 0; _i < 2; ++_i) \
;         __builtin_amdgcn_global_load_lds((const unsigned*)((const char*)(gbase) + (voff)[_i]), (LAS unsigned*)(lds + (bufoff) + ldsw + _i * 8192), 16, 0, 0); } while (0)
; #define PG8_STAGE_A(bufoff, kptr, half, VO) do { if constexpr (GATHER) { _Pragma("unroll") for (int _i = 0; _i < 2; ++_i) \
;         __builtin_amdgcn_global_load_lds((const unsigned*)((const char*)(kptr) + (VO)[half][_i]), (LAS unsigned*)(lds + (bufoff) + ldsw + _i * 8192), 16, 0, 0); } \
;         else { PG8_STAGE(bufoff, (kptr) + (half) * hstepA, voffA); } } while (0)
; #define PG8_LDA(dst, b, h) do { _Pragma("unroll") for (int m = 0; m < 4; ++m) _Pragma("unroll") for (int k = 0; k < 2; ++k) dst[m][k] = *(const LAS bf16x8*)(lds + PG8_SA(b, h) + aoff + m * 2048 + k * 1024); } while (0)
; #define PG8_MMA(ai, bj, At, Bt) do { __builtin_amdgcn_s_setprio(1); _Pragma("unroll") for (int m = 0; m < 4; ++m) _Pragma("unroll") for (int n = 0; n < 2; ++n) _Pragma("unroll") for (int k = 0; k < 2; ++k) \
;         acc[ai][bj][m][n] = __builtin_amdgcn_mfma_f32_16x16x32_bf16(Bt[n][k], At[m][k], acc[ai][bj][m][n], 0, 0, 0); __builtin_amdgcn_s_setprio(0); } while (0)
; #define PG8_WAIT_V(n) asm volatile("s_waitcnt vmcnt(" #n ")" ::: "memory")
; #define PG8_WAIT_L(n) asm volatile("s_waitcnt lgkmcnt(" #n ")" ::: "memory")
; #define PG8_BAR __builtin_amdgcn_s_barrier()
; #define PG8_SCHED __builtin_amdgcn_sched_barrier(0)
;     ...
;             PG8_LDA(At, 1, 1); PG8_STAGE(PG8_SB(1, 0), b3, voffB); PG8_STAGE(PG8_SB(1, 1), b3 + hstepB, voffB); PG8_STAGE_A(PG8_SA(1, 0), a3, 0, g2);
;             PG8_WAIT_V(8); PG8_WAIT_L(0); PG8_BAR; PG8_MMA(1, 0, At, B0); PG8_MMA(1, 1, At, B1); PG8_BAR; PG8_SCHED;
	s_add_i32 s20, s22, s12
	v_lshl_add_u64 v[204:205], v[204:205], 0, s[8:9]
	s_mov_b32 m0, s20
	ds_read_b128 v[180:183], v147 offset:49152
	ds_read_b128 v[184:187], v147 offset:50176
	ds_read_b128 v[188:191], v147 offset:51200
	ds_read_b128 v[192:195], v147 offset:52224
	ds_read_b128 v[196:199], v147 offset:53248
	ds_read_b128 v[200:203], v147 offset:54272
	ds_read_b128 v[216:219], v147 offset:55296
	ds_read_b128 v[220:223], v147 offset:56320
	global_load_lds_dwordx4 v[204:205], off
	s_add_i32 m0, s20, 0x2000
	s_add_u32 s0, s0, 0x80080
	v_lshl_add_u64 v[204:205], v[208:209], 0, s[8:9]
	s_addc_u32 s1, s1, 0
	s_add_i32 s20, s23, s12
	global_load_lds_dwordx4 v[204:205], off
	v_lshl_add_u64 v[204:205], s[0:1], 0, v[132:133]
	s_mov_b32 m0, s20
	s_nop 0
	global_load_lds_dwordx4 v[204:205], off
	v_lshl_add_u64 v[204:205], s[0:1], 0, v[136:137]
	s_add_i32 m0, s20, 0x2000
	s_nop 0
	global_load_lds_dwordx4 v[204:205], off
	v_lshl_add_u64 v[204:205], v[210:211], 0, s[8:9]
	s_mov_b32 m0, s49
	s_nop 0
	global_load_lds_dwordx4 v[204:205], off
	v_lshl_add_u64 v[204:205], v[212:213], 0, s[8:9]
	s_mov_b32 m0, s50
	s_nop 0
	global_load_lds_dwordx4 v[204:205], off
	s_waitcnt vmcnt(8)
	s_waitcnt lgkmcnt(0)
	s_barrier
	s_waitcnt lgkmcnt(0)
	v_mfma_f32_16x16x32_bf16 v[62:65], v[148:151], v[180:183], v[62:65]
	v_mfma_f32_16x16x32_bf16 v[58:61], v[156:159], v[180:183], v[58:61]
	v_mfma_f32_16x16x32_bf16 v[54:57], v[148:151], v[188:191], v[54:57]
	v_mfma_f32_16x16x32_bf16 v[50:53], v[156:159], v[188:191], v[50:53]
	v_mfma_f32_16x16x32_bf16 v[38:41], v[148:151], v[196:199], v[38:41]
	v_mfma_f32_16x16x32_bf16 v[34:37], v[156:159], v[196:199], v[34:37]
	v_mfma_f32_16x16x32_bf16 v[22:25], v[148:151], v[216:219], v[22:25]
	v_mfma_f32_16x16x32_bf16 v[18:21], v[156:159], v[216:219], v[18:21]
	v_mfma_f32_16x16x32_bf16 v[62:65], v[152:155], v[184:187], v[62:65]
	v_mfma_f32_16x16x32_bf16 v[58:61], v[160:163], v[184:187], v[58:61]
	v_mfma_f32_16x16x32_bf16 v[54:57], v[152:155], v[192:195], v[54:57]
	v_mfma_f32_16x16x32_bf16 v[50:53], v[160:163], v[192:195], v[50:53]
	v_mfma_f32_16x16x32_bf16 v[38:41], v[152:155], v[200:203], v[38:41]
	v_mfma_f32_16x16x32_bf16 v[34:37], v[160:163], v[200:203], v[34:37]
	v_mfma_f32_16x16x32_bf16 v[22:25], v[152:155], v[220:223], v[22:25]
	v_mfma_f32_16x16x32_bf16 v[18:21], v[160:163], v[220:223], v[18:21]
	v_mfma_f32_16x16x32_bf16 v[46:49], v[164:167], v[180:183], v[46:49]
	v_mfma_f32_16x16x32_bf16 v[42:45], v[172:175], v[180:183], v[42:45]
	v_mfma_f32_16x16x32_bf16 v[30:33], v[164:167], v[188:191], v[30:33]
	v_mfma_f32_16x16x32_bf16 v[26:29], v[172:175], v[188:191], v[26:29]
	v_mfma_f32_16x16x32_bf16 v[14:17], v[164:167], v[196:199], v[14:17]
	v_mfma_f32_16x16x32_bf16 v[10:13], v[172:175], v[196:199], v[10:13]
	v_mfma_f32_16x16x32_bf16 v[6:9], v[164:167], v[216:219], v[6:9]
	v_mfma_f32_16x16x32_bf16 v[2:5], v[172:175], v[216:219], v[2:5]
	v_mfma_f32_16x16x32_bf16 v[46:49], v[168:171], v[184:187], v[46:49]
	v_mfma_f32_16x16x32_bf16 v[42:45], v[176:179], v[184:187], v[42:45]
	v_mfma_f32_16x16x32_bf16 v[30:33], v[168:171], v[192:195], v[30:33]
	v_mfma_f32_16x16x32_bf16 v[26:29], v[176:179], v[192:195], v[26:29]
	v_mfma_f32_16x16x32_bf16 v[14:17], v[168:171], v[200:203], v[14:17]
	v_mfma_f32_16x16x32_bf16 v[10:13], v[176:179], v[200:203], v[10:13]
	v_mfma_f32_16x16x32_bf16 v[6:9], v[168:171], v[220:223], v[6:9]
	v_mfma_f32_16x16x32_bf16 v[2:5], v[176:179], v[220:223], v[2:5]
	s_barrier
	s_add_i32 s19, s19, 2
	s_add_u32 s24, s24, 0x100
	s_addc_u32 s25, s25, 0
	s_add_u32 s17, s17, 0x100
	s_addc_u32 s18, s18, 0
	s_cmp_gt_u32 s19, 29
	s_cbranch_scc0 .LBB0_224
	s_and_b64 vcc, exec, s[36:37]
	s_cbranch_vccz .LBB0_227
	s_barrier

; #define PG8_GOFF(u, o) do { _Pragma("unroll") for (int _h = 0; _h < 2; ++_h) _Pragma("unroll") for (int _i = 0; _i < 2; ++_i) { const int _r = (u).pm * 256 + _h * 128 + gR[_i]; \
;         const int _tok = _r < nvalid ? rowtok[(u).pb * EROWS + _r] : 0; (o)[_h][_i] = (unsigned)(_tok * g.lda + gCc[_i]) * 2u; } } while (0)
;     __device__ __forceinline__ bool next(int i, Unit& u) const {
;         const int nwg = nM * nN; const long L = (long)i * G + c; if (L >= (long)nwg * nB) return false;
;         const int pb = (int)(L / nwg); int wgid = (int)(L % nwg);
;         { const int q = nwg / 8, r = nwg % 8, xcd = wgid % 8, off = wgid / 8; wgid = (xcd < r ? xcd * (q + 1) : r * (q + 1) + (xcd - r) * q) + off; }
;         const int nig = 8 * nN, gid = wgid / nig, fm = gid * 8, gsz = (nM - fm) < 8 ? (nM - fm) : 8;
;         u.pm = fm + ((wgid % nig) % gsz); u.pn = (wgid % nig) / gsz; u.pb = pb;
;         u.a = A + (size_t)pb * sA + (size_t)u.pm * 256 * lda * 2; u.b = B + (size_t)pb * sB + (size_t)u.pn * 256 * ldb * 2; return true;
;     ...
;     for (int i = 0; i < 2; ++i) { int R, C; stage_rc(tid * 16 + i * 8192, R, C); const int Rb = Epi::PERM ? ((R & ~31) + perm32(R & 31)) : R;
;         voffA[i] = (unsigned)(R * g.lda + C) * 2u; voffB[i] = (unsigned)(Rb * g.ldb + C) * 2u; gR[i] = R; gCc[i] = C; }
;     unsigned gC[2][2], gN[2][2];
;     ...
;     const size_t kstep = (size_t)(BK * 2);
;     const size_t hstepA = (size_t)HALF * g.lda * 2, hstepB = (size_t)HALF * g.ldb * 2;
;     const unsigned ldsw = (unsigned)wid * 1024u;
;     const int aoff = lds_byte(wr * 64 + fr, fq * 8), boff = lds_byte(wc * 32 + fr, fq * 8);
;     ...
;     Unit cur, nxt; int ui = 0;
;     if (!S.next(0, cur)) return;
;     f32x4 acc[2][2][4][2];
; #pragma unroll
;     for (int a = 0; a < 2; ++a)
; #pragma unroll
;         for (int b = 0; b < 2; ++b)
; #pragma unroll
;             for (int m = 0; m < 4; ++m)
; #pragma unroll
;                 for (int n = 0; n < 2; ++n) acc[a][b][m][n] = (f32x4){0.f, 0.f, 0.f, 0.f};
;     bf16x8 At[4][2], B0[2][2], B1[2][2];
;     const char* cA = cur.a; const char* cB = cur.b;
;     if constexpr (GATHER) { PG8_GOFF(cur, gC); }
;     if constexpr (SP2) {
;         PG8_STAGE(PG8_SB(0, 0), cB, voffB); PG8_STAGE(PG8_SB(0, 1), cB + hstepB, voffB); PG8_STAGE_A(PG8_SA(0, 0), cA, 0, gC); PG8_STAGE_A(PG8_SA(0, 1), cA, 1, gC);
;         if (wr == 1) PG8_BAR;
.LBB0_390:
	v_ashrrev_i32_e32 v3, 31, v10
	v_lshrrev_b32_e32 v3, 26, v3
	v_add_u32_e32 v3, v10, v3
	v_ashrrev_i32_e32 v11, 6, v3
	v_bfe_i32 v3, v10, 27, 1
	v_lshlrev_b32_e32 v2, 4, v10
	v_lshrrev_b32_e32 v3, 22, v3
	v_add_u32_e32 v3, v2, v3
	v_and_b32_e32 v3, 0xfffffc00, v3
	v_sub_u32_e32 v3, v2, v3
	v_lshrrev_b32_e32 v4, 4, v3
	v_bitop3_b32 v4, v4, v3, 32 bitop3:0x6c
	v_ashrrev_i32_e32 v3, 31, v3
	v_lshrrev_b32_e32 v3, 26, v3
	v_add_u32_e32 v3, v4, v3
	v_ashrrev_i32_e32 v12, 6, v3
	v_lshlrev_b32_e32 v5, 3, v11
	v_mul_i32_i24_e32 v6, 64, v12
	v_and_b32_e32 v5, -16, v5
	v_sub_u32_e32 v4, v4, v6
	v_add_u32_e32 v3, v12, v5
	v_lshlrev_b32_e32 v5, 5, v11
	v_ashrrev_i16_sdwa v4, v245, sext(v4) dst_sel:DWORD dst_unused:UNUSED_PAD src0_sel:DWORD src1_sel:BYTE_0
	v_and_b32_e32 v5, 32, v5
	v_bfe_i32 v13, v4, 0, 16
	v_and_b32_e32 v7, 3, v12
	s_mov_b32 s1, 0xfffe0
	v_add_lshl_u32 v5, v5, v13, 1
	v_add_u32_e32 v2, 0x2000, v2
	v_lshlrev_b32_e32 v4, 1, v3
	v_lshrrev_b32_e32 v6, 2, v3
	v_and_or_b32 v7, v3, s1, v7
	v_lshl_add_u32 v130, v3, 12, v5
	v_ashrrev_i32_e32 v3, 31, v2
	v_lshrrev_b32_e32 v3, 22, v3
	v_add_u32_e32 v3, v2, v3
	v_ashrrev_i32_e32 v14, 10, v3
	v_mul_i32_i24_e32 v3, 0x400, v14
	v_sub_u32_e32 v2, v2, v3
	v_and_b32_e32 v4, 24, v4
	v_and_b32_e32 v6, 4, v6
	v_lshrrev_b32_e32 v3, 4, v2
	v_or3_b32 v4, v7, v6, v4
	v_bitop3_b32 v2, v3, v2, 32 bitop3:0x6c
	v_lshl_add_u32 v132, v4, 12, v5
	v_ashrrev_i32_e32 v4, 31, v2
	v_lshrrev_b32_e32 v4, 26, v4
	v_lshlrev_b32_e32 v3, 3, v14
	v_add_u32_e32 v4, v2, v4
	v_and_b32_e32 v3, -16, v3
	v_ashrrev_i32_e32 v15, 6, v4
	v_add_u32_e32 v3, v15, v3
	v_and_b32_e32 v6, 3, v15
	v_and_or_b32 v6, v3, s1, v6
	v_readlane_b32 s1, v254, 43
	s_add_i32 s0, s0, s1
	s_sext_i32_i16 s1, s0
	s_mulk_i32 s1, 0x8889
	s_lshr_b32 s1, s1, 16
	s_add_i32 s1, s1, s0
	s_sext_i32_i16 s2, s1
	v_and_b32_e32 v4, 0xc0, v4
	s_ashr_i32 s2, s2, 6
	s_bfe_u32 s1, s1, 0x1000f
	v_sub_u32_e32 v2, v2, v4
	s_add_i32 s1, s2, s1
	v_ashrrev_i16_sdwa v2, v245, sext(v2) dst_sel:DWORD dst_unused:UNUSED_PAD src0_sel:DWORD src1_sel:BYTE_0
	s_sext_i32_i16 s2, s1
	v_lshlrev_b32_e32 v5, 5, v14
	v_bfe_i32 v16, v2, 0, 16
	v_lshlrev_b32_e32 v2, 1, v3
	v_lshrrev_b32_e32 v4, 2, v3
	s_lshl_b32 s2, s2, 3
	v_and_b32_e32 v5, 32, v5
	v_and_b32_e32 v2, 24, v2
	v_and_b32_e32 v4, 4, v4
	s_sub_i32 s3, 36, s2
	s_mulk_i32 s1, 0x78
	v_or3_b32 v2, v6, v4, v2
	v_add_lshl_u32 v4, v5, v16, 1
	s_min_u32 s3, s3, 8
	s_sub_i32 s15, s0, s1
	v_lshl_add_u32 v134, v3, 12, v4
	s_sext_i32_i16 s0, s15
	v_cvt_f32_ubyte0_e32 v3, s3
	v_lshl_add_u32 v136, v2, 12, v4
	v_cvt_f32_i32_e32 v2, s0
	v_rcp_iflag_f32_e32 v4, v3
	s_ashr_i32 s14, s12, 6
	s_ashr_i32 s0, s0, 30
	s_ashr_i32 s13, s12, 8
	v_mul_f32_e32 v4, v2, v4
	v_trunc_f32_e32 v4, v4
	v_fma_f32 v2, -v4, v3, v2
	v_cvt_i32_f32_e32 v4, v4
	s_lshl_b32 s26, s14, 10
	s_or_b32 s4, s0, 1
	v_cmp_ge_f32_e64 s[0:1], |v2|, v3
	s_and_b64 s[0:1], s[0:1], exec
	s_cselect_b32 s0, s4, 0
	v_readfirstlane_b32 s1, v4
	s_add_i32 s4, s1, s0
	s_mul_i32 s0, s4, s3
	s_sub_i32 s0, s15, s0
	s_sext_i32_i8 s0, s0
	s_add_i32 s40, s2, s0
	s_ashr_i32 s41, s40, 31
	s_lshl_b64 s[0:1], s[40:41], 20
	v_readlane_b32 s2, v252, 24
	v_readlane_b32 s3, v252, 25
	s_add_u32 s0, s2, s0
	s_addc_u32 s1, s3, s1
	s_bfe_i64 s[2:3], s[4:5], 0x80000
	s_lshl_b64 s[2:3], s[2:3], 20
	v_readlane_b32 s15, v252, 31
	s_add_u32 s30, s15, s2
	v_readlane_b32 s2, v252, 32
	s_addc_u32 s31, s2, s3
	s_add_i32 s27, s26, 0
	s_add_i32 m0, s27, 0x10000
	v_mov_b32_e32 v133, v207
	global_load_lds_dwordx4 v132, s[30:31]
	s_add_i32 m0, s27, 0x12000
	s_add_u32 s2, s30, 0x80000
	global_load_lds_dwordx4 v136, s[30:31]
	s_addc_u32 s3, s31, 0
	s_add_i32 m0, s27, 0x14000
	s_add_i32 s41, s27, 0x2000
	global_load_lds_dwordx4 v132, s[2:3]
	s_add_i32 m0, s27, 0x16000
	v_mov_b32_e32 v137, v207
	global_load_lds_dwordx4 v136, s[2:3]
	s_mov_b32 m0, s27
	s_add_u32 s2, s0, 0x80000
	global_load_lds_dwordx4 v130, s[0:1]
	s_mov_b32 m0, s41
	s_addc_u32 s3, s1, 0
	s_add_i32 s48, s27, 0x4000
	global_load_lds_dwordx4 v134, s[0:1]
	s_mov_b32 m0, s48
	s_add_i32 s49, s27, 0x6000
	global_load_lds_dwordx4 v130, s[2:3]
	s_mov_b32 m0, s49
	v_mov_b32_e32 v131, v207
	global_load_lds_dwordx4 v134, s[2:3]
	v_mov_b32_e32 v135, v207
	s_cmp_eq_u32 s13, 1
	v_lshl_add_u64 v[8:9], s[30:31], 0, v[132:133]
	v_lshl_add_u64 v[6:7], s[30:31], 0, v[136:137]
	v_lshl_add_u64 v[2:3], s[0:1], 0, v[130:131]
	s_cselect_b64 s[2:3], -1, 0
	s_cmp_lg_u32 s13, 1
	v_lshl_add_u64 v[4:5], s[0:1], 0, v[134:135]
	s_cbranch_scc1 .LBB0_392
	s_barrier
	s_setprio 1

; #define PG8_STAGE(bufoff, gbase, voff) do { _Pragma("unroll") for (int _i = 0; _i < 2; ++_i) \
;         __builtin_amdgcn_global_load_lds((const unsigned*)((const char*)(gbase) + (voff)[_i]), (LAS unsigned*)(lds + (bufoff) + ldsw + _i * 8192), 16, 0, 0); } while (0)
; #define PG8_STAGE_A(bufoff, kptr, half, VO) do { if constexpr (GATHER) { _Pragma("unroll") for (int _i = 0; _i < 2; ++_i) \
;         __builtin_amdgcn_global_load_lds((const unsigned*)((const char*)(kptr) + (VO)[half][_i]), (LAS unsigned*)(lds + (bufoff) + ldsw + _i * 8192), 16, 0, 0); } \
;         else { PG8_STAGE(bufoff, (kptr) + (half) * hstepA, voffA); } } while (0)
; #define PG8_LDA(dst, b, h) do { _Pragma("unroll") for (int m = 0; m < 4; ++m) _Pragma("unroll") for (int k = 0; k < 2; ++k) dst[m][k] = *(const LAS bf16x8*)(lds + PG8_SA(b, h) + aoff + m * 2048 + k * 1024); } while (0)
; #define PG8_LDB(dst, b, h) do { _Pragma("unroll") for (int n = 0; n < 2; ++n) _Pragma("unroll") for (int k = 0; k < 2; ++k) dst[n][k] = *(const LAS bf16x8*)(lds + PG8_SB(b, h) + boff + n * 2048 + k * 1024); } while (0)
; #define PG8_WAIT_V(n) asm volatile("s_waitcnt vmcnt(" #n ")" ::: "memory")
; #define PG8_WAIT_L(n) asm volatile("s_waitcnt lgkmcnt(" #n ")" ::: "memory")
;     ...
;         for (int t = 0; t < nt; t += 2) {
;             const bool last = (t == nt - 2);
;             const char* a1 = cA + (size_t)(t + 1) * kstep;
;             const char* a2 = last ? nA : cA + (size_t)(t + 2) * kstep; const char* b2 = last ? nB : cB + (size_t)(t + 2) * kstep;
;             const char* a3 = a2 + kstep; const char* b3 = b2 + kstep;
;             unsigned g2[2][2];
;             if constexpr (GATHER) {
; #pragma unroll
;                 for (int _h = 0; _h < 2; ++_h)
; #pragma unroll
;                     for (int _i = 0; _i < 2; ++_i) g2[_h][_i] = last ? gN[_h][_i] : gC[_h][_i]; }
;             if constexpr (SP2) {
;             PG8_LDB(B0, 0, 0); PG8_LDB(B1, 0, 1); PG8_SCHED; PG8_LDA(At, 0, 0); PG8_STAGE_A(PG8_SA(1, 1), a1, 1, gC);
;             PG8_WAIT_V(8); PG8_WAIT_L(0); PG8_BAR; PG8_MMA(0, 0, At, B0); PG8_MMA(0, 1, At, B1); PG8_BAR; PG8_SCHED;
;             PG8_LDA(At, 0, 1); PG8_STAGE(PG8_SB(0, 0), b2, voffB); PG8_STAGE(PG8_SB(0, 1), b2 + hstepB, voffB); PG8_STAGE_A(PG8_SA(0, 0), a2, 0, g2);
;             PG8_WAIT_V(8); PG8_WAIT_L(0); PG8_BAR; PG8_MMA(1, 0, At, B0); PG8_MMA(1, 1, At, B1); PG8_BAR; PG8_SCHED;
.LBB0_402:
	s_add_u32 s0, s24, 0xfff80080
	s_addc_u32 s1, s25, -1
	s_add_i32 s16, 0, 0x10000
	s_cmp_eq_u32 s15, 28
	s_cselect_b32 s31, s45, s1
	s_cselect_b32 s30, s44, s0
	s_cselect_b32 s1, s47, s14
	s_cselect_b32 s0, s46, s13
	s_add_i32 s18, 0, 0x14000
	v_add_u32_e32 v160, s16, v143
	v_add_u32_e32 v176, s18, v143
	ds_read_b128 v[148:151], v160
	ds_read_b128 v[152:155], v160 offset:1024
	ds_read_b128 v[156:159], v160 offset:2048
	ds_read_b128 v[160:163], v160 offset:3072
	ds_read_b128 v[164:167], v176
	ds_read_b128 v[168:171], v176 offset:1024
	ds_read_b128 v[172:175], v176 offset:2048
	ds_read_b128 v[176:179], v176 offset:3072
	v_lshl_add_u64 v[204:205], s[24:25], 0, v[138:139]
	s_add_i32 m0, s27, 0xc000
	ds_read_b128 v[180:183], v147
	ds_read_b128 v[184:187], v147 offset:1024
	ds_read_b128 v[188:191], v147 offset:2048
	ds_read_b128 v[192:195], v147 offset:3072
	ds_read_b128 v[196:199], v147 offset:4096
	ds_read_b128 v[200:203], v147 offset:5120
	ds_read_b128 v[216:219], v147 offset:6144
	ds_read_b128 v[220:223], v147 offset:7168
	global_load_lds_dwordx4 v[204:205], off
	v_lshl_add_u64 v[204:205], s[24:25], 0, v[140:141]
	s_add_i32 m0, s27, 0xe000
	s_nop 0
	global_load_lds_dwordx4 v[204:205], off
	s_waitcnt vmcnt(8)
	s_waitcnt lgkmcnt(0)
	s_barrier
	s_waitcnt lgkmcnt(0)
	v_mfma_f32_16x16x32_bf16 v[126:129], v[148:151], v[180:183], v[126:129]
	v_mfma_f32_16x16x32_bf16 v[122:125], v[156:159], v[180:183], v[122:125]
	v_mfma_f32_16x16x32_bf16 v[118:121], v[148:151], v[188:191], v[118:121]
	v_mfma_f32_16x16x32_bf16 v[114:117], v[156:159], v[188:191], v[114:117]
	v_mfma_f32_16x16x32_bf16 v[102:105], v[148:151], v[196:199], v[102:105]
	v_mfma_f32_16x16x32_bf16 v[98:101], v[156:159], v[196:199], v[98:101]
	v_mfma_f32_16x16x32_bf16 v[86:89], v[148:151], v[216:219], v[86:89]
	v_mfma_f32_16x16x32_bf16 v[82:85], v[156:159], v[216:219], v[82:85]
	v_mfma_f32_16x16x32_bf16 v[126:129], v[152:155], v[184:187], v[126:129]
	v_mfma_f32_16x16x32_bf16 v[122:125], v[160:163], v[184:187], v[122:125]
	v_mfma_f32_16x16x32_bf16 v[118:121], v[152:155], v[192:195], v[118:121]
	v_mfma_f32_16x16x32_bf16 v[114:117], v[160:163], v[192:195], v[114:117]
	v_mfma_f32_16x16x32_bf16 v[102:105], v[152:155], v[200:203], v[102:105]
	v_mfma_f32_16x16x32_bf16 v[98:101], v[160:163], v[200:203], v[98:101]
	v_mfma_f32_16x16x32_bf16 v[86:89], v[152:155], v[220:223], v[86:89]
	v_mfma_f32_16x16x32_bf16 v[82:85], v[160:163], v[220:223], v[82:85]
	v_mfma_f32_16x16x32_bf16 v[110:113], v[164:167], v[180:183], v[110:113]
	v_mfma_f32_16x16x32_bf16 v[106:109], v[172:175], v[180:183], v[106:109]
	v_mfma_f32_16x16x32_bf16 v[94:97], v[164:167], v[188:191], v[94:97]
	v_mfma_f32_16x16x32_bf16 v[90:93], v[172:175], v[188:191], v[90:93]
	v_mfma_f32_16x16x32_bf16 v[78:81], v[164:167], v[196:199], v[78:81]
	v_mfma_f32_16x16x32_bf16 v[74:77], v[172:175], v[196:199], v[74:77]
	v_mfma_f32_16x16x32_bf16 v[70:73], v[164:167], v[216:219], v[70:73]
	v_mfma_f32_16x16x32_bf16 v[66:69], v[172:175], v[216:219], v[66:69]
	v_mfma_f32_16x16x32_bf16 v[110:113], v[168:171], v[184:187], v[110:113]
	v_mfma_f32_16x16x32_bf16 v[106:109], v[176:179], v[184:187], v[106:109]
	v_mfma_f32_16x16x32_bf16 v[94:97], v[168:171], v[192:195], v[94:97]
	v_mfma_f32_16x16x32_bf16 v[90:93], v[176:179], v[192:195], v[90:93]
	v_mfma_f32_16x16x32_bf16 v[78:81], v[168:171], v[200:203], v[78:81]
	v_mfma_f32_16x16x32_bf16 v[74:77], v[176:179], v[200:203], v[74:77]
	v_mfma_f32_16x16x32_bf16 v[70:73], v[168:171], v[220:223], v[70:73]
	v_mfma_f32_16x16x32_bf16 v[66:69], v[176:179], v[220:223], v[66:69]
	s_barrier
	s_add_i32 s16, s16, s26
	v_lshl_add_u64 v[204:205], s[0:1], 0, v[132:133]
	s_mov_b32 m0, s16
	ds_read_b128 v[180:183], v147 offset:16384
	ds_read_b128 v[184:187], v147 offset:17408
	ds_read_b128 v[188:191], v147 offset:18432
	ds_read_b128 v[192:195], v147 offset:19456
	ds_read_b128 v[196:199], v147 offset:20480
	ds_read_b128 v[200:203], v147 offset:21504
	ds_read_b128 v[216:219], v147 offset:22528
	ds_read_b128 v[220:223], v147 offset:23552
	global_load_lds_dwordx4 v[204:205], off
	s_add_i32 m0, s16, 0x2000
	s_add_u32 s16, s0, 0x80000
	v_lshl_add_u64 v[208:209], s[0:1], 0, v[136:137]
	s_addc_u32 s17, s1, 0
	s_add_i32 s18, s18, s26
	global_load_lds_dwordx4 v[208:209], off
	v_lshl_add_u64 v[210:211], s[16:17], 0, v[132:133]
	s_mov_b32 m0, s18
	v_lshl_add_u64 v[212:213], s[30:31], 0, v[134:135]
	global_load_lds_dwordx4 v[210:211], off
	v_lshl_add_u64 v[210:211], s[16:17], 0, v[136:137]
	s_add_i32 m0, s18, 0x2000
	s_nop 0
	global_load_lds_dwordx4 v[210:211], off
	v_lshl_add_u64 v[210:211], s[30:31], 0, v[130:131]
	s_mov_b32 m0, s27
	s_nop 0
	global_load_lds_dwordx4 v[210:211], off
	s_mov_b32 m0, s41
	s_nop 0
	global_load_lds_dwordx4 v[212:213], off
	s_waitcnt vmcnt(8)
	s_waitcnt lgkmcnt(0)
	s_barrier
; #define PG8_STAGE(bufoff, gbase, voff) do { _Pragma("unroll") for (int _i = 0; _i < 2; ++_i) \
;         __builtin_amdgcn_global_load_lds((const unsigned*)((const char*)(gbase) + (voff)[_i]), (LAS unsigned*)(lds + (bufoff) + ldsw + _i * 8192), 16, 0, 0); } while (0)
; #define PG8_STAGE_A(bufoff, kptr, half, VO) do { if constexpr (GATHER) { _Pragma("unroll") for (int _i = 0; _i < 2; ++_i) \
;         __builtin_amdgcn_global_load_lds((const unsigned*)((const char*)(kptr) + (VO)[half][_i]), (LAS unsigned*)(lds + (bufoff) + ldsw + _i * 8192), 16, 0, 0); } \
;         else { PG8_STAGE(bufoff, (kptr) + (half) * hstepA, voffA); } } while (0)
; #define PG8_LDA(dst, b, h) do { _Pragma("unroll") for (int m = 0; m < 4; ++m) _Pragma("unroll") for (int k = 0; k < 2; ++k) dst[m][k] = *(const LAS bf16x8*)(lds + PG8_SA(b, h) + aoff + m * 2048 + k * 1024); } while (0)
; #define PG8_LDB(dst, b, h) do { _Pragma("unroll") for (int n = 0; n < 2; ++n) _Pragma("unroll") for (int k = 0; k < 2; ++k) dst[n][k] = *(const LAS bf16x8*)(lds + PG8_SB(b, h) + boff + n * 2048 + k * 1024); } while (0)
; #define PG8_MMA(ai, bj, At, Bt) do { __builtin_amdgcn_s_setprio(1); _Pragma("unroll") for (int m = 0; m < 4; ++m) _Pragma("unroll") for (int n = 0; n < 2; ++n) _Pragma("unroll") for (int k = 0; k < 2; ++k) \
;         acc[ai][bj][m][n] = __builtin_amdgcn_mfma_f32_16x16x32_bf16(Bt[n][k], At[m][k], acc[ai][bj][m][n], 0, 0, 0); __builtin_amdgcn_s_setprio(0); } while (0)
; #define PG8_WAIT_V(n) asm volatile("s_waitcnt vmcnt(" #n ")" ::: "memory")
; #define PG8_WAIT_L(n) asm volatile("s_waitcnt lgkmcnt(" #n ")" ::: "memory")
; #define PG8_BAR __builtin_amdgcn_s_barrier()
; #define PG8_SCHED __builtin_amdgcn_sched_barrier(0)
;     ...
;             PG8_WAIT_V(8); PG8_WAIT_L(0); PG8_BAR; PG8_MMA(1, 0, At, B0); PG8_MMA(1, 1, At, B1); PG8_BAR; PG8_SCHED;
;             PG8_LDB(B0, 1, 0); PG8_LDB(B1, 1, 1); PG8_SCHED; PG8_LDA(At, 1, 0); PG8_STAGE_A(PG8_SA(0, 1), a2, 1, g2);
;             PG8_WAIT_V(8); PG8_WAIT_L(0); PG8_BAR; PG8_MMA(0, 0, At, B0); PG8_MMA(0, 1, At, B1); PG8_BAR; PG8_SCHED;
;             PG8_LDA(At, 1, 1); PG8_STAGE(PG8_SB(1, 0), b3, voffB); PG8_STAGE(PG8_SB(1, 1), b3 + hstepB, voffB); PG8_STAGE_A(PG8_SA(1, 0), a3, 0, g2);
	s_waitcnt lgkmcnt(0)
	v_mfma_f32_16x16x32_bf16 v[62:65], v[148:151], v[180:183], v[62:65]
	v_mfma_f32_16x16x32_bf16 v[58:61], v[156:159], v[180:183], v[58:61]
	v_mfma_f32_16x16x32_bf16 v[54:57], v[148:151], v[188:191], v[54:57]
	v_mfma_f32_16x16x32_bf16 v[50:53], v[156:159], v[188:191], v[50:53]
	v_mfma_f32_16x16x32_bf16 v[38:41], v[148:151], v[196:199], v[38:41]
	v_mfma_f32_16x16x32_bf16 v[34:37], v[156:159], v[196:199], v[34:37]
	v_mfma_f32_16x16x32_bf16 v[22:25], v[148:151], v[216:219], v[22:25]
	v_mfma_f32_16x16x32_bf16 v[18:21], v[156:159], v[216:219], v[18:21]
	v_mfma_f32_16x16x32_bf16 v[62:65], v[152:155], v[184:187], v[62:65]
	v_mfma_f32_16x16x32_bf16 v[58:61], v[160:163], v[184:187], v[58:61]
	v_mfma_f32_16x16x32_bf16 v[54:57], v[152:155], v[192:195], v[54:57]
	v_mfma_f32_16x16x32_bf16 v[50:53], v[160:163], v[192:195], v[50:53]
	v_mfma_f32_16x16x32_bf16 v[38:41], v[152:155], v[200:203], v[38:41]
	v_mfma_f32_16x16x32_bf16 v[34:37], v[160:163], v[200:203], v[34:37]
	v_mfma_f32_16x16x32_bf16 v[22:25], v[152:155], v[220:223], v[22:25]
	v_mfma_f32_16x16x32_bf16 v[18:21], v[160:163], v[220:223], v[18:21]
	v_mfma_f32_16x16x32_bf16 v[46:49], v[164:167], v[180:183], v[46:49]
	v_mfma_f32_16x16x32_bf16 v[42:45], v[172:175], v[180:183], v[42:45]
	v_mfma_f32_16x16x32_bf16 v[30:33], v[164:167], v[188:191], v[30:33]
	v_mfma_f32_16x16x32_bf16 v[26:29], v[172:175], v[188:191], v[26:29]
	v_mfma_f32_16x16x32_bf16 v[14:17], v[164:167], v[196:199], v[14:17]
	v_mfma_f32_16x16x32_bf16 v[10:13], v[172:175], v[196:199], v[10:13]
	v_mfma_f32_16x16x32_bf16 v[6:9], v[164:167], v[216:219], v[6:9]
	v_mfma_f32_16x16x32_bf16 v[2:5], v[172:175], v[216:219], v[2:5]
	v_mfma_f32_16x16x32_bf16 v[46:49], v[168:171], v[184:187], v[46:49]
	v_mfma_f32_16x16x32_bf16 v[42:45], v[176:179], v[184:187], v[42:45]
	v_mfma_f32_16x16x32_bf16 v[30:33], v[168:171], v[192:195], v[30:33]
	v_mfma_f32_16x16x32_bf16 v[26:29], v[176:179], v[192:195], v[26:29]
	v_mfma_f32_16x16x32_bf16 v[14:17], v[168:171], v[200:203], v[14:17]
	v_mfma_f32_16x16x32_bf16 v[10:13], v[176:179], v[200:203], v[10:13]
	v_mfma_f32_16x16x32_bf16 v[6:9], v[168:171], v[220:223], v[6:9]
	v_mfma_f32_16x16x32_bf16 v[2:5], v[176:179], v[220:223], v[2:5]
	s_barrier
	s_add_i32 s18, 0, 0x18000
	s_add_i32 s19, 0, 0x1c000
	v_add_u32_e32 v160, s18, v143
	v_add_u32_e32 v176, s19, v143
	ds_read_b128 v[148:151], v160
	ds_read_b128 v[152:155], v160 offset:1024
	ds_read_b128 v[156:159], v160 offset:2048
	ds_read_b128 v[160:163], v160 offset:3072
	ds_read_b128 v[164:167], v176
	ds_read_b128 v[168:171], v176 offset:1024
	ds_read_b128 v[172:175], v176 offset:2048
	ds_read_b128 v[176:179], v176 offset:3072
	s_add_u32 s16, s30, 0x80000
	s_addc_u32 s17, s31, 0
	s_mov_b32 m0, s48
	v_lshl_add_u64 v[224:225], s[16:17], 0, v[130:131]
	ds_read_b128 v[180:183], v147 offset:32768
	ds_read_b128 v[184:187], v147 offset:33792
	ds_read_b128 v[188:191], v147 offset:34816
	ds_read_b128 v[192:195], v147 offset:35840
	ds_read_b128 v[196:199], v147 offset:36864
	ds_read_b128 v[200:203], v147 offset:37888
	ds_read_b128 v[216:219], v147 offset:38912
	ds_read_b128 v[220:223], v147 offset:39936
	global_load_lds_dwordx4 v[224:225], off
	v_lshl_add_u64 v[224:225], s[16:17], 0, v[134:135]
	s_mov_b32 m0, s49
	s_nop 0
	global_load_lds_dwordx4 v[224:225], off
	s_waitcnt vmcnt(8)
	s_waitcnt lgkmcnt(0)
	s_barrier
	s_waitcnt lgkmcnt(0)
	v_mfma_f32_16x16x32_bf16 v[126:129], v[148:151], v[180:183], v[126:129]
	v_mfma_f32_16x16x32_bf16 v[122:125], v[156:159], v[180:183], v[122:125]
	v_mfma_f32_16x16x32_bf16 v[118:121], v[148:151], v[188:191], v[118:121]
	v_mfma_f32_16x16x32_bf16 v[114:117], v[156:159], v[188:191], v[114:117]
	v_mfma_f32_16x16x32_bf16 v[102:105], v[148:151], v[196:199], v[102:105]
	v_mfma_f32_16x16x32_bf16 v[98:101], v[156:159], v[196:199], v[98:101]
	v_mfma_f32_16x16x32_bf16 v[86:89], v[148:151], v[216:219], v[86:89]
	v_mfma_f32_16x16x32_bf16 v[82:85], v[156:159], v[216:219], v[82:85]
	v_mfma_f32_16x16x32_bf16 v[126:129], v[152:155], v[184:187], v[126:129]
	v_mfma_f32_16x16x32_bf16 v[122:125], v[160:163], v[184:187], v[122:125]
	v_mfma_f32_16x16x32_bf16 v[118:121], v[152:155], v[192:195], v[118:121]
	v_mfma_f32_16x16x32_bf16 v[114:117], v[160:163], v[192:195], v[114:117]
	v_mfma_f32_16x16x32_bf16 v[102:105], v[152:155], v[200:203], v[102:105]
	v_mfma_f32_16x16x32_bf16 v[98:101], v[160:163], v[200:203], v[98:101]
	v_mfma_f32_16x16x32_bf16 v[86:89], v[152:155], v[220:223], v[86:89]
	v_mfma_f32_16x16x32_bf16 v[82:85], v[160:163], v[220:223], v[82:85]
	v_mfma_f32_16x16x32_bf16 v[110:113], v[164:167], v[180:183], v[110:113]
	v_mfma_f32_16x16x32_bf16 v[106:109], v[172:175], v[180:183], v[106:109]
	v_mfma_f32_16x16x32_bf16 v[94:97], v[164:167], v[188:191], v[94:97]
	v_mfma_f32_16x16x32_bf16 v[90:93], v[172:175], v[188:191], v[90:93]
	v_mfma_f32_16x16x32_bf16 v[78:81], v[164:167], v[196:199], v[78:81]
	v_mfma_f32_16x16x32_bf16 v[74:77], v[172:175], v[196:199], v[74:77]
	v_mfma_f32_16x16x32_bf16 v[70:73], v[164:167], v[216:219], v[70:73]
	v_mfma_f32_16x16x32_bf16 v[66:69], v[172:175], v[216:219], v[66:69]
	v_mfma_f32_16x16x32_bf16 v[110:113], v[168:171], v[184:187], v[110:113]
	v_mfma_f32_16x16x32_bf16 v[106:109], v[176:179], v[184:187], v[106:109]
	v_mfma_f32_16x16x32_bf16 v[94:97], v[168:171], v[192:195], v[94:97]
	v_mfma_f32_16x16x32_bf16 v[90:93], v[176:179], v[192:195], v[90:93]
	v_mfma_f32_16x16x32_bf16 v[78:81], v[168:171], v[200:203], v[78:81]
	v_mfma_f32_16x16x32_bf16 v[74:77], v[176:179], v[200:203], v[74:77]
	v_mfma_f32_16x16x32_bf16 v[70:73], v[168:171], v[220:223], v[70:73]
	v_mfma_f32_16x16x32_bf16 v[66:69], v[176:179], v[220:223], v[66:69]
	s_barrier
; #define PG8_STAGE(bufoff, gbase, voff) do { _Pragma("unroll") for (int _i = 0; _i < 2; ++_i) \
;         __builtin_amdgcn_global_load_lds((const unsigned*)((const char*)(gbase) + (voff)[_i]), (LAS unsigned*)(lds + (bufoff) + ldsw + _i * 8192), 16, 0, 0); } while (0)
; #define PG8_STAGE_A(bufoff, kptr, half, VO) do { if constexpr (GATHER) { _Pragma("unroll") for (int _i = 0; _i < 2; ++_i) \
;         __builtin_amdgcn_global_load_lds((const unsigned*)((const char*)(kptr) + (VO)[half][_i]), (LAS unsigned*)(lds + (bufoff) + ldsw + _i * 8192), 16, 0, 0); } \
;         else { PG8_STAGE(bufoff, (kptr) + (half) * hstepA, voffA); } } while (0)
; #define PG8_LDA(dst, b, h) do { _Pragma("unroll") for (int m = 0; m < 4; ++m) _Pragma("unroll") for (int k = 0; k < 2; ++k) dst[m][k] = *(const LAS bf16x8*)(lds + PG8_SA(b, h) + aoff + m * 2048 + k * 1024); } while (0)
; #define PG8_MMA(ai, bj, At, Bt) do { __builtin_amdgcn_s_setprio(1); _Pragma("unroll") for (int m = 0; m < 4; ++m) _Pragma("unroll") for (int n = 0; n < 2; ++n) _Pragma("unroll") for (int k = 0; k < 2; ++k) \
;         acc[ai][bj][m][n] = __builtin_amdgcn_mfma_f32_16x16x32_bf16(Bt[n][k], At[m][k], acc[ai][bj][m][n], 0, 0, 0); __builtin_amdgcn_s_setprio(0); } while (0)
; #define PG8_WAIT_V(n) asm volatile("s_waitcnt vmcnt(" #n ")" ::: "memory")
; #define PG8_WAIT_L(n) asm volatile("s_waitcnt lgkmcnt(" #n ")" ::: "memory")
; #define PG8_BAR __builtin_amdgcn_s_barrier()
; #define PG8_SCHED __builtin_amdgcn_sched_barrier(0)
;     ...
;         for (int t = 0; t < nt; t += 2) {
;     ...
;             PG8_LDA(At, 1, 1); PG8_STAGE(PG8_SB(1, 0), b3, voffB); PG8_STAGE(PG8_SB(1, 1), b3 + hstepB, voffB); PG8_STAGE_A(PG8_SA(1, 0), a3, 0, g2);
;             PG8_WAIT_V(8); PG8_WAIT_L(0); PG8_BAR; PG8_MMA(1, 0, At, B0); PG8_MMA(1, 1, At, B1); PG8_BAR; PG8_SCHED;
;     ...
;         if constexpr (ALIGN_EPI) { if (wr == 0) PG8_BAR; }
	s_add_i32 s16, s18, s26
	v_lshl_add_u64 v[204:205], v[204:205], 0, s[8:9]
	s_mov_b32 m0, s16
	ds_read_b128 v[180:183], v147 offset:49152
	ds_read_b128 v[184:187], v147 offset:50176
	ds_read_b128 v[188:191], v147 offset:51200
	ds_read_b128 v[192:195], v147 offset:52224
	ds_read_b128 v[196:199], v147 offset:53248
	ds_read_b128 v[200:203], v147 offset:54272
	ds_read_b128 v[216:219], v147 offset:55296
	ds_read_b128 v[220:223], v147 offset:56320
	global_load_lds_dwordx4 v[204:205], off
	s_add_i32 m0, s16, 0x2000
	s_add_u32 s0, s0, 0x80080
	v_lshl_add_u64 v[204:205], v[208:209], 0, s[8:9]
	s_addc_u32 s1, s1, 0
	s_add_i32 s16, s19, s26
	global_load_lds_dwordx4 v[204:205], off
	v_lshl_add_u64 v[204:205], s[0:1], 0, v[132:133]
	s_mov_b32 m0, s16
	s_nop 0
	global_load_lds_dwordx4 v[204:205], off
	v_lshl_add_u64 v[204:205], s[0:1], 0, v[136:137]
	s_add_i32 m0, s16, 0x2000
	s_nop 0
	global_load_lds_dwordx4 v[204:205], off
	v_lshl_add_u64 v[204:205], v[210:211], 0, s[8:9]
	s_mov_b32 m0, s50
	s_nop 0
	global_load_lds_dwordx4 v[204:205], off
	v_lshl_add_u64 v[204:205], v[212:213], 0, s[8:9]
	s_mov_b32 m0, s51
	s_nop 0
	global_load_lds_dwordx4 v[204:205], off
	s_waitcnt vmcnt(8)
	s_waitcnt lgkmcnt(0)
	s_barrier
	s_waitcnt lgkmcnt(0)
	v_mfma_f32_16x16x32_bf16 v[62:65], v[148:151], v[180:183], v[62:65]
	v_mfma_f32_16x16x32_bf16 v[58:61], v[156:159], v[180:183], v[58:61]
	v_mfma_f32_16x16x32_bf16 v[54:57], v[148:151], v[188:191], v[54:57]
	v_mfma_f32_16x16x32_bf16 v[50:53], v[156:159], v[188:191], v[50:53]
	v_mfma_f32_16x16x32_bf16 v[38:41], v[148:151], v[196:199], v[38:41]
	v_mfma_f32_16x16x32_bf16 v[34:37], v[156:159], v[196:199], v[34:37]
	v_mfma_f32_16x16x32_bf16 v[22:25], v[148:151], v[216:219], v[22:25]
	v_mfma_f32_16x16x32_bf16 v[18:21], v[156:159], v[216:219], v[18:21]
	v_mfma_f32_16x16x32_bf16 v[62:65], v[152:155], v[184:187], v[62:65]
	v_mfma_f32_16x16x32_bf16 v[58:61], v[160:163], v[184:187], v[58:61]
	v_mfma_f32_16x16x32_bf16 v[54:57], v[152:155], v[192:195], v[54:57]
	v_mfma_f32_16x16x32_bf16 v[50:53], v[160:163], v[192:195], v[50:53]
	v_mfma_f32_16x16x32_bf16 v[38:41], v[152:155], v[200:203], v[38:41]
	v_mfma_f32_16x16x32_bf16 v[34:37], v[160:163], v[200:203], v[34:37]
	v_mfma_f32_16x16x32_bf16 v[22:25], v[152:155], v[220:223], v[22:25]
	v_mfma_f32_16x16x32_bf16 v[18:21], v[160:163], v[220:223], v[18:21]
	v_mfma_f32_16x16x32_bf16 v[46:49], v[164:167], v[180:183], v[46:49]
	v_mfma_f32_16x16x32_bf16 v[42:45], v[172:175], v[180:183], v[42:45]
	v_mfma_f32_16x16x32_bf16 v[30:33], v[164:167], v[188:191], v[30:33]
	v_mfma_f32_16x16x32_bf16 v[26:29], v[172:175], v[188:191], v[26:29]
	v_mfma_f32_16x16x32_bf16 v[14:17], v[164:167], v[196:199], v[14:17]
	v_mfma_f32_16x16x32_bf16 v[10:13], v[172:175], v[196:199], v[10:13]
	v_mfma_f32_16x16x32_bf16 v[6:9], v[164:167], v[216:219], v[6:9]
	v_mfma_f32_16x16x32_bf16 v[2:5], v[172:175], v[216:219], v[2:5]
	v_mfma_f32_16x16x32_bf16 v[46:49], v[168:171], v[184:187], v[46:49]
	v_mfma_f32_16x16x32_bf16 v[42:45], v[176:179], v[184:187], v[42:45]
	v_mfma_f32_16x16x32_bf16 v[30:33], v[168:171], v[192:195], v[30:33]
	v_mfma_f32_16x16x32_bf16 v[26:29], v[176:179], v[192:195], v[26:29]
	v_mfma_f32_16x16x32_bf16 v[14:17], v[168:171], v[200:203], v[14:17]
	v_mfma_f32_16x16x32_bf16 v[10:13], v[176:179], v[200:203], v[10:13]
	v_mfma_f32_16x16x32_bf16 v[6:9], v[168:171], v[220:223], v[6:9]
	v_mfma_f32_16x16x32_bf16 v[2:5], v[176:179], v[220:223], v[2:5]
	s_barrier
	s_add_i32 s15, s15, 2
	s_add_u32 s24, s24, 0x100
	s_addc_u32 s25, s25, 0
	s_add_u32 s13, s13, 0x100
	s_addc_u32 s14, s14, 0
	s_cmp_gt_u32 s15, 29
	s_cbranch_scc0 .LBB0_402
	s_and_b64 vcc, exec, s[38:39]
	s_cbranch_vccz .LBB0_405
	s_barrier

; #define REPLOOP(id) for (int rep_ = 0; rep_ < NREP(id); ++rep_)
; #define REPBAR(id) do { if (rep_ + 1 < NREP(id)) xcd_barrier(bar); } while (0)
; #define SEAM(k) do { if (IN(k) && IN((k) + 1)) xcd_barrier(bar); } while (0)
; __global__ void __launch_bounds__(512, 2) fwd(Params p) {
;     ...
;         SEAM(pb + 0);
;         if (PSEL(3) && IN(pb + 1)) REPLOOP(3) { ph_rowsplit(p, l, lds); __syncthreads();  REPBAR(3); }
;         SEAM(pb + 1);
;         if (PSEL(4) && IN(pb + 2)) REPLOOP(4) {
.LBB0_463:
	s_setprio 0
	v_readlane_b32 s0, v255, 54
	v_readlane_b32 s1, v255, 55
	s_xor_b64 s[76:77], s[0:1], -1
	s_cmp_le_i32 s86, s4
	s_cselect_b64 s[0:1], -1, 0
	s_cmp_lt_i32 s4, s87
	s_cselect_b64 s[2:3], -1, 0
	s_and_b64 s[2:3], s[0:1], s[2:3]
	s_mov_b64 s[0:1], -1
	s_and_b64 vcc, exec, s[2:3]
	s_cbranch_vccnz .LBB0_465
	v_readlane_b32 s0, v252, 5
	v_readlane_b32 s1, v252, 6
	s_mul_i32 s0, s0, 13
	s_add_i32 s4, s0, 4
	s_mov_b64 s[0:1], 0

; #define REPLOOP(id) for (int rep_ = 0; rep_ < NREP(id); ++rep_)
; #define SEAM(k) do { if (IN(k) && IN((k) + 1)) xcd_barrier(bar); } while (0)
; __global__ void __launch_bounds__(512, 2) fwd(Params p) {
;     ...
;         SEAM(pb + 2);
;         if (PSEL(5) && IN(pb + 3)) REPLOOP(5) {
.LBB0_590:
	s_setprio 0
	s_cmp_le_i32 s86, s4
	s_cselect_b64 s[0:1], -1, 0
	s_cmp_lt_i32 s4, s87
	s_cselect_b64 s[2:3], -1, 0
	s_and_b64 s[2:3], s[0:1], s[2:3]
	s_mov_b64 s[0:1], -1
	s_and_b64 vcc, exec, s[2:3]
	s_cbranch_vccnz .LBB0_592
	v_readlane_b32 s0, v255, 56
	s_add_i32 s4, s0, 5
	s_mov_b64 s[0:1], 0

; #define PG8_STAGE(bufoff, gbase, voff) do { _Pragma("unroll") for (int _i = 0; _i < 2; ++_i) \
;         __builtin_amdgcn_global_load_lds((const unsigned*)((const char*)(gbase) + (voff)[_i]), (LAS unsigned*)(lds + (bufoff) + ldsw + _i * 8192), 16, 0, 0); } while (0)
; #define PG8_STAGE_A(bufoff, kptr, half, VO) do { if constexpr (GATHER) { _Pragma("unroll") for (int _i = 0; _i < 2; ++_i) \
;         __builtin_amdgcn_global_load_lds((const unsigned*)((const char*)(kptr) + (VO)[half][_i]), (LAS unsigned*)(lds + (bufoff) + ldsw + _i * 8192), 16, 0, 0); } \
;         else { PG8_STAGE(bufoff, (kptr) + (half) * hstepA, voffA); } } while (0)
; #define PG8_WAIT_V(n) asm volatile("s_waitcnt vmcnt(" #n ")" ::: "memory")
; #define PG8_BAR __builtin_amdgcn_s_barrier()
;     ...
;     for (int i = 0; i < 2; ++i) { int R, C; stage_rc(tid * 16 + i * 8192, R, C); const int Rb = Epi::PERM ? ((R & ~31) + perm32(R & 31)) : R;
;         voffA[i] = (unsigned)(R * g.lda + C) * 2u; voffB[i] = (unsigned)(Rb * g.ldb + C) * 2u; gR[i] = R; gCc[i] = C; }
;     ...
;     if constexpr (SP2) {
;         PG8_STAGE(PG8_SB(0, 0), cB, voffB); PG8_STAGE(PG8_SB(0, 1), cB + hstepB, voffB); PG8_STAGE_A(PG8_SA(0, 0), cA, 0, gC); PG8_STAGE_A(PG8_SA(0, 1), cA, 1, gC);
;         if (wr == 1) PG8_BAR;
;         PG8_WAIT_V(2); PG8_BAR;
;         PG8_STAGE(PG8_SB(1, 0), cB + kstep, voffB); PG8_STAGE_A(PG8_SA(1, 0), cA + kstep, 0, gC); PG8_STAGE(PG8_SB(1, 1), cB + hstepB + kstep, voffB);
;         PG8_WAIT_V(6); PG8_BAR;
.LBB0_599:
	s_andn2_b64 vcc, exec, s[2:3]
	s_cbranch_vccnz .LBB0_659
	v_ashrrev_i32_e32 v3, 31, v10
	v_lshrrev_b32_e32 v3, 26, v3
	v_add_u32_e32 v3, v10, v3
	v_ashrrev_i32_e32 v11, 6, v3
	v_bfe_i32 v3, v10, 27, 1
	v_lshlrev_b32_e32 v2, 4, v10
	v_lshrrev_b32_e32 v3, 22, v3
	v_add_u32_e32 v3, v2, v3
	v_and_b32_e32 v3, 0xfffffc00, v3
	v_sub_u32_e32 v3, v2, v3
	v_lshrrev_b32_e32 v4, 4, v3
	v_bitop3_b32 v4, v4, v3, 32 bitop3:0x6c
	v_ashrrev_i32_e32 v3, 31, v3
	v_lshrrev_b32_e32 v3, 26, v3
	v_lshlrev_b32_e32 v5, 3, v11
	v_add_u32_e32 v3, v4, v3
	v_and_b32_e32 v5, 0x1fffff0, v5
	v_ashrrev_i32_e32 v13, 6, v3
	v_add_u32_e32 v3, v13, v5
	v_lshlrev_b32_e32 v5, 5, v11
	v_and_b32_e32 v12, 32, v5
	v_mul_i32_i24_e32 v5, 64, v13
	v_sub_u32_e32 v4, v4, v5
	s_movk_i32 s2, 0x180
	v_ashrrev_i16_sdwa v4, v245, sext(v4) dst_sel:DWORD dst_unused:UNUSED_PAD src0_sel:DWORD src1_sel:BYTE_0
	v_mul_lo_u32 v3, v3, s2
	v_bfe_i32 v14, v4, 0, 16
	v_or_b32_e32 v3, v3, v12
	v_add_u32_e32 v2, 0x2000, v2
	v_add_lshl_u32 v194, v3, v14, 1
	v_ashrrev_i32_e32 v3, 31, v2
	v_lshrrev_b32_e32 v3, 22, v3
	v_add_u32_e32 v3, v2, v3
	v_ashrrev_i32_e32 v15, 10, v3
	v_mul_i32_i24_e32 v3, 0x400, v15
	v_sub_u32_e32 v2, v2, v3
	v_lshrrev_b32_e32 v3, 4, v2
	v_bitop3_b32 v2, v3, v2, 32 bitop3:0x6c
	v_ashrrev_i32_e32 v4, 31, v2
	v_lshrrev_b32_e32 v4, 26, v4
	v_add_u32_e32 v4, v2, v4
	v_lshlrev_b32_e32 v3, 3, v15
	v_ashrrev_i32_e32 v17, 6, v4
	v_and_b32_e32 v4, 0xc0, v4
	s_ashr_i32 s13, s12, 6
	v_and_b32_e32 v3, 0x1fffff0, v3
	v_sub_u32_e32 v2, v2, v4
	s_lshl_b32 s60, s13, 10
	v_add_u32_e32 v3, v17, v3
	v_lshlrev_b32_e32 v5, 5, v15
	v_ashrrev_i16_sdwa v2, v245, sext(v2) dst_sel:DWORD dst_unused:UNUSED_PAD src0_sel:DWORD src1_sel:BYTE_0
	s_add_i32 s61, s60, 0
	v_and_b32_e32 v16, 32, v5
	v_bfe_i32 v18, v2, 0, 16
	v_mul_lo_u32 v2, v3, s2
	s_add_i32 m0, s61, 0x10000
	s_ashr_i32 s59, s12, 8
	v_or_b32_e32 v2, v2, v16
	global_load_lds_dwordx4 v194, s[0:1]
	s_add_i32 m0, s61, 0x12000
	v_add_lshl_u32 v196, v2, v18, 1
	s_add_u32 s2, s0, 0x18000
	global_load_lds_dwordx4 v196, s[0:1]
	s_addc_u32 s3, s1, 0
	s_add_i32 m0, s61, 0x14000
	s_add_i32 s63, s61, 0x2000
	global_load_lds_dwordx4 v194, s[2:3]
	s_add_i32 m0, s61, 0x16000
	v_mov_b32_e32 v195, v207
	global_load_lds_dwordx4 v196, s[2:3]
	s_mov_b32 m0, s61
	s_add_u32 s2, s38, 0x18000
	global_load_lds_dwordx4 v194, s[38:39]
	s_mov_b32 m0, s63
	s_addc_u32 s3, s39, 0
	s_add_i32 s64, s61, 0x4000
	global_load_lds_dwordx4 v196, s[38:39]
	s_mov_b32 m0, s64
	s_add_i32 s65, s61, 0x6000
	global_load_lds_dwordx4 v194, s[2:3]
	s_mov_b32 m0, s65
	v_mov_b32_e32 v197, v207
	global_load_lds_dwordx4 v196, s[2:3]
	s_cmp_eq_u32 s59, 1
	v_lshl_add_u64 v[8:9], s[0:1], 0, v[194:195]
	v_lshl_add_u64 v[6:7], s[0:1], 0, v[196:197]
	v_lshl_add_u64 v[2:3], s[38:39], 0, v[194:195]
	s_cselect_b64 s[2:3], -1, 0
	s_cmp_lg_u32 s59, 1
	v_lshl_add_u64 v[4:5], s[38:39], 0, v[196:197]
	s_cbranch_scc1 .LBB0_602
	s_barrier
	s_setprio 1

; #define PG8_STAGE(bufoff, gbase, voff) do { _Pragma("unroll") for (int _i = 0; _i < 2; ++_i) \
;         __builtin_amdgcn_global_load_lds((const unsigned*)((const char*)(gbase) + (voff)[_i]), (LAS unsigned*)(lds + (bufoff) + ldsw + _i * 8192), 16, 0, 0); } while (0)
; #define PG8_STAGE_A(bufoff, kptr, half, VO) do { if constexpr (GATHER) { _Pragma("unroll") for (int _i = 0; _i < 2; ++_i) \
;         __builtin_amdgcn_global_load_lds((const unsigned*)((const char*)(kptr) + (VO)[half][_i]), (LAS unsigned*)(lds + (bufoff) + ldsw + _i * 8192), 16, 0, 0); } \
;         else { PG8_STAGE(bufoff, (kptr) + (half) * hstepA, voffA); } } while (0)
; #define PG8_LDA(dst, b, h) do { _Pragma("unroll") for (int m = 0; m < 4; ++m) _Pragma("unroll") for (int k = 0; k < 2; ++k) dst[m][k] = *(const LAS bf16x8*)(lds + PG8_SA(b, h) + aoff + m * 2048 + k * 1024); } while (0)
; #define PG8_LDB(dst, b, h) do { _Pragma("unroll") for (int n = 0; n < 2; ++n) _Pragma("unroll") for (int k = 0; k < 2; ++k) dst[n][k] = *(const LAS bf16x8*)(lds + PG8_SB(b, h) + boff + n * 2048 + k * 1024); } while (0)
; #define PG8_WAIT_V(n) asm volatile("s_waitcnt vmcnt(" #n ")" ::: "memory")
; #define PG8_WAIT_L(n) asm volatile("s_waitcnt lgkmcnt(" #n ")" ::: "memory")
;     ...
;         for (int t = 0; t < nt; t += 2) {
;             const bool last = (t == nt - 2);
;             const char* a1 = cA + (size_t)(t + 1) * kstep;
;             const char* a2 = last ? nA : cA + (size_t)(t + 2) * kstep; const char* b2 = last ? nB : cB + (size_t)(t + 2) * kstep;
;             const char* a3 = a2 + kstep; const char* b3 = b2 + kstep;
;             unsigned g2[2][2];
;             if constexpr (GATHER) {
; #pragma unroll
;                 for (int _h = 0; _h < 2; ++_h)
; #pragma unroll
;                     for (int _i = 0; _i < 2; ++_i) g2[_h][_i] = last ? gN[_h][_i] : gC[_h][_i]; }
;             if constexpr (SP2) {
;             PG8_LDB(B0, 0, 0); PG8_LDB(B1, 0, 1); PG8_SCHED; PG8_LDA(At, 0, 0); PG8_STAGE_A(PG8_SA(1, 1), a1, 1, gC);
;             PG8_WAIT_V(8); PG8_WAIT_L(0); PG8_BAR; PG8_MMA(0, 0, At, B0); PG8_MMA(0, 1, At, B1); PG8_BAR; PG8_SCHED;
;             PG8_LDA(At, 0, 1); PG8_STAGE(PG8_SB(0, 0), b2, voffB); PG8_STAGE(PG8_SB(0, 1), b2 + hstepB, voffB); PG8_STAGE_A(PG8_SA(0, 0), a2, 0, g2);
;             PG8_WAIT_V(8); PG8_WAIT_L(0); PG8_BAR; PG8_MMA(1, 0, At, B0); PG8_MMA(1, 1, At, B1); PG8_BAR; PG8_SCHED;
.LBB0_615:
	s_add_u32 s0, s38, 0x100
	s_addc_u32 s1, s39, 0
	s_add_i32 s15, 0, 0x10000
	s_cmp_eq_u32 s14, 2
	s_cselect_b32 s31, s45, s1
	s_cselect_b32 s30, s44, s0
	s_cselect_b32 s25, s47, s13
	s_cselect_b32 s24, s46, s12
	s_add_i32 s18, 0, 0x14000
	s_waitcnt vmcnt(0)
	v_add_u32_e32 v106, s15, v217
	v_add_u32_e32 v150, s18, v217
	ds_read_b128 v[82:85], v106
	ds_read_b128 v[86:89], v106 offset:1024
	ds_read_b128 v[102:105], v106 offset:2048
	ds_read_b128 v[106:109], v106 offset:3072
	ds_read_b128 v[122:125], v150
	ds_read_b128 v[126:129], v150 offset:1024
	ds_read_b128 v[146:149], v150 offset:2048
	ds_read_b128 v[150:153], v150 offset:3072
	v_lshl_add_u64 v[208:209], s[38:39], 0, v[202:203]
	s_add_i32 m0, s61, 0xc000
	ds_read_b128 v[162:165], v221
	ds_read_b128 v[166:169], v221 offset:1024
	ds_read_b128 v[170:173], v221 offset:2048
	ds_read_b128 v[174:177], v221 offset:3072
	ds_read_b128 v[178:181], v221 offset:4096
	ds_read_b128 v[182:185], v221 offset:5120
	ds_read_b128 v[186:189], v221 offset:6144
	ds_read_b128 v[190:193], v221 offset:7168
	global_load_lds_dwordx4 v[208:209], off
	v_lshl_add_u64 v[208:209], s[38:39], 0, v[204:205]
	s_add_i32 m0, s61, 0xe000
	s_nop 0
	global_load_lds_dwordx4 v[208:209], off
	s_waitcnt vmcnt(8)
	s_waitcnt lgkmcnt(0)
	s_barrier
	s_waitcnt lgkmcnt(0)
	v_mfma_f32_16x16x32_bf16 v[158:161], v[82:85], v[162:165], v[158:161]
	v_mfma_f32_16x16x32_bf16 v[154:157], v[102:105], v[162:165], v[154:157]
	v_mfma_f32_16x16x32_bf16 v[134:137], v[82:85], v[170:173], v[134:137]
	v_mfma_f32_16x16x32_bf16 v[130:133], v[102:105], v[170:173], v[130:133]
	v_mfma_f32_16x16x32_bf16 v[110:113], v[82:85], v[178:181], v[110:113]
	v_mfma_f32_16x16x32_bf16 v[98:101], v[102:105], v[178:181], v[98:101]
	v_mfma_f32_16x16x32_bf16 v[78:81], v[82:85], v[186:189], v[78:81]
	v_mfma_f32_16x16x32_bf16 v[74:77], v[102:105], v[186:189], v[74:77]
	v_mfma_f32_16x16x32_bf16 v[158:161], v[86:89], v[166:169], v[158:161]
	v_mfma_f32_16x16x32_bf16 v[154:157], v[106:109], v[166:169], v[154:157]
	v_mfma_f32_16x16x32_bf16 v[134:137], v[86:89], v[174:177], v[134:137]
	v_mfma_f32_16x16x32_bf16 v[130:133], v[106:109], v[174:177], v[130:133]
	v_mfma_f32_16x16x32_bf16 v[110:113], v[86:89], v[182:185], v[110:113]
	v_mfma_f32_16x16x32_bf16 v[98:101], v[106:109], v[182:185], v[98:101]
	v_mfma_f32_16x16x32_bf16 v[78:81], v[86:89], v[190:193], v[78:81]
	v_mfma_f32_16x16x32_bf16 v[74:77], v[106:109], v[190:193], v[74:77]
	v_mfma_f32_16x16x32_bf16 v[142:145], v[122:125], v[162:165], v[142:145]
	v_mfma_f32_16x16x32_bf16 v[138:141], v[146:149], v[162:165], v[138:141]
	v_mfma_f32_16x16x32_bf16 v[118:121], v[122:125], v[170:173], v[118:121]
	v_mfma_f32_16x16x32_bf16 v[114:117], v[146:149], v[170:173], v[114:117]
	v_mfma_f32_16x16x32_bf16 v[94:97], v[122:125], v[178:181], v[94:97]
	v_mfma_f32_16x16x32_bf16 v[90:93], v[146:149], v[178:181], v[90:93]
	v_mfma_f32_16x16x32_bf16 v[70:73], v[122:125], v[186:189], v[70:73]
	v_mfma_f32_16x16x32_bf16 v[66:69], v[146:149], v[186:189], v[66:69]
	v_mfma_f32_16x16x32_bf16 v[142:145], v[126:129], v[166:169], v[142:145]
	v_mfma_f32_16x16x32_bf16 v[138:141], v[150:153], v[166:169], v[138:141]
	v_mfma_f32_16x16x32_bf16 v[118:121], v[126:129], v[174:177], v[118:121]
	v_mfma_f32_16x16x32_bf16 v[114:117], v[150:153], v[174:177], v[114:117]
	v_mfma_f32_16x16x32_bf16 v[94:97], v[126:129], v[182:185], v[94:97]
	v_mfma_f32_16x16x32_bf16 v[90:93], v[150:153], v[182:185], v[90:93]
	v_mfma_f32_16x16x32_bf16 v[70:73], v[126:129], v[190:193], v[70:73]
	v_mfma_f32_16x16x32_bf16 v[66:69], v[150:153], v[190:193], v[66:69]
	s_barrier
	s_add_i32 s15, s15, s60
	v_lshl_add_u64 v[208:209], s[24:25], 0, v[194:195]
	s_mov_b32 m0, s15
	ds_read_b128 v[162:165], v221 offset:16384
	ds_read_b128 v[166:169], v221 offset:17408
	ds_read_b128 v[170:173], v221 offset:18432
	ds_read_b128 v[174:177], v221 offset:19456
	ds_read_b128 v[178:181], v221 offset:20480
	ds_read_b128 v[182:185], v221 offset:21504
	ds_read_b128 v[186:189], v221 offset:22528
	ds_read_b128 v[190:193], v221 offset:23552
	global_load_lds_dwordx4 v[208:209], off
	s_add_i32 m0, s15, 0x2000
	s_add_u32 s16, s24, 0x18000
	v_lshl_add_u64 v[210:211], s[24:25], 0, v[196:197]
	s_addc_u32 s17, s25, 0
	s_add_i32 s15, s18, s60
	global_load_lds_dwordx4 v[210:211], off
	v_lshl_add_u64 v[212:213], s[16:17], 0, v[194:195]
	s_mov_b32 m0, s15
	v_lshl_add_u64 v[222:223], s[30:31], 0, v[196:197]
	global_load_lds_dwordx4 v[212:213], off
	v_lshl_add_u64 v[212:213], s[16:17], 0, v[196:197]
	s_add_i32 m0, s15, 0x2000
	s_nop 0
	global_load_lds_dwordx4 v[212:213], off
	v_lshl_add_u64 v[212:213], s[30:31], 0, v[194:195]
	s_mov_b32 m0, s61
	s_nop 0
	global_load_lds_dwordx4 v[212:213], off
	s_mov_b32 m0, s63
	s_nop 0
	global_load_lds_dwordx4 v[222:223], off
	s_waitcnt vmcnt(8)
	s_waitcnt lgkmcnt(0)
	s_barrier
; #define PG8_STAGE(bufoff, gbase, voff) do { _Pragma("unroll") for (int _i = 0; _i < 2; ++_i) \
;         __builtin_amdgcn_global_load_lds((const unsigned*)((const char*)(gbase) + (voff)[_i]), (LAS unsigned*)(lds + (bufoff) + ldsw + _i * 8192), 16, 0, 0); } while (0)
; #define PG8_STAGE_A(bufoff, kptr, half, VO) do { if constexpr (GATHER) { _Pragma("unroll") for (int _i = 0; _i < 2; ++_i) \
;         __builtin_amdgcn_global_load_lds((const unsigned*)((const char*)(kptr) + (VO)[half][_i]), (LAS unsigned*)(lds + (bufoff) + ldsw + _i * 8192), 16, 0, 0); } \
;         else { PG8_STAGE(bufoff, (kptr) + (half) * hstepA, voffA); } } while (0)
; #define PG8_LDA(dst, b, h) do { _Pragma("unroll") for (int m = 0; m < 4; ++m) _Pragma("unroll") for (int k = 0; k < 2; ++k) dst[m][k] = *(const LAS bf16x8*)(lds + PG8_SA(b, h) + aoff + m * 2048 + k * 1024); } while (0)
; #define PG8_LDB(dst, b, h) do { _Pragma("unroll") for (int n = 0; n < 2; ++n) _Pragma("unroll") for (int k = 0; k < 2; ++k) dst[n][k] = *(const LAS bf16x8*)(lds + PG8_SB(b, h) + boff + n * 2048 + k * 1024); } while (0)
; #define PG8_MMA(ai, bj, At, Bt) do { __builtin_amdgcn_s_setprio(1); _Pragma("unroll") for (int m = 0; m < 4; ++m) _Pragma("unroll") for (int n = 0; n < 2; ++n) _Pragma("unroll") for (int k = 0; k < 2; ++k) \
;         acc[ai][bj][m][n] = __builtin_amdgcn_mfma_f32_16x16x32_bf16(Bt[n][k], At[m][k], acc[ai][bj][m][n], 0, 0, 0); __builtin_amdgcn_s_setprio(0); } while (0)
; #define PG8_WAIT_V(n) asm volatile("s_waitcnt vmcnt(" #n ")" ::: "memory")
; #define PG8_WAIT_L(n) asm volatile("s_waitcnt lgkmcnt(" #n ")" ::: "memory")
; #define PG8_BAR __builtin_amdgcn_s_barrier()
; #define PG8_SCHED __builtin_amdgcn_sched_barrier(0)
;     ...
;             PG8_WAIT_V(8); PG8_WAIT_L(0); PG8_BAR; PG8_MMA(1, 0, At, B0); PG8_MMA(1, 1, At, B1); PG8_BAR; PG8_SCHED;
;             PG8_LDB(B0, 1, 0); PG8_LDB(B1, 1, 1); PG8_SCHED; PG8_LDA(At, 1, 0); PG8_STAGE_A(PG8_SA(0, 1), a2, 1, g2);
;             PG8_WAIT_V(8); PG8_WAIT_L(0); PG8_BAR; PG8_MMA(0, 0, At, B0); PG8_MMA(0, 1, At, B1); PG8_BAR; PG8_SCHED;
;             PG8_LDA(At, 1, 1); PG8_STAGE(PG8_SB(1, 0), b3, voffB); PG8_STAGE(PG8_SB(1, 1), b3 + hstepB, voffB); PG8_STAGE_A(PG8_SA(1, 0), a3, 0, g2);
	s_waitcnt lgkmcnt(0)
	v_mfma_f32_16x16x32_bf16 v[62:65], v[82:85], v[162:165], v[62:65]
	v_mfma_f32_16x16x32_bf16 v[58:61], v[102:105], v[162:165], v[58:61]
	v_mfma_f32_16x16x32_bf16 v[46:49], v[82:85], v[170:173], v[46:49]
	v_mfma_f32_16x16x32_bf16 v[42:45], v[102:105], v[170:173], v[42:45]
	v_mfma_f32_16x16x32_bf16 v[30:33], v[82:85], v[178:181], v[30:33]
	v_mfma_f32_16x16x32_bf16 v[26:29], v[102:105], v[178:181], v[26:29]
	v_mfma_f32_16x16x32_bf16 v[14:17], v[82:85], v[186:189], v[14:17]
	v_mfma_f32_16x16x32_bf16 v[10:13], v[102:105], v[186:189], v[10:13]
	v_mfma_f32_16x16x32_bf16 v[62:65], v[86:89], v[166:169], v[62:65]
	v_mfma_f32_16x16x32_bf16 v[58:61], v[106:109], v[166:169], v[58:61]
	v_mfma_f32_16x16x32_bf16 v[46:49], v[86:89], v[174:177], v[46:49]
	v_mfma_f32_16x16x32_bf16 v[42:45], v[106:109], v[174:177], v[42:45]
	v_mfma_f32_16x16x32_bf16 v[30:33], v[86:89], v[182:185], v[30:33]
	v_mfma_f32_16x16x32_bf16 v[26:29], v[106:109], v[182:185], v[26:29]
	v_mfma_f32_16x16x32_bf16 v[14:17], v[86:89], v[190:193], v[14:17]
	v_mfma_f32_16x16x32_bf16 v[10:13], v[106:109], v[190:193], v[10:13]
	v_mfma_f32_16x16x32_bf16 v[54:57], v[122:125], v[162:165], v[54:57]
	v_mfma_f32_16x16x32_bf16 v[50:53], v[146:149], v[162:165], v[50:53]
	v_mfma_f32_16x16x32_bf16 v[38:41], v[122:125], v[170:173], v[38:41]
	v_mfma_f32_16x16x32_bf16 v[34:37], v[146:149], v[170:173], v[34:37]
	v_mfma_f32_16x16x32_bf16 v[22:25], v[122:125], v[178:181], v[22:25]
	v_mfma_f32_16x16x32_bf16 v[18:21], v[146:149], v[178:181], v[18:21]
	v_mfma_f32_16x16x32_bf16 v[6:9], v[122:125], v[186:189], v[6:9]
	v_mfma_f32_16x16x32_bf16 v[2:5], v[146:149], v[186:189], v[2:5]
	v_mfma_f32_16x16x32_bf16 v[54:57], v[126:129], v[166:169], v[54:57]
	v_mfma_f32_16x16x32_bf16 v[50:53], v[150:153], v[166:169], v[50:53]
	v_mfma_f32_16x16x32_bf16 v[38:41], v[126:129], v[174:177], v[38:41]
	v_mfma_f32_16x16x32_bf16 v[34:37], v[150:153], v[174:177], v[34:37]
	v_mfma_f32_16x16x32_bf16 v[22:25], v[126:129], v[182:185], v[22:25]
	v_mfma_f32_16x16x32_bf16 v[18:21], v[150:153], v[182:185], v[18:21]
	v_mfma_f32_16x16x32_bf16 v[6:9], v[126:129], v[190:193], v[6:9]
	v_mfma_f32_16x16x32_bf16 v[2:5], v[150:153], v[190:193], v[2:5]
	s_barrier
	s_add_i32 s15, 0, 0x18000
	s_add_i32 s18, 0, 0x1c000
	v_add_u32_e32 v106, s15, v217
	v_add_u32_e32 v150, s18, v217
	ds_read_b128 v[82:85], v106
	ds_read_b128 v[86:89], v106 offset:1024
	ds_read_b128 v[102:105], v106 offset:2048
	ds_read_b128 v[106:109], v106 offset:3072
	ds_read_b128 v[122:125], v150
	ds_read_b128 v[126:129], v150 offset:1024
	ds_read_b128 v[146:149], v150 offset:2048
	ds_read_b128 v[150:153], v150 offset:3072
	s_add_u32 s16, s30, 0x18000
	s_addc_u32 s17, s31, 0
	s_mov_b32 m0, s64
	v_lshl_add_u64 v[224:225], s[16:17], 0, v[194:195]
	ds_read_b128 v[162:165], v221 offset:32768
	ds_read_b128 v[166:169], v221 offset:33792
	ds_read_b128 v[170:173], v221 offset:34816
	ds_read_b128 v[174:177], v221 offset:35840
	ds_read_b128 v[178:181], v221 offset:36864
	ds_read_b128 v[182:185], v221 offset:37888
	ds_read_b128 v[186:189], v221 offset:38912
	ds_read_b128 v[190:193], v221 offset:39936
	global_load_lds_dwordx4 v[224:225], off
	v_lshl_add_u64 v[224:225], s[16:17], 0, v[196:197]
	s_mov_b32 m0, s65
	s_nop 0
	global_load_lds_dwordx4 v[224:225], off
	s_waitcnt vmcnt(8)
	s_waitcnt lgkmcnt(0)
	s_barrier
	s_waitcnt lgkmcnt(0)
	v_mfma_f32_16x16x32_bf16 v[158:161], v[82:85], v[162:165], v[158:161]
	v_mfma_f32_16x16x32_bf16 v[154:157], v[102:105], v[162:165], v[154:157]
	v_mfma_f32_16x16x32_bf16 v[134:137], v[82:85], v[170:173], v[134:137]
	v_mfma_f32_16x16x32_bf16 v[130:133], v[102:105], v[170:173], v[130:133]
	v_mfma_f32_16x16x32_bf16 v[110:113], v[82:85], v[178:181], v[110:113]
	v_mfma_f32_16x16x32_bf16 v[98:101], v[102:105], v[178:181], v[98:101]
	v_mfma_f32_16x16x32_bf16 v[78:81], v[82:85], v[186:189], v[78:81]
	v_mfma_f32_16x16x32_bf16 v[74:77], v[102:105], v[186:189], v[74:77]
	v_mfma_f32_16x16x32_bf16 v[158:161], v[86:89], v[166:169], v[158:161]
	v_mfma_f32_16x16x32_bf16 v[154:157], v[106:109], v[166:169], v[154:157]
	v_mfma_f32_16x16x32_bf16 v[134:137], v[86:89], v[174:177], v[134:137]
	v_mfma_f32_16x16x32_bf16 v[130:133], v[106:109], v[174:177], v[130:133]
	v_mfma_f32_16x16x32_bf16 v[110:113], v[86:89], v[182:185], v[110:113]
	v_mfma_f32_16x16x32_bf16 v[98:101], v[106:109], v[182:185], v[98:101]
	v_mfma_f32_16x16x32_bf16 v[78:81], v[86:89], v[190:193], v[78:81]
	v_mfma_f32_16x16x32_bf16 v[74:77], v[106:109], v[190:193], v[74:77]
	v_mfma_f32_16x16x32_bf16 v[142:145], v[122:125], v[162:165], v[142:145]
	v_mfma_f32_16x16x32_bf16 v[138:141], v[146:149], v[162:165], v[138:141]
	v_mfma_f32_16x16x32_bf16 v[118:121], v[122:125], v[170:173], v[118:121]
	v_mfma_f32_16x16x32_bf16 v[114:117], v[146:149], v[170:173], v[114:117]
	v_mfma_f32_16x16x32_bf16 v[94:97], v[122:125], v[178:181], v[94:97]
	v_mfma_f32_16x16x32_bf16 v[90:93], v[146:149], v[178:181], v[90:93]
	v_mfma_f32_16x16x32_bf16 v[70:73], v[122:125], v[186:189], v[70:73]
	v_mfma_f32_16x16x32_bf16 v[66:69], v[146:149], v[186:189], v[66:69]
	v_mfma_f32_16x16x32_bf16 v[142:145], v[126:129], v[166:169], v[142:145]
	v_mfma_f32_16x16x32_bf16 v[138:141], v[150:153], v[166:169], v[138:141]
	v_mfma_f32_16x16x32_bf16 v[118:121], v[126:129], v[174:177], v[118:121]
	v_mfma_f32_16x16x32_bf16 v[114:117], v[150:153], v[174:177], v[114:117]
	v_mfma_f32_16x16x32_bf16 v[94:97], v[126:129], v[182:185], v[94:97]
	v_mfma_f32_16x16x32_bf16 v[90:93], v[150:153], v[182:185], v[90:93]
	v_mfma_f32_16x16x32_bf16 v[70:73], v[126:129], v[190:193], v[70:73]
	v_mfma_f32_16x16x32_bf16 v[66:69], v[150:153], v[190:193], v[66:69]
	s_barrier
; #define PG8_STAGE(bufoff, gbase, voff) do { _Pragma("unroll") for (int _i = 0; _i < 2; ++_i) \
;         __builtin_amdgcn_global_load_lds((const unsigned*)((const char*)(gbase) + (voff)[_i]), (LAS unsigned*)(lds + (bufoff) + ldsw + _i * 8192), 16, 0, 0); } while (0)
; #define PG8_STAGE_A(bufoff, kptr, half, VO) do { if constexpr (GATHER) { _Pragma("unroll") for (int _i = 0; _i < 2; ++_i) \
;         __builtin_amdgcn_global_load_lds((const unsigned*)((const char*)(kptr) + (VO)[half][_i]), (LAS unsigned*)(lds + (bufoff) + ldsw + _i * 8192), 16, 0, 0); } \
;         else { PG8_STAGE(bufoff, (kptr) + (half) * hstepA, voffA); } } while (0)
; #define PG8_LDA(dst, b, h) do { _Pragma("unroll") for (int m = 0; m < 4; ++m) _Pragma("unroll") for (int k = 0; k < 2; ++k) dst[m][k] = *(const LAS bf16x8*)(lds + PG8_SA(b, h) + aoff + m * 2048 + k * 1024); } while (0)
; #define PG8_MMA(ai, bj, At, Bt) do { __builtin_amdgcn_s_setprio(1); _Pragma("unroll") for (int m = 0; m < 4; ++m) _Pragma("unroll") for (int n = 0; n < 2; ++n) _Pragma("unroll") for (int k = 0; k < 2; ++k) \
;         acc[ai][bj][m][n] = __builtin_amdgcn_mfma_f32_16x16x32_bf16(Bt[n][k], At[m][k], acc[ai][bj][m][n], 0, 0, 0); __builtin_amdgcn_s_setprio(0); } while (0)
; #define PG8_WAIT_V(n) asm volatile("s_waitcnt vmcnt(" #n ")" ::: "memory")
; #define PG8_WAIT_L(n) asm volatile("s_waitcnt lgkmcnt(" #n ")" ::: "memory")
; #define PG8_BAR __builtin_amdgcn_s_barrier()
; #define PG8_SCHED __builtin_amdgcn_sched_barrier(0)
;     ...
;             PG8_LDA(At, 1, 1); PG8_STAGE(PG8_SB(1, 0), b3, voffB); PG8_STAGE(PG8_SB(1, 1), b3 + hstepB, voffB); PG8_STAGE_A(PG8_SA(1, 0), a3, 0, g2);
;             PG8_WAIT_V(8); PG8_WAIT_L(0); PG8_BAR; PG8_MMA(1, 0, At, B0); PG8_MMA(1, 1, At, B1); PG8_BAR; PG8_SCHED;
;     ...
;         if constexpr (ALIGN_EPI) { if (wr == 0) PG8_BAR; }
	s_add_i32 s15, s15, s60
	v_lshl_add_u64 v[208:209], v[208:209], 0, s[8:9]
	s_mov_b32 m0, s15
	ds_read_b128 v[162:165], v221 offset:49152
	ds_read_b128 v[166:169], v221 offset:50176
	ds_read_b128 v[170:173], v221 offset:51200
	ds_read_b128 v[174:177], v221 offset:52224
	ds_read_b128 v[178:181], v221 offset:53248
	ds_read_b128 v[182:185], v221 offset:54272
	ds_read_b128 v[186:189], v221 offset:55296
	ds_read_b128 v[190:193], v221 offset:56320
	global_load_lds_dwordx4 v[208:209], off
	s_add_i32 m0, s15, 0x2000
	s_add_u32 s16, s24, 0x18080
	v_lshl_add_u64 v[208:209], v[210:211], 0, s[8:9]
	s_addc_u32 s17, s25, 0
	s_add_i32 s15, s18, s60
	global_load_lds_dwordx4 v[208:209], off
	v_lshl_add_u64 v[208:209], s[16:17], 0, v[194:195]
	s_mov_b32 m0, s15
	s_nop 0
	global_load_lds_dwordx4 v[208:209], off
	v_lshl_add_u64 v[208:209], s[16:17], 0, v[196:197]
	s_add_i32 m0, s15, 0x2000
	s_nop 0
	global_load_lds_dwordx4 v[208:209], off
	v_lshl_add_u64 v[208:209], v[212:213], 0, s[8:9]
	s_mov_b32 m0, s67
	s_nop 0
	global_load_lds_dwordx4 v[208:209], off
	v_lshl_add_u64 v[208:209], v[222:223], 0, s[8:9]
	s_mov_b32 m0, s68
	s_nop 0
	global_load_lds_dwordx4 v[208:209], off
	s_waitcnt vmcnt(8)
	s_waitcnt lgkmcnt(0)
	s_barrier
	s_waitcnt lgkmcnt(0)
	v_mfma_f32_16x16x32_bf16 v[62:65], v[82:85], v[162:165], v[62:65]
	v_mfma_f32_16x16x32_bf16 v[58:61], v[102:105], v[162:165], v[58:61]
	v_mfma_f32_16x16x32_bf16 v[46:49], v[82:85], v[170:173], v[46:49]
	v_mfma_f32_16x16x32_bf16 v[42:45], v[102:105], v[170:173], v[42:45]
	v_mfma_f32_16x16x32_bf16 v[30:33], v[82:85], v[178:181], v[30:33]
	v_mfma_f32_16x16x32_bf16 v[26:29], v[102:105], v[178:181], v[26:29]
	v_mfma_f32_16x16x32_bf16 v[14:17], v[82:85], v[186:189], v[14:17]
	v_mfma_f32_16x16x32_bf16 v[10:13], v[102:105], v[186:189], v[10:13]
	v_mfma_f32_16x16x32_bf16 v[62:65], v[86:89], v[166:169], v[62:65]
	v_mfma_f32_16x16x32_bf16 v[58:61], v[106:109], v[166:169], v[58:61]
	v_mfma_f32_16x16x32_bf16 v[46:49], v[86:89], v[174:177], v[46:49]
	v_mfma_f32_16x16x32_bf16 v[42:45], v[106:109], v[174:177], v[42:45]
	v_mfma_f32_16x16x32_bf16 v[30:33], v[86:89], v[182:185], v[30:33]
	v_mfma_f32_16x16x32_bf16 v[26:29], v[106:109], v[182:185], v[26:29]
	v_mfma_f32_16x16x32_bf16 v[14:17], v[86:89], v[190:193], v[14:17]
	v_mfma_f32_16x16x32_bf16 v[10:13], v[106:109], v[190:193], v[10:13]
	v_mfma_f32_16x16x32_bf16 v[54:57], v[122:125], v[162:165], v[54:57]
	v_mfma_f32_16x16x32_bf16 v[50:53], v[146:149], v[162:165], v[50:53]
	v_mfma_f32_16x16x32_bf16 v[38:41], v[122:125], v[170:173], v[38:41]
	v_mfma_f32_16x16x32_bf16 v[34:37], v[146:149], v[170:173], v[34:37]
	v_mfma_f32_16x16x32_bf16 v[22:25], v[122:125], v[178:181], v[22:25]
	v_mfma_f32_16x16x32_bf16 v[18:21], v[146:149], v[178:181], v[18:21]
	v_mfma_f32_16x16x32_bf16 v[6:9], v[122:125], v[186:189], v[6:9]
	v_mfma_f32_16x16x32_bf16 v[2:5], v[146:149], v[186:189], v[2:5]
	v_mfma_f32_16x16x32_bf16 v[54:57], v[126:129], v[166:169], v[54:57]
	v_mfma_f32_16x16x32_bf16 v[50:53], v[150:153], v[166:169], v[50:53]
	v_mfma_f32_16x16x32_bf16 v[38:41], v[126:129], v[174:177], v[38:41]
	v_mfma_f32_16x16x32_bf16 v[34:37], v[150:153], v[174:177], v[34:37]
	v_mfma_f32_16x16x32_bf16 v[22:25], v[126:129], v[182:185], v[22:25]
	v_mfma_f32_16x16x32_bf16 v[18:21], v[150:153], v[182:185], v[18:21]
	v_mfma_f32_16x16x32_bf16 v[6:9], v[126:129], v[190:193], v[6:9]
	v_mfma_f32_16x16x32_bf16 v[2:5], v[150:153], v[190:193], v[2:5]
	s_barrier
	s_add_i32 s14, s14, 2
	s_add_u32 s12, s12, 0x100
	s_addc_u32 s13, s13, 0
	s_cmp_gt_u32 s14, 3
	s_mov_b64 s[38:39], s[0:1]
	s_cbranch_scc0 .LBB0_615
	s_and_b64 vcc, exec, s[42:43]
	s_cbranch_vccz .LBB0_618
	s_barrier

;     __device__ __forceinline__ void init(const void* A_, const void* B_, int G_, int c_) { T.init(A_, B_, DM, DM, NLAT / 256, INP / 256, 1, 0, 0, G_, c_, 0); }
; #define PG8_STAGE(bufoff, gbase, voff) do { _Pragma("unroll") for (int _i = 0; _i < 2; ++_i) \
;         __builtin_amdgcn_global_load_lds((const unsigned*)((const char*)(gbase) + (voff)[_i]), (LAS unsigned*)(lds + (bufoff) + ldsw + _i * 8192), 16, 0, 0); } while (0)
; #define PG8_STAGE_A(bufoff, kptr, half, VO) do { if constexpr (GATHER) { _Pragma("unroll") for (int _i = 0; _i < 2; ++_i) \
;         __builtin_amdgcn_global_load_lds((const unsigned*)((const char*)(kptr) + (VO)[half][_i]), (LAS unsigned*)(lds + (bufoff) + ldsw + _i * 8192), 16, 0, 0); } \
;         else { PG8_STAGE(bufoff, (kptr) + (half) * hstepA, voffA); } } while (0)
; #define PG8_WAIT_V(n) asm volatile("s_waitcnt vmcnt(" #n ")" ::: "memory")
; #define PG8_BAR __builtin_amdgcn_s_barrier()
;     ...
;     for (int i = 0; i < 2; ++i) { int R, C; stage_rc(tid * 16 + i * 8192, R, C); const int Rb = Epi::PERM ? ((R & ~31) + perm32(R & 31)) : R;
;         voffA[i] = (unsigned)(R * g.lda + C) * 2u; voffB[i] = (unsigned)(Rb * g.ldb + C) * 2u; gR[i] = R; gCc[i] = C; }
;     ...
;     if constexpr (SP2) {
;         PG8_STAGE(PG8_SB(0, 0), cB, voffB); PG8_STAGE(PG8_SB(0, 1), cB + hstepB, voffB); PG8_STAGE_A(PG8_SA(0, 0), cA, 0, gC); PG8_STAGE_A(PG8_SA(0, 1), cA, 1, gC);
;         if (wr == 1) PG8_BAR;
;         PG8_WAIT_V(2); PG8_BAR;
;         PG8_STAGE(PG8_SB(1, 0), cB + kstep, voffB); PG8_STAGE_A(PG8_SA(1, 0), cA + kstep, 0, gC); PG8_STAGE(PG8_SB(1, 1), cB + hstepB + kstep, voffB);
;         PG8_WAIT_V(6); PG8_BAR;
; __global__ void __launch_bounds__(512, 2) fwd(Params p) {
;     ...
;             if (C_SEL & 2) { pg8::TileSched S; S.init(ws + WS_KVA, (bf16_t*)(ws + WS_WTUKV) + (size_t)l * 1024 * 256, 256, 256, MT / 256, 2, 1, 0, 0, G, c, 112);
.LBB0_659:
	v_readlane_b32 s0, v252, 5
	v_readlane_b32 s1, v252, 6
	s_lshl_b64 s[0:1], s[0:1], 19
	v_readlane_b32 s2, v253, 25
	s_add_u32 s12, s2, s0
	v_readlane_b32 s0, v253, 26
	s_addc_u32 s13, s0, s1
	v_readlane_b32 s0, v254, 49
	v_mov_b32_e32 v2, v0
	v_readlane_b32 s1, v254, 50
	s_andn2_b64 vcc, exec, s[0:1]
	v_readfirstlane_b32 s0, v2
	s_cbranch_vccnz .LBB0_675
	v_lshlrev_b32_e32 v3, 4, v2
	v_add_u32_e32 v4, 0x2000, v3
	v_ashrrev_i32_e32 v5, 31, v4
	v_lshrrev_b32_e32 v5, 22, v5
	v_add_u32_e32 v5, v4, v5
	v_ashrrev_i32_e32 v5, 10, v5
	v_mul_i32_i24_e32 v6, 0x400, v5
	v_sub_u32_e32 v4, v4, v6
	v_lshrrev_b32_e32 v6, 4, v4
	v_bitop3_b32 v4, v6, v4, 32 bitop3:0x6c
	v_ashrrev_i32_e32 v6, 31, v4
	v_lshrrev_b32_e32 v6, 26, v6
	v_add_u32_e32 v6, v4, v6
	v_lshlrev_b32_e32 v8, 3, v5
	v_ashrrev_i32_e32 v7, 6, v6
	v_and_b32_e32 v8, -16, v8
	v_and_b32_e32 v6, 0xc0, v6
	v_add_u32_e32 v8, v7, v8
	v_sub_u32_e32 v4, v4, v6
	v_and_b32_e32 v7, 3, v7
	s_mov_b32 s2, 0x7fffe0
	v_lshrrev_b32_e32 v9, 2, v8
	v_lshlrev_b32_e32 v10, 1, v8
	v_lshlrev_b32_e32 v5, 5, v5
	v_ashrrev_i16_sdwa v4, v245, sext(v4) dst_sel:DWORD dst_unused:UNUSED_PAD src0_sel:DWORD src1_sel:BYTE_0
	v_and_or_b32 v7, v8, s2, v7
	v_and_b32_e32 v9, 4, v9
	v_and_b32_e32 v10, 24, v10
	v_and_b32_e32 v5, 32, v5
	v_bfe_i32 v4, v4, 0, 16
	v_or3_b32 v7, v7, v9, v10
	v_add_lshl_u32 v4, v5, v4, 1
	v_lshl_add_u32 v130, v7, 9, v4
	v_lshl_add_u32 v132, v8, 9, v4
	v_bfe_i32 v4, v2, 27, 1
	v_lshrrev_b32_e32 v4, 22, v4
	v_add_u32_e32 v4, v3, v4
	v_and_b32_e32 v4, 0xfffffc00, v4
	v_sub_u32_e32 v3, v3, v4
	v_ashrrev_i32_e32 v5, 31, v2
	v_lshrrev_b32_e32 v4, 4, v3
	v_lshrrev_b32_e32 v5, 26, v5
	v_bitop3_b32 v4, v4, v3, 32 bitop3:0x6c
	v_ashrrev_i32_e32 v3, 31, v3
	v_add_u32_e32 v5, v2, v5
	v_lshrrev_b32_e32 v3, 26, v3
	v_ashrrev_i32_e32 v5, 6, v5
	v_add_u32_e32 v3, v4, v3
	v_lshlrev_b32_e32 v6, 3, v5
	v_ashrrev_i32_e32 v3, 6, v3
	v_and_b32_e32 v6, -16, v6
	v_add_u32_e32 v6, v3, v6
	v_and_b32_e32 v7, 3, v3
	v_mul_i32_i24_e32 v3, 64, v3
	s_ashr_i32 s4, s0, 6
	v_sub_u32_e32 v3, v4, v3
	s_ashr_i32 s1, s0, 8
	s_lshl_b32 s26, s4, 10
	v_and_or_b32 v7, v6, s2, v7
	v_lshrrev_b32_e32 v8, 2, v6
	v_lshlrev_b32_e32 v9, 1, v6
	v_lshlrev_b32_e32 v5, 5, v5
	v_ashrrev_i16_sdwa v3, v245, sext(v3) dst_sel:DWORD dst_unused:UNUSED_PAD src0_sel:DWORD src1_sel:BYTE_0
	v_readlane_b32 s2, v254, 54
	v_and_b32_e32 v8, 4, v8
	v_and_b32_e32 v9, 24, v9
	v_and_b32_e32 v5, 32, v5
	v_bfe_i32 v3, v3, 0, 16
	v_readlane_b32 s3, v254, 55
	s_add_u32 s46, s12, s2
	v_or3_b32 v7, v7, v8, v9
	v_add_lshl_u32 v3, v5, v3, 1
	s_addc_u32 s47, s13, s3
	s_add_i32 s27, s26, 0
	v_lshl_add_u32 v206, v7, 9, v3
	s_add_i32 m0, s27, 0x10000
	v_lshl_add_u32 v134, v6, 9, v3
	global_load_lds_dwordx4 v206, s[46:47]
	s_add_i32 m0, s27, 0x12000
	s_add_u32 s2, s46, 0x10000
	global_load_lds_dwordx4 v130, s[46:47]
	s_addc_u32 s3, s47, 0
	s_add_i32 m0, s27, 0x14000
	s_add_i32 s60, s27, 0x2000
	global_load_lds_dwordx4 v206, s[2:3]
	s_add_i32 m0, s27, 0x16000
	s_add_i32 s61, s27, 0x4000
	global_load_lds_dwordx4 v130, s[2:3]
	v_readlane_b32 s2, v254, 56
	s_mov_b32 m0, s27
	v_readlane_b32 s3, v254, 57
	s_add_i32 s63, s27, 0x6000
	s_cmp_eq_u32 s1, 1
	s_nop 2
	global_load_lds_dwordx4 v134, s[2:3]
	s_mov_b32 m0, s60
	s_nop 0
	global_load_lds_dwordx4 v132, s[2:3]
	v_readlane_b32 s2, v254, 58
	s_mov_b32 m0, s61
	v_readlane_b32 s3, v254, 59
	s_nop 4
	global_load_lds_dwordx4 v134, s[2:3]
	s_mov_b32 m0, s63
	s_nop 0
	global_load_lds_dwordx4 v132, s[2:3]
	s_cselect_b64 s[2:3], -1, 0
	s_cmp_lg_u32 s1, 1
	s_cbranch_scc1 .LBB0_662
	s_barrier
	s_setprio 1

; #define PG8_GOFF(u, o) do { _Pragma("unroll") for (int _h = 0; _h < 2; ++_h) _Pragma("unroll") for (int _i = 0; _i < 2; ++_i) { const int _r = (u).pm * 256 + _h * 128 + gR[_i]; \
;         const int _tok = _r < nvalid ? rowtok[(u).pb * EROWS + _r] : 0; (o)[_h][_i] = (unsigned)(_tok * g.lda + gCc[_i]) * 2u; } } while (0)
; #define PG8_STAGE(bufoff, gbase, voff) do { _Pragma("unroll") for (int _i = 0; _i < 2; ++_i) \
;         __builtin_amdgcn_global_load_lds((const unsigned*)((const char*)(gbase) + (voff)[_i]), (LAS unsigned*)(lds + (bufoff) + ldsw + _i * 8192), 16, 0, 0); } while (0)
; #define PG8_LDA(dst, b, h) do { _Pragma("unroll") for (int m = 0; m < 4; ++m) _Pragma("unroll") for (int k = 0; k < 2; ++k) dst[m][k] = *(const LAS bf16x8*)(lds + PG8_SA(b, h) + aoff + m * 2048 + k * 1024); } while (0)
;     ...
;         const bool has_next = S.next(ui + 1, nxt);
;         const char* nA = has_next ? nxt.a : cA; const char* nB = has_next ? nxt.b : cB;
;         if constexpr (GATHER) { if (has_next) { PG8_GOFF(nxt, gN); } else {
; #pragma unroll
;             for (int _h = 0; _h < 2; ++_h)
; #pragma unroll
;                 for (int _i = 0; _i < 2; ++_i) gN[_h][_i] = gC[_h][_i]; } }
; #pragma nounroll
;         for (int t = 0; t < nt; t += 2) {
;             const bool last = (t == nt - 2);
;             const char* a1 = cA + (size_t)(t + 1) * kstep;
;             const char* a2 = last ? nA : cA + (size_t)(t + 2) * kstep; const char* b2 = last ? nB : cB + (size_t)(t + 2) * kstep;
;             const char* a3 = a2 + kstep; const char* b3 = b2 + kstep;
;             unsigned g2[2][2];
;             if constexpr (GATHER) {
; #pragma unroll
;                 for (int _h = 0; _h < 2; ++_h)
; #pragma unroll
;                     for (int _i = 0; _i < 2; ++_i) g2[_h][_i] = last ? gN[_h][_i] : gC[_h][_i]; }
;             if constexpr (SP2) {
;             PG8_LDB(B0, 0, 0); PG8_LDB(B1, 0, 1); PG8_SCHED; PG8_LDA(At, 0, 0); PG8_STAGE_A(PG8_SA(1, 1), a1, 1, gC);
;             PG8_WAIT_V(8); PG8_WAIT_L(0); PG8_BAR; PG8_MMA(0, 0, At, B0); PG8_MMA(0, 1, At, B1); PG8_BAR; PG8_SCHED;
;             PG8_LDA(At, 0, 1); PG8_STAGE(PG8_SB(0, 0), b2, voffB); PG8_STAGE(PG8_SB(0, 1), b2 + hstepB, voffB); PG8_STAGE_A(PG8_SA(0, 0), a2, 0, g2);
;             PG8_WAIT_V(8); PG8_WAIT_L(0); PG8_BAR; PG8_MMA(1, 0, At, B0); PG8_MMA(1, 1, At, B1); PG8_BAR; PG8_SCHED;
.LBB0_668:
	s_add_u32 s16, s48, s30
	s_addc_u32 s17, s49, s31
	s_add_u32 s18, s16, 0x100
	s_addc_u32 s19, s17, 0
	s_and_b64 s[14:15], s[0:1], exec
	s_cselect_b32 s51, s43, s19
	s_cselect_b32 s50, s42, s18
	s_add_u32 s14, s46, s30
	s_addc_u32 s15, s47, s31
	s_add_u32 s14, s14, 0x100
	s_addc_u32 s15, s15, 0
	s_add_i32 s22, 0, 0x10000
	s_and_b64 s[0:1], s[0:1], exec
	s_cselect_b32 s55, s45, s15
	s_cselect_b32 s54, s44, s14
	s_add_i32 s1, 0, 0x14000
	s_add_u32 s58, s16, 0x10080
	s_addc_u32 s59, s17, 0
	s_add_i32 s21, s22, s26
	s_add_i32 m0, s27, 0xc000
	s_add_i32 s34, s27, 0xe000
	s_add_i32 s18, s21, 0x2000
	s_add_u32 s56, s54, 0x10000
	v_add_u32_e32 v152, s22, v138
	v_add_u32_e32 v168, s1, v138
	s_addc_u32 s57, s55, 0
	s_add_i32 s20, s1, s26
	ds_read_b128 v[140:143], v152
	ds_read_b128 v[144:147], v152 offset:1024
	ds_read_b128 v[148:151], v152 offset:2048
	ds_read_b128 v[152:155], v152 offset:3072
	ds_read_b128 v[156:159], v168
	ds_read_b128 v[160:163], v168 offset:1024
	ds_read_b128 v[164:167], v168 offset:2048
	ds_read_b128 v[168:171], v168 offset:3072
	s_add_i32 s19, s20, 0x2000
	s_add_i32 s17, 0, 0x18000
	s_add_i32 s16, 0, 0x1c000
	s_add_u32 s30, s50, 0x10000
	s_addc_u32 s31, s51, 0
	s_add_i32 s15, s17, s26
	s_add_i32 s14, s15, 0x2000
	s_add_u32 s0, s54, 0x10080
	s_addc_u32 s1, s55, 0
	s_add_i32 s23, s16, s26
	s_add_i32 s22, s23, 0x2000
	v_lshl_add_u64 v[204:205], s[58:59], 0, v[134:135]
	ds_read_b128 v[172:175], v139
	ds_read_b128 v[176:179], v139 offset:1024
	ds_read_b128 v[180:183], v139 offset:2048
	ds_read_b128 v[184:187], v139 offset:3072
	ds_read_b128 v[188:191], v139 offset:4096
	ds_read_b128 v[192:195], v139 offset:5120
	ds_read_b128 v[196:199], v139 offset:6144
	ds_read_b128 v[200:203], v139 offset:7168
	global_load_lds_dwordx4 v[204:205], off
	v_lshl_add_u64 v[204:205], s[58:59], 0, v[132:133]
	s_mov_b32 m0, s34
	s_nop 0
	global_load_lds_dwordx4 v[204:205], off
	s_waitcnt vmcnt(8)
	s_waitcnt lgkmcnt(0)
	s_barrier
	s_waitcnt lgkmcnt(0)
	v_mfma_f32_16x16x32_bf16 v[126:129], v[140:143], v[172:175], v[126:129]
	v_mfma_f32_16x16x32_bf16 v[122:125], v[148:151], v[172:175], v[122:125]
	v_mfma_f32_16x16x32_bf16 v[118:121], v[140:143], v[180:183], v[118:121]
	v_mfma_f32_16x16x32_bf16 v[114:117], v[148:151], v[180:183], v[114:117]
	v_mfma_f32_16x16x32_bf16 v[102:105], v[140:143], v[188:191], v[102:105]
	v_mfma_f32_16x16x32_bf16 v[98:101], v[148:151], v[188:191], v[98:101]
	v_mfma_f32_16x16x32_bf16 v[86:89], v[140:143], v[196:199], v[86:89]
	v_mfma_f32_16x16x32_bf16 v[82:85], v[148:151], v[196:199], v[82:85]
	v_mfma_f32_16x16x32_bf16 v[126:129], v[144:147], v[176:179], v[126:129]
	v_mfma_f32_16x16x32_bf16 v[122:125], v[152:155], v[176:179], v[122:125]
	v_mfma_f32_16x16x32_bf16 v[118:121], v[144:147], v[184:187], v[118:121]
	v_mfma_f32_16x16x32_bf16 v[114:117], v[152:155], v[184:187], v[114:117]
	v_mfma_f32_16x16x32_bf16 v[102:105], v[144:147], v[192:195], v[102:105]
	v_mfma_f32_16x16x32_bf16 v[98:101], v[152:155], v[192:195], v[98:101]
	v_mfma_f32_16x16x32_bf16 v[86:89], v[144:147], v[200:203], v[86:89]
	v_mfma_f32_16x16x32_bf16 v[82:85], v[152:155], v[200:203], v[82:85]
	v_mfma_f32_16x16x32_bf16 v[110:113], v[156:159], v[172:175], v[110:113]
	v_mfma_f32_16x16x32_bf16 v[106:109], v[164:167], v[172:175], v[106:109]
	v_mfma_f32_16x16x32_bf16 v[94:97], v[156:159], v[180:183], v[94:97]
	v_mfma_f32_16x16x32_bf16 v[90:93], v[164:167], v[180:183], v[90:93]
	v_mfma_f32_16x16x32_bf16 v[78:81], v[156:159], v[188:191], v[78:81]
	v_mfma_f32_16x16x32_bf16 v[74:77], v[164:167], v[188:191], v[74:77]
	v_mfma_f32_16x16x32_bf16 v[70:73], v[156:159], v[196:199], v[70:73]
	v_mfma_f32_16x16x32_bf16 v[66:69], v[164:167], v[196:199], v[66:69]
	v_mfma_f32_16x16x32_bf16 v[110:113], v[160:163], v[176:179], v[110:113]
	v_mfma_f32_16x16x32_bf16 v[106:109], v[168:171], v[176:179], v[106:109]
	v_mfma_f32_16x16x32_bf16 v[94:97], v[160:163], v[184:187], v[94:97]
	v_mfma_f32_16x16x32_bf16 v[90:93], v[168:171], v[184:187], v[90:93]
	v_mfma_f32_16x16x32_bf16 v[78:81], v[160:163], v[192:195], v[78:81]
	v_mfma_f32_16x16x32_bf16 v[74:77], v[168:171], v[192:195], v[74:77]
	v_mfma_f32_16x16x32_bf16 v[70:73], v[160:163], v[200:203], v[70:73]
	v_mfma_f32_16x16x32_bf16 v[66:69], v[168:171], v[200:203], v[66:69]
	s_barrier
	s_mov_b32 m0, s21
	v_lshl_add_u64 v[204:205], s[54:55], 0, v[206:207]
	ds_read_b128 v[172:175], v139 offset:16384
	ds_read_b128 v[176:179], v139 offset:17408
	ds_read_b128 v[180:183], v139 offset:18432
	ds_read_b128 v[184:187], v139 offset:19456
	ds_read_b128 v[188:191], v139 offset:20480
	ds_read_b128 v[192:195], v139 offset:21504
	ds_read_b128 v[196:199], v139 offset:22528
	ds_read_b128 v[200:203], v139 offset:23552
	global_load_lds_dwordx4 v[204:205], off
	v_lshl_add_u64 v[208:209], s[54:55], 0, v[130:131]
	s_mov_b32 m0, s18
	v_lshl_add_u64 v[210:211], s[56:57], 0, v[206:207]
	global_load_lds_dwordx4 v[208:209], off
	s_mov_b32 m0, s20
	v_lshl_add_u64 v[212:213], s[50:51], 0, v[132:133]
	global_load_lds_dwordx4 v[210:211], off
	v_lshl_add_u64 v[210:211], s[56:57], 0, v[130:131]
	s_mov_b32 m0, s19
	s_nop 0
	global_load_lds_dwordx4 v[210:211], off
	v_lshl_add_u64 v[210:211], s[50:51], 0, v[134:135]
	s_mov_b32 m0, s27
	s_nop 0
	global_load_lds_dwordx4 v[210:211], off
	s_mov_b32 m0, s60
	s_nop 0
	global_load_lds_dwordx4 v[212:213], off
	s_waitcnt vmcnt(8)
	s_waitcnt lgkmcnt(0)
	s_barrier
; #define PG8_STAGE(bufoff, gbase, voff) do { _Pragma("unroll") for (int _i = 0; _i < 2; ++_i) \
;         __builtin_amdgcn_global_load_lds((const unsigned*)((const char*)(gbase) + (voff)[_i]), (LAS unsigned*)(lds + (bufoff) + ldsw + _i * 8192), 16, 0, 0); } while (0)
; #define PG8_STAGE_A(bufoff, kptr, half, VO) do { if constexpr (GATHER) { _Pragma("unroll") for (int _i = 0; _i < 2; ++_i) \
;         __builtin_amdgcn_global_load_lds((const unsigned*)((const char*)(kptr) + (VO)[half][_i]), (LAS unsigned*)(lds + (bufoff) + ldsw + _i * 8192), 16, 0, 0); } \
;         else { PG8_STAGE(bufoff, (kptr) + (half) * hstepA, voffA); } } while (0)
; #define PG8_LDA(dst, b, h) do { _Pragma("unroll") for (int m = 0; m < 4; ++m) _Pragma("unroll") for (int k = 0; k < 2; ++k) dst[m][k] = *(const LAS bf16x8*)(lds + PG8_SA(b, h) + aoff + m * 2048 + k * 1024); } while (0)
; #define PG8_LDB(dst, b, h) do { _Pragma("unroll") for (int n = 0; n < 2; ++n) _Pragma("unroll") for (int k = 0; k < 2; ++k) dst[n][k] = *(const LAS bf16x8*)(lds + PG8_SB(b, h) + boff + n * 2048 + k * 1024); } while (0)
; #define PG8_MMA(ai, bj, At, Bt) do { __builtin_amdgcn_s_setprio(1); _Pragma("unroll") for (int m = 0; m < 4; ++m) _Pragma("unroll") for (int n = 0; n < 2; ++n) _Pragma("unroll") for (int k = 0; k < 2; ++k) \
;         acc[ai][bj][m][n] = __builtin_amdgcn_mfma_f32_16x16x32_bf16(Bt[n][k], At[m][k], acc[ai][bj][m][n], 0, 0, 0); __builtin_amdgcn_s_setprio(0); } while (0)
; #define PG8_WAIT_V(n) asm volatile("s_waitcnt vmcnt(" #n ")" ::: "memory")
; #define PG8_WAIT_L(n) asm volatile("s_waitcnt lgkmcnt(" #n ")" ::: "memory")
; #define PG8_BAR __builtin_amdgcn_s_barrier()
; #define PG8_SCHED __builtin_amdgcn_sched_barrier(0)
;     ...
;             PG8_WAIT_V(8); PG8_WAIT_L(0); PG8_BAR; PG8_MMA(1, 0, At, B0); PG8_MMA(1, 1, At, B1); PG8_BAR; PG8_SCHED;
;             PG8_LDB(B0, 1, 0); PG8_LDB(B1, 1, 1); PG8_SCHED; PG8_LDA(At, 1, 0); PG8_STAGE_A(PG8_SA(0, 1), a2, 1, g2);
;             PG8_WAIT_V(8); PG8_WAIT_L(0); PG8_BAR; PG8_MMA(0, 0, At, B0); PG8_MMA(0, 1, At, B1); PG8_BAR; PG8_SCHED;
;             PG8_LDA(At, 1, 1); PG8_STAGE(PG8_SB(1, 0), b3, voffB); PG8_STAGE(PG8_SB(1, 1), b3 + hstepB, voffB); PG8_STAGE_A(PG8_SA(1, 0), a3, 0, g2);
	s_waitcnt lgkmcnt(0)
	v_mfma_f32_16x16x32_bf16 v[62:65], v[140:143], v[172:175], v[62:65]
	v_mfma_f32_16x16x32_bf16 v[58:61], v[148:151], v[172:175], v[58:61]
	v_mfma_f32_16x16x32_bf16 v[54:57], v[140:143], v[180:183], v[54:57]
	v_mfma_f32_16x16x32_bf16 v[50:53], v[148:151], v[180:183], v[50:53]
	v_mfma_f32_16x16x32_bf16 v[38:41], v[140:143], v[188:191], v[38:41]
	v_mfma_f32_16x16x32_bf16 v[34:37], v[148:151], v[188:191], v[34:37]
	v_mfma_f32_16x16x32_bf16 v[22:25], v[140:143], v[196:199], v[22:25]
	v_mfma_f32_16x16x32_bf16 v[18:21], v[148:151], v[196:199], v[18:21]
	v_mfma_f32_16x16x32_bf16 v[62:65], v[144:147], v[176:179], v[62:65]
	v_mfma_f32_16x16x32_bf16 v[58:61], v[152:155], v[176:179], v[58:61]
	v_mfma_f32_16x16x32_bf16 v[54:57], v[144:147], v[184:187], v[54:57]
	v_mfma_f32_16x16x32_bf16 v[50:53], v[152:155], v[184:187], v[50:53]
	v_mfma_f32_16x16x32_bf16 v[38:41], v[144:147], v[192:195], v[38:41]
	v_mfma_f32_16x16x32_bf16 v[34:37], v[152:155], v[192:195], v[34:37]
	v_mfma_f32_16x16x32_bf16 v[22:25], v[144:147], v[200:203], v[22:25]
	v_mfma_f32_16x16x32_bf16 v[18:21], v[152:155], v[200:203], v[18:21]
	v_mfma_f32_16x16x32_bf16 v[46:49], v[156:159], v[172:175], v[46:49]
	v_mfma_f32_16x16x32_bf16 v[42:45], v[164:167], v[172:175], v[42:45]
	v_mfma_f32_16x16x32_bf16 v[30:33], v[156:159], v[180:183], v[30:33]
	v_mfma_f32_16x16x32_bf16 v[26:29], v[164:167], v[180:183], v[26:29]
	v_mfma_f32_16x16x32_bf16 v[14:17], v[156:159], v[188:191], v[14:17]
	v_mfma_f32_16x16x32_bf16 v[10:13], v[164:167], v[188:191], v[10:13]
	v_mfma_f32_16x16x32_bf16 v[6:9], v[156:159], v[196:199], v[6:9]
	v_mfma_f32_16x16x32_bf16 v[2:5], v[164:167], v[196:199], v[2:5]
	v_mfma_f32_16x16x32_bf16 v[46:49], v[160:163], v[176:179], v[46:49]
	v_mfma_f32_16x16x32_bf16 v[42:45], v[168:171], v[176:179], v[42:45]
	v_mfma_f32_16x16x32_bf16 v[30:33], v[160:163], v[184:187], v[30:33]
	v_mfma_f32_16x16x32_bf16 v[26:29], v[168:171], v[184:187], v[26:29]
	v_mfma_f32_16x16x32_bf16 v[14:17], v[160:163], v[192:195], v[14:17]
	v_mfma_f32_16x16x32_bf16 v[10:13], v[168:171], v[192:195], v[10:13]
	v_mfma_f32_16x16x32_bf16 v[6:9], v[160:163], v[200:203], v[6:9]
	v_mfma_f32_16x16x32_bf16 v[2:5], v[168:171], v[200:203], v[2:5]
	s_barrier
	v_add_u32_e32 v152, s17, v138
	v_add_u32_e32 v168, s16, v138
	ds_read_b128 v[140:143], v152
	ds_read_b128 v[144:147], v152 offset:1024
	ds_read_b128 v[148:151], v152 offset:2048
	ds_read_b128 v[152:155], v152 offset:3072
	ds_read_b128 v[156:159], v168
	ds_read_b128 v[160:163], v168 offset:1024
	ds_read_b128 v[164:167], v168 offset:2048
	ds_read_b128 v[168:171], v168 offset:3072
	s_mov_b32 m0, s61
	v_lshl_add_u64 v[216:217], s[30:31], 0, v[134:135]
	ds_read_b128 v[172:175], v139 offset:32768
	ds_read_b128 v[176:179], v139 offset:33792
	ds_read_b128 v[180:183], v139 offset:34816
	ds_read_b128 v[184:187], v139 offset:35840
	ds_read_b128 v[188:191], v139 offset:36864
	ds_read_b128 v[192:195], v139 offset:37888
	ds_read_b128 v[196:199], v139 offset:38912
	ds_read_b128 v[200:203], v139 offset:39936
	global_load_lds_dwordx4 v[216:217], off
	v_lshl_add_u64 v[216:217], s[30:31], 0, v[132:133]
	s_mov_b32 m0, s63
	s_nop 0
	global_load_lds_dwordx4 v[216:217], off
	s_waitcnt vmcnt(8)
	s_waitcnt lgkmcnt(0)
	s_barrier
	s_waitcnt lgkmcnt(0)
	v_mfma_f32_16x16x32_bf16 v[126:129], v[140:143], v[172:175], v[126:129]
	v_mfma_f32_16x16x32_bf16 v[122:125], v[148:151], v[172:175], v[122:125]
	v_mfma_f32_16x16x32_bf16 v[118:121], v[140:143], v[180:183], v[118:121]
	v_mfma_f32_16x16x32_bf16 v[114:117], v[148:151], v[180:183], v[114:117]
	v_mfma_f32_16x16x32_bf16 v[102:105], v[140:143], v[188:191], v[102:105]
	v_mfma_f32_16x16x32_bf16 v[98:101], v[148:151], v[188:191], v[98:101]
	v_mfma_f32_16x16x32_bf16 v[86:89], v[140:143], v[196:199], v[86:89]
	v_mfma_f32_16x16x32_bf16 v[82:85], v[148:151], v[196:199], v[82:85]
	v_mfma_f32_16x16x32_bf16 v[126:129], v[144:147], v[176:179], v[126:129]
	v_mfma_f32_16x16x32_bf16 v[122:125], v[152:155], v[176:179], v[122:125]
	v_mfma_f32_16x16x32_bf16 v[118:121], v[144:147], v[184:187], v[118:121]
	v_mfma_f32_16x16x32_bf16 v[114:117], v[152:155], v[184:187], v[114:117]
	v_mfma_f32_16x16x32_bf16 v[102:105], v[144:147], v[192:195], v[102:105]
	v_mfma_f32_16x16x32_bf16 v[98:101], v[152:155], v[192:195], v[98:101]
	v_mfma_f32_16x16x32_bf16 v[86:89], v[144:147], v[200:203], v[86:89]
	v_mfma_f32_16x16x32_bf16 v[82:85], v[152:155], v[200:203], v[82:85]
	v_mfma_f32_16x16x32_bf16 v[110:113], v[156:159], v[172:175], v[110:113]
	v_mfma_f32_16x16x32_bf16 v[106:109], v[164:167], v[172:175], v[106:109]
	v_mfma_f32_16x16x32_bf16 v[94:97], v[156:159], v[180:183], v[94:97]
	v_mfma_f32_16x16x32_bf16 v[90:93], v[164:167], v[180:183], v[90:93]
	v_mfma_f32_16x16x32_bf16 v[78:81], v[156:159], v[188:191], v[78:81]
	v_mfma_f32_16x16x32_bf16 v[74:77], v[164:167], v[188:191], v[74:77]
	v_mfma_f32_16x16x32_bf16 v[70:73], v[156:159], v[196:199], v[70:73]
	v_mfma_f32_16x16x32_bf16 v[66:69], v[164:167], v[196:199], v[66:69]
	v_mfma_f32_16x16x32_bf16 v[110:113], v[160:163], v[176:179], v[110:113]
	v_mfma_f32_16x16x32_bf16 v[106:109], v[168:171], v[176:179], v[106:109]
	v_mfma_f32_16x16x32_bf16 v[94:97], v[160:163], v[184:187], v[94:97]
	v_mfma_f32_16x16x32_bf16 v[90:93], v[168:171], v[184:187], v[90:93]
	v_mfma_f32_16x16x32_bf16 v[78:81], v[160:163], v[192:195], v[78:81]
	v_mfma_f32_16x16x32_bf16 v[74:77], v[168:171], v[192:195], v[74:77]
	v_mfma_f32_16x16x32_bf16 v[70:73], v[160:163], v[200:203], v[70:73]
	v_mfma_f32_16x16x32_bf16 v[66:69], v[168:171], v[200:203], v[66:69]
	s_barrier
; #define PG8_STAGE(bufoff, gbase, voff) do { _Pragma("unroll") for (int _i = 0; _i < 2; ++_i) \
;         __builtin_amdgcn_global_load_lds((const unsigned*)((const char*)(gbase) + (voff)[_i]), (LAS unsigned*)(lds + (bufoff) + ldsw + _i * 8192), 16, 0, 0); } while (0)
; #define PG8_STAGE_A(bufoff, kptr, half, VO) do { if constexpr (GATHER) { _Pragma("unroll") for (int _i = 0; _i < 2; ++_i) \
;         __builtin_amdgcn_global_load_lds((const unsigned*)((const char*)(kptr) + (VO)[half][_i]), (LAS unsigned*)(lds + (bufoff) + ldsw + _i * 8192), 16, 0, 0); } \
;         else { PG8_STAGE(bufoff, (kptr) + (half) * hstepA, voffA); } } while (0)
; #define PG8_LDA(dst, b, h) do { _Pragma("unroll") for (int m = 0; m < 4; ++m) _Pragma("unroll") for (int k = 0; k < 2; ++k) dst[m][k] = *(const LAS bf16x8*)(lds + PG8_SA(b, h) + aoff + m * 2048 + k * 1024); } while (0)
; #define PG8_MMA(ai, bj, At, Bt) do { __builtin_amdgcn_s_setprio(1); _Pragma("unroll") for (int m = 0; m < 4; ++m) _Pragma("unroll") for (int n = 0; n < 2; ++n) _Pragma("unroll") for (int k = 0; k < 2; ++k) \
;         acc[ai][bj][m][n] = __builtin_amdgcn_mfma_f32_16x16x32_bf16(Bt[n][k], At[m][k], acc[ai][bj][m][n], 0, 0, 0); __builtin_amdgcn_s_setprio(0); } while (0)
; #define PG8_WAIT_V(n) asm volatile("s_waitcnt vmcnt(" #n ")" ::: "memory")
; #define PG8_WAIT_L(n) asm volatile("s_waitcnt lgkmcnt(" #n ")" ::: "memory")
; #define PG8_BAR __builtin_amdgcn_s_barrier()
; #define PG8_SCHED __builtin_amdgcn_sched_barrier(0)
;     ...
;             PG8_LDA(At, 1, 1); PG8_STAGE(PG8_SB(1, 0), b3, voffB); PG8_STAGE(PG8_SB(1, 1), b3 + hstepB, voffB); PG8_STAGE_A(PG8_SA(1, 0), a3, 0, g2);
;             PG8_WAIT_V(8); PG8_WAIT_L(0); PG8_BAR; PG8_MMA(1, 0, At, B0); PG8_MMA(1, 1, At, B1); PG8_BAR; PG8_SCHED;
;     ...
;         if constexpr (ALIGN_EPI) { if (wr == 0) PG8_BAR; }
	s_mov_b32 m0, s15
	v_lshl_add_u64 v[204:205], v[204:205], 0, s[8:9]
	ds_read_b128 v[172:175], v139 offset:49152
	ds_read_b128 v[176:179], v139 offset:50176
	ds_read_b128 v[180:183], v139 offset:51200
	ds_read_b128 v[184:187], v139 offset:52224
	ds_read_b128 v[188:191], v139 offset:53248
	ds_read_b128 v[192:195], v139 offset:54272
	ds_read_b128 v[196:199], v139 offset:55296
	ds_read_b128 v[200:203], v139 offset:56320
	global_load_lds_dwordx4 v[204:205], off
	v_lshl_add_u64 v[204:205], v[208:209], 0, s[8:9]
	s_mov_b32 m0, s14
	s_nop 0
	global_load_lds_dwordx4 v[204:205], off
	v_lshl_add_u64 v[204:205], s[0:1], 0, v[206:207]
	s_mov_b32 m0, s23
	s_nop 0
	global_load_lds_dwordx4 v[204:205], off
	v_lshl_add_u64 v[204:205], s[0:1], 0, v[130:131]
	s_mov_b32 m0, s22
	s_nop 0
	global_load_lds_dwordx4 v[204:205], off
	v_lshl_add_u64 v[204:205], v[210:211], 0, s[8:9]
	s_mov_b32 m0, s64
	s_nop 0
	global_load_lds_dwordx4 v[204:205], off
	v_lshl_add_u64 v[204:205], v[212:213], 0, s[8:9]
	s_mov_b32 m0, s65
	s_nop 0
	global_load_lds_dwordx4 v[204:205], off
	s_waitcnt vmcnt(8)
	s_waitcnt lgkmcnt(0)
	s_barrier
	s_waitcnt lgkmcnt(0)
	v_mfma_f32_16x16x32_bf16 v[62:65], v[140:143], v[172:175], v[62:65]
	v_mfma_f32_16x16x32_bf16 v[58:61], v[148:151], v[172:175], v[58:61]
	v_mfma_f32_16x16x32_bf16 v[54:57], v[140:143], v[180:183], v[54:57]
	v_mfma_f32_16x16x32_bf16 v[50:53], v[148:151], v[180:183], v[50:53]
	v_mfma_f32_16x16x32_bf16 v[38:41], v[140:143], v[188:191], v[38:41]
	v_mfma_f32_16x16x32_bf16 v[34:37], v[148:151], v[188:191], v[34:37]
	v_mfma_f32_16x16x32_bf16 v[22:25], v[140:143], v[196:199], v[22:25]
	v_mfma_f32_16x16x32_bf16 v[18:21], v[148:151], v[196:199], v[18:21]
	v_mfma_f32_16x16x32_bf16 v[62:65], v[144:147], v[176:179], v[62:65]
	v_mfma_f32_16x16x32_bf16 v[58:61], v[152:155], v[176:179], v[58:61]
	v_mfma_f32_16x16x32_bf16 v[54:57], v[144:147], v[184:187], v[54:57]
	v_mfma_f32_16x16x32_bf16 v[50:53], v[152:155], v[184:187], v[50:53]
	v_mfma_f32_16x16x32_bf16 v[38:41], v[144:147], v[192:195], v[38:41]
	v_mfma_f32_16x16x32_bf16 v[34:37], v[152:155], v[192:195], v[34:37]
	v_mfma_f32_16x16x32_bf16 v[22:25], v[144:147], v[200:203], v[22:25]
	v_mfma_f32_16x16x32_bf16 v[18:21], v[152:155], v[200:203], v[18:21]
	v_mfma_f32_16x16x32_bf16 v[46:49], v[156:159], v[172:175], v[46:49]
	v_mfma_f32_16x16x32_bf16 v[42:45], v[164:167], v[172:175], v[42:45]
	v_mfma_f32_16x16x32_bf16 v[30:33], v[156:159], v[180:183], v[30:33]
	v_mfma_f32_16x16x32_bf16 v[26:29], v[164:167], v[180:183], v[26:29]
	v_mfma_f32_16x16x32_bf16 v[14:17], v[156:159], v[188:191], v[14:17]
	v_mfma_f32_16x16x32_bf16 v[10:13], v[164:167], v[188:191], v[10:13]
	v_mfma_f32_16x16x32_bf16 v[6:9], v[156:159], v[196:199], v[6:9]
	v_mfma_f32_16x16x32_bf16 v[2:5], v[164:167], v[196:199], v[2:5]
	v_mfma_f32_16x16x32_bf16 v[46:49], v[160:163], v[176:179], v[46:49]
	v_mfma_f32_16x16x32_bf16 v[42:45], v[168:171], v[176:179], v[42:45]
	v_mfma_f32_16x16x32_bf16 v[30:33], v[160:163], v[184:187], v[30:33]
	v_mfma_f32_16x16x32_bf16 v[26:29], v[168:171], v[184:187], v[26:29]
	v_mfma_f32_16x16x32_bf16 v[14:17], v[160:163], v[192:195], v[14:17]
	v_mfma_f32_16x16x32_bf16 v[10:13], v[168:171], v[192:195], v[10:13]
	v_mfma_f32_16x16x32_bf16 v[6:9], v[160:163], v[200:203], v[6:9]
	v_mfma_f32_16x16x32_bf16 v[2:5], v[168:171], v[200:203], v[2:5]
	s_barrier
	s_andn2_b64 vcc, exec, s[24:25]
	s_mov_b64 s[0:1], -1
	s_mov_b64 s[24:25], 0
	s_mov_b64 s[30:31], 0x100
	s_cbranch_vccz .LBB0_668
	s_and_b64 vcc, exec, s[38:39]
	s_cbranch_vccz .LBB0_671
	s_barrier

;     __device__ __forceinline__ void init(const void* A_, const void* B_, int G_, int c_) { T.init(A_, B_, DM, DM, NLAT / 256, INP / 256, 1, 0, 0, G_, c_, 0); }
; #define PG8_STAGE(bufoff, gbase, voff) do { _Pragma("unroll") for (int _i = 0; _i < 2; ++_i) \
;         __builtin_amdgcn_global_load_lds((const unsigned*)((const char*)(gbase) + (voff)[_i]), (LAS unsigned*)(lds + (bufoff) + ldsw + _i * 8192), 16, 0, 0); } while (0)
; #define PG8_STAGE_A(bufoff, kptr, half, VO) do { if constexpr (GATHER) { _Pragma("unroll") for (int _i = 0; _i < 2; ++_i) \
;         __builtin_amdgcn_global_load_lds((const unsigned*)((const char*)(kptr) + (VO)[half][_i]), (LAS unsigned*)(lds + (bufoff) + ldsw + _i * 8192), 16, 0, 0); } \
;         else { PG8_STAGE(bufoff, (kptr) + (half) * hstepA, voffA); } } while (0)
; #define PG8_WAIT_V(n) asm volatile("s_waitcnt vmcnt(" #n ")" ::: "memory")
; #define PG8_BAR __builtin_amdgcn_s_barrier()
;     ...
;     for (int i = 0; i < 2; ++i) { int R, C; stage_rc(tid * 16 + i * 8192, R, C); const int Rb = Epi::PERM ? ((R & ~31) + perm32(R & 31)) : R;
;         voffA[i] = (unsigned)(R * g.lda + C) * 2u; voffB[i] = (unsigned)(Rb * g.ldb + C) * 2u; gR[i] = R; gCc[i] = C; }
;     ...
;     if constexpr (SP2) {
;         PG8_STAGE(PG8_SB(0, 0), cB, voffB); PG8_STAGE(PG8_SB(0, 1), cB + hstepB, voffB); PG8_STAGE_A(PG8_SA(0, 0), cA, 0, gC); PG8_STAGE_A(PG8_SA(0, 1), cA, 1, gC);
;         if (wr == 1) PG8_BAR;
;         PG8_WAIT_V(2); PG8_BAR;
;         PG8_STAGE(PG8_SB(1, 0), cB + kstep, voffB); PG8_STAGE_A(PG8_SA(1, 0), cA + kstep, 0, gC); PG8_STAGE(PG8_SB(1, 1), cB + hstepB + kstep, voffB);
;         PG8_WAIT_V(6); PG8_BAR;
; __global__ void __launch_bounds__(512, 2) fwd(Params p) {
;     ...
;             if (C_SEL & 4) { pg8::TileSched S; S.init((bf16_t*)(ws + WS_WTUKV) + (size_t)l * 1024 * 256 + 512 * 256, ws + WS_KVA, 256, 256, 2, MT / 256, 1, 0, 0, G, c, 184);
.LBB0_675:
	v_readlane_b32 s0, v254, 61
	v_mov_b32_e32 v2, v0
	v_readlane_b32 s1, v254, 62
	s_andn2_b64 vcc, exec, s[0:1]
	v_readfirstlane_b32 s0, v2
	s_cbranch_vccnz .LBB0_691
	v_lshlrev_b32_e32 v3, 4, v2
	v_add_u32_e32 v4, 0x2000, v3
	v_ashrrev_i32_e32 v5, 31, v4
	v_lshrrev_b32_e32 v5, 22, v5
	v_add_u32_e32 v5, v4, v5
	v_ashrrev_i32_e32 v5, 10, v5
	v_mul_i32_i24_e32 v6, 0x400, v5
	v_sub_u32_e32 v4, v4, v6
	v_lshrrev_b32_e32 v6, 4, v4
	v_bitop3_b32 v4, v6, v4, 32 bitop3:0x6c
	v_ashrrev_i32_e32 v6, 31, v4
	v_lshrrev_b32_e32 v6, 26, v6
	v_add_u32_e32 v6, v4, v6
	v_lshlrev_b32_e32 v8, 3, v5
	v_ashrrev_i32_e32 v7, 6, v6
	v_and_b32_e32 v8, -16, v8
	v_and_b32_e32 v6, 0xc0, v6
	v_add_u32_e32 v8, v7, v8
	v_sub_u32_e32 v4, v4, v6
	v_and_b32_e32 v7, 3, v7
	s_mov_b32 s2, 0x7fffe0
	v_lshrrev_b32_e32 v9, 2, v8
	v_lshlrev_b32_e32 v10, 1, v8
	v_lshlrev_b32_e32 v5, 5, v5
	v_ashrrev_i16_sdwa v4, v245, sext(v4) dst_sel:DWORD dst_unused:UNUSED_PAD src0_sel:DWORD src1_sel:BYTE_0
	v_and_or_b32 v7, v8, s2, v7
	v_and_b32_e32 v9, 4, v9
	v_and_b32_e32 v10, 24, v10
	v_and_b32_e32 v5, 32, v5
	v_bfe_i32 v4, v4, 0, 16
	v_or3_b32 v7, v7, v9, v10
	v_add_lshl_u32 v4, v5, v4, 1
	v_lshl_add_u32 v130, v7, 9, v4
	v_lshl_add_u32 v132, v8, 9, v4
	v_bfe_i32 v4, v2, 27, 1
	v_lshrrev_b32_e32 v4, 22, v4
	v_add_u32_e32 v4, v3, v4
	v_and_b32_e32 v4, 0xfffffc00, v4
	v_sub_u32_e32 v3, v3, v4
	v_ashrrev_i32_e32 v5, 31, v2
	v_lshrrev_b32_e32 v4, 4, v3
	v_lshrrev_b32_e32 v5, 26, v5
	v_bitop3_b32 v4, v4, v3, 32 bitop3:0x6c
	v_ashrrev_i32_e32 v3, 31, v3
	v_add_u32_e32 v5, v2, v5
	v_lshrrev_b32_e32 v3, 26, v3
	v_ashrrev_i32_e32 v5, 6, v5
	v_add_u32_e32 v3, v4, v3
	v_lshlrev_b32_e32 v6, 3, v5
	s_ashr_i32 s1, s0, 6
	v_ashrrev_i32_e32 v3, 6, v3
	v_and_b32_e32 v6, -16, v6
	s_ashr_i32 s4, s0, 8
	s_lshl_b32 s26, s1, 10
	v_add_u32_e32 v6, v3, v6
	v_and_b32_e32 v7, 3, v3
	v_mul_i32_i24_e32 v3, 64, v3
	s_add_u32 s12, s12, 0x40000
	v_sub_u32_e32 v3, v4, v3
	s_addc_u32 s13, s13, 0
	v_and_or_b32 v7, v6, s2, v7
	v_lshrrev_b32_e32 v8, 2, v6
	v_lshlrev_b32_e32 v9, 1, v6
	v_lshlrev_b32_e32 v5, 5, v5
	v_ashrrev_i16_sdwa v3, v245, sext(v3) dst_sel:DWORD dst_unused:UNUSED_PAD src0_sel:DWORD src1_sel:BYTE_0
	v_readlane_b32 s2, v255, 0
	v_and_b32_e32 v8, 4, v8
	v_and_b32_e32 v9, 24, v9
	v_and_b32_e32 v5, 32, v5
	v_bfe_i32 v3, v3, 0, 16
	v_readlane_b32 s3, v255, 1
	s_add_u32 s46, s12, s2
	v_or3_b32 v7, v7, v8, v9
	v_add_lshl_u32 v3, v5, v3, 1
	s_addc_u32 s47, s13, s3
	s_add_i32 s27, s26, 0
	v_readlane_b32 s2, v255, 7
	v_lshl_add_u32 v134, v7, 9, v3
	s_add_i32 m0, s27, 0x10000
	v_readlane_b32 s3, v255, 8
	s_add_i32 s60, s27, 0x2000
	v_lshl_add_u32 v136, v6, 9, v3
	s_nop 2
	global_load_lds_dwordx4 v134, s[2:3]
	s_add_i32 m0, s27, 0x12000
	s_nop 0
	global_load_lds_dwordx4 v130, s[2:3]
	v_readlane_b32 s2, v255, 5
	s_add_i32 m0, s27, 0x14000
	v_readlane_b32 s3, v255, 6
	s_nop 4
	global_load_lds_dwordx4 v134, s[2:3]
	s_add_i32 m0, s27, 0x16000
	s_nop 0
	global_load_lds_dwordx4 v130, s[2:3]
	s_mov_b32 m0, s27
	s_add_u32 s2, s46, 0x10000
	global_load_lds_dwordx4 v136, s[46:47]
	s_mov_b32 m0, s60
	s_addc_u32 s3, s47, 0
	s_add_i32 s61, s27, 0x4000
	global_load_lds_dwordx4 v132, s[46:47]
	s_mov_b32 m0, s61
	s_add_i32 s63, s27, 0x6000
	global_load_lds_dwordx4 v136, s[2:3]
	s_mov_b32 m0, s63
	s_cmp_eq_u32 s4, 1
	global_load_lds_dwordx4 v132, s[2:3]
	s_cselect_b64 s[2:3], -1, 0
	s_cmp_lg_u32 s4, 1
	s_cbranch_scc1 .LBB0_678
	s_barrier
	s_setprio 1

; #define PG8_GOFF(u, o) do { _Pragma("unroll") for (int _h = 0; _h < 2; ++_h) _Pragma("unroll") for (int _i = 0; _i < 2; ++_i) { const int _r = (u).pm * 256 + _h * 128 + gR[_i]; \
;         const int _tok = _r < nvalid ? rowtok[(u).pb * EROWS + _r] : 0; (o)[_h][_i] = (unsigned)(_tok * g.lda + gCc[_i]) * 2u; } } while (0)
; #define PG8_STAGE(bufoff, gbase, voff) do { _Pragma("unroll") for (int _i = 0; _i < 2; ++_i) \
;         __builtin_amdgcn_global_load_lds((const unsigned*)((const char*)(gbase) + (voff)[_i]), (LAS unsigned*)(lds + (bufoff) + ldsw + _i * 8192), 16, 0, 0); } while (0)
; #define PG8_LDA(dst, b, h) do { _Pragma("unroll") for (int m = 0; m < 4; ++m) _Pragma("unroll") for (int k = 0; k < 2; ++k) dst[m][k] = *(const LAS bf16x8*)(lds + PG8_SA(b, h) + aoff + m * 2048 + k * 1024); } while (0)
;     ...
;         const bool has_next = S.next(ui + 1, nxt);
;         const char* nA = has_next ? nxt.a : cA; const char* nB = has_next ? nxt.b : cB;
;         if constexpr (GATHER) { if (has_next) { PG8_GOFF(nxt, gN); } else {
; #pragma unroll
;             for (int _h = 0; _h < 2; ++_h)
; #pragma unroll
;                 for (int _i = 0; _i < 2; ++_i) gN[_h][_i] = gC[_h][_i]; } }
; #pragma nounroll
;         for (int t = 0; t < nt; t += 2) {
;             const bool last = (t == nt - 2);
;             const char* a1 = cA + (size_t)(t + 1) * kstep;
;             const char* a2 = last ? nA : cA + (size_t)(t + 2) * kstep; const char* b2 = last ? nB : cB + (size_t)(t + 2) * kstep;
;             const char* a3 = a2 + kstep; const char* b3 = b2 + kstep;
;             unsigned g2[2][2];
;             if constexpr (GATHER) {
; #pragma unroll
;                 for (int _h = 0; _h < 2; ++_h)
; #pragma unroll
;                     for (int _i = 0; _i < 2; ++_i) g2[_h][_i] = last ? gN[_h][_i] : gC[_h][_i]; }
;             if constexpr (SP2) {
;             PG8_LDB(B0, 0, 0); PG8_LDB(B1, 0, 1); PG8_SCHED; PG8_LDA(At, 0, 0); PG8_STAGE_A(PG8_SA(1, 1), a1, 1, gC);
;             PG8_WAIT_V(8); PG8_WAIT_L(0); PG8_BAR; PG8_MMA(0, 0, At, B0); PG8_MMA(0, 1, At, B1); PG8_BAR; PG8_SCHED;
;             PG8_LDA(At, 0, 1); PG8_STAGE(PG8_SB(0, 0), b2, voffB); PG8_STAGE(PG8_SB(0, 1), b2 + hstepB, voffB); PG8_STAGE_A(PG8_SA(0, 0), a2, 0, g2);
;             PG8_WAIT_V(8); PG8_WAIT_L(0); PG8_BAR; PG8_MMA(1, 0, At, B0); PG8_MMA(1, 1, At, B1); PG8_BAR; PG8_SCHED;
.LBB0_684:
	s_add_u32 s16, s46, s48
	s_addc_u32 s17, s47, s49
	s_add_u32 s18, s16, 0x100
	s_addc_u32 s19, s17, 0
	s_and_b64 s[14:15], s[0:1], exec
	s_cselect_b32 s51, s43, s19
	s_cselect_b32 s50, s42, s18
	s_add_u32 s14, s24, s48
	s_addc_u32 s15, s25, s49
	s_add_u32 s14, s14, 0x100
	s_addc_u32 s15, s15, 0
	s_add_i32 s22, 0, 0x10000
	s_and_b64 s[0:1], s[0:1], exec
	s_cselect_b32 s55, s45, s15
	s_cselect_b32 s54, s44, s14
	s_add_i32 s1, 0, 0x14000
	s_add_u32 s58, s16, 0x10080
	s_addc_u32 s59, s17, 0
	s_add_i32 s21, s22, s26
	s_add_i32 m0, s27, 0xc000
	s_add_i32 s35, s27, 0xe000
	s_add_i32 s18, s21, 0x2000
	v_add_u32_e32 v143, s22, v144
	s_add_u32 s56, s54, 0x10000
	ds_read_b128 v[146:149], v143
	ds_read_b128 v[150:153], v143 offset:1024
	ds_read_b128 v[154:157], v143 offset:2048
	ds_read_b128 v[158:161], v143 offset:3072
	v_add_u32_e32 v143, s1, v144
	s_addc_u32 s57, s55, 0
	s_add_i32 s20, s1, s26
	ds_read_b128 v[162:165], v143
	ds_read_b128 v[166:169], v143 offset:1024
	ds_read_b128 v[170:173], v143 offset:2048
	ds_read_b128 v[174:177], v143 offset:3072
	s_add_i32 s19, s20, 0x2000
	s_add_i32 s17, 0, 0x18000
	s_add_i32 s16, 0, 0x1c000
	s_add_u32 s48, s50, 0x10000
	s_addc_u32 s49, s51, 0
	s_add_i32 s15, s17, s26
	s_add_i32 s14, s15, 0x2000
	s_add_u32 s0, s54, 0x10080
	s_addc_u32 s1, s55, 0
	s_add_i32 s23, s16, s26
	s_add_i32 s22, s23, 0x2000
	v_lshl_add_u64 v[208:209], s[58:59], 0, v[136:137]
	ds_read_b128 v[178:181], v145
	ds_read_b128 v[182:185], v145 offset:1024
	ds_read_b128 v[186:189], v145 offset:2048
	ds_read_b128 v[190:193], v145 offset:3072
	ds_read_b128 v[194:197], v145 offset:4096
	ds_read_b128 v[198:201], v145 offset:5120
	ds_read_b128 v[202:205], v145 offset:6144
	ds_read_b128 v[216:219], v145 offset:7168
	global_load_lds_dwordx4 v[208:209], off
	v_lshl_add_u64 v[208:209], s[58:59], 0, v[132:133]
	s_mov_b32 m0, s35
	s_nop 0
	global_load_lds_dwordx4 v[208:209], off
	s_waitcnt vmcnt(8)
	s_waitcnt lgkmcnt(0)
	s_barrier
	s_waitcnt lgkmcnt(0)
	v_mfma_f32_16x16x32_bf16 v[126:129], v[146:149], v[178:181], v[126:129]
	v_mfma_f32_16x16x32_bf16 v[122:125], v[154:157], v[178:181], v[122:125]
	v_mfma_f32_16x16x32_bf16 v[118:121], v[146:149], v[186:189], v[118:121]
	v_mfma_f32_16x16x32_bf16 v[114:117], v[154:157], v[186:189], v[114:117]
	v_mfma_f32_16x16x32_bf16 v[102:105], v[146:149], v[194:197], v[102:105]
	v_mfma_f32_16x16x32_bf16 v[98:101], v[154:157], v[194:197], v[98:101]
	v_mfma_f32_16x16x32_bf16 v[86:89], v[146:149], v[202:205], v[86:89]
	v_mfma_f32_16x16x32_bf16 v[82:85], v[154:157], v[202:205], v[82:85]
	v_mfma_f32_16x16x32_bf16 v[126:129], v[150:153], v[182:185], v[126:129]
	v_mfma_f32_16x16x32_bf16 v[122:125], v[158:161], v[182:185], v[122:125]
	v_mfma_f32_16x16x32_bf16 v[118:121], v[150:153], v[190:193], v[118:121]
	v_mfma_f32_16x16x32_bf16 v[114:117], v[158:161], v[190:193], v[114:117]
	v_mfma_f32_16x16x32_bf16 v[102:105], v[150:153], v[198:201], v[102:105]
	v_mfma_f32_16x16x32_bf16 v[98:101], v[158:161], v[198:201], v[98:101]
	v_mfma_f32_16x16x32_bf16 v[86:89], v[150:153], v[216:219], v[86:89]
	v_mfma_f32_16x16x32_bf16 v[82:85], v[158:161], v[216:219], v[82:85]
	v_mfma_f32_16x16x32_bf16 v[110:113], v[162:165], v[178:181], v[110:113]
	v_mfma_f32_16x16x32_bf16 v[106:109], v[170:173], v[178:181], v[106:109]
	v_mfma_f32_16x16x32_bf16 v[94:97], v[162:165], v[186:189], v[94:97]
	v_mfma_f32_16x16x32_bf16 v[90:93], v[170:173], v[186:189], v[90:93]
	v_mfma_f32_16x16x32_bf16 v[78:81], v[162:165], v[194:197], v[78:81]
	v_mfma_f32_16x16x32_bf16 v[74:77], v[170:173], v[194:197], v[74:77]
	v_mfma_f32_16x16x32_bf16 v[70:73], v[162:165], v[202:205], v[70:73]
	v_mfma_f32_16x16x32_bf16 v[66:69], v[170:173], v[202:205], v[66:69]
	v_mfma_f32_16x16x32_bf16 v[110:113], v[166:169], v[182:185], v[110:113]
	v_mfma_f32_16x16x32_bf16 v[106:109], v[174:177], v[182:185], v[106:109]
	v_mfma_f32_16x16x32_bf16 v[94:97], v[166:169], v[190:193], v[94:97]
	v_mfma_f32_16x16x32_bf16 v[90:93], v[174:177], v[190:193], v[90:93]
	v_mfma_f32_16x16x32_bf16 v[78:81], v[166:169], v[198:201], v[78:81]
	v_mfma_f32_16x16x32_bf16 v[74:77], v[174:177], v[198:201], v[74:77]
	v_mfma_f32_16x16x32_bf16 v[70:73], v[166:169], v[216:219], v[70:73]
	v_mfma_f32_16x16x32_bf16 v[66:69], v[174:177], v[216:219], v[66:69]
	s_barrier
	s_mov_b32 m0, s21
	v_lshl_add_u64 v[208:209], s[54:55], 0, v[134:135]
	ds_read_b128 v[178:181], v145 offset:16384
	ds_read_b128 v[182:185], v145 offset:17408
	ds_read_b128 v[186:189], v145 offset:18432
	ds_read_b128 v[190:193], v145 offset:19456
	ds_read_b128 v[194:197], v145 offset:20480
	ds_read_b128 v[198:201], v145 offset:21504
	ds_read_b128 v[202:205], v145 offset:22528
	ds_read_b128 v[216:219], v145 offset:23552
	global_load_lds_dwordx4 v[208:209], off
	v_lshl_add_u64 v[210:211], s[54:55], 0, v[130:131]
	s_mov_b32 m0, s18
	v_lshl_add_u64 v[212:213], s[56:57], 0, v[134:135]
	global_load_lds_dwordx4 v[210:211], off
	s_mov_b32 m0, s20
	v_lshl_add_u64 v[220:221], s[50:51], 0, v[132:133]
	global_load_lds_dwordx4 v[212:213], off
	v_lshl_add_u64 v[212:213], s[56:57], 0, v[130:131]
	s_mov_b32 m0, s19
	s_nop 0
	global_load_lds_dwordx4 v[212:213], off
	v_lshl_add_u64 v[212:213], s[50:51], 0, v[136:137]
	s_mov_b32 m0, s27
	s_nop 0
	global_load_lds_dwordx4 v[212:213], off
	s_mov_b32 m0, s60
	s_nop 0
	global_load_lds_dwordx4 v[220:221], off
	s_waitcnt vmcnt(8)
	s_waitcnt lgkmcnt(0)
	s_barrier
; #define PG8_STAGE(bufoff, gbase, voff) do { _Pragma("unroll") for (int _i = 0; _i < 2; ++_i) \
;         __builtin_amdgcn_global_load_lds((const unsigned*)((const char*)(gbase) + (voff)[_i]), (LAS unsigned*)(lds + (bufoff) + ldsw + _i * 8192), 16, 0, 0); } while (0)
; #define PG8_STAGE_A(bufoff, kptr, half, VO) do { if constexpr (GATHER) { _Pragma("unroll") for (int _i = 0; _i < 2; ++_i) \
;         __builtin_amdgcn_global_load_lds((const unsigned*)((const char*)(kptr) + (VO)[half][_i]), (LAS unsigned*)(lds + (bufoff) + ldsw + _i * 8192), 16, 0, 0); } \
;         else { PG8_STAGE(bufoff, (kptr) + (half) * hstepA, voffA); } } while (0)
; #define PG8_LDA(dst, b, h) do { _Pragma("unroll") for (int m = 0; m < 4; ++m) _Pragma("unroll") for (int k = 0; k < 2; ++k) dst[m][k] = *(const LAS bf16x8*)(lds + PG8_SA(b, h) + aoff + m * 2048 + k * 1024); } while (0)
; #define PG8_LDB(dst, b, h) do { _Pragma("unroll") for (int n = 0; n < 2; ++n) _Pragma("unroll") for (int k = 0; k < 2; ++k) dst[n][k] = *(const LAS bf16x8*)(lds + PG8_SB(b, h) + boff + n * 2048 + k * 1024); } while (0)
; #define PG8_MMA(ai, bj, At, Bt) do { __builtin_amdgcn_s_setprio(1); _Pragma("unroll") for (int m = 0; m < 4; ++m) _Pragma("unroll") for (int n = 0; n < 2; ++n) _Pragma("unroll") for (int k = 0; k < 2; ++k) \
;         acc[ai][bj][m][n] = __builtin_amdgcn_mfma_f32_16x16x32_bf16(Bt[n][k], At[m][k], acc[ai][bj][m][n], 0, 0, 0); __builtin_amdgcn_s_setprio(0); } while (0)
; #define PG8_WAIT_V(n) asm volatile("s_waitcnt vmcnt(" #n ")" ::: "memory")
; #define PG8_WAIT_L(n) asm volatile("s_waitcnt lgkmcnt(" #n ")" ::: "memory")
; #define PG8_BAR __builtin_amdgcn_s_barrier()
; #define PG8_SCHED __builtin_amdgcn_sched_barrier(0)
;     ...
;             PG8_WAIT_V(8); PG8_WAIT_L(0); PG8_BAR; PG8_MMA(1, 0, At, B0); PG8_MMA(1, 1, At, B1); PG8_BAR; PG8_SCHED;
;             PG8_LDB(B0, 1, 0); PG8_LDB(B1, 1, 1); PG8_SCHED; PG8_LDA(At, 1, 0); PG8_STAGE_A(PG8_SA(0, 1), a2, 1, g2);
;             PG8_WAIT_V(8); PG8_WAIT_L(0); PG8_BAR; PG8_MMA(0, 0, At, B0); PG8_MMA(0, 1, At, B1); PG8_BAR; PG8_SCHED;
;             PG8_LDA(At, 1, 1); PG8_STAGE(PG8_SB(1, 0), b3, voffB); PG8_STAGE(PG8_SB(1, 1), b3 + hstepB, voffB); PG8_STAGE_A(PG8_SA(1, 0), a3, 0, g2);
	s_waitcnt lgkmcnt(0)
	v_mfma_f32_16x16x32_bf16 v[62:65], v[146:149], v[178:181], v[62:65]
	v_mfma_f32_16x16x32_bf16 v[58:61], v[154:157], v[178:181], v[58:61]
	v_mfma_f32_16x16x32_bf16 v[54:57], v[146:149], v[186:189], v[54:57]
	v_mfma_f32_16x16x32_bf16 v[50:53], v[154:157], v[186:189], v[50:53]
	v_mfma_f32_16x16x32_bf16 v[38:41], v[146:149], v[194:197], v[38:41]
	v_mfma_f32_16x16x32_bf16 v[34:37], v[154:157], v[194:197], v[34:37]
	v_mfma_f32_16x16x32_bf16 v[22:25], v[146:149], v[202:205], v[22:25]
	v_mfma_f32_16x16x32_bf16 v[18:21], v[154:157], v[202:205], v[18:21]
	v_mfma_f32_16x16x32_bf16 v[62:65], v[150:153], v[182:185], v[62:65]
	v_mfma_f32_16x16x32_bf16 v[58:61], v[158:161], v[182:185], v[58:61]
	v_mfma_f32_16x16x32_bf16 v[54:57], v[150:153], v[190:193], v[54:57]
	v_mfma_f32_16x16x32_bf16 v[50:53], v[158:161], v[190:193], v[50:53]
	v_mfma_f32_16x16x32_bf16 v[38:41], v[150:153], v[198:201], v[38:41]
	v_mfma_f32_16x16x32_bf16 v[34:37], v[158:161], v[198:201], v[34:37]
	v_mfma_f32_16x16x32_bf16 v[22:25], v[150:153], v[216:219], v[22:25]
	v_mfma_f32_16x16x32_bf16 v[18:21], v[158:161], v[216:219], v[18:21]
	v_mfma_f32_16x16x32_bf16 v[46:49], v[162:165], v[178:181], v[46:49]
	v_mfma_f32_16x16x32_bf16 v[42:45], v[170:173], v[178:181], v[42:45]
	v_mfma_f32_16x16x32_bf16 v[30:33], v[162:165], v[186:189], v[30:33]
	v_mfma_f32_16x16x32_bf16 v[26:29], v[170:173], v[186:189], v[26:29]
	v_mfma_f32_16x16x32_bf16 v[14:17], v[162:165], v[194:197], v[14:17]
	v_mfma_f32_16x16x32_bf16 v[10:13], v[170:173], v[194:197], v[10:13]
	v_mfma_f32_16x16x32_bf16 v[6:9], v[162:165], v[202:205], v[6:9]
	v_mfma_f32_16x16x32_bf16 v[2:5], v[170:173], v[202:205], v[2:5]
	v_mfma_f32_16x16x32_bf16 v[46:49], v[166:169], v[182:185], v[46:49]
	v_mfma_f32_16x16x32_bf16 v[42:45], v[174:177], v[182:185], v[42:45]
	v_mfma_f32_16x16x32_bf16 v[30:33], v[166:169], v[190:193], v[30:33]
	v_mfma_f32_16x16x32_bf16 v[26:29], v[174:177], v[190:193], v[26:29]
	v_mfma_f32_16x16x32_bf16 v[14:17], v[166:169], v[198:201], v[14:17]
	v_mfma_f32_16x16x32_bf16 v[10:13], v[174:177], v[198:201], v[10:13]
	v_mfma_f32_16x16x32_bf16 v[6:9], v[166:169], v[216:219], v[6:9]
	v_mfma_f32_16x16x32_bf16 v[2:5], v[174:177], v[216:219], v[2:5]
	s_barrier
	v_add_u32_e32 v143, s17, v144
	ds_read_b128 v[146:149], v143
	ds_read_b128 v[150:153], v143 offset:1024
	ds_read_b128 v[154:157], v143 offset:2048
	ds_read_b128 v[158:161], v143 offset:3072
	v_add_u32_e32 v143, s16, v144
	ds_read_b128 v[162:165], v143
	ds_read_b128 v[166:169], v143 offset:1024
	ds_read_b128 v[170:173], v143 offset:2048
	ds_read_b128 v[174:177], v143 offset:3072
	s_mov_b32 m0, s61
	v_lshl_add_u64 v[222:223], s[48:49], 0, v[136:137]
	ds_read_b128 v[178:181], v145 offset:32768
	ds_read_b128 v[182:185], v145 offset:33792
	ds_read_b128 v[186:189], v145 offset:34816
	ds_read_b128 v[190:193], v145 offset:35840
	ds_read_b128 v[194:197], v145 offset:36864
	ds_read_b128 v[198:201], v145 offset:37888
	ds_read_b128 v[202:205], v145 offset:38912
	ds_read_b128 v[216:219], v145 offset:39936
	global_load_lds_dwordx4 v[222:223], off
	v_lshl_add_u64 v[222:223], s[48:49], 0, v[132:133]
	s_mov_b32 m0, s63
	s_nop 0
	global_load_lds_dwordx4 v[222:223], off
	s_waitcnt vmcnt(8)
	s_waitcnt lgkmcnt(0)
	s_barrier
	s_waitcnt lgkmcnt(0)
	v_mfma_f32_16x16x32_bf16 v[126:129], v[146:149], v[178:181], v[126:129]
	v_mfma_f32_16x16x32_bf16 v[122:125], v[154:157], v[178:181], v[122:125]
	v_mfma_f32_16x16x32_bf16 v[118:121], v[146:149], v[186:189], v[118:121]
	v_mfma_f32_16x16x32_bf16 v[114:117], v[154:157], v[186:189], v[114:117]
	v_mfma_f32_16x16x32_bf16 v[102:105], v[146:149], v[194:197], v[102:105]
	v_mfma_f32_16x16x32_bf16 v[98:101], v[154:157], v[194:197], v[98:101]
	v_mfma_f32_16x16x32_bf16 v[86:89], v[146:149], v[202:205], v[86:89]
	v_mfma_f32_16x16x32_bf16 v[82:85], v[154:157], v[202:205], v[82:85]
	v_mfma_f32_16x16x32_bf16 v[126:129], v[150:153], v[182:185], v[126:129]
	v_mfma_f32_16x16x32_bf16 v[122:125], v[158:161], v[182:185], v[122:125]
	v_mfma_f32_16x16x32_bf16 v[118:121], v[150:153], v[190:193], v[118:121]
	v_mfma_f32_16x16x32_bf16 v[114:117], v[158:161], v[190:193], v[114:117]
	v_mfma_f32_16x16x32_bf16 v[102:105], v[150:153], v[198:201], v[102:105]
	v_mfma_f32_16x16x32_bf16 v[98:101], v[158:161], v[198:201], v[98:101]
	v_mfma_f32_16x16x32_bf16 v[86:89], v[150:153], v[216:219], v[86:89]
	v_mfma_f32_16x16x32_bf16 v[82:85], v[158:161], v[216:219], v[82:85]
	v_mfma_f32_16x16x32_bf16 v[110:113], v[162:165], v[178:181], v[110:113]
	v_mfma_f32_16x16x32_bf16 v[106:109], v[170:173], v[178:181], v[106:109]
	v_mfma_f32_16x16x32_bf16 v[94:97], v[162:165], v[186:189], v[94:97]
	v_mfma_f32_16x16x32_bf16 v[90:93], v[170:173], v[186:189], v[90:93]
	v_mfma_f32_16x16x32_bf16 v[78:81], v[162:165], v[194:197], v[78:81]
	v_mfma_f32_16x16x32_bf16 v[74:77], v[170:173], v[194:197], v[74:77]
	v_mfma_f32_16x16x32_bf16 v[70:73], v[162:165], v[202:205], v[70:73]
	v_mfma_f32_16x16x32_bf16 v[66:69], v[170:173], v[202:205], v[66:69]
	v_mfma_f32_16x16x32_bf16 v[110:113], v[166:169], v[182:185], v[110:113]
	v_mfma_f32_16x16x32_bf16 v[106:109], v[174:177], v[182:185], v[106:109]
	v_mfma_f32_16x16x32_bf16 v[94:97], v[166:169], v[190:193], v[94:97]
	v_mfma_f32_16x16x32_bf16 v[90:93], v[174:177], v[190:193], v[90:93]
	v_mfma_f32_16x16x32_bf16 v[78:81], v[166:169], v[198:201], v[78:81]
	v_mfma_f32_16x16x32_bf16 v[74:77], v[174:177], v[198:201], v[74:77]
	v_mfma_f32_16x16x32_bf16 v[70:73], v[166:169], v[216:219], v[70:73]
	v_mfma_f32_16x16x32_bf16 v[66:69], v[174:177], v[216:219], v[66:69]
	s_barrier
; #define PG8_STAGE(bufoff, gbase, voff) do { _Pragma("unroll") for (int _i = 0; _i < 2; ++_i) \
;         __builtin_amdgcn_global_load_lds((const unsigned*)((const char*)(gbase) + (voff)[_i]), (LAS unsigned*)(lds + (bufoff) + ldsw + _i * 8192), 16, 0, 0); } while (0)
; #define PG8_STAGE_A(bufoff, kptr, half, VO) do { if constexpr (GATHER) { _Pragma("unroll") for (int _i = 0; _i < 2; ++_i) \
;         __builtin_amdgcn_global_load_lds((const unsigned*)((const char*)(kptr) + (VO)[half][_i]), (LAS unsigned*)(lds + (bufoff) + ldsw + _i * 8192), 16, 0, 0); } \
;         else { PG8_STAGE(bufoff, (kptr) + (half) * hstepA, voffA); } } while (0)
; #define PG8_LDA(dst, b, h) do { _Pragma("unroll") for (int m = 0; m < 4; ++m) _Pragma("unroll") for (int k = 0; k < 2; ++k) dst[m][k] = *(const LAS bf16x8*)(lds + PG8_SA(b, h) + aoff + m * 2048 + k * 1024); } while (0)
; #define PG8_MMA(ai, bj, At, Bt) do { __builtin_amdgcn_s_setprio(1); _Pragma("unroll") for (int m = 0; m < 4; ++m) _Pragma("unroll") for (int n = 0; n < 2; ++n) _Pragma("unroll") for (int k = 0; k < 2; ++k) \
;         acc[ai][bj][m][n] = __builtin_amdgcn_mfma_f32_16x16x32_bf16(Bt[n][k], At[m][k], acc[ai][bj][m][n], 0, 0, 0); __builtin_amdgcn_s_setprio(0); } while (0)
; #define PG8_WAIT_V(n) asm volatile("s_waitcnt vmcnt(" #n ")" ::: "memory")
; #define PG8_WAIT_L(n) asm volatile("s_waitcnt lgkmcnt(" #n ")" ::: "memory")
; #define PG8_BAR __builtin_amdgcn_s_barrier()
; #define PG8_SCHED __builtin_amdgcn_sched_barrier(0)
;     ...
;             PG8_LDA(At, 1, 1); PG8_STAGE(PG8_SB(1, 0), b3, voffB); PG8_STAGE(PG8_SB(1, 1), b3 + hstepB, voffB); PG8_STAGE_A(PG8_SA(1, 0), a3, 0, g2);
;             PG8_WAIT_V(8); PG8_WAIT_L(0); PG8_BAR; PG8_MMA(1, 0, At, B0); PG8_MMA(1, 1, At, B1); PG8_BAR; PG8_SCHED;
;     ...
;         if constexpr (ALIGN_EPI) { if (wr == 0) PG8_BAR; }
	s_mov_b32 m0, s15
	v_lshl_add_u64 v[208:209], v[208:209], 0, s[8:9]
	ds_read_b128 v[178:181], v145 offset:49152
	ds_read_b128 v[182:185], v145 offset:50176
	ds_read_b128 v[186:189], v145 offset:51200
	ds_read_b128 v[190:193], v145 offset:52224
	ds_read_b128 v[194:197], v145 offset:53248
	ds_read_b128 v[198:201], v145 offset:54272
	ds_read_b128 v[202:205], v145 offset:55296
	ds_read_b128 v[216:219], v145 offset:56320
	global_load_lds_dwordx4 v[208:209], off
	v_lshl_add_u64 v[208:209], v[210:211], 0, s[8:9]
	s_mov_b32 m0, s14
	s_nop 0
	global_load_lds_dwordx4 v[208:209], off
	v_lshl_add_u64 v[208:209], s[0:1], 0, v[134:135]
	s_mov_b32 m0, s23
	s_nop 0
	global_load_lds_dwordx4 v[208:209], off
	v_lshl_add_u64 v[208:209], s[0:1], 0, v[130:131]
	s_mov_b32 m0, s22
	s_nop 0
	global_load_lds_dwordx4 v[208:209], off
	v_lshl_add_u64 v[208:209], v[212:213], 0, s[8:9]
	s_mov_b32 m0, s64
	s_nop 0
	global_load_lds_dwordx4 v[208:209], off
	v_lshl_add_u64 v[208:209], v[220:221], 0, s[8:9]
	s_mov_b32 m0, s65
	s_nop 0
	global_load_lds_dwordx4 v[208:209], off
	s_waitcnt vmcnt(8)
	s_waitcnt lgkmcnt(0)
	s_barrier
	s_waitcnt lgkmcnt(0)
	v_mfma_f32_16x16x32_bf16 v[62:65], v[146:149], v[178:181], v[62:65]
	v_mfma_f32_16x16x32_bf16 v[58:61], v[154:157], v[178:181], v[58:61]
	v_mfma_f32_16x16x32_bf16 v[54:57], v[146:149], v[186:189], v[54:57]
	v_mfma_f32_16x16x32_bf16 v[50:53], v[154:157], v[186:189], v[50:53]
	v_mfma_f32_16x16x32_bf16 v[38:41], v[146:149], v[194:197], v[38:41]
	v_mfma_f32_16x16x32_bf16 v[34:37], v[154:157], v[194:197], v[34:37]
	v_mfma_f32_16x16x32_bf16 v[22:25], v[146:149], v[202:205], v[22:25]
	v_mfma_f32_16x16x32_bf16 v[18:21], v[154:157], v[202:205], v[18:21]
	v_mfma_f32_16x16x32_bf16 v[62:65], v[150:153], v[182:185], v[62:65]
	v_mfma_f32_16x16x32_bf16 v[58:61], v[158:161], v[182:185], v[58:61]
	v_mfma_f32_16x16x32_bf16 v[54:57], v[150:153], v[190:193], v[54:57]
	v_mfma_f32_16x16x32_bf16 v[50:53], v[158:161], v[190:193], v[50:53]
	v_mfma_f32_16x16x32_bf16 v[38:41], v[150:153], v[198:201], v[38:41]
	v_mfma_f32_16x16x32_bf16 v[34:37], v[158:161], v[198:201], v[34:37]
	v_mfma_f32_16x16x32_bf16 v[22:25], v[150:153], v[216:219], v[22:25]
	v_mfma_f32_16x16x32_bf16 v[18:21], v[158:161], v[216:219], v[18:21]
	v_mfma_f32_16x16x32_bf16 v[46:49], v[162:165], v[178:181], v[46:49]
	v_mfma_f32_16x16x32_bf16 v[42:45], v[170:173], v[178:181], v[42:45]
	v_mfma_f32_16x16x32_bf16 v[30:33], v[162:165], v[186:189], v[30:33]
	v_mfma_f32_16x16x32_bf16 v[26:29], v[170:173], v[186:189], v[26:29]
	v_mfma_f32_16x16x32_bf16 v[14:17], v[162:165], v[194:197], v[14:17]
	v_mfma_f32_16x16x32_bf16 v[10:13], v[170:173], v[194:197], v[10:13]
	v_mfma_f32_16x16x32_bf16 v[6:9], v[162:165], v[202:205], v[6:9]
	v_mfma_f32_16x16x32_bf16 v[2:5], v[170:173], v[202:205], v[2:5]
	v_mfma_f32_16x16x32_bf16 v[46:49], v[166:169], v[182:185], v[46:49]
	v_mfma_f32_16x16x32_bf16 v[42:45], v[174:177], v[182:185], v[42:45]
	v_mfma_f32_16x16x32_bf16 v[30:33], v[166:169], v[190:193], v[30:33]
	v_mfma_f32_16x16x32_bf16 v[26:29], v[174:177], v[190:193], v[26:29]
	v_mfma_f32_16x16x32_bf16 v[14:17], v[166:169], v[198:201], v[14:17]
	v_mfma_f32_16x16x32_bf16 v[10:13], v[174:177], v[198:201], v[10:13]
	v_mfma_f32_16x16x32_bf16 v[6:9], v[166:169], v[216:219], v[6:9]
	v_mfma_f32_16x16x32_bf16 v[2:5], v[174:177], v[216:219], v[2:5]
	s_barrier
	s_andn2_b64 vcc, exec, s[30:31]
	s_mov_b64 s[0:1], -1
	s_mov_b64 s[30:31], 0
	s_mov_b64 s[48:49], 0x100
	s_cbranch_vccz .LBB0_684
	s_and_b64 vcc, exec, s[38:39]
	s_cbranch_vccz .LBB0_687
	s_barrier

;     __device__ __forceinline__ void init(const void* A_, const void* B_, int G_, int c_) { T.init(A_, B_, DM, DM, NLAT / 256, INP / 256, 1, 0, 0, G_, c_, 0); }
; #define PG8_STAGE(bufoff, gbase, voff) do { _Pragma("unroll") for (int _i = 0; _i < 2; ++_i) \
;         __builtin_amdgcn_global_load_lds((const unsigned*)((const char*)(gbase) + (voff)[_i]), (LAS unsigned*)(lds + (bufoff) + ldsw + _i * 8192), 16, 0, 0); } while (0)
; #define PG8_STAGE_A(bufoff, kptr, half, VO) do { if constexpr (GATHER) { _Pragma("unroll") for (int _i = 0; _i < 2; ++_i) \
;         __builtin_amdgcn_global_load_lds((const unsigned*)((const char*)(kptr) + (VO)[half][_i]), (LAS unsigned*)(lds + (bufoff) + ldsw + _i * 8192), 16, 0, 0); } \
;         else { PG8_STAGE(bufoff, (kptr) + (half) * hstepA, voffA); } } while (0)
; #define PG8_WAIT_V(n) asm volatile("s_waitcnt vmcnt(" #n ")" ::: "memory")
; #define PG8_BAR __builtin_amdgcn_s_barrier()
;     ...
;     for (int i = 0; i < 2; ++i) { int R, C; stage_rc(tid * 16 + i * 8192, R, C); const int Rb = Epi::PERM ? ((R & ~31) + perm32(R & 31)) : R;
;         voffA[i] = (unsigned)(R * g.lda + C) * 2u; voffB[i] = (unsigned)(Rb * g.ldb + C) * 2u; gR[i] = R; gCc[i] = C; }
;     ...
;     if constexpr (SP2) {
;         PG8_STAGE(PG8_SB(0, 0), cB, voffB); PG8_STAGE(PG8_SB(0, 1), cB + hstepB, voffB); PG8_STAGE_A(PG8_SA(0, 0), cA, 0, gC); PG8_STAGE_A(PG8_SA(0, 1), cA, 1, gC);
;         if (wr == 1) PG8_BAR;
;         PG8_WAIT_V(2); PG8_BAR;
;         PG8_STAGE(PG8_SB(1, 0), cB + kstep, voffB); PG8_STAGE_A(PG8_SA(1, 0), cA + kstep, 0, gC); PG8_STAGE(PG8_SB(1, 1), cB + hstepB + kstep, voffB);
;         PG8_WAIT_V(6); PG8_BAR;
; __global__ void __launch_bounds__(512, 2) fwd(Params p) {
;     ...
;             if (C_SEL & 8) { pg8::TileSched S; S.init(ws + WS_UPK, (bf16_t*)(ws + WS_WST) + (size_t)l * 32 * 256 * 256, 512, 256, 3, 1, 32, (size_t)768 * 512 * 2, (size_t)256 * 256 * 2, G, c, G == 256 ? 112 : 0);
.LBB0_693:
	s_and_b64 vcc, exec, s[2:3]
	s_cbranch_vccnz .LBB0_725
	v_bfe_i32 v5, v2, 27, 1
	v_lshlrev_b32_e32 v3, 4, v2
	v_lshrrev_b32_e32 v5, 22, v5
	v_add_u32_e32 v5, v3, v5
	v_and_b32_e32 v5, 0xfffffc00, v5
	v_ashrrev_i32_e32 v4, 31, v2
	v_sub_u32_e32 v5, v3, v5
	v_lshrrev_b32_e32 v4, 26, v4
	v_lshrrev_b32_e32 v6, 4, v5
	v_add_u32_e32 v4, v2, v4
	v_bitop3_b32 v6, v6, v5, 32 bitop3:0x6c
	v_ashrrev_i32_e32 v5, 31, v5
	v_ashrrev_i32_e32 v4, 6, v4
	v_lshrrev_b32_e32 v5, 26, v5
	v_lshlrev_b32_e32 v7, 3, v4
	v_add_u32_e32 v5, v6, v5
	v_and_b32_e32 v7, -16, v7
	v_ashrrev_i32_e32 v5, 6, v5
	v_add_u32_e32 v7, v5, v7
	v_mul_i32_i24_e32 v5, 64, v5
	v_lshlrev_b32_e32 v4, 5, v4
	v_sub_u32_e32 v5, v6, v5
	v_and_b32_e32 v4, 32, v4
	v_ashrrev_i16_sdwa v5, v245, sext(v5) dst_sel:DWORD dst_unused:UNUSED_PAD src0_sel:DWORD src1_sel:BYTE_0
	v_add_u32_sdwa v4, v4, sext(v5) dst_sel:DWORD dst_unused:UNUSED_PAD src0_sel:DWORD src1_sel:WORD_0
	v_lshlrev_b32_e32 v5, 10, v7
	v_lshl_add_u32 v130, v4, 1, v5
	v_lshlrev_b32_e32 v4, 9, v7
	v_add_u32_e32 v3, 0x2000, v3
	v_sub_u32_e32 v206, v130, v4
	v_ashrrev_i32_e32 v4, 31, v3
	v_lshrrev_b32_e32 v4, 22, v4
	v_add_u32_e32 v4, v3, v4
	v_ashrrev_i32_e32 v4, 10, v4
	v_mul_i32_i24_e32 v5, 0x400, v4
	v_sub_u32_e32 v3, v3, v5
	v_lshrrev_b32_e32 v5, 4, v3
	v_bitop3_b32 v3, v5, v3, 32 bitop3:0x6c
	v_ashrrev_i32_e32 v6, 31, v3
	v_lshrrev_b32_e32 v6, 26, v6
	v_add_u32_e32 v6, v3, v6
	v_lshlrev_b32_e32 v5, 3, v4
	v_ashrrev_i32_e32 v7, 6, v6
	v_and_b32_e32 v6, 0xc0, v6
	s_ashr_i32 s12, s0, 6
	v_and_b32_e32 v5, -16, v5
	v_lshlrev_b32_e32 v4, 5, v4
	v_sub_u32_e32 v3, v3, v6
	s_lshl_b32 s27, s12, 10
	v_add_u32_e32 v5, v7, v5
	v_and_b32_e32 v4, 32, v4
	v_ashrrev_i16_sdwa v3, v245, sext(v3) dst_sel:DWORD dst_unused:UNUSED_PAD src0_sel:DWORD src1_sel:BYTE_0
	s_add_i32 s63, s27, 0
	v_add_u32_sdwa v3, v4, sext(v3) dst_sel:DWORD dst_unused:UNUSED_PAD src0_sel:DWORD src1_sel:WORD_0
	v_lshlrev_b32_e32 v4, 10, v5
	s_add_i32 m0, s63, 0x10000
	s_ashr_i32 s1, s0, 8
	v_lshl_add_u32 v132, v3, 1, v4
	v_lshlrev_b32_e32 v3, 9, v5
	global_load_lds_dwordx4 v206, s[38:39]
	s_add_i32 m0, s63, 0x12000
	v_sub_u32_e32 v134, v132, v3
	s_add_u32 s2, s38, 0x10000
	global_load_lds_dwordx4 v134, s[38:39]
	s_addc_u32 s3, s39, 0
	s_add_i32 m0, s63, 0x14000
	s_add_i32 s64, s63, 0x2000
	global_load_lds_dwordx4 v206, s[2:3]
	s_add_i32 m0, s63, 0x16000
	s_nop 0
	global_load_lds_dwordx4 v134, s[2:3]
	s_mov_b32 m0, s63
	s_add_u32 s2, s40, 0x20000
	global_load_lds_dwordx4 v130, s[40:41]
	s_mov_b32 m0, s64
	s_addc_u32 s3, s41, 0
	s_add_i32 s65, s63, 0x4000
	global_load_lds_dwordx4 v132, s[40:41]
	s_mov_b32 m0, s65
	s_add_i32 s66, s63, 0x6000
	global_load_lds_dwordx4 v130, s[2:3]
	s_mov_b32 m0, s66
	s_cmp_eq_u32 s1, 1
	global_load_lds_dwordx4 v132, s[2:3]
	s_cselect_b64 s[2:3], -1, 0
	s_cmp_lg_u32 s1, 1
	s_cbranch_scc1 .LBB0_696
	s_barrier
	s_setprio 1

; #define PG8_GOFF(u, o) do { _Pragma("unroll") for (int _h = 0; _h < 2; ++_h) _Pragma("unroll") for (int _i = 0; _i < 2; ++_i) { const int _r = (u).pm * 256 + _h * 128 + gR[_i]; \
;         const int _tok = _r < nvalid ? rowtok[(u).pb * EROWS + _r] : 0; (o)[_h][_i] = (unsigned)(_tok * g.lda + gCc[_i]) * 2u; } } while (0)
; #define PG8_STAGE(bufoff, gbase, voff) do { _Pragma("unroll") for (int _i = 0; _i < 2; ++_i) \
;         __builtin_amdgcn_global_load_lds((const unsigned*)((const char*)(gbase) + (voff)[_i]), (LAS unsigned*)(lds + (bufoff) + ldsw + _i * 8192), 16, 0, 0); } while (0)
; #define PG8_LDA(dst, b, h) do { _Pragma("unroll") for (int m = 0; m < 4; ++m) _Pragma("unroll") for (int k = 0; k < 2; ++k) dst[m][k] = *(const LAS bf16x8*)(lds + PG8_SA(b, h) + aoff + m * 2048 + k * 1024); } while (0)
;     ...
;         const bool has_next = S.next(ui + 1, nxt);
;         const char* nA = has_next ? nxt.a : cA; const char* nB = has_next ? nxt.b : cB;
;         if constexpr (GATHER) { if (has_next) { PG8_GOFF(nxt, gN); } else {
; #pragma unroll
;             for (int _h = 0; _h < 2; ++_h)
; #pragma unroll
;                 for (int _i = 0; _i < 2; ++_i) gN[_h][_i] = gC[_h][_i]; } }
; #pragma nounroll
;         for (int t = 0; t < nt; t += 2) {
;             const bool last = (t == nt - 2);
;             const char* a1 = cA + (size_t)(t + 1) * kstep;
;             const char* a2 = last ? nA : cA + (size_t)(t + 2) * kstep; const char* b2 = last ? nB : cB + (size_t)(t + 2) * kstep;
;             const char* a3 = a2 + kstep; const char* b3 = b2 + kstep;
;             unsigned g2[2][2];
;             if constexpr (GATHER) {
; #pragma unroll
;                 for (int _h = 0; _h < 2; ++_h)
; #pragma unroll
;                     for (int _i = 0; _i < 2; ++_i) g2[_h][_i] = last ? gN[_h][_i] : gC[_h][_i]; }
;             if constexpr (SP2) {
;             PG8_LDB(B0, 0, 0); PG8_LDB(B1, 0, 1); PG8_SCHED; PG8_LDA(At, 0, 0); PG8_STAGE_A(PG8_SA(1, 1), a1, 1, gC);
;             PG8_WAIT_V(8); PG8_WAIT_L(0); PG8_BAR; PG8_MMA(0, 0, At, B0); PG8_MMA(0, 1, At, B1); PG8_BAR; PG8_SCHED;
;             PG8_LDA(At, 0, 1); PG8_STAGE(PG8_SB(0, 0), b2, voffB); PG8_STAGE(PG8_SB(0, 1), b2 + hstepB, voffB); PG8_STAGE_A(PG8_SA(0, 0), a2, 0, g2);
;             PG8_WAIT_V(8); PG8_WAIT_L(0); PG8_BAR; PG8_MMA(1, 0, At, B0); PG8_MMA(1, 1, At, B1); PG8_BAR; PG8_SCHED;
.LBB0_702:
	s_add_u32 s16, s40, s30
	s_addc_u32 s17, s41, s31
	s_add_u32 s18, s16, 0x100
	s_addc_u32 s19, s17, 0
	s_and_b64 s[14:15], s[0:1], exec
	s_cselect_b32 s55, s49, s19
	s_cselect_b32 s54, s48, s18
	s_add_u32 s14, s38, s30
	s_addc_u32 s15, s39, s31
	s_add_u32 s14, s14, 0x100
	s_addc_u32 s15, s15, 0
	s_add_i32 s22, 0, 0x10000
	s_and_b64 s[0:1], s[0:1], exec
	s_cselect_b32 s57, s51, s15
	s_cselect_b32 s56, s50, s14
	s_add_i32 s1, 0, 0x14000
	s_add_u32 s60, s16, 0x20080
	s_addc_u32 s61, s17, 0
	s_add_i32 s21, s22, s27
	s_add_i32 m0, s63, 0xc000
	s_add_i32 s34, s63, 0xe000
	s_add_i32 s18, s21, 0x2000
	v_add_u32_e32 v138, s22, v141
	s_add_u32 s58, s56, 0x10000
	ds_read_b128 v[144:147], v138
	ds_read_b128 v[148:151], v138 offset:1024
	ds_read_b128 v[152:155], v138 offset:2048
	ds_read_b128 v[156:159], v138 offset:3072
	v_add_u32_e32 v138, s1, v141
	s_addc_u32 s59, s57, 0
	s_add_i32 s20, s1, s27
	ds_read_b128 v[160:163], v138
	ds_read_b128 v[164:167], v138 offset:1024
	ds_read_b128 v[168:171], v138 offset:2048
	ds_read_b128 v[172:175], v138 offset:3072
	s_add_i32 s19, s20, 0x2000
	s_add_i32 s17, 0, 0x18000
	s_add_i32 s16, 0, 0x1c000
	s_add_u32 s30, s54, 0x20000
	s_addc_u32 s31, s55, 0
	s_add_i32 s15, s17, s27
	s_add_i32 s14, s15, 0x2000
	s_add_u32 s0, s56, 0x10080
	s_addc_u32 s1, s57, 0
	s_add_i32 s23, s16, s27
	s_add_i32 s22, s23, 0x2000
	v_lshl_add_u64 v[138:139], s[60:61], 0, v[130:131]
	ds_read_b128 v[176:179], v142
	ds_read_b128 v[180:183], v142 offset:1024
	ds_read_b128 v[184:187], v142 offset:2048
	ds_read_b128 v[188:191], v142 offset:3072
	ds_read_b128 v[192:195], v142 offset:4096
	ds_read_b128 v[196:199], v142 offset:5120
	ds_read_b128 v[200:203], v142 offset:6144
	ds_read_b128 v[216:219], v142 offset:7168
	global_load_lds_dwordx4 v[138:139], off
	v_lshl_add_u64 v[138:139], s[60:61], 0, v[132:133]
	s_mov_b32 m0, s34
	s_nop 0
	global_load_lds_dwordx4 v[138:139], off
	s_waitcnt vmcnt(8)
	s_waitcnt lgkmcnt(0)
	s_barrier
	s_waitcnt lgkmcnt(0)
	v_mfma_f32_16x16x32_bf16 v[126:129], v[144:147], v[176:179], v[126:129]
	v_mfma_f32_16x16x32_bf16 v[122:125], v[152:155], v[176:179], v[122:125]
	v_mfma_f32_16x16x32_bf16 v[118:121], v[144:147], v[184:187], v[118:121]
	v_mfma_f32_16x16x32_bf16 v[114:117], v[152:155], v[184:187], v[114:117]
	v_mfma_f32_16x16x32_bf16 v[102:105], v[144:147], v[192:195], v[102:105]
	v_mfma_f32_16x16x32_bf16 v[98:101], v[152:155], v[192:195], v[98:101]
	v_mfma_f32_16x16x32_bf16 v[86:89], v[144:147], v[200:203], v[86:89]
	v_mfma_f32_16x16x32_bf16 v[82:85], v[152:155], v[200:203], v[82:85]
	v_mfma_f32_16x16x32_bf16 v[126:129], v[148:151], v[180:183], v[126:129]
	v_mfma_f32_16x16x32_bf16 v[122:125], v[156:159], v[180:183], v[122:125]
	v_mfma_f32_16x16x32_bf16 v[118:121], v[148:151], v[188:191], v[118:121]
	v_mfma_f32_16x16x32_bf16 v[114:117], v[156:159], v[188:191], v[114:117]
	v_mfma_f32_16x16x32_bf16 v[102:105], v[148:151], v[196:199], v[102:105]
	v_mfma_f32_16x16x32_bf16 v[98:101], v[156:159], v[196:199], v[98:101]
	v_mfma_f32_16x16x32_bf16 v[86:89], v[148:151], v[216:219], v[86:89]
	v_mfma_f32_16x16x32_bf16 v[82:85], v[156:159], v[216:219], v[82:85]
	v_mfma_f32_16x16x32_bf16 v[110:113], v[160:163], v[176:179], v[110:113]
	v_mfma_f32_16x16x32_bf16 v[106:109], v[168:171], v[176:179], v[106:109]
	v_mfma_f32_16x16x32_bf16 v[94:97], v[160:163], v[184:187], v[94:97]
	v_mfma_f32_16x16x32_bf16 v[90:93], v[168:171], v[184:187], v[90:93]
	v_mfma_f32_16x16x32_bf16 v[78:81], v[160:163], v[192:195], v[78:81]
	v_mfma_f32_16x16x32_bf16 v[74:77], v[168:171], v[192:195], v[74:77]
	v_mfma_f32_16x16x32_bf16 v[70:73], v[160:163], v[200:203], v[70:73]
	v_mfma_f32_16x16x32_bf16 v[66:69], v[168:171], v[200:203], v[66:69]
	v_mfma_f32_16x16x32_bf16 v[110:113], v[164:167], v[180:183], v[110:113]
	v_mfma_f32_16x16x32_bf16 v[106:109], v[172:175], v[180:183], v[106:109]
	v_mfma_f32_16x16x32_bf16 v[94:97], v[164:167], v[188:191], v[94:97]
	v_mfma_f32_16x16x32_bf16 v[90:93], v[172:175], v[188:191], v[90:93]
	v_mfma_f32_16x16x32_bf16 v[78:81], v[164:167], v[196:199], v[78:81]
	v_mfma_f32_16x16x32_bf16 v[74:77], v[172:175], v[196:199], v[74:77]
	v_mfma_f32_16x16x32_bf16 v[70:73], v[164:167], v[216:219], v[70:73]
	v_mfma_f32_16x16x32_bf16 v[66:69], v[172:175], v[216:219], v[66:69]
	s_barrier
	s_mov_b32 m0, s21
	v_lshl_add_u64 v[138:139], s[56:57], 0, v[206:207]
	ds_read_b128 v[176:179], v142 offset:16384
	ds_read_b128 v[180:183], v142 offset:17408
	ds_read_b128 v[184:187], v142 offset:18432
	ds_read_b128 v[188:191], v142 offset:19456
	ds_read_b128 v[192:195], v142 offset:20480
	ds_read_b128 v[196:199], v142 offset:21504
	ds_read_b128 v[200:203], v142 offset:22528
	ds_read_b128 v[216:219], v142 offset:23552
	global_load_lds_dwordx4 v[138:139], off
	v_lshl_add_u64 v[204:205], s[56:57], 0, v[134:135]
	s_mov_b32 m0, s18
	v_lshl_add_u64 v[208:209], s[58:59], 0, v[206:207]
	global_load_lds_dwordx4 v[204:205], off
	s_mov_b32 m0, s20
	v_lshl_add_u64 v[210:211], s[54:55], 0, v[132:133]
	global_load_lds_dwordx4 v[208:209], off
	v_lshl_add_u64 v[208:209], s[58:59], 0, v[134:135]
	s_mov_b32 m0, s19
	s_nop 0
	global_load_lds_dwordx4 v[208:209], off
	v_lshl_add_u64 v[208:209], s[54:55], 0, v[130:131]
	s_mov_b32 m0, s63
	s_nop 0
	global_load_lds_dwordx4 v[208:209], off
	s_mov_b32 m0, s64
	s_nop 0
	global_load_lds_dwordx4 v[210:211], off
	s_waitcnt vmcnt(8)
	s_waitcnt lgkmcnt(0)
	s_barrier
; #define PG8_STAGE(bufoff, gbase, voff) do { _Pragma("unroll") for (int _i = 0; _i < 2; ++_i) \
;         __builtin_amdgcn_global_load_lds((const unsigned*)((const char*)(gbase) + (voff)[_i]), (LAS unsigned*)(lds + (bufoff) + ldsw + _i * 8192), 16, 0, 0); } while (0)
; #define PG8_STAGE_A(bufoff, kptr, half, VO) do { if constexpr (GATHER) { _Pragma("unroll") for (int _i = 0; _i < 2; ++_i) \
;         __builtin_amdgcn_global_load_lds((const unsigned*)((const char*)(kptr) + (VO)[half][_i]), (LAS unsigned*)(lds + (bufoff) + ldsw + _i * 8192), 16, 0, 0); } \
;         else { PG8_STAGE(bufoff, (kptr) + (half) * hstepA, voffA); } } while (0)
; #define PG8_LDA(dst, b, h) do { _Pragma("unroll") for (int m = 0; m < 4; ++m) _Pragma("unroll") for (int k = 0; k < 2; ++k) dst[m][k] = *(const LAS bf16x8*)(lds + PG8_SA(b, h) + aoff + m * 2048 + k * 1024); } while (0)
; #define PG8_LDB(dst, b, h) do { _Pragma("unroll") for (int n = 0; n < 2; ++n) _Pragma("unroll") for (int k = 0; k < 2; ++k) dst[n][k] = *(const LAS bf16x8*)(lds + PG8_SB(b, h) + boff + n * 2048 + k * 1024); } while (0)
; #define PG8_MMA(ai, bj, At, Bt) do { __builtin_amdgcn_s_setprio(1); _Pragma("unroll") for (int m = 0; m < 4; ++m) _Pragma("unroll") for (int n = 0; n < 2; ++n) _Pragma("unroll") for (int k = 0; k < 2; ++k) \
;         acc[ai][bj][m][n] = __builtin_amdgcn_mfma_f32_16x16x32_bf16(Bt[n][k], At[m][k], acc[ai][bj][m][n], 0, 0, 0); __builtin_amdgcn_s_setprio(0); } while (0)
; #define PG8_WAIT_V(n) asm volatile("s_waitcnt vmcnt(" #n ")" ::: "memory")
; #define PG8_WAIT_L(n) asm volatile("s_waitcnt lgkmcnt(" #n ")" ::: "memory")
; #define PG8_BAR __builtin_amdgcn_s_barrier()
; #define PG8_SCHED __builtin_amdgcn_sched_barrier(0)
;     ...
;             PG8_WAIT_V(8); PG8_WAIT_L(0); PG8_BAR; PG8_MMA(1, 0, At, B0); PG8_MMA(1, 1, At, B1); PG8_BAR; PG8_SCHED;
;             PG8_LDB(B0, 1, 0); PG8_LDB(B1, 1, 1); PG8_SCHED; PG8_LDA(At, 1, 0); PG8_STAGE_A(PG8_SA(0, 1), a2, 1, g2);
;             PG8_WAIT_V(8); PG8_WAIT_L(0); PG8_BAR; PG8_MMA(0, 0, At, B0); PG8_MMA(0, 1, At, B1); PG8_BAR; PG8_SCHED;
;             PG8_LDA(At, 1, 1); PG8_STAGE(PG8_SB(1, 0), b3, voffB); PG8_STAGE(PG8_SB(1, 1), b3 + hstepB, voffB); PG8_STAGE_A(PG8_SA(1, 0), a3, 0, g2);
	s_waitcnt lgkmcnt(0)
	v_mfma_f32_16x16x32_bf16 v[62:65], v[144:147], v[176:179], v[62:65]
	v_mfma_f32_16x16x32_bf16 v[58:61], v[152:155], v[176:179], v[58:61]
	v_mfma_f32_16x16x32_bf16 v[54:57], v[144:147], v[184:187], v[54:57]
	v_mfma_f32_16x16x32_bf16 v[50:53], v[152:155], v[184:187], v[50:53]
	v_mfma_f32_16x16x32_bf16 v[38:41], v[144:147], v[192:195], v[38:41]
	v_mfma_f32_16x16x32_bf16 v[34:37], v[152:155], v[192:195], v[34:37]
	v_mfma_f32_16x16x32_bf16 v[22:25], v[144:147], v[200:203], v[22:25]
	v_mfma_f32_16x16x32_bf16 v[18:21], v[152:155], v[200:203], v[18:21]
	v_mfma_f32_16x16x32_bf16 v[62:65], v[148:151], v[180:183], v[62:65]
	v_mfma_f32_16x16x32_bf16 v[58:61], v[156:159], v[180:183], v[58:61]
	v_mfma_f32_16x16x32_bf16 v[54:57], v[148:151], v[188:191], v[54:57]
	v_mfma_f32_16x16x32_bf16 v[50:53], v[156:159], v[188:191], v[50:53]
	v_mfma_f32_16x16x32_bf16 v[38:41], v[148:151], v[196:199], v[38:41]
	v_mfma_f32_16x16x32_bf16 v[34:37], v[156:159], v[196:199], v[34:37]
	v_mfma_f32_16x16x32_bf16 v[22:25], v[148:151], v[216:219], v[22:25]
	v_mfma_f32_16x16x32_bf16 v[18:21], v[156:159], v[216:219], v[18:21]
	v_mfma_f32_16x16x32_bf16 v[46:49], v[160:163], v[176:179], v[46:49]
	v_mfma_f32_16x16x32_bf16 v[42:45], v[168:171], v[176:179], v[42:45]
	v_mfma_f32_16x16x32_bf16 v[30:33], v[160:163], v[184:187], v[30:33]
	v_mfma_f32_16x16x32_bf16 v[26:29], v[168:171], v[184:187], v[26:29]
	v_mfma_f32_16x16x32_bf16 v[14:17], v[160:163], v[192:195], v[14:17]
	v_mfma_f32_16x16x32_bf16 v[10:13], v[168:171], v[192:195], v[10:13]
	v_mfma_f32_16x16x32_bf16 v[6:9], v[160:163], v[200:203], v[6:9]
	v_mfma_f32_16x16x32_bf16 v[2:5], v[168:171], v[200:203], v[2:5]
	v_mfma_f32_16x16x32_bf16 v[46:49], v[164:167], v[180:183], v[46:49]
	v_mfma_f32_16x16x32_bf16 v[42:45], v[172:175], v[180:183], v[42:45]
	v_mfma_f32_16x16x32_bf16 v[30:33], v[164:167], v[188:191], v[30:33]
	v_mfma_f32_16x16x32_bf16 v[26:29], v[172:175], v[188:191], v[26:29]
	v_mfma_f32_16x16x32_bf16 v[14:17], v[164:167], v[196:199], v[14:17]
	v_mfma_f32_16x16x32_bf16 v[10:13], v[172:175], v[196:199], v[10:13]
	v_mfma_f32_16x16x32_bf16 v[6:9], v[164:167], v[216:219], v[6:9]
	v_mfma_f32_16x16x32_bf16 v[2:5], v[172:175], v[216:219], v[2:5]
	s_barrier
	v_add_u32_e32 v143, s17, v141
	ds_read_b128 v[144:147], v143
	ds_read_b128 v[148:151], v143 offset:1024
	ds_read_b128 v[152:155], v143 offset:2048
	ds_read_b128 v[156:159], v143 offset:3072
	v_add_u32_e32 v143, s16, v141
	ds_read_b128 v[160:163], v143
	ds_read_b128 v[164:167], v143 offset:1024
	ds_read_b128 v[168:171], v143 offset:2048
	ds_read_b128 v[172:175], v143 offset:3072
	s_mov_b32 m0, s65
	v_lshl_add_u64 v[212:213], s[30:31], 0, v[130:131]
	ds_read_b128 v[176:179], v142 offset:32768
	ds_read_b128 v[180:183], v142 offset:33792
	ds_read_b128 v[184:187], v142 offset:34816
	ds_read_b128 v[188:191], v142 offset:35840
	ds_read_b128 v[192:195], v142 offset:36864
	ds_read_b128 v[196:199], v142 offset:37888
	ds_read_b128 v[200:203], v142 offset:38912
	ds_read_b128 v[216:219], v142 offset:39936
	global_load_lds_dwordx4 v[212:213], off
	v_lshl_add_u64 v[212:213], s[30:31], 0, v[132:133]
	s_mov_b32 m0, s66
	s_nop 0
	global_load_lds_dwordx4 v[212:213], off
	s_waitcnt vmcnt(8)
	s_waitcnt lgkmcnt(0)
	s_barrier
	s_waitcnt lgkmcnt(0)
	v_mfma_f32_16x16x32_bf16 v[126:129], v[144:147], v[176:179], v[126:129]
	v_mfma_f32_16x16x32_bf16 v[122:125], v[152:155], v[176:179], v[122:125]
	v_mfma_f32_16x16x32_bf16 v[118:121], v[144:147], v[184:187], v[118:121]
	v_mfma_f32_16x16x32_bf16 v[114:117], v[152:155], v[184:187], v[114:117]
	v_mfma_f32_16x16x32_bf16 v[102:105], v[144:147], v[192:195], v[102:105]
	v_mfma_f32_16x16x32_bf16 v[98:101], v[152:155], v[192:195], v[98:101]
	v_mfma_f32_16x16x32_bf16 v[86:89], v[144:147], v[200:203], v[86:89]
	v_mfma_f32_16x16x32_bf16 v[82:85], v[152:155], v[200:203], v[82:85]
	v_mfma_f32_16x16x32_bf16 v[126:129], v[148:151], v[180:183], v[126:129]
	v_mfma_f32_16x16x32_bf16 v[122:125], v[156:159], v[180:183], v[122:125]
	v_mfma_f32_16x16x32_bf16 v[118:121], v[148:151], v[188:191], v[118:121]
	v_mfma_f32_16x16x32_bf16 v[114:117], v[156:159], v[188:191], v[114:117]
	v_mfma_f32_16x16x32_bf16 v[102:105], v[148:151], v[196:199], v[102:105]
	v_mfma_f32_16x16x32_bf16 v[98:101], v[156:159], v[196:199], v[98:101]
	v_mfma_f32_16x16x32_bf16 v[86:89], v[148:151], v[216:219], v[86:89]
	v_mfma_f32_16x16x32_bf16 v[82:85], v[156:159], v[216:219], v[82:85]
	v_mfma_f32_16x16x32_bf16 v[110:113], v[160:163], v[176:179], v[110:113]
	v_mfma_f32_16x16x32_bf16 v[106:109], v[168:171], v[176:179], v[106:109]
	v_mfma_f32_16x16x32_bf16 v[94:97], v[160:163], v[184:187], v[94:97]
	v_mfma_f32_16x16x32_bf16 v[90:93], v[168:171], v[184:187], v[90:93]
	v_mfma_f32_16x16x32_bf16 v[78:81], v[160:163], v[192:195], v[78:81]
	v_mfma_f32_16x16x32_bf16 v[74:77], v[168:171], v[192:195], v[74:77]
	v_mfma_f32_16x16x32_bf16 v[70:73], v[160:163], v[200:203], v[70:73]
	v_mfma_f32_16x16x32_bf16 v[66:69], v[168:171], v[200:203], v[66:69]
	v_mfma_f32_16x16x32_bf16 v[110:113], v[164:167], v[180:183], v[110:113]
	v_mfma_f32_16x16x32_bf16 v[106:109], v[172:175], v[180:183], v[106:109]
	v_mfma_f32_16x16x32_bf16 v[94:97], v[164:167], v[188:191], v[94:97]
	v_mfma_f32_16x16x32_bf16 v[90:93], v[172:175], v[188:191], v[90:93]
	v_mfma_f32_16x16x32_bf16 v[78:81], v[164:167], v[196:199], v[78:81]
	v_mfma_f32_16x16x32_bf16 v[74:77], v[172:175], v[196:199], v[74:77]
	v_mfma_f32_16x16x32_bf16 v[70:73], v[164:167], v[216:219], v[70:73]
	v_mfma_f32_16x16x32_bf16 v[66:69], v[172:175], v[216:219], v[66:69]
	s_barrier
; #define PG8_STAGE(bufoff, gbase, voff) do { _Pragma("unroll") for (int _i = 0; _i < 2; ++_i) \
;         __builtin_amdgcn_global_load_lds((const unsigned*)((const char*)(gbase) + (voff)[_i]), (LAS unsigned*)(lds + (bufoff) + ldsw + _i * 8192), 16, 0, 0); } while (0)
; #define PG8_STAGE_A(bufoff, kptr, half, VO) do { if constexpr (GATHER) { _Pragma("unroll") for (int _i = 0; _i < 2; ++_i) \
;         __builtin_amdgcn_global_load_lds((const unsigned*)((const char*)(kptr) + (VO)[half][_i]), (LAS unsigned*)(lds + (bufoff) + ldsw + _i * 8192), 16, 0, 0); } \
;         else { PG8_STAGE(bufoff, (kptr) + (half) * hstepA, voffA); } } while (0)
; #define PG8_LDA(dst, b, h) do { _Pragma("unroll") for (int m = 0; m < 4; ++m) _Pragma("unroll") for (int k = 0; k < 2; ++k) dst[m][k] = *(const LAS bf16x8*)(lds + PG8_SA(b, h) + aoff + m * 2048 + k * 1024); } while (0)
; #define PG8_MMA(ai, bj, At, Bt) do { __builtin_amdgcn_s_setprio(1); _Pragma("unroll") for (int m = 0; m < 4; ++m) _Pragma("unroll") for (int n = 0; n < 2; ++n) _Pragma("unroll") for (int k = 0; k < 2; ++k) \
;         acc[ai][bj][m][n] = __builtin_amdgcn_mfma_f32_16x16x32_bf16(Bt[n][k], At[m][k], acc[ai][bj][m][n], 0, 0, 0); __builtin_amdgcn_s_setprio(0); } while (0)
; #define PG8_WAIT_V(n) asm volatile("s_waitcnt vmcnt(" #n ")" ::: "memory")
; #define PG8_WAIT_L(n) asm volatile("s_waitcnt lgkmcnt(" #n ")" ::: "memory")
; #define PG8_BAR __builtin_amdgcn_s_barrier()
; #define PG8_SCHED __builtin_amdgcn_sched_barrier(0)
;     ...
;             PG8_LDA(At, 1, 1); PG8_STAGE(PG8_SB(1, 0), b3, voffB); PG8_STAGE(PG8_SB(1, 1), b3 + hstepB, voffB); PG8_STAGE_A(PG8_SA(1, 0), a3, 0, g2);
;             PG8_WAIT_V(8); PG8_WAIT_L(0); PG8_BAR; PG8_MMA(1, 0, At, B0); PG8_MMA(1, 1, At, B1); PG8_BAR; PG8_SCHED;
;     ...
;         if constexpr (ALIGN_EPI) { if (wr == 0) PG8_BAR; }
	s_mov_b32 m0, s15
	v_lshl_add_u64 v[138:139], v[138:139], 0, s[8:9]
	ds_read_b128 v[176:179], v142 offset:49152
	ds_read_b128 v[180:183], v142 offset:50176
	ds_read_b128 v[184:187], v142 offset:51200
	ds_read_b128 v[188:191], v142 offset:52224
	ds_read_b128 v[192:195], v142 offset:53248
	ds_read_b128 v[196:199], v142 offset:54272
	ds_read_b128 v[200:203], v142 offset:55296
	ds_read_b128 v[216:219], v142 offset:56320
	global_load_lds_dwordx4 v[138:139], off
	v_lshl_add_u64 v[138:139], v[204:205], 0, s[8:9]
	s_mov_b32 m0, s14
	s_nop 0
	global_load_lds_dwordx4 v[138:139], off
	v_lshl_add_u64 v[138:139], s[0:1], 0, v[206:207]
	s_mov_b32 m0, s23
	s_nop 0
	global_load_lds_dwordx4 v[138:139], off
	v_lshl_add_u64 v[138:139], s[0:1], 0, v[134:135]
	s_mov_b32 m0, s22
	s_nop 0
	global_load_lds_dwordx4 v[138:139], off
	v_lshl_add_u64 v[138:139], v[208:209], 0, s[8:9]
	s_mov_b32 m0, s67
	s_nop 0
	global_load_lds_dwordx4 v[138:139], off
	v_lshl_add_u64 v[138:139], v[210:211], 0, s[8:9]
	s_mov_b32 m0, s68
	s_nop 0
	global_load_lds_dwordx4 v[138:139], off
	s_waitcnt vmcnt(8)
	s_waitcnt lgkmcnt(0)
	s_barrier
	s_waitcnt lgkmcnt(0)
	v_mfma_f32_16x16x32_bf16 v[62:65], v[144:147], v[176:179], v[62:65]
	v_mfma_f32_16x16x32_bf16 v[58:61], v[152:155], v[176:179], v[58:61]
	v_mfma_f32_16x16x32_bf16 v[54:57], v[144:147], v[184:187], v[54:57]
	v_mfma_f32_16x16x32_bf16 v[50:53], v[152:155], v[184:187], v[50:53]
	v_mfma_f32_16x16x32_bf16 v[38:41], v[144:147], v[192:195], v[38:41]
	v_mfma_f32_16x16x32_bf16 v[34:37], v[152:155], v[192:195], v[34:37]
	v_mfma_f32_16x16x32_bf16 v[22:25], v[144:147], v[200:203], v[22:25]
	v_mfma_f32_16x16x32_bf16 v[18:21], v[152:155], v[200:203], v[18:21]
	v_mfma_f32_16x16x32_bf16 v[62:65], v[148:151], v[180:183], v[62:65]
	v_mfma_f32_16x16x32_bf16 v[58:61], v[156:159], v[180:183], v[58:61]
	v_mfma_f32_16x16x32_bf16 v[54:57], v[148:151], v[188:191], v[54:57]
	v_mfma_f32_16x16x32_bf16 v[50:53], v[156:159], v[188:191], v[50:53]
	v_mfma_f32_16x16x32_bf16 v[38:41], v[148:151], v[196:199], v[38:41]
	v_mfma_f32_16x16x32_bf16 v[34:37], v[156:159], v[196:199], v[34:37]
	v_mfma_f32_16x16x32_bf16 v[22:25], v[148:151], v[216:219], v[22:25]
	v_mfma_f32_16x16x32_bf16 v[18:21], v[156:159], v[216:219], v[18:21]
	v_mfma_f32_16x16x32_bf16 v[46:49], v[160:163], v[176:179], v[46:49]
	v_mfma_f32_16x16x32_bf16 v[42:45], v[168:171], v[176:179], v[42:45]
	v_mfma_f32_16x16x32_bf16 v[30:33], v[160:163], v[184:187], v[30:33]
	v_mfma_f32_16x16x32_bf16 v[26:29], v[168:171], v[184:187], v[26:29]
	v_mfma_f32_16x16x32_bf16 v[14:17], v[160:163], v[192:195], v[14:17]
	v_mfma_f32_16x16x32_bf16 v[10:13], v[168:171], v[192:195], v[10:13]
	v_mfma_f32_16x16x32_bf16 v[6:9], v[160:163], v[200:203], v[6:9]
	v_mfma_f32_16x16x32_bf16 v[2:5], v[168:171], v[200:203], v[2:5]
	v_mfma_f32_16x16x32_bf16 v[46:49], v[164:167], v[180:183], v[46:49]
	v_mfma_f32_16x16x32_bf16 v[42:45], v[172:175], v[180:183], v[42:45]
	v_mfma_f32_16x16x32_bf16 v[30:33], v[164:167], v[188:191], v[30:33]
	v_mfma_f32_16x16x32_bf16 v[26:29], v[172:175], v[188:191], v[26:29]
	v_mfma_f32_16x16x32_bf16 v[14:17], v[164:167], v[196:199], v[14:17]
	v_mfma_f32_16x16x32_bf16 v[10:13], v[172:175], v[196:199], v[10:13]
	v_mfma_f32_16x16x32_bf16 v[6:9], v[164:167], v[216:219], v[6:9]
	v_mfma_f32_16x16x32_bf16 v[2:5], v[172:175], v[216:219], v[2:5]
	s_barrier
	s_andn2_b64 vcc, exec, s[24:25]
	s_mov_b64 s[0:1], -1
	s_mov_b64 s[24:25], 0
	s_mov_b64 s[30:31], 0x100
	s_cbranch_vccz .LBB0_702
	s_and_b64 vcc, exec, s[42:43]
	s_cbranch_vccz .LBB0_705
	s_barrier

; __device__ __forceinline__ int opaque_tid() { int t = threadIdx.x; asm volatile("" : "+v"(t)); return t; }
; __device__ __forceinline__ unsigned char* opaque_ptr(unsigned char* q) { long z = 0; asm volatile("" : "+s"(z)); return q + z; }
; template <bool MAIN, bool CONV>
; __device__ __forceinline__ void b_row(const Params& p, unsigned char* ws, int l, int row, int lane) {
;     ...
;     if (CONV) {
;         ca = *(const u32x4*)(pr + C_CVC + c0); ch = *(const u32x4*)(pr + C_CVH + c0); bg = *(const u32x4*)(pr + C_CVB + c0);
;         if (t > 0) { pa = *(const u32x4*)(pr - INP + C_CVC + c0); ph = *(const u32x4*)(pr - INP + C_CVH + c0); }
;         if (t < seqlen - 1) { na = *(const u32x4*)(pr + INP + C_CVC + c0); nh = *(const u32x4*)(pr + INP + C_CVH + c0); }
;         const float* cw = p.in[I_CONVW] + (size_t)l * 3 * 512 + c0;
;         cw0a = *(const f32x4*)cw; cw0b = *(const f32x4*)(cw + 4); cw1a = *(const f32x4*)(cw + 512); cw1b = *(const f32x4*)(cw + 516); cw2a = *(const f32x4*)(cw + 1024); cw2b = *(const f32x4*)(cw + 1028);
;     }
; __global__ void __launch_bounds__(512, 2) fwd(Params p) {
;     ...
;             if (G == 256) { const int j = c < 112 ? c : (c >= 208 ? 112 + (c - 208) : -1);
;                 if (j >= 0) { unsigned char* wsq = opaque_ptr(p.ws); const int t_ = opaque_tid(); const int nit = (l == 0 ? MT : NLAT) / 8;
;                     for (int it = j; it < nit; it += 160) b_row<false, true>(p, wsq, l, it * 8 + (t_ >> 6), t_ & 63); } }
.Lcv_trip:
	s_setprio 0
	v_lshl_add_u64 v[212:213], v[228:229], 0, v[206:207]
	v_add_co_u32_e32 v214, vcc, 0x1f1b9000, v212
	s_movk_i32 s0, 0x2000
	s_nop 0
	v_addc_co_u32_e32 v215, vcc, 0, v213, vcc
	global_load_dwordx4 v[96:99], v[214:215], off offset:2432
	global_load_dwordx4 v[100:103], v[214:215], off offset:1408
	global_load_dwordx4 v[104:107], v[214:215], off offset:384
	v_add_co_u32_e32 v216, vcc, 0x1f1b7000, v212
	s_nop 1
	v_addc_co_u32_e32 v217, vcc, 0, v213, vcc
	global_load_dwordx4 v[108:111], v[216:217], off offset:1920
	global_load_dwordx4 v[112:115], v[216:217], off offset:2944
	v_add_co_u32_e32 v218, vcc, 0x1f1bb000, v212
	s_nop 1
	v_addc_co_u32_e32 v219, vcc, 0, v213, vcc
	global_load_dwordx4 v[116:119], v[218:219], off offset:896
	global_load_dwordx4 v[120:123], v[218:219], off offset:1920
	v_cmp_gt_i32_e32 vcc, s0, v230
	v_mov_b32_e32 v221, 0xff
	v_mov_b32_e32 v220, 0x7ff
	s_nop 0
	v_cndmask_b32_e32 v221, v221, v220, vcc
	v_and_b32_e32 v220, v221, v230
	s_add_i32 s12, s12, 0xa0
	s_cmp_lt_i32 s12, s2
	s_cselect_b32 s0, 0x960000, 0
	s_cselect_b32 s13, 0x500, 0
	s_mov_b32 s1, 0
	v_lshl_add_u64 v[228:229], v[228:229], 0, s[0:1]
	v_add_u32_e32 v230, s13, v230
	v_lshl_add_u64 v[212:213], v[228:229], 0, v[206:207]
	v_add_co_u32_e32 v214, vcc, 0x1f1b9000, v212
	s_movk_i32 s0, 0x2000
	s_nop 0
	v_addc_co_u32_e32 v215, vcc, 0, v213, vcc
	global_load_dwordx4 v[124:127], v[214:215], off offset:2432
	global_load_dwordx4 v[128:131], v[214:215], off offset:1408
	global_load_dwordx4 v[132:135], v[214:215], off offset:384
	v_add_co_u32_e32 v216, vcc, 0x1f1b7000, v212
	s_nop 1
	v_addc_co_u32_e32 v217, vcc, 0, v213, vcc
	global_load_dwordx4 v[136:139], v[216:217], off offset:1920
	global_load_dwordx4 v[140:143], v[216:217], off offset:2944
	v_add_co_u32_e32 v218, vcc, 0x1f1bb000, v212
	s_nop 1
	v_addc_co_u32_e32 v219, vcc, 0, v213, vcc
	global_load_dwordx4 v[144:147], v[218:219], off offset:896
	global_load_dwordx4 v[148:151], v[218:219], off offset:1920
	v_cmp_gt_i32_e32 vcc, s0, v230
	v_mov_b32_e32 v223, 0xff
	v_mov_b32_e32 v222, 0x7ff
	s_nop 0
	v_cndmask_b32_e32 v223, v223, v222, vcc
	v_and_b32_e32 v222, v223, v230
	s_add_i32 s12, s12, 0xa0
	s_cmp_lt_i32 s12, s2
	s_cselect_b32 s0, 0x960000, 0
	s_cselect_b32 s13, 0x500, 0
	s_mov_b32 s1, 0
	v_lshl_add_u64 v[228:229], v[228:229], 0, s[0:1]
	v_add_u32_e32 v230, s13, v230
	v_lshl_add_u64 v[212:213], v[228:229], 0, v[206:207]
	v_add_co_u32_e32 v214, vcc, 0x1f1b9000, v212
	s_movk_i32 s0, 0x2000
	s_nop 0
	v_addc_co_u32_e32 v215, vcc, 0, v213, vcc
	global_load_dwordx4 v[152:155], v[214:215], off offset:2432
	global_load_dwordx4 v[156:159], v[214:215], off offset:1408
	global_load_dwordx4 v[160:163], v[214:215], off offset:384
	v_add_co_u32_e32 v216, vcc, 0x1f1b7000, v212
	s_nop 1
	v_addc_co_u32_e32 v217, vcc, 0, v213, vcc
	global_load_dwordx4 v[164:167], v[216:217], off offset:1920
	global_load_dwordx4 v[168:171], v[216:217], off offset:2944
	v_add_co_u32_e32 v218, vcc, 0x1f1bb000, v212
	s_nop 1
	v_addc_co_u32_e32 v219, vcc, 0, v213, vcc
	global_load_dwordx4 v[172:175], v[218:219], off offset:896
	global_load_dwordx4 v[176:179], v[218:219], off offset:1920
	v_cmp_gt_i32_e32 vcc, s0, v230
	v_mov_b32_e32 v225, 0xff
	v_mov_b32_e32 v224, 0x7ff
	s_nop 0
	v_cndmask_b32_e32 v225, v225, v224, vcc
	v_and_b32_e32 v224, v225, v230
	s_add_i32 s12, s12, 0xa0
	s_cmp_lt_i32 s12, s2
	s_cselect_b32 s0, 0x960000, 0
	s_cselect_b32 s13, 0x500, 0
	s_mov_b32 s1, 0
	v_lshl_add_u64 v[228:229], v[228:229], 0, s[0:1]
	v_add_u32_e32 v230, s13, v230
	v_lshl_add_u64 v[212:213], v[228:229], 0, v[206:207]
	v_add_co_u32_e32 v214, vcc, 0x1f1b9000, v212
	s_movk_i32 s0, 0x2000
	s_nop 0
	v_addc_co_u32_e32 v215, vcc, 0, v213, vcc
	global_load_dwordx4 v[180:183], v[214:215], off offset:2432
	global_load_dwordx4 v[184:187], v[214:215], off offset:1408
	global_load_dwordx4 v[188:191], v[214:215], off offset:384
	v_add_co_u32_e32 v216, vcc, 0x1f1b7000, v212
	s_nop 1
	v_addc_co_u32_e32 v217, vcc, 0, v213, vcc
	global_load_dwordx4 v[192:195], v[216:217], off offset:1920
	global_load_dwordx4 v[196:199], v[216:217], off offset:2944
	v_add_co_u32_e32 v218, vcc, 0x1f1bb000, v212
	s_nop 1
	v_addc_co_u32_e32 v219, vcc, 0, v213, vcc
	global_load_dwordx4 v[200:203], v[218:219], off offset:896
	global_load_dwordx4 v[208:211], v[218:219], off offset:1920
	v_cmp_gt_i32_e32 vcc, s0, v230
	v_mov_b32_e32 v227, 0xff
	v_mov_b32_e32 v226, 0x7ff
	s_nop 0
	v_cndmask_b32_e32 v227, v227, v226, vcc
	v_and_b32_e32 v226, v227, v230
	s_add_i32 s12, s12, 0xa0
	s_cmp_lt_i32 s12, s2
	s_cselect_b32 s0, 0x960000, 0
	s_cselect_b32 s13, 0x500, 0
	s_mov_b32 s1, 0
	v_lshl_add_u64 v[228:229], v[228:229], 0, s[0:1]
	v_add_u32_e32 v230, s13, v230
	s_waitcnt vmcnt(0)
; __device__ __forceinline__ unsigned cvt_pk_bf16(float lo, float hi) { const f32x2 v = {lo, hi}; const bf16x2_t b = __builtin_convertvector(v, bf16x2_t); return __builtin_bit_cast(unsigned, b); }
; __device__ __forceinline__ float bflo(unsigned w) { return __uint_as_float(w << 16); }
; __device__ __forceinline__ float bfhi(unsigned w) { return __uint_as_float(w & 0xffff0000u); }
;     #define CONV_Z(dst, a_, h_) do { \
;               dst[0] = bflo(a_.x) * bflo(h_.x); dst[1] = bfhi(a_.x) * bfhi(h_.x); dst[2] = bflo(a_.y) * bflo(h_.y); dst[3] = bfhi(a_.y) * bfhi(h_.y); \
;               dst[4] = bflo(a_.z) * bflo(h_.z); dst[5] = bfhi(a_.z) * bfhi(h_.z); dst[6] = bflo(a_.w) * bflo(h_.w); dst[7] = bfhi(a_.w) * bfhi(h_.w); } while (0)
; template <bool MAIN, bool CONV>
; __device__ __forceinline__ void b_row(const Params& p, unsigned char* ws, int l, int row, int lane) {
;     ...
;         { float zp[8], zc[8], zn[8];
;     ...
;           CONV_Z(zc, ca, ch); CONV_Z(zp, pa, ph); CONV_Z(zn, na, nh);
;     ...
;           float bgf[8] = {bflo(bg.x), bfhi(bg.x), bflo(bg.y), bfhi(bg.y), bflo(bg.z), bfhi(bg.z), bflo(bg.w), bfhi(bg.w)};
;           const float w0[8] = {cw0a[0], cw0a[1], cw0a[2], cw0a[3], cw0b[0], cw0b[1], cw0b[2], cw0b[3]}, w1[8] = {cw1a[0], cw1a[1], cw1a[2], cw1a[3], cw1b[0], cw1b[1], cw1b[2], cw1b[3]},
;                       w2[8] = {cw2a[0], cw2a[1], cw2a[2], cw2a[3], cw2b[0], cw2b[1], cw2b[2], cw2b[3]};
;           float o[8];
;     #pragma unroll
;           for (int j = 0; j < 8; ++j) o[j] = bgf[j] * (w0[j] * zp[j] + w1[j] * zc[j] + w2[j] * zn[j]);
;           u32x4 w; w.x = cvt_pk_bf16(o[0], o[1]); w.y = cvt_pk_bf16(o[2], o[3]); w.z = cvt_pk_bf16(o[4], o[5]); w.w = cvt_pk_bf16(o[6], o[7]);
;           *(u32x4*)(CAT + (size_t)row * DM + 1536 + c0) = w; }
	v_cmp_ne_u32_e32 vcc, 0, v220
	v_mov_b32_e32 v22, v96
	v_mov_b32_e32 v23, v97
	v_mov_b32_e32 v24, v98
	v_mov_b32_e32 v25, v99
	v_mov_b32_e32 v30, v100
	v_mov_b32_e32 v31, v101
	v_mov_b32_e32 v32, v102
	v_mov_b32_e32 v33, v103
	v_mov_b32_e32 v2, v104
	v_mov_b32_e32 v3, v105
	v_mov_b32_e32 v4, v106
	v_mov_b32_e32 v5, v107
	v_cndmask_b32_e32 v34, 0, v108, vcc
	v_cndmask_b32_e32 v35, 0, v109, vcc
	v_cndmask_b32_e32 v36, 0, v110, vcc
	v_cndmask_b32_e32 v37, 0, v111, vcc
	v_cndmask_b32_e32 v26, 0, v112, vcc
	v_cndmask_b32_e32 v27, 0, v113, vcc
	v_cndmask_b32_e32 v28, 0, v114, vcc
	v_cndmask_b32_e32 v29, 0, v115, vcc
	v_cmp_ne_u32_e32 vcc, v220, v221
	s_nop 1
	v_cndmask_b32_e32 v38, 0, v116, vcc
	v_cndmask_b32_e32 v39, 0, v117, vcc
	v_cndmask_b32_e32 v40, 0, v118, vcc
	v_cndmask_b32_e32 v41, 0, v119, vcc
	v_cndmask_b32_e32 v18, 0, v120, vcc
	v_cndmask_b32_e32 v19, 0, v121, vcc
	v_cndmask_b32_e32 v20, 0, v122, vcc
	v_cndmask_b32_e32 v21, 0, v123, vcc
	v_lshlrev_b32_e32 v50, 16, v30
	v_and_b32_e32 v51, 0xffff0000, v30
	v_lshlrev_b32_e32 v66, 16, v22
	v_and_b32_e32 v67, 0xffff0000, v22
	v_lshlrev_b32_e32 v30, 16, v31
	v_and_b32_e32 v31, 0xffff0000, v31
	v_lshlrev_b32_e32 v22, 16, v23
	v_and_b32_e32 v23, 0xffff0000, v23
	v_lshlrev_b32_e32 v68, 16, v26
	v_and_b32_e32 v69, 0xffff0000, v26
	v_pk_mul_f32 v[22:23], v[30:31], v[22:23]
	v_lshlrev_b32_e32 v30, 16, v35
	v_and_b32_e32 v31, 0xffff0000, v35
	v_lshlrev_b32_e32 v26, 16, v27
	v_and_b32_e32 v27, 0xffff0000, v27
	v_pk_mul_f32 v[50:51], v[50:51], v[66:67]
	v_lshlrev_b32_e32 v66, 16, v34
	v_and_b32_e32 v67, 0xffff0000, v34
	v_lshlrev_b32_e32 v70, 16, v18
	v_and_b32_e32 v71, 0xffff0000, v18
	v_pk_mul_f32 v[26:27], v[26:27], v[30:31]
	v_lshlrev_b32_e32 v30, 16, v39
	v_and_b32_e32 v31, 0xffff0000, v39
	v_lshlrev_b32_e32 v18, 16, v19
	v_and_b32_e32 v19, 0xffff0000, v19
	v_pk_mul_f32 v[66:67], v[68:69], v[66:67]
	v_lshlrev_b32_e32 v68, 16, v38
	v_and_b32_e32 v69, 0xffff0000, v38
	v_pk_mul_f32 v[18:19], v[18:19], v[30:31]
	v_pk_mul_f32 v[68:69], v[70:71], v[68:69]
	v_lshlrev_b32_e32 v70, 16, v2
	v_and_b32_e32 v71, 0xffff0000, v2
	v_lshlrev_b32_e32 v2, 16, v3
	v_and_b32_e32 v3, 0xffff0000, v3
	v_lshlrev_b32_e32 v30, 16, v20
	v_and_b32_e32 v31, 0xffff0000, v20
	v_lshlrev_b32_e32 v20, 16, v21
	v_and_b32_e32 v21, 0xffff0000, v21
	s_addk_i32 s3, 0xa0
	s_cmp_lt_i32 s3, s2
	s_cselect_b32 s0, 0x500000, 0
	s_mov_b32 s1, 0
	v_pk_mul_f32 v[22:23], v[22:23], v[86:87]
	s_nop 0
	v_pk_fma_f32 v[22:23], v[26:27], v[78:79], v[22:23]
	v_lshlrev_b32_e32 v26, 16, v28
	v_pk_fma_f32 v[18:19], v[18:19], v[94:95], v[22:23]
	v_lshlrev_b32_e32 v22, 16, v24
	v_pk_mul_f32 v[18:19], v[18:19], v[2:3]
	v_lshlrev_b32_e32 v2, 16, v32
	v_and_b32_e32 v3, 0xffff0000, v32
	v_and_b32_e32 v23, 0xffff0000, v24
	v_pk_mul_f32 v[2:3], v[2:3], v[22:23]
	v_lshlrev_b32_e32 v22, 16, v36
	v_and_b32_e32 v23, 0xffff0000, v36
	v_and_b32_e32 v27, 0xffff0000, v28
	v_pk_mul_f32 v[22:23], v[26:27], v[22:23]
	v_lshlrev_b32_e32 v26, 16, v40
	v_and_b32_e32 v27, 0xffff0000, v40
	v_pk_mul_f32 v[2:3], v[2:3], v[80:81]
	v_pk_mul_f32 v[26:27], v[30:31], v[26:27]
	v_pk_fma_f32 v[2:3], v[22:23], v[72:73], v[2:3]
	v_lshlrev_b32_e32 v30, 16, v4
	v_and_b32_e32 v31, 0xffff0000, v4
	v_pk_fma_f32 v[2:3], v[26:27], v[88:89], v[2:3]
	v_lshlrev_b32_e32 v10, 16, v25
	v_pk_mul_f32 v[6:7], v[2:3], v[30:31]
	v_lshlrev_b32_e32 v2, 16, v33
	v_and_b32_e32 v3, 0xffff0000, v33
	v_and_b32_e32 v11, 0xffff0000, v25
	v_pk_mul_f32 v[2:3], v[2:3], v[10:11]
	v_lshlrev_b32_e32 v10, 16, v37
	v_and_b32_e32 v11, 0xffff0000, v37
	v_lshlrev_b32_e32 v14, 16, v29
	v_and_b32_e32 v15, 0xffff0000, v29
	v_pk_mul_f32 v[50:51], v[50:51], v[84:85]
	v_pk_mul_f32 v[10:11], v[14:15], v[10:11]
	v_lshlrev_b32_e32 v14, 16, v41
	v_and_b32_e32 v15, 0xffff0000, v41
	v_pk_mul_f32 v[2:3], v[2:3], v[82:83]
	v_pk_fma_f32 v[50:51], v[66:67], v[76:77], v[50:51]
	v_pk_mul_f32 v[14:15], v[20:21], v[14:15]
	v_pk_fma_f32 v[2:3], v[10:11], v[74:75], v[2:3]
	v_pk_fma_f32 v[50:51], v[68:69], v[92:93], v[50:51]
	v_lshlrev_b32_e32 v4, 16, v5
	v_and_b32_e32 v5, 0xffff0000, v5
	v_pk_fma_f32 v[2:3], v[14:15], v[90:91], v[2:3]
	v_pk_mul_f32 v[50:51], v[50:51], v[70:71]
	v_pk_mul_f32 v[8:9], v[2:3], v[4:5]
	v_cvt_pk_bf16_f32 v4, v6, v7
	v_lshl_add_u64 v[6:7], v[46:47], 0, v[206:207]
	v_lshl_add_u64 v[46:47], v[46:47], 0, s[0:1]
	v_cvt_pk_bf16_f32 v2, v50, v51
	v_cvt_pk_bf16_f32 v3, v18, v19
	v_cvt_pk_bf16_f32 v5, v8, v9
	global_store_dwordx4 v[6:7], v[2:5], off
	s_nop 1
	v_cmp_ne_u32_e32 vcc, 0, v222
	v_mov_b32_e32 v22, v124
	v_mov_b32_e32 v23, v125
	v_mov_b32_e32 v24, v126
	v_mov_b32_e32 v25, v127
	v_mov_b32_e32 v30, v128
	v_mov_b32_e32 v31, v129
	v_mov_b32_e32 v32, v130
	v_mov_b32_e32 v33, v131
	v_mov_b32_e32 v2, v132
	v_mov_b32_e32 v3, v133
	v_mov_b32_e32 v4, v134
	v_mov_b32_e32 v5, v135
	v_cndmask_b32_e32 v34, 0, v136, vcc
	v_cndmask_b32_e32 v35, 0, v137, vcc
	v_cndmask_b32_e32 v36, 0, v138, vcc
	v_cndmask_b32_e32 v37, 0, v139, vcc
	v_cndmask_b32_e32 v26, 0, v140, vcc
	v_cndmask_b32_e32 v27, 0, v141, vcc
	v_cndmask_b32_e32 v28, 0, v142, vcc
	v_cndmask_b32_e32 v29, 0, v143, vcc
	v_cmp_ne_u32_e32 vcc, v222, v223
	s_nop 1
	v_cndmask_b32_e32 v38, 0, v144, vcc
	v_cndmask_b32_e32 v39, 0, v145, vcc
	v_cndmask_b32_e32 v40, 0, v146, vcc
	v_cndmask_b32_e32 v41, 0, v147, vcc
	v_cndmask_b32_e32 v18, 0, v148, vcc
	v_cndmask_b32_e32 v19, 0, v149, vcc
	v_cndmask_b32_e32 v20, 0, v150, vcc
	v_cndmask_b32_e32 v21, 0, v151, vcc
	v_lshlrev_b32_e32 v50, 16, v30
	v_and_b32_e32 v51, 0xffff0000, v30
	v_lshlrev_b32_e32 v66, 16, v22
	v_and_b32_e32 v67, 0xffff0000, v22
	v_lshlrev_b32_e32 v30, 16, v31
	v_and_b32_e32 v31, 0xffff0000, v31
	v_lshlrev_b32_e32 v22, 16, v23
; __device__ __forceinline__ unsigned cvt_pk_bf16(float lo, float hi) { const f32x2 v = {lo, hi}; const bf16x2_t b = __builtin_convertvector(v, bf16x2_t); return __builtin_bit_cast(unsigned, b); }
; __device__ __forceinline__ float bflo(unsigned w) { return __uint_as_float(w << 16); }
; __device__ __forceinline__ float bfhi(unsigned w) { return __uint_as_float(w & 0xffff0000u); }
;     #define CONV_Z(dst, a_, h_) do { \
;               dst[0] = bflo(a_.x) * bflo(h_.x); dst[1] = bfhi(a_.x) * bfhi(h_.x); dst[2] = bflo(a_.y) * bflo(h_.y); dst[3] = bfhi(a_.y) * bfhi(h_.y); \
;               dst[4] = bflo(a_.z) * bflo(h_.z); dst[5] = bfhi(a_.z) * bfhi(h_.z); dst[6] = bflo(a_.w) * bflo(h_.w); dst[7] = bfhi(a_.w) * bfhi(h_.w); } while (0)
; template <bool MAIN, bool CONV>
; __device__ __forceinline__ void b_row(const Params& p, unsigned char* ws, int l, int row, int lane) {
;     ...
;         { float zp[8], zc[8], zn[8];
;     ...
;           CONV_Z(zc, ca, ch); CONV_Z(zp, pa, ph); CONV_Z(zn, na, nh);
;     ...
;           float bgf[8] = {bflo(bg.x), bfhi(bg.x), bflo(bg.y), bfhi(bg.y), bflo(bg.z), bfhi(bg.z), bflo(bg.w), bfhi(bg.w)};
;           const float w0[8] = {cw0a[0], cw0a[1], cw0a[2], cw0a[3], cw0b[0], cw0b[1], cw0b[2], cw0b[3]}, w1[8] = {cw1a[0], cw1a[1], cw1a[2], cw1a[3], cw1b[0], cw1b[1], cw1b[2], cw1b[3]},
;                       w2[8] = {cw2a[0], cw2a[1], cw2a[2], cw2a[3], cw2b[0], cw2b[1], cw2b[2], cw2b[3]};
;           float o[8];
;     #pragma unroll
;           for (int j = 0; j < 8; ++j) o[j] = bgf[j] * (w0[j] * zp[j] + w1[j] * zc[j] + w2[j] * zn[j]);
;           u32x4 w; w.x = cvt_pk_bf16(o[0], o[1]); w.y = cvt_pk_bf16(o[2], o[3]); w.z = cvt_pk_bf16(o[4], o[5]); w.w = cvt_pk_bf16(o[6], o[7]);
;           *(u32x4*)(CAT + (size_t)row * DM + 1536 + c0) = w; }
	v_and_b32_e32 v23, 0xffff0000, v23
	v_lshlrev_b32_e32 v68, 16, v26
	v_and_b32_e32 v69, 0xffff0000, v26
	v_pk_mul_f32 v[22:23], v[30:31], v[22:23]
	v_lshlrev_b32_e32 v30, 16, v35
	v_and_b32_e32 v31, 0xffff0000, v35
	v_lshlrev_b32_e32 v26, 16, v27
	v_and_b32_e32 v27, 0xffff0000, v27
	v_pk_mul_f32 v[50:51], v[50:51], v[66:67]
	v_lshlrev_b32_e32 v66, 16, v34
	v_and_b32_e32 v67, 0xffff0000, v34
	v_lshlrev_b32_e32 v70, 16, v18
	v_and_b32_e32 v71, 0xffff0000, v18
	v_pk_mul_f32 v[26:27], v[26:27], v[30:31]
	v_lshlrev_b32_e32 v30, 16, v39
	v_and_b32_e32 v31, 0xffff0000, v39
	v_lshlrev_b32_e32 v18, 16, v19
	v_and_b32_e32 v19, 0xffff0000, v19
	v_pk_mul_f32 v[66:67], v[68:69], v[66:67]
	v_lshlrev_b32_e32 v68, 16, v38
	v_and_b32_e32 v69, 0xffff0000, v38
	v_pk_mul_f32 v[18:19], v[18:19], v[30:31]
	v_pk_mul_f32 v[68:69], v[70:71], v[68:69]
	v_lshlrev_b32_e32 v70, 16, v2
	v_and_b32_e32 v71, 0xffff0000, v2
	v_lshlrev_b32_e32 v2, 16, v3
	v_and_b32_e32 v3, 0xffff0000, v3
	v_lshlrev_b32_e32 v30, 16, v20
	v_and_b32_e32 v31, 0xffff0000, v20
	v_lshlrev_b32_e32 v20, 16, v21
	v_and_b32_e32 v21, 0xffff0000, v21
	s_addk_i32 s3, 0xa0
	s_cmp_lt_i32 s3, s2
	s_cselect_b32 s0, 0x500000, 0
	s_mov_b32 s1, 0
	v_pk_mul_f32 v[22:23], v[22:23], v[86:87]
	s_nop 0
	v_pk_fma_f32 v[22:23], v[26:27], v[78:79], v[22:23]
	v_lshlrev_b32_e32 v26, 16, v28
	v_pk_fma_f32 v[18:19], v[18:19], v[94:95], v[22:23]
	v_lshlrev_b32_e32 v22, 16, v24
	v_pk_mul_f32 v[18:19], v[18:19], v[2:3]
	v_lshlrev_b32_e32 v2, 16, v32
	v_and_b32_e32 v3, 0xffff0000, v32
	v_and_b32_e32 v23, 0xffff0000, v24
	v_pk_mul_f32 v[2:3], v[2:3], v[22:23]
	v_lshlrev_b32_e32 v22, 16, v36
	v_and_b32_e32 v23, 0xffff0000, v36
	v_and_b32_e32 v27, 0xffff0000, v28
	v_pk_mul_f32 v[22:23], v[26:27], v[22:23]
	v_lshlrev_b32_e32 v26, 16, v40
	v_and_b32_e32 v27, 0xffff0000, v40
	v_pk_mul_f32 v[2:3], v[2:3], v[80:81]
	v_pk_mul_f32 v[26:27], v[30:31], v[26:27]
	v_pk_fma_f32 v[2:3], v[22:23], v[72:73], v[2:3]
	v_lshlrev_b32_e32 v30, 16, v4
	v_and_b32_e32 v31, 0xffff0000, v4
	v_pk_fma_f32 v[2:3], v[26:27], v[88:89], v[2:3]
	v_lshlrev_b32_e32 v10, 16, v25
	v_pk_mul_f32 v[6:7], v[2:3], v[30:31]
	v_lshlrev_b32_e32 v2, 16, v33
	v_and_b32_e32 v3, 0xffff0000, v33
	v_and_b32_e32 v11, 0xffff0000, v25
	v_pk_mul_f32 v[2:3], v[2:3], v[10:11]
	v_lshlrev_b32_e32 v10, 16, v37
	v_and_b32_e32 v11, 0xffff0000, v37
	v_lshlrev_b32_e32 v14, 16, v29
	v_and_b32_e32 v15, 0xffff0000, v29
	v_pk_mul_f32 v[50:51], v[50:51], v[84:85]
	v_pk_mul_f32 v[10:11], v[14:15], v[10:11]
	v_lshlrev_b32_e32 v14, 16, v41
	v_and_b32_e32 v15, 0xffff0000, v41
	v_pk_mul_f32 v[2:3], v[2:3], v[82:83]
	v_pk_fma_f32 v[50:51], v[66:67], v[76:77], v[50:51]
	v_pk_mul_f32 v[14:15], v[20:21], v[14:15]
	v_pk_fma_f32 v[2:3], v[10:11], v[74:75], v[2:3]
	v_pk_fma_f32 v[50:51], v[68:69], v[92:93], v[50:51]
	v_lshlrev_b32_e32 v4, 16, v5
	v_and_b32_e32 v5, 0xffff0000, v5
	v_pk_fma_f32 v[2:3], v[14:15], v[90:91], v[2:3]
	v_pk_mul_f32 v[50:51], v[50:51], v[70:71]
	v_pk_mul_f32 v[8:9], v[2:3], v[4:5]
	v_cvt_pk_bf16_f32 v4, v6, v7
	v_lshl_add_u64 v[6:7], v[46:47], 0, v[206:207]
	v_lshl_add_u64 v[46:47], v[46:47], 0, s[0:1]
	v_cvt_pk_bf16_f32 v2, v50, v51
	v_cvt_pk_bf16_f32 v3, v18, v19
	v_cvt_pk_bf16_f32 v5, v8, v9
	global_store_dwordx4 v[6:7], v[2:5], off
	s_nop 1
	v_cmp_ne_u32_e32 vcc, 0, v224
	v_mov_b32_e32 v22, v152
	v_mov_b32_e32 v23, v153
	v_mov_b32_e32 v24, v154
	v_mov_b32_e32 v25, v155
	v_mov_b32_e32 v30, v156
	v_mov_b32_e32 v31, v157
	v_mov_b32_e32 v32, v158
	v_mov_b32_e32 v33, v159
	v_mov_b32_e32 v2, v160
	v_mov_b32_e32 v3, v161
	v_mov_b32_e32 v4, v162
	v_mov_b32_e32 v5, v163
	v_cndmask_b32_e32 v34, 0, v164, vcc
	v_cndmask_b32_e32 v35, 0, v165, vcc
	v_cndmask_b32_e32 v36, 0, v166, vcc
	v_cndmask_b32_e32 v37, 0, v167, vcc
	v_cndmask_b32_e32 v26, 0, v168, vcc
	v_cndmask_b32_e32 v27, 0, v169, vcc
	v_cndmask_b32_e32 v28, 0, v170, vcc
	v_cndmask_b32_e32 v29, 0, v171, vcc
	v_cmp_ne_u32_e32 vcc, v224, v225
	s_nop 1
	v_cndmask_b32_e32 v38, 0, v172, vcc
	v_cndmask_b32_e32 v39, 0, v173, vcc
	v_cndmask_b32_e32 v40, 0, v174, vcc
	v_cndmask_b32_e32 v41, 0, v175, vcc
	v_cndmask_b32_e32 v18, 0, v176, vcc
	v_cndmask_b32_e32 v19, 0, v177, vcc
	v_cndmask_b32_e32 v20, 0, v178, vcc
	v_cndmask_b32_e32 v21, 0, v179, vcc
	v_lshlrev_b32_e32 v50, 16, v30
	v_and_b32_e32 v51, 0xffff0000, v30
	v_lshlrev_b32_e32 v66, 16, v22
	v_and_b32_e32 v67, 0xffff0000, v22
	v_lshlrev_b32_e32 v30, 16, v31
	v_and_b32_e32 v31, 0xffff0000, v31
	v_lshlrev_b32_e32 v22, 16, v23
	v_and_b32_e32 v23, 0xffff0000, v23
	v_lshlrev_b32_e32 v68, 16, v26
	v_and_b32_e32 v69, 0xffff0000, v26
	v_pk_mul_f32 v[22:23], v[30:31], v[22:23]
	v_lshlrev_b32_e32 v30, 16, v35
	v_and_b32_e32 v31, 0xffff0000, v35
	v_lshlrev_b32_e32 v26, 16, v27
	v_and_b32_e32 v27, 0xffff0000, v27
	v_pk_mul_f32 v[50:51], v[50:51], v[66:67]
	v_lshlrev_b32_e32 v66, 16, v34
	v_and_b32_e32 v67, 0xffff0000, v34
	v_lshlrev_b32_e32 v70, 16, v18
	v_and_b32_e32 v71, 0xffff0000, v18
	v_pk_mul_f32 v[26:27], v[26:27], v[30:31]
	v_lshlrev_b32_e32 v30, 16, v39
	v_and_b32_e32 v31, 0xffff0000, v39
	v_lshlrev_b32_e32 v18, 16, v19
	v_and_b32_e32 v19, 0xffff0000, v19
	v_pk_mul_f32 v[66:67], v[68:69], v[66:67]
	v_lshlrev_b32_e32 v68, 16, v38
	v_and_b32_e32 v69, 0xffff0000, v38
	v_pk_mul_f32 v[18:19], v[18:19], v[30:31]
	v_pk_mul_f32 v[68:69], v[70:71], v[68:69]
	v_lshlrev_b32_e32 v70, 16, v2
	v_and_b32_e32 v71, 0xffff0000, v2
	v_lshlrev_b32_e32 v2, 16, v3
	v_and_b32_e32 v3, 0xffff0000, v3
	v_lshlrev_b32_e32 v30, 16, v20
	v_and_b32_e32 v31, 0xffff0000, v20
	v_lshlrev_b32_e32 v20, 16, v21
	v_and_b32_e32 v21, 0xffff0000, v21
	s_addk_i32 s3, 0xa0
	s_cmp_lt_i32 s3, s2
	s_cselect_b32 s0, 0x500000, 0
; __device__ __forceinline__ unsigned cvt_pk_bf16(float lo, float hi) { const f32x2 v = {lo, hi}; const bf16x2_t b = __builtin_convertvector(v, bf16x2_t); return __builtin_bit_cast(unsigned, b); }
; __device__ __forceinline__ float bflo(unsigned w) { return __uint_as_float(w << 16); }
; __device__ __forceinline__ float bfhi(unsigned w) { return __uint_as_float(w & 0xffff0000u); }
;     #define CONV_Z(dst, a_, h_) do { \
;               dst[0] = bflo(a_.x) * bflo(h_.x); dst[1] = bfhi(a_.x) * bfhi(h_.x); dst[2] = bflo(a_.y) * bflo(h_.y); dst[3] = bfhi(a_.y) * bfhi(h_.y); \
;               dst[4] = bflo(a_.z) * bflo(h_.z); dst[5] = bfhi(a_.z) * bfhi(h_.z); dst[6] = bflo(a_.w) * bflo(h_.w); dst[7] = bfhi(a_.w) * bfhi(h_.w); } while (0)
; template <bool MAIN, bool CONV>
; __device__ __forceinline__ void b_row(const Params& p, unsigned char* ws, int l, int row, int lane) {
;     ...
;         { float zp[8], zc[8], zn[8];
;     ...
;           CONV_Z(zc, ca, ch); CONV_Z(zp, pa, ph); CONV_Z(zn, na, nh);
;     ...
;           float bgf[8] = {bflo(bg.x), bfhi(bg.x), bflo(bg.y), bfhi(bg.y), bflo(bg.z), bfhi(bg.z), bflo(bg.w), bfhi(bg.w)};
;           const float w0[8] = {cw0a[0], cw0a[1], cw0a[2], cw0a[3], cw0b[0], cw0b[1], cw0b[2], cw0b[3]}, w1[8] = {cw1a[0], cw1a[1], cw1a[2], cw1a[3], cw1b[0], cw1b[1], cw1b[2], cw1b[3]},
;                       w2[8] = {cw2a[0], cw2a[1], cw2a[2], cw2a[3], cw2b[0], cw2b[1], cw2b[2], cw2b[3]};
;           float o[8];
;     #pragma unroll
;           for (int j = 0; j < 8; ++j) o[j] = bgf[j] * (w0[j] * zp[j] + w1[j] * zc[j] + w2[j] * zn[j]);
;           u32x4 w; w.x = cvt_pk_bf16(o[0], o[1]); w.y = cvt_pk_bf16(o[2], o[3]); w.z = cvt_pk_bf16(o[4], o[5]); w.w = cvt_pk_bf16(o[6], o[7]);
;           *(u32x4*)(CAT + (size_t)row * DM + 1536 + c0) = w; }
	s_mov_b32 s1, 0
	v_pk_mul_f32 v[22:23], v[22:23], v[86:87]
	s_nop 0
	v_pk_fma_f32 v[22:23], v[26:27], v[78:79], v[22:23]
	v_lshlrev_b32_e32 v26, 16, v28
	v_pk_fma_f32 v[18:19], v[18:19], v[94:95], v[22:23]
	v_lshlrev_b32_e32 v22, 16, v24
	v_pk_mul_f32 v[18:19], v[18:19], v[2:3]
	v_lshlrev_b32_e32 v2, 16, v32
	v_and_b32_e32 v3, 0xffff0000, v32
	v_and_b32_e32 v23, 0xffff0000, v24
	v_pk_mul_f32 v[2:3], v[2:3], v[22:23]
	v_lshlrev_b32_e32 v22, 16, v36
	v_and_b32_e32 v23, 0xffff0000, v36
	v_and_b32_e32 v27, 0xffff0000, v28
	v_pk_mul_f32 v[22:23], v[26:27], v[22:23]
	v_lshlrev_b32_e32 v26, 16, v40
	v_and_b32_e32 v27, 0xffff0000, v40
	v_pk_mul_f32 v[2:3], v[2:3], v[80:81]
	v_pk_mul_f32 v[26:27], v[30:31], v[26:27]
	v_pk_fma_f32 v[2:3], v[22:23], v[72:73], v[2:3]
	v_lshlrev_b32_e32 v30, 16, v4
	v_and_b32_e32 v31, 0xffff0000, v4
	v_pk_fma_f32 v[2:3], v[26:27], v[88:89], v[2:3]
	v_lshlrev_b32_e32 v10, 16, v25
	v_pk_mul_f32 v[6:7], v[2:3], v[30:31]
	v_lshlrev_b32_e32 v2, 16, v33
	v_and_b32_e32 v3, 0xffff0000, v33
	v_and_b32_e32 v11, 0xffff0000, v25
	v_pk_mul_f32 v[2:3], v[2:3], v[10:11]
	v_lshlrev_b32_e32 v10, 16, v37
	v_and_b32_e32 v11, 0xffff0000, v37
	v_lshlrev_b32_e32 v14, 16, v29
	v_and_b32_e32 v15, 0xffff0000, v29
	v_pk_mul_f32 v[50:51], v[50:51], v[84:85]
	v_pk_mul_f32 v[10:11], v[14:15], v[10:11]
	v_lshlrev_b32_e32 v14, 16, v41
	v_and_b32_e32 v15, 0xffff0000, v41
	v_pk_mul_f32 v[2:3], v[2:3], v[82:83]
	v_pk_fma_f32 v[50:51], v[66:67], v[76:77], v[50:51]
	v_pk_mul_f32 v[14:15], v[20:21], v[14:15]
	v_pk_fma_f32 v[2:3], v[10:11], v[74:75], v[2:3]
	v_pk_fma_f32 v[50:51], v[68:69], v[92:93], v[50:51]
	v_lshlrev_b32_e32 v4, 16, v5
	v_and_b32_e32 v5, 0xffff0000, v5
	v_pk_fma_f32 v[2:3], v[14:15], v[90:91], v[2:3]
	v_pk_mul_f32 v[50:51], v[50:51], v[70:71]
	v_pk_mul_f32 v[8:9], v[2:3], v[4:5]
	v_cvt_pk_bf16_f32 v4, v6, v7
	v_lshl_add_u64 v[6:7], v[46:47], 0, v[206:207]
	v_lshl_add_u64 v[46:47], v[46:47], 0, s[0:1]
	v_cvt_pk_bf16_f32 v2, v50, v51
	v_cvt_pk_bf16_f32 v3, v18, v19
	v_cvt_pk_bf16_f32 v5, v8, v9
	global_store_dwordx4 v[6:7], v[2:5], off
	s_nop 1
	v_cmp_ne_u32_e32 vcc, 0, v226
	v_mov_b32_e32 v22, v180
	v_mov_b32_e32 v23, v181
	v_mov_b32_e32 v24, v182
	v_mov_b32_e32 v25, v183
	v_mov_b32_e32 v30, v184
	v_mov_b32_e32 v31, v185
	v_mov_b32_e32 v32, v186
	v_mov_b32_e32 v33, v187
	v_mov_b32_e32 v2, v188
	v_mov_b32_e32 v3, v189
	v_mov_b32_e32 v4, v190
	v_mov_b32_e32 v5, v191
	v_cndmask_b32_e32 v34, 0, v192, vcc
	v_cndmask_b32_e32 v35, 0, v193, vcc
	v_cndmask_b32_e32 v36, 0, v194, vcc
	v_cndmask_b32_e32 v37, 0, v195, vcc
	v_cndmask_b32_e32 v26, 0, v196, vcc
	v_cndmask_b32_e32 v27, 0, v197, vcc
	v_cndmask_b32_e32 v28, 0, v198, vcc
	v_cndmask_b32_e32 v29, 0, v199, vcc
	v_cmp_ne_u32_e32 vcc, v226, v227
	s_nop 1
	v_cndmask_b32_e32 v38, 0, v200, vcc
	v_cndmask_b32_e32 v39, 0, v201, vcc
	v_cndmask_b32_e32 v40, 0, v202, vcc
	v_cndmask_b32_e32 v41, 0, v203, vcc
	v_cndmask_b32_e32 v18, 0, v208, vcc
	v_cndmask_b32_e32 v19, 0, v209, vcc
	v_cndmask_b32_e32 v20, 0, v210, vcc
	v_cndmask_b32_e32 v21, 0, v211, vcc
	v_lshlrev_b32_e32 v50, 16, v30
	v_and_b32_e32 v51, 0xffff0000, v30
	v_lshlrev_b32_e32 v66, 16, v22
	v_and_b32_e32 v67, 0xffff0000, v22
	v_lshlrev_b32_e32 v30, 16, v31
	v_and_b32_e32 v31, 0xffff0000, v31
	v_lshlrev_b32_e32 v22, 16, v23
	v_and_b32_e32 v23, 0xffff0000, v23
	v_lshlrev_b32_e32 v68, 16, v26
	v_and_b32_e32 v69, 0xffff0000, v26
	v_pk_mul_f32 v[22:23], v[30:31], v[22:23]
	v_lshlrev_b32_e32 v30, 16, v35
	v_and_b32_e32 v31, 0xffff0000, v35
	v_lshlrev_b32_e32 v26, 16, v27
	v_and_b32_e32 v27, 0xffff0000, v27
	v_pk_mul_f32 v[50:51], v[50:51], v[66:67]
	v_lshlrev_b32_e32 v66, 16, v34
	v_and_b32_e32 v67, 0xffff0000, v34
	v_lshlrev_b32_e32 v70, 16, v18
	v_and_b32_e32 v71, 0xffff0000, v18
	v_pk_mul_f32 v[26:27], v[26:27], v[30:31]
	v_lshlrev_b32_e32 v30, 16, v39
	v_and_b32_e32 v31, 0xffff0000, v39
	v_lshlrev_b32_e32 v18, 16, v19
	v_and_b32_e32 v19, 0xffff0000, v19
	v_pk_mul_f32 v[66:67], v[68:69], v[66:67]
	v_lshlrev_b32_e32 v68, 16, v38
	v_and_b32_e32 v69, 0xffff0000, v38
	v_pk_mul_f32 v[18:19], v[18:19], v[30:31]
	v_pk_mul_f32 v[68:69], v[70:71], v[68:69]
	v_lshlrev_b32_e32 v70, 16, v2
	v_and_b32_e32 v71, 0xffff0000, v2
	v_lshlrev_b32_e32 v2, 16, v3
	v_and_b32_e32 v3, 0xffff0000, v3
	v_lshlrev_b32_e32 v30, 16, v20
	v_and_b32_e32 v31, 0xffff0000, v20
	v_lshlrev_b32_e32 v20, 16, v21
	v_and_b32_e32 v21, 0xffff0000, v21
	s_addk_i32 s3, 0xa0
	s_cmp_lt_i32 s3, s2
	s_cselect_b32 s0, 0x500000, 0
	s_mov_b32 s1, 0
	v_pk_mul_f32 v[22:23], v[22:23], v[86:87]
	s_nop 0
	v_pk_fma_f32 v[22:23], v[26:27], v[78:79], v[22:23]
	v_lshlrev_b32_e32 v26, 16, v28
	v_pk_fma_f32 v[18:19], v[18:19], v[94:95], v[22:23]
	v_lshlrev_b32_e32 v22, 16, v24
	v_pk_mul_f32 v[18:19], v[18:19], v[2:3]
	v_lshlrev_b32_e32 v2, 16, v32
	v_and_b32_e32 v3, 0xffff0000, v32
	v_and_b32_e32 v23, 0xffff0000, v24
	v_pk_mul_f32 v[2:3], v[2:3], v[22:23]
	v_lshlrev_b32_e32 v22, 16, v36
	v_and_b32_e32 v23, 0xffff0000, v36
	v_and_b32_e32 v27, 0xffff0000, v28
	v_pk_mul_f32 v[22:23], v[26:27], v[22:23]
	v_lshlrev_b32_e32 v26, 16, v40
	v_and_b32_e32 v27, 0xffff0000, v40
	v_pk_mul_f32 v[2:3], v[2:3], v[80:81]
	v_pk_mul_f32 v[26:27], v[30:31], v[26:27]
	v_pk_fma_f32 v[2:3], v[22:23], v[72:73], v[2:3]
	v_lshlrev_b32_e32 v30, 16, v4
	v_and_b32_e32 v31, 0xffff0000, v4
	v_pk_fma_f32 v[2:3], v[26:27], v[88:89], v[2:3]
	v_lshlrev_b32_e32 v10, 16, v25
	v_pk_mul_f32 v[6:7], v[2:3], v[30:31]
	v_lshlrev_b32_e32 v2, 16, v33
	v_and_b32_e32 v3, 0xffff0000, v33
	v_and_b32_e32 v11, 0xffff0000, v25
	v_pk_mul_f32 v[2:3], v[2:3], v[10:11]
	v_lshlrev_b32_e32 v10, 16, v37
	v_and_b32_e32 v11, 0xffff0000, v37
	v_lshlrev_b32_e32 v14, 16, v29
	v_and_b32_e32 v15, 0xffff0000, v29
	v_pk_mul_f32 v[50:51], v[50:51], v[84:85]
	v_pk_mul_f32 v[10:11], v[14:15], v[10:11]
	v_lshlrev_b32_e32 v14, 16, v41
	v_and_b32_e32 v15, 0xffff0000, v41
	v_pk_mul_f32 v[2:3], v[2:3], v[82:83]
	v_pk_fma_f32 v[50:51], v[66:67], v[76:77], v[50:51]
	v_pk_mul_f32 v[14:15], v[20:21], v[14:15]
	v_pk_fma_f32 v[2:3], v[10:11], v[74:75], v[2:3]
	v_pk_fma_f32 v[50:51], v[68:69], v[92:93], v[50:51]
	v_lshlrev_b32_e32 v4, 16, v5
	v_and_b32_e32 v5, 0xffff0000, v5
	v_pk_fma_f32 v[2:3], v[14:15], v[90:91], v[2:3]
	v_pk_mul_f32 v[50:51], v[50:51], v[70:71]
	v_pk_mul_f32 v[8:9], v[2:3], v[4:5]
	v_cvt_pk_bf16_f32 v4, v6, v7
	v_lshl_add_u64 v[6:7], v[46:47], 0, v[206:207]
	v_lshl_add_u64 v[46:47], v[46:47], 0, s[0:1]
	v_cvt_pk_bf16_f32 v2, v50, v51
	v_cvt_pk_bf16_f32 v3, v18, v19
	v_cvt_pk_bf16_f32 v5, v8, v9
	global_store_dwordx4 v[6:7], v[2:5], off
	s_nop 1
	s_cmp_lt_i32 s3, s2
	s_cbranch_scc1 .Lcv_trip

; #define LAS __attribute__((address_space(3)))
; __device__ __forceinline__ int opaque_tid() { int t = threadIdx.x; asm volatile("" : "+v"(t)); return t; }
; __device__ __forceinline__ unsigned char* opaque_ptr(unsigned char* q) { long z = 0; asm volatile("" : "+s"(z)); return q + z; }
; __device__ __forceinline__ void ph_attn_carry(const Params& p, int l, LAS unsigned char* lds) {
;     unsigned char* ws = opaque_ptr(p.ws); const int tid = opaque_tid();
;     const int natt = (l == 0) ? 288 : 256;
;     const bf16_t* QB = (const bf16_t*)(ws + WS_QB); const bf16_t* KC = (const bf16_t*)(ws + WS_KC); const bf16_t* VT = (const bf16_t*)(ws + WS_VT); bf16_t* CAT = (bf16_t*)(ws + WS_CAT);
;     unsigned ncarry = 0u;
;     for (int it = natt + (int)blockIdx.x; it < natt + 256; it += gridDim.x, ++ncarry) {
;         {
;             const int u = it - natt; const int z = u >> 7, b = (u >> 5) & 3, g = u & 31, lane = tid & 63, w = tid >> 6;
;             const f32x2 a16 = ((const f32x2*)(ws + WS_A16))[(((size_t)l * 2 + z) * 32 + g) * 64 + lane];
;             const float* EST = (const float*)(ws + WS_EST) + (size_t)g * 768 * 256 + z * 128 + lane;
;             bf16_t* UP = (bf16_t*)(ws + WS_UPK) + (size_t)g * 768 * 512 + 256 + z * 128 + lane;
;             LAS f32x2* seg = (LAS f32x2*)lds;
;             float er[18], ei[18];
; #pragma unroll
;             for (int i = 0; i < 18; ++i) { const int st = w * 18 + i; int chunk;
;                 if (z == 0) chunk = st < 16 ? (512 + b * 16 + st) : (b * 128 + (st - 16)); else chunk = st < 16 ? (512 + b * 16 + (15 - st)) : (b * 128 + (143 - st));
;                 er[i] = EST[(size_t)chunk * 256]; ei[i] = EST[(size_t)chunk * 256 + 64]; }
.LBB0_783:
	s_setprio 0
	s_cmp_gt_i32 s86, s4
	s_cselect_b64 s[0:1], -1, 0
	s_cmp_ge_i32 s4, s87
	s_cselect_b64 s[2:3], -1, 0
	s_or_b64 s[0:1], s[0:1], s[2:3]
	s_and_b64 vcc, exec, s[0:1]
	s_cbranch_vccnz .LBB0_1341
	v_readlane_b32 s0, v252, 20
	v_readlane_b32 s1, v252, 21
	s_and_b64 s[0:1], s[0:1], exec
	s_movk_i32 s0, 0x120
	s_cselect_b32 s26, s0, 0x100
	s_mov_b64 s[2:3], 0
	v_readlane_b32 s0, v253, 35
	s_add_u32 s27, s84, s2
	v_readlane_b32 s1, v253, 36
	s_addc_u32 s30, s85, s3
	s_waitcnt vmcnt(0)
	v_mov_b32_e32 v3, v0
	s_andn2_b64 vcc, exec, s[0:1]
	s_mov_b32 s24, 0
	s_cbranch_vccnz .LBB0_1223
	v_readlane_b32 s0, v252, 5
	s_add_i32 s4, s26, 0x100
	s_lshl_b32 s25, s0, 1
	s_add_i32 s31, s26, s92
	v_ashrrev_i32_e32 v28, 6, v3
	s_add_u32 s48, s27, 0x3d742000
	s_addc_u32 s49, s30, 0
	v_mul_lo_u32 v29, v28, 18
	v_and_b32_e32 v2, 63, v3
	s_add_u32 s50, s27, 0x33cf8000
	v_or_b32_e32 v32, 1, v29
	s_addc_u32 s51, s30, 0
	v_lshl_add_u32 v30, v3, 3, 0
	v_lshl_add_u32 v31, v2, 3, 0
	v_cmp_lt_i32_e64 s[36:37], 0, v28
	v_cmp_lt_i32_e64 s[38:39], 15, v32
	v_add_u32_e32 v33, 2, v29
	v_add_u32_e32 v34, 3, v29
	v_add_u32_e32 v35, 4, v29
	v_add_u32_e32 v36, 5, v29
	v_add_u32_e32 v37, 6, v29
	v_add_u32_e32 v38, 7, v29
	v_add_u32_e32 v39, 8, v29
	v_add_u32_e32 v40, 9, v29
	v_add_u32_e32 v41, 10, v29
	v_add_u32_e32 v42, 11, v29
	v_add_u32_e32 v43, 12, v29
	v_add_u32_e32 v44, 13, v29
	v_add_u32_e32 v45, 14, v29
	v_add_u32_e32 v46, 15, v29
	v_add_u32_e32 v47, 16, v29
	v_cmp_lt_i32_e64 s[40:41], -1, v28
	v_add_u32_e32 v48, 17, v29
	v_lshlrev_b32_e32 v206, 2, v2
	v_readlane_b32 s1, v252, 6
	s_branch .LBB0_788

;     __device__ __forceinline__ void init(const void* A_, const void* B_, int G_, int c_) { T.init(A_, B_, DM, DM, NLAT / 256, INP / 256, 1, 0, 0, G_, c_, 0); }
; #define PG8_STAGE(bufoff, gbase, voff) do { _Pragma("unroll") for (int _i = 0; _i < 2; ++_i) \
;         __builtin_amdgcn_global_load_lds((const unsigned*)((const char*)(gbase) + (voff)[_i]), (LAS unsigned*)(lds + (bufoff) + ldsw + _i * 8192), 16, 0, 0); } while (0)
; #define PG8_STAGE_A(bufoff, kptr, half, VO) do { if constexpr (GATHER) { _Pragma("unroll") for (int _i = 0; _i < 2; ++_i) \
;         __builtin_amdgcn_global_load_lds((const unsigned*)((const char*)(kptr) + (VO)[half][_i]), (LAS unsigned*)(lds + (bufoff) + ldsw + _i * 8192), 16, 0, 0); } \
;         else { PG8_STAGE(bufoff, (kptr) + (half) * hstepA, voffA); } } while (0)
; #define PG8_WAIT_V(n) asm volatile("s_waitcnt vmcnt(" #n ")" ::: "memory")
; #define PG8_BAR __builtin_amdgcn_s_barrier()
;     ...
;     for (int i = 0; i < 2; ++i) { int R, C; stage_rc(tid * 16 + i * 8192, R, C); const int Rb = Epi::PERM ? ((R & ~31) + perm32(R & 31)) : R;
;         voffA[i] = (unsigned)(R * g.lda + C) * 2u; voffB[i] = (unsigned)(Rb * g.ldb + C) * 2u; gR[i] = R; gCc[i] = C; }
;     ...
;     if constexpr (SP2) {
;         PG8_STAGE(PG8_SB(0, 0), cB, voffB); PG8_STAGE(PG8_SB(0, 1), cB + hstepB, voffB); PG8_STAGE_A(PG8_SA(0, 0), cA, 0, gC); PG8_STAGE_A(PG8_SA(0, 1), cA, 1, gC);
;         if (wr == 1) PG8_BAR;
;         PG8_WAIT_V(2); PG8_BAR;
;         PG8_STAGE(PG8_SB(1, 0), cB + kstep, voffB); PG8_STAGE_A(PG8_SA(1, 0), cA + kstep, 0, gC); PG8_STAGE(PG8_SB(1, 1), cB + hstepB + kstep, voffB);
;         PG8_WAIT_V(6); PG8_BAR;
; __global__ void __launch_bounds__(512, 2) fwd(Params p) {
;     ...
;             { pg8::TileSched S; S.init(ws + WS_UPK, (bf16_t*)(ws + WS_G2B) + (size_t)l * 32 * 256 * 512, 512, 512, 3, 1, 32, (size_t)768 * 512 * 2, (size_t)256 * 512 * 2, G, c, (l == 0 && G == 256) ? 32 : 0);
;               pg8::EpiS2 E{(bf16_t*)(ws + WS_GB)};
;               pg8::Unit u0; if (S.next(0, u0)) { carry_wait(p, l); pg8::gemm_phase(lds, pg8::Desc{512, 512, 512}, S, E); }
.LBB0_1310:
	s_or_b64 exec, exec, s[0:1]
	v_mov_b32_e32 v11, v0
	s_barrier
	v_readlane_b32 s0, v252, 5
	v_ashrrev_i32_e32 v3, 31, v11
	v_lshrrev_b32_e32 v3, 26, v3
	v_add_u32_e32 v3, v11, v3
	v_ashrrev_i32_e32 v10, 6, v3
	v_bfe_i32 v3, v11, 27, 1
	v_lshlrev_b32_e32 v2, 4, v11
	v_lshrrev_b32_e32 v3, 22, v3
	v_add_u32_e32 v3, v2, v3
	v_and_b32_e32 v3, 0xfffffc00, v3
	v_sub_u32_e32 v3, v2, v3
	v_lshrrev_b32_e32 v4, 4, v3
	v_bitop3_b32 v4, v4, v3, 32 bitop3:0x6c
	v_ashrrev_i32_e32 v3, 31, v3
	v_lshrrev_b32_e32 v3, 26, v3
	v_add_u32_e32 v3, v4, v3
	v_ashrrev_i32_e32 v12, 6, v3
	v_lshlrev_b32_e32 v5, 3, v10
	v_mul_i32_i24_e32 v6, 64, v12
	v_readlane_b32 s1, v252, 6
	v_and_b32_e32 v5, -16, v5
	v_sub_u32_e32 v4, v4, v6
	s_ashr_i32 s4, s26, 31
	s_lshl_b64 s[0:1], s[0:1], 23
	v_readlane_b32 s2, v253, 37
	v_add_u32_e32 v3, v12, v5
	v_lshlrev_b32_e32 v5, 5, v10
	v_ashrrev_i16_sdwa v4, v245, sext(v4) dst_sel:DWORD dst_unused:UNUSED_PAD src0_sel:DWORD src1_sel:BYTE_0
	s_add_u32 s12, s2, s0
	v_readlane_b32 s0, v253, 38
	v_and_b32_e32 v5, 32, v5
	v_bfe_i32 v13, v4, 0, 16
	s_addc_u32 s13, s0, s1
	v_and_b32_e32 v7, 3, v12
	s_mov_b32 s0, 0x3fffe0
	v_add_lshl_u32 v5, v5, v13, 1
	v_add_u32_e32 v2, 0x2000, v2
	v_lshlrev_b32_e32 v4, 1, v3
	v_lshrrev_b32_e32 v6, 2, v3
	v_and_or_b32 v7, v3, s0, v7
	v_lshl_add_u32 v130, v3, 10, v5
	v_ashrrev_i32_e32 v3, 31, v2
	v_lshrrev_b32_e32 v3, 22, v3
	v_add_u32_e32 v3, v2, v3
	v_ashrrev_i32_e32 v14, 10, v3
	v_mul_i32_i24_e32 v3, 0x400, v14
	v_sub_u32_e32 v2, v2, v3
	v_and_b32_e32 v4, 24, v4
	v_and_b32_e32 v6, 4, v6
	v_lshrrev_b32_e32 v3, 4, v2
	v_or3_b32 v4, v7, v6, v4
	v_bitop3_b32 v2, v3, v2, 32 bitop3:0x6c
	v_readfirstlane_b32 s14, v11
	v_lshl_add_u32 v132, v4, 10, v5
	v_ashrrev_i32_e32 v4, 31, v2
	v_lshrrev_b32_e32 v4, 26, v4
	s_ashr_i32 s16, s14, 6
	s_ashr_i32 s15, s14, 8
	v_lshlrev_b32_e32 v3, 3, v14
	v_add_u32_e32 v4, v2, v4
	s_lshl_b32 s27, s16, 10
	s_mul_i32 s3, s4, 0x55555556
	s_mul_hi_u32 s17, s26, 0x55555556
	v_and_b32_e32 v3, -16, v3
	v_ashrrev_i32_e32 v15, 6, v4
	s_mul_hi_u32 s2, s4, 0x55555556
	s_add_u32 s17, s3, s17
	v_add_u32_e32 v3, v15, v3
	v_and_b32_e32 v6, 3, v15
	s_mul_i32 s1, s26, 0x55555555
	s_addc_u32 s18, s2, 0
	v_and_or_b32 v6, v3, s0, v6
	s_mul_hi_u32 s0, s26, 0x55555555
	s_add_u32 s1, s1, s17
	s_addc_u32 s0, s0, 0
	s_add_u32 s0, s18, s0
	s_addc_u32 s1, 0, 0
	s_mul_i32 s18, s4, 0x55555555
	s_mul_hi_u32 s17, s4, 0x55555555
	s_add_u32 s0, s18, s0
	s_addc_u32 s1, s17, s1
	s_add_i32 s2, s2, s18
	s_add_i32 s2, s2, s3
	s_add_u32 s0, s0, s3
	s_addc_u32 s1, s1, s2
	s_lshr_b32 s2, s1, 31
	s_add_u32 s48, s0, s2
	s_addc_u32 s49, s1, 0
	s_mul_i32 s0, s49, 3
	s_mul_hi_u32 s1, s48, 3
	s_add_i32 s1, s1, s0
	s_mul_i32 s0, s48, 3
	s_sub_u32 s50, s26, s0
	s_subb_u32 s51, s4, s1
	s_mul_i32 s0, s49, 0xc0000
	s_mul_hi_u32 s1, s48, 0xc0000
	s_add_i32 s1, s1, s0
	s_mul_i32 s0, s48, 0xc0000
	v_readlane_b32 s2, v255, 17
	s_add_u32 s2, s2, s0
	v_readlane_b32 s0, v255, 18
	s_addc_u32 s3, s0, s1
	s_lshl_b64 s[0:1], s[50:51], 18
	v_and_b32_e32 v4, 0xc0, v4
	s_add_u32 s24, s2, s0
	v_sub_u32_e32 v2, v2, v4
	s_addc_u32 s25, s3, s1
	s_lshl_b64 s[0:1], s[48:49], 18
	v_ashrrev_i16_sdwa v2, v245, sext(v2) dst_sel:DWORD dst_unused:UNUSED_PAD src0_sel:DWORD src1_sel:BYTE_0
	s_add_u32 s0, s12, s0
	v_lshlrev_b32_e32 v5, 5, v14
	v_bfe_i32 v16, v2, 0, 16
	v_lshlrev_b32_e32 v2, 1, v3
	v_lshrrev_b32_e32 v4, 2, v3
	s_addc_u32 s1, s13, s1
	s_add_i32 s51, s27, 0
	v_and_b32_e32 v5, 32, v5
	v_and_b32_e32 v2, 24, v2
	v_and_b32_e32 v4, 4, v4
	s_add_i32 m0, s51, 0x10000
	v_or3_b32 v2, v6, v4, v2
	v_add_lshl_u32 v4, v5, v16, 1
	global_load_lds_dwordx4 v132, s[0:1]
	s_add_i32 m0, s51, 0x12000
	v_lshl_add_u32 v136, v2, 10, v4
	s_add_u32 s2, s0, 0x20000
	global_load_lds_dwordx4 v136, s[0:1]
	s_addc_u32 s3, s1, 0
	s_add_i32 m0, s51, 0x14000
	s_add_i32 s54, s51, 0x2000
	global_load_lds_dwordx4 v132, s[2:3]
	s_add_i32 m0, s51, 0x16000
	v_lshl_add_u32 v134, v3, 10, v4
	global_load_lds_dwordx4 v136, s[2:3]
	s_mov_b32 m0, s51
	s_add_u32 s2, s24, 0x20000
	global_load_lds_dwordx4 v130, s[24:25]
	s_mov_b32 m0, s54
	s_addc_u32 s3, s25, 0
	s_add_i32 s55, s51, 0x4000
	global_load_lds_dwordx4 v134, s[24:25]
	s_mov_b32 m0, s55
	s_add_i32 s56, s51, 0x6000
	global_load_lds_dwordx4 v130, s[2:3]
	s_mov_b32 m0, s56
	v_mov_b32_e32 v133, v207
	global_load_lds_dwordx4 v134, s[2:3]
	v_mov_b32_e32 v137, v207
	v_mov_b32_e32 v131, v207
	v_mov_b32_e32 v135, v207
	s_cmp_eq_u32 s15, 1
	v_lshl_add_u64 v[8:9], s[0:1], 0, v[132:133]
	v_lshl_add_u64 v[6:7], s[0:1], 0, v[136:137]
	v_lshl_add_u64 v[2:3], s[24:25], 0, v[130:131]
	s_cselect_b64 s[2:3], -1, 0
	s_cmp_lg_u32 s15, 1
	v_lshl_add_u64 v[4:5], s[24:25], 0, v[134:135]
	s_cbranch_scc1 .LBB0_1312
	s_barrier
	s_setprio 1

; #define PG8_STAGE(bufoff, gbase, voff) do { _Pragma("unroll") for (int _i = 0; _i < 2; ++_i) \
;         __builtin_amdgcn_global_load_lds((const unsigned*)((const char*)(gbase) + (voff)[_i]), (LAS unsigned*)(lds + (bufoff) + ldsw + _i * 8192), 16, 0, 0); } while (0)
; #define PG8_STAGE_A(bufoff, kptr, half, VO) do { if constexpr (GATHER) { _Pragma("unroll") for (int _i = 0; _i < 2; ++_i) \
;         __builtin_amdgcn_global_load_lds((const unsigned*)((const char*)(kptr) + (VO)[half][_i]), (LAS unsigned*)(lds + (bufoff) + ldsw + _i * 8192), 16, 0, 0); } \
;         else { PG8_STAGE(bufoff, (kptr) + (half) * hstepA, voffA); } } while (0)
; #define PG8_LDA(dst, b, h) do { _Pragma("unroll") for (int m = 0; m < 4; ++m) _Pragma("unroll") for (int k = 0; k < 2; ++k) dst[m][k] = *(const LAS bf16x8*)(lds + PG8_SA(b, h) + aoff + m * 2048 + k * 1024); } while (0)
; #define PG8_LDB(dst, b, h) do { _Pragma("unroll") for (int n = 0; n < 2; ++n) _Pragma("unroll") for (int k = 0; k < 2; ++k) dst[n][k] = *(const LAS bf16x8*)(lds + PG8_SB(b, h) + boff + n * 2048 + k * 1024); } while (0)
; #define PG8_WAIT_V(n) asm volatile("s_waitcnt vmcnt(" #n ")" ::: "memory")
; #define PG8_WAIT_L(n) asm volatile("s_waitcnt lgkmcnt(" #n ")" ::: "memory")
;     ...
;         for (int t = 0; t < nt; t += 2) {
;             const bool last = (t == nt - 2);
;             const char* a1 = cA + (size_t)(t + 1) * kstep;
;             const char* a2 = last ? nA : cA + (size_t)(t + 2) * kstep; const char* b2 = last ? nB : cB + (size_t)(t + 2) * kstep;
;             const char* a3 = a2 + kstep; const char* b3 = b2 + kstep;
;             unsigned g2[2][2];
;             if constexpr (GATHER) {
; #pragma unroll
;                 for (int _h = 0; _h < 2; ++_h)
; #pragma unroll
;                     for (int _i = 0; _i < 2; ++_i) g2[_h][_i] = last ? gN[_h][_i] : gC[_h][_i]; }
;             if constexpr (SP2) {
;             PG8_LDB(B0, 0, 0); PG8_LDB(B1, 0, 1); PG8_SCHED; PG8_LDA(At, 0, 0); PG8_STAGE_A(PG8_SA(1, 1), a1, 1, gC);
;             PG8_WAIT_V(8); PG8_WAIT_L(0); PG8_BAR; PG8_MMA(0, 0, At, B0); PG8_MMA(0, 1, At, B1); PG8_BAR; PG8_SCHED;
;             PG8_LDA(At, 0, 1); PG8_STAGE(PG8_SB(0, 0), b2, voffB); PG8_STAGE(PG8_SB(0, 1), b2 + hstepB, voffB); PG8_STAGE_A(PG8_SA(0, 0), a2, 0, g2);
;             PG8_WAIT_V(8); PG8_WAIT_L(0); PG8_BAR; PG8_MMA(1, 0, At, B0); PG8_MMA(1, 1, At, B1); PG8_BAR; PG8_SCHED;
.LBB0_1318:
	s_add_u32 s0, s24, 0xfffe0080
	s_addc_u32 s1, s25, -1
	s_add_i32 s17, 0, 0x10000
	s_cmp_eq_u32 s16, 4
	s_cselect_b32 s31, s45, s1
	s_cselect_b32 s30, s44, s0
	v_add_u32_e32 v147, s17, v144
	s_cselect_b32 s1, s47, s15
	s_cselect_b32 s0, s46, s14
	s_add_i32 s20, 0, 0x14000
	ds_read_b128 v[148:151], v147
	ds_read_b128 v[152:155], v147 offset:1024
	ds_read_b128 v[156:159], v147 offset:2048
	ds_read_b128 v[160:163], v147 offset:3072
	v_add_u32_e32 v147, s20, v144
	ds_read_b128 v[164:167], v147
	ds_read_b128 v[168:171], v147 offset:1024
	ds_read_b128 v[172:175], v147 offset:2048
	ds_read_b128 v[176:179], v147 offset:3072
	v_lshl_add_u64 v[204:205], s[24:25], 0, v[140:141]
	s_add_i32 m0, s51, 0xc000
	ds_read_b128 v[180:183], v146
	ds_read_b128 v[184:187], v146 offset:1024
	ds_read_b128 v[188:191], v146 offset:2048
	ds_read_b128 v[192:195], v146 offset:3072
	ds_read_b128 v[196:199], v146 offset:4096
	ds_read_b128 v[200:203], v146 offset:5120
	ds_read_b128 v[216:219], v146 offset:6144
	ds_read_b128 v[220:223], v146 offset:7168
	global_load_lds_dwordx4 v[204:205], off
	v_lshl_add_u64 v[204:205], s[24:25], 0, v[142:143]
	s_add_i32 m0, s51, 0xe000
	s_nop 0
	global_load_lds_dwordx4 v[204:205], off
	s_waitcnt vmcnt(8)
	s_waitcnt lgkmcnt(0)
	s_barrier
	s_waitcnt lgkmcnt(0)
	v_mfma_f32_16x16x32_bf16 v[126:129], v[148:151], v[180:183], v[126:129]
	v_mfma_f32_16x16x32_bf16 v[122:125], v[156:159], v[180:183], v[122:125]
	v_mfma_f32_16x16x32_bf16 v[110:113], v[148:151], v[188:191], v[110:113]
	v_mfma_f32_16x16x32_bf16 v[106:109], v[156:159], v[188:191], v[106:109]
	v_mfma_f32_16x16x32_bf16 v[94:97], v[148:151], v[196:199], v[94:97]
	v_mfma_f32_16x16x32_bf16 v[90:93], v[156:159], v[196:199], v[90:93]
	v_mfma_f32_16x16x32_bf16 v[78:81], v[148:151], v[216:219], v[78:81]
	v_mfma_f32_16x16x32_bf16 v[74:77], v[156:159], v[216:219], v[74:77]
	v_mfma_f32_16x16x32_bf16 v[126:129], v[152:155], v[184:187], v[126:129]
	v_mfma_f32_16x16x32_bf16 v[122:125], v[160:163], v[184:187], v[122:125]
	v_mfma_f32_16x16x32_bf16 v[110:113], v[152:155], v[192:195], v[110:113]
	v_mfma_f32_16x16x32_bf16 v[106:109], v[160:163], v[192:195], v[106:109]
	v_mfma_f32_16x16x32_bf16 v[94:97], v[152:155], v[200:203], v[94:97]
	v_mfma_f32_16x16x32_bf16 v[90:93], v[160:163], v[200:203], v[90:93]
	v_mfma_f32_16x16x32_bf16 v[78:81], v[152:155], v[220:223], v[78:81]
	v_mfma_f32_16x16x32_bf16 v[74:77], v[160:163], v[220:223], v[74:77]
	v_mfma_f32_16x16x32_bf16 v[118:121], v[164:167], v[180:183], v[118:121]
	v_mfma_f32_16x16x32_bf16 v[114:117], v[172:175], v[180:183], v[114:117]
	v_mfma_f32_16x16x32_bf16 v[102:105], v[164:167], v[188:191], v[102:105]
	v_mfma_f32_16x16x32_bf16 v[98:101], v[172:175], v[188:191], v[98:101]
	v_mfma_f32_16x16x32_bf16 v[86:89], v[164:167], v[196:199], v[86:89]
	v_mfma_f32_16x16x32_bf16 v[82:85], v[172:175], v[196:199], v[82:85]
	v_mfma_f32_16x16x32_bf16 v[70:73], v[164:167], v[216:219], v[70:73]
	v_mfma_f32_16x16x32_bf16 v[66:69], v[172:175], v[216:219], v[66:69]
	v_mfma_f32_16x16x32_bf16 v[118:121], v[168:171], v[184:187], v[118:121]
	v_mfma_f32_16x16x32_bf16 v[114:117], v[176:179], v[184:187], v[114:117]
	v_mfma_f32_16x16x32_bf16 v[102:105], v[168:171], v[192:195], v[102:105]
	v_mfma_f32_16x16x32_bf16 v[98:101], v[176:179], v[192:195], v[98:101]
	v_mfma_f32_16x16x32_bf16 v[86:89], v[168:171], v[200:203], v[86:89]
	v_mfma_f32_16x16x32_bf16 v[82:85], v[176:179], v[200:203], v[82:85]
	v_mfma_f32_16x16x32_bf16 v[70:73], v[168:171], v[220:223], v[70:73]
	v_mfma_f32_16x16x32_bf16 v[66:69], v[176:179], v[220:223], v[66:69]
	s_barrier
	s_add_i32 s17, s17, s27
	v_lshl_add_u64 v[204:205], s[0:1], 0, v[132:133]
	s_mov_b32 m0, s17
	ds_read_b128 v[180:183], v146 offset:16384
	ds_read_b128 v[184:187], v146 offset:17408
	ds_read_b128 v[188:191], v146 offset:18432
	ds_read_b128 v[192:195], v146 offset:19456
	ds_read_b128 v[196:199], v146 offset:20480
	ds_read_b128 v[200:203], v146 offset:21504
	ds_read_b128 v[216:219], v146 offset:22528
	ds_read_b128 v[220:223], v146 offset:23552
	global_load_lds_dwordx4 v[204:205], off
	s_add_i32 m0, s17, 0x2000
	s_add_u32 s18, s0, 0x20000
	v_lshl_add_u64 v[208:209], s[0:1], 0, v[136:137]
	s_addc_u32 s19, s1, 0
	s_add_i32 s17, s20, s27
	global_load_lds_dwordx4 v[208:209], off
	v_lshl_add_u64 v[210:211], s[18:19], 0, v[132:133]
	s_mov_b32 m0, s17
	v_lshl_add_u64 v[212:213], s[30:31], 0, v[134:135]
	global_load_lds_dwordx4 v[210:211], off
	v_lshl_add_u64 v[210:211], s[18:19], 0, v[136:137]
	s_add_i32 m0, s17, 0x2000
	s_nop 0
	global_load_lds_dwordx4 v[210:211], off
	v_lshl_add_u64 v[210:211], s[30:31], 0, v[130:131]
	s_mov_b32 m0, s51
	s_nop 0
	global_load_lds_dwordx4 v[210:211], off
	s_mov_b32 m0, s54
	s_nop 0
	global_load_lds_dwordx4 v[212:213], off
	s_waitcnt vmcnt(8)
	s_waitcnt lgkmcnt(0)
	s_barrier
; #define PG8_STAGE(bufoff, gbase, voff) do { _Pragma("unroll") for (int _i = 0; _i < 2; ++_i) \
;         __builtin_amdgcn_global_load_lds((const unsigned*)((const char*)(gbase) + (voff)[_i]), (LAS unsigned*)(lds + (bufoff) + ldsw + _i * 8192), 16, 0, 0); } while (0)
; #define PG8_STAGE_A(bufoff, kptr, half, VO) do { if constexpr (GATHER) { _Pragma("unroll") for (int _i = 0; _i < 2; ++_i) \
;         __builtin_amdgcn_global_load_lds((const unsigned*)((const char*)(kptr) + (VO)[half][_i]), (LAS unsigned*)(lds + (bufoff) + ldsw + _i * 8192), 16, 0, 0); } \
;         else { PG8_STAGE(bufoff, (kptr) + (half) * hstepA, voffA); } } while (0)
; #define PG8_WAIT_V(n) asm volatile("s_waitcnt vmcnt(" #n ")" ::: "memory")
;     ...
;         for (int t = 0; t < nt; t += 2) {
;             const bool last = (t == nt - 2);
;             const char* a1 = cA + (size_t)(t + 1) * kstep;
;             const char* a2 = last ? nA : cA + (size_t)(t + 2) * kstep; const char* b2 = last ? nB : cB + (size_t)(t + 2) * kstep;
;             const char* a3 = a2 + kstep; const char* b3 = b2 + kstep;
;             unsigned g2[2][2];
;             if constexpr (GATHER) {
; #pragma unroll
;                 for (int _h = 0; _h < 2; ++_h)
; #pragma unroll
;                     for (int _i = 0; _i < 2; ++_i) g2[_h][_i] = last ? gN[_h][_i] : gC[_h][_i]; }
;             if constexpr (SP2) {
;             PG8_LDB(B0, 0, 0); PG8_LDB(B1, 0, 1); PG8_SCHED; PG8_LDA(At, 0, 0); PG8_STAGE_A(PG8_SA(1, 1), a1, 1, gC);
;             PG8_WAIT_V(8); PG8_WAIT_L(0); PG8_BAR; PG8_MMA(0, 0, At, B0); PG8_MMA(0, 1, At, B1); PG8_BAR; PG8_SCHED;
;             PG8_LDA(At, 0, 1); PG8_STAGE(PG8_SB(0, 0), b2, voffB); PG8_STAGE(PG8_SB(0, 1), b2 + hstepB, voffB); PG8_STAGE_A(PG8_SA(0, 0), a2, 0, g2);
;             PG8_WAIT_V(8); PG8_WAIT_L(0); PG8_BAR; PG8_MMA(1, 0, At, B0); PG8_MMA(1, 1, At, B1); PG8_BAR; PG8_SCHED;
;             PG8_LDB(B0, 1, 0); PG8_LDB(B1, 1, 1); PG8_SCHED; PG8_LDA(At, 1, 0); PG8_STAGE_A(PG8_SA(0, 1), a2, 1, g2);
;             PG8_WAIT_V(8); PG8_WAIT_L(0); PG8_BAR; PG8_MMA(0, 0, At, B0); PG8_MMA(0, 1, At, B1); PG8_BAR; PG8_SCHED;
;             PG8_LDA(At, 1, 1); PG8_STAGE(PG8_SB(1, 0), b3, voffB); PG8_STAGE(PG8_SB(1, 1), b3 + hstepB, voffB); PG8_STAGE_A(PG8_SA(1, 0), a3, 0, g2);
;             PG8_WAIT_V(8); PG8_WAIT_L(0); PG8_BAR; PG8_MMA(1, 0, At, B0); PG8_MMA(1, 1, At, B1); PG8_BAR; PG8_SCHED;
	s_waitcnt lgkmcnt(0)
	v_mfma_f32_16x16x32_bf16 v[62:65], v[148:151], v[180:183], v[62:65]
	v_mfma_f32_16x16x32_bf16 v[58:61], v[156:159], v[180:183], v[58:61]
	v_mfma_f32_16x16x32_bf16 v[46:49], v[148:151], v[188:191], v[46:49]
	v_mfma_f32_16x16x32_bf16 v[42:45], v[156:159], v[188:191], v[42:45]
	v_mfma_f32_16x16x32_bf16 v[30:33], v[148:151], v[196:199], v[30:33]
	v_mfma_f32_16x16x32_bf16 v[26:29], v[156:159], v[196:199], v[26:29]
	v_mfma_f32_16x16x32_bf16 v[14:17], v[148:151], v[216:219], v[14:17]
	v_mfma_f32_16x16x32_bf16 v[10:13], v[156:159], v[216:219], v[10:13]
	v_mfma_f32_16x16x32_bf16 v[62:65], v[152:155], v[184:187], v[62:65]
	v_mfma_f32_16x16x32_bf16 v[58:61], v[160:163], v[184:187], v[58:61]
	v_mfma_f32_16x16x32_bf16 v[46:49], v[152:155], v[192:195], v[46:49]
	v_mfma_f32_16x16x32_bf16 v[42:45], v[160:163], v[192:195], v[42:45]
	v_mfma_f32_16x16x32_bf16 v[30:33], v[152:155], v[200:203], v[30:33]
	v_mfma_f32_16x16x32_bf16 v[26:29], v[160:163], v[200:203], v[26:29]
	v_mfma_f32_16x16x32_bf16 v[14:17], v[152:155], v[220:223], v[14:17]
	v_mfma_f32_16x16x32_bf16 v[10:13], v[160:163], v[220:223], v[10:13]
	v_mfma_f32_16x16x32_bf16 v[54:57], v[164:167], v[180:183], v[54:57]
	v_mfma_f32_16x16x32_bf16 v[50:53], v[172:175], v[180:183], v[50:53]
	v_mfma_f32_16x16x32_bf16 v[38:41], v[164:167], v[188:191], v[38:41]
	v_mfma_f32_16x16x32_bf16 v[34:37], v[172:175], v[188:191], v[34:37]
	v_mfma_f32_16x16x32_bf16 v[22:25], v[164:167], v[196:199], v[22:25]
	v_mfma_f32_16x16x32_bf16 v[18:21], v[172:175], v[196:199], v[18:21]
	v_mfma_f32_16x16x32_bf16 v[6:9], v[164:167], v[216:219], v[6:9]
	v_mfma_f32_16x16x32_bf16 v[2:5], v[172:175], v[216:219], v[2:5]
	v_mfma_f32_16x16x32_bf16 v[54:57], v[168:171], v[184:187], v[54:57]
	v_mfma_f32_16x16x32_bf16 v[50:53], v[176:179], v[184:187], v[50:53]
	v_mfma_f32_16x16x32_bf16 v[38:41], v[168:171], v[192:195], v[38:41]
	v_mfma_f32_16x16x32_bf16 v[34:37], v[176:179], v[192:195], v[34:37]
	v_mfma_f32_16x16x32_bf16 v[22:25], v[168:171], v[200:203], v[22:25]
	v_mfma_f32_16x16x32_bf16 v[18:21], v[176:179], v[200:203], v[18:21]
	v_mfma_f32_16x16x32_bf16 v[6:9], v[168:171], v[220:223], v[6:9]
	v_mfma_f32_16x16x32_bf16 v[2:5], v[176:179], v[220:223], v[2:5]
	s_barrier
	s_add_i32 s17, 0, 0x18000
	v_add_u32_e32 v147, s17, v144
	s_add_i32 s20, 0, 0x1c000
	ds_read_b128 v[148:151], v147
	ds_read_b128 v[152:155], v147 offset:1024
	ds_read_b128 v[156:159], v147 offset:2048
	ds_read_b128 v[160:163], v147 offset:3072
	v_add_u32_e32 v147, s20, v144
	ds_read_b128 v[164:167], v147
	ds_read_b128 v[168:171], v147 offset:1024
	ds_read_b128 v[172:175], v147 offset:2048
	ds_read_b128 v[176:179], v147 offset:3072
	s_add_u32 s18, s30, 0x20000
	s_addc_u32 s19, s31, 0
	s_mov_b32 m0, s55
	v_lshl_add_u64 v[224:225], s[18:19], 0, v[130:131]
	ds_read_b128 v[180:183], v146 offset:32768
	ds_read_b128 v[184:187], v146 offset:33792
	ds_read_b128 v[188:191], v146 offset:34816
	ds_read_b128 v[192:195], v146 offset:35840
	ds_read_b128 v[196:199], v146 offset:36864
	ds_read_b128 v[200:203], v146 offset:37888
	ds_read_b128 v[216:219], v146 offset:38912
	ds_read_b128 v[220:223], v146 offset:39936
	global_load_lds_dwordx4 v[224:225], off
	v_lshl_add_u64 v[224:225], s[18:19], 0, v[134:135]
	s_mov_b32 m0, s56
	s_nop 0
	global_load_lds_dwordx4 v[224:225], off
	s_waitcnt vmcnt(8)
	s_waitcnt lgkmcnt(0)
	s_barrier
	s_waitcnt lgkmcnt(0)
	v_mfma_f32_16x16x32_bf16 v[126:129], v[148:151], v[180:183], v[126:129]
	v_mfma_f32_16x16x32_bf16 v[122:125], v[156:159], v[180:183], v[122:125]
	v_mfma_f32_16x16x32_bf16 v[110:113], v[148:151], v[188:191], v[110:113]
	v_mfma_f32_16x16x32_bf16 v[106:109], v[156:159], v[188:191], v[106:109]
	v_mfma_f32_16x16x32_bf16 v[94:97], v[148:151], v[196:199], v[94:97]
	v_mfma_f32_16x16x32_bf16 v[90:93], v[156:159], v[196:199], v[90:93]
	v_mfma_f32_16x16x32_bf16 v[78:81], v[148:151], v[216:219], v[78:81]
	v_mfma_f32_16x16x32_bf16 v[74:77], v[156:159], v[216:219], v[74:77]
	v_mfma_f32_16x16x32_bf16 v[126:129], v[152:155], v[184:187], v[126:129]
	v_mfma_f32_16x16x32_bf16 v[122:125], v[160:163], v[184:187], v[122:125]
	v_mfma_f32_16x16x32_bf16 v[110:113], v[152:155], v[192:195], v[110:113]
	v_mfma_f32_16x16x32_bf16 v[106:109], v[160:163], v[192:195], v[106:109]
	v_mfma_f32_16x16x32_bf16 v[94:97], v[152:155], v[200:203], v[94:97]
	v_mfma_f32_16x16x32_bf16 v[90:93], v[160:163], v[200:203], v[90:93]
	v_mfma_f32_16x16x32_bf16 v[78:81], v[152:155], v[220:223], v[78:81]
	v_mfma_f32_16x16x32_bf16 v[74:77], v[160:163], v[220:223], v[74:77]
	v_mfma_f32_16x16x32_bf16 v[118:121], v[164:167], v[180:183], v[118:121]
	v_mfma_f32_16x16x32_bf16 v[114:117], v[172:175], v[180:183], v[114:117]
	v_mfma_f32_16x16x32_bf16 v[102:105], v[164:167], v[188:191], v[102:105]
	v_mfma_f32_16x16x32_bf16 v[98:101], v[172:175], v[188:191], v[98:101]
	v_mfma_f32_16x16x32_bf16 v[86:89], v[164:167], v[196:199], v[86:89]
	v_mfma_f32_16x16x32_bf16 v[82:85], v[172:175], v[196:199], v[82:85]
	v_mfma_f32_16x16x32_bf16 v[70:73], v[164:167], v[216:219], v[70:73]
	v_mfma_f32_16x16x32_bf16 v[66:69], v[172:175], v[216:219], v[66:69]
	v_mfma_f32_16x16x32_bf16 v[118:121], v[168:171], v[184:187], v[118:121]
	v_mfma_f32_16x16x32_bf16 v[114:117], v[176:179], v[184:187], v[114:117]
	v_mfma_f32_16x16x32_bf16 v[102:105], v[168:171], v[192:195], v[102:105]
	v_mfma_f32_16x16x32_bf16 v[98:101], v[176:179], v[192:195], v[98:101]
	v_mfma_f32_16x16x32_bf16 v[86:89], v[168:171], v[200:203], v[86:89]
	v_mfma_f32_16x16x32_bf16 v[82:85], v[176:179], v[200:203], v[82:85]
	v_mfma_f32_16x16x32_bf16 v[70:73], v[168:171], v[220:223], v[70:73]
	v_mfma_f32_16x16x32_bf16 v[66:69], v[176:179], v[220:223], v[66:69]
	s_barrier
; #define PG8_STAGE(bufoff, gbase, voff) do { _Pragma("unroll") for (int _i = 0; _i < 2; ++_i) \
;         __builtin_amdgcn_global_load_lds((const unsigned*)((const char*)(gbase) + (voff)[_i]), (LAS unsigned*)(lds + (bufoff) + ldsw + _i * 8192), 16, 0, 0); } while (0)
; #define PG8_STAGE_A(bufoff, kptr, half, VO) do { if constexpr (GATHER) { _Pragma("unroll") for (int _i = 0; _i < 2; ++_i) \
;         __builtin_amdgcn_global_load_lds((const unsigned*)((const char*)(kptr) + (VO)[half][_i]), (LAS unsigned*)(lds + (bufoff) + ldsw + _i * 8192), 16, 0, 0); } \
;         else { PG8_STAGE(bufoff, (kptr) + (half) * hstepA, voffA); } } while (0)
; #define PG8_WAIT_V(n) asm volatile("s_waitcnt vmcnt(" #n ")" ::: "memory")
;     ...
;         for (int t = 0; t < nt; t += 2) {
;             const bool last = (t == nt - 2);
;             const char* a1 = cA + (size_t)(t + 1) * kstep;
;             const char* a2 = last ? nA : cA + (size_t)(t + 2) * kstep; const char* b2 = last ? nB : cB + (size_t)(t + 2) * kstep;
;             const char* a3 = a2 + kstep; const char* b3 = b2 + kstep;
;             unsigned g2[2][2];
;             if constexpr (GATHER) {
; #pragma unroll
;                 for (int _h = 0; _h < 2; ++_h)
; #pragma unroll
;                     for (int _i = 0; _i < 2; ++_i) g2[_h][_i] = last ? gN[_h][_i] : gC[_h][_i]; }
;             if constexpr (SP2) {
;             PG8_LDB(B0, 0, 0); PG8_LDB(B1, 0, 1); PG8_SCHED; PG8_LDA(At, 0, 0); PG8_STAGE_A(PG8_SA(1, 1), a1, 1, gC);
;             PG8_WAIT_V(8); PG8_WAIT_L(0); PG8_BAR; PG8_MMA(0, 0, At, B0); PG8_MMA(0, 1, At, B1); PG8_BAR; PG8_SCHED;
;             PG8_LDA(At, 0, 1); PG8_STAGE(PG8_SB(0, 0), b2, voffB); PG8_STAGE(PG8_SB(0, 1), b2 + hstepB, voffB); PG8_STAGE_A(PG8_SA(0, 0), a2, 0, g2);
;             PG8_WAIT_V(8); PG8_WAIT_L(0); PG8_BAR; PG8_MMA(1, 0, At, B0); PG8_MMA(1, 1, At, B1); PG8_BAR; PG8_SCHED;
;             PG8_LDB(B0, 1, 0); PG8_LDB(B1, 1, 1); PG8_SCHED; PG8_LDA(At, 1, 0); PG8_STAGE_A(PG8_SA(0, 1), a2, 1, g2);
;             PG8_WAIT_V(8); PG8_WAIT_L(0); PG8_BAR; PG8_MMA(0, 0, At, B0); PG8_MMA(0, 1, At, B1); PG8_BAR; PG8_SCHED;
;             PG8_LDA(At, 1, 1); PG8_STAGE(PG8_SB(1, 0), b3, voffB); PG8_STAGE(PG8_SB(1, 1), b3 + hstepB, voffB); PG8_STAGE_A(PG8_SA(1, 0), a3, 0, g2);
;             PG8_WAIT_V(8); PG8_WAIT_L(0); PG8_BAR; PG8_MMA(1, 0, At, B0); PG8_MMA(1, 1, At, B1); PG8_BAR; PG8_SCHED;
	s_add_i32 s17, s17, s27
	v_lshl_add_u64 v[204:205], v[204:205], 0, s[8:9]
	s_mov_b32 m0, s17
	ds_read_b128 v[180:183], v146 offset:49152
	ds_read_b128 v[184:187], v146 offset:50176
	ds_read_b128 v[188:191], v146 offset:51200
	ds_read_b128 v[192:195], v146 offset:52224
	ds_read_b128 v[196:199], v146 offset:53248
	ds_read_b128 v[200:203], v146 offset:54272
	ds_read_b128 v[216:219], v146 offset:55296
	ds_read_b128 v[220:223], v146 offset:56320
	global_load_lds_dwordx4 v[204:205], off
	s_add_i32 m0, s17, 0x2000
	s_add_u32 s0, s0, 0x20080
	v_lshl_add_u64 v[204:205], v[208:209], 0, s[8:9]
	s_addc_u32 s1, s1, 0
	s_add_i32 s17, s20, s27
	global_load_lds_dwordx4 v[204:205], off
	v_lshl_add_u64 v[204:205], s[0:1], 0, v[132:133]
	s_mov_b32 m0, s17
	s_nop 0
	global_load_lds_dwordx4 v[204:205], off
	v_lshl_add_u64 v[204:205], s[0:1], 0, v[136:137]
	s_add_i32 m0, s17, 0x2000
	s_nop 0
	global_load_lds_dwordx4 v[204:205], off
	v_lshl_add_u64 v[204:205], v[210:211], 0, s[8:9]
	s_mov_b32 m0, s57
	s_nop 0
	global_load_lds_dwordx4 v[204:205], off
	v_lshl_add_u64 v[204:205], v[212:213], 0, s[8:9]
	s_mov_b32 m0, s58
	s_nop 0
	global_load_lds_dwordx4 v[204:205], off
	s_waitcnt vmcnt(8)
	s_waitcnt lgkmcnt(0)
	s_barrier
	s_waitcnt lgkmcnt(0)
	v_mfma_f32_16x16x32_bf16 v[62:65], v[148:151], v[180:183], v[62:65]
	v_mfma_f32_16x16x32_bf16 v[58:61], v[156:159], v[180:183], v[58:61]
	v_mfma_f32_16x16x32_bf16 v[46:49], v[148:151], v[188:191], v[46:49]
	v_mfma_f32_16x16x32_bf16 v[42:45], v[156:159], v[188:191], v[42:45]
	v_mfma_f32_16x16x32_bf16 v[30:33], v[148:151], v[196:199], v[30:33]
	v_mfma_f32_16x16x32_bf16 v[26:29], v[156:159], v[196:199], v[26:29]
	v_mfma_f32_16x16x32_bf16 v[14:17], v[148:151], v[216:219], v[14:17]
	v_mfma_f32_16x16x32_bf16 v[10:13], v[156:159], v[216:219], v[10:13]
	v_mfma_f32_16x16x32_bf16 v[62:65], v[152:155], v[184:187], v[62:65]
	v_mfma_f32_16x16x32_bf16 v[58:61], v[160:163], v[184:187], v[58:61]
	v_mfma_f32_16x16x32_bf16 v[46:49], v[152:155], v[192:195], v[46:49]
	v_mfma_f32_16x16x32_bf16 v[42:45], v[160:163], v[192:195], v[42:45]
	v_mfma_f32_16x16x32_bf16 v[30:33], v[152:155], v[200:203], v[30:33]
	v_mfma_f32_16x16x32_bf16 v[26:29], v[160:163], v[200:203], v[26:29]
	v_mfma_f32_16x16x32_bf16 v[14:17], v[152:155], v[220:223], v[14:17]
	v_mfma_f32_16x16x32_bf16 v[10:13], v[160:163], v[220:223], v[10:13]
	v_mfma_f32_16x16x32_bf16 v[54:57], v[164:167], v[180:183], v[54:57]
	v_mfma_f32_16x16x32_bf16 v[50:53], v[172:175], v[180:183], v[50:53]
	v_mfma_f32_16x16x32_bf16 v[38:41], v[164:167], v[188:191], v[38:41]
	v_mfma_f32_16x16x32_bf16 v[34:37], v[172:175], v[188:191], v[34:37]
	v_mfma_f32_16x16x32_bf16 v[22:25], v[164:167], v[196:199], v[22:25]
	v_mfma_f32_16x16x32_bf16 v[18:21], v[172:175], v[196:199], v[18:21]
	v_mfma_f32_16x16x32_bf16 v[6:9], v[164:167], v[216:219], v[6:9]
	v_mfma_f32_16x16x32_bf16 v[2:5], v[172:175], v[216:219], v[2:5]
	v_mfma_f32_16x16x32_bf16 v[54:57], v[168:171], v[184:187], v[54:57]
	v_mfma_f32_16x16x32_bf16 v[50:53], v[176:179], v[184:187], v[50:53]
	v_mfma_f32_16x16x32_bf16 v[38:41], v[168:171], v[192:195], v[38:41]
	v_mfma_f32_16x16x32_bf16 v[34:37], v[176:179], v[192:195], v[34:37]
	v_mfma_f32_16x16x32_bf16 v[22:25], v[168:171], v[200:203], v[22:25]
	v_mfma_f32_16x16x32_bf16 v[18:21], v[176:179], v[200:203], v[18:21]
	v_mfma_f32_16x16x32_bf16 v[6:9], v[168:171], v[220:223], v[6:9]
	v_mfma_f32_16x16x32_bf16 v[2:5], v[176:179], v[220:223], v[2:5]
	s_barrier
	s_add_i32 s16, s16, 2
	s_add_u32 s24, s24, 0x100
	s_addc_u32 s25, s25, 0
	s_add_u32 s14, s14, 0x100
	s_addc_u32 s15, s15, 0
	s_cmp_gt_u32 s16, 5
	s_cbranch_scc0 .LBB0_1318
	s_and_b64 vcc, exec, s[38:39]
	s_cbranch_vccz .LBB0_1321
	s_barrier

;     __device__ __forceinline__ void init(const void* A_, const void* B_, int G_, int c_) { T.init(A_, B_, DM, DM, NLAT / 256, INP / 256, 1, 0, 0, G_, c_, 0); }
; #define REPLOOP(id) for (int rep_ = 0; rep_ < NREP(id); ++rep_)
; #define REPBAR(id) do { if (rep_ + 1 < NREP(id)) xcd_barrier(bar); } while (0)
; #define SEAM(k) do { if (IN(k) && IN((k) + 1)) xcd_barrier(bar); } while (0)
; __global__ void __launch_bounds__(512, 2) fwd(Params p) {
;     ...
;             REPBAR(5); }
;         if (PSEL(6) && IN(pb + 4)) REPLOOP(6) { }
;         SEAM(pb + 4);
;         if (PSEL(7) && IN(pb + 5)) REPLOOP(7) {
;             pg8::TileSched S; S.init(ws + WS_GB, (bf16_t*)(ws + WS_WTGLU) + (size_t)l * 512 * 512, 512, 512, (l == 0 ? MT : NLAT) / 256, 2, 1, 0, 0, G, c, 0);
;             pg8::EpiGlu E{(const bf16_t*)(ws + WS_GB), p.in[I_BGLU] + l * 512, (bf16_t*)(ws + WS_CAT)};
;             if (c < (l == 0 ? 72 : 64) || G != 256) pg8::gemm_phase(lds, pg8::Desc{512, 512, 512}, S, E);
.LBB0_1391:
	s_setprio 0
	s_cmp_le_i32 s86, s4
	s_cselect_b64 s[2:3], -1, 0
	s_and_b64 s[2:3], s[2:3], s[0:1]
	s_mov_b64 s[0:1], -1
	s_and_b64 vcc, exec, s[2:3]
	s_cbranch_vccnz .LBB0_1393
	v_readlane_b32 s0, v255, 56
	s_add_i32 s4, s0, 8
	s_mov_b64 s[0:1], 0

; #define PG8_BAR __builtin_amdgcn_s_barrier()
;     __device__ __forceinline__ bool next(int i, Unit& u) const {
;         const int nwg = nM * nN; const long L = (long)i * G + c; if (L >= (long)nwg * nB) return false;
;         const int pb = (int)(L / nwg); int wgid = (int)(L % nwg);
;         { const int q = nwg / 8, r = nwg % 8, xcd = wgid % 8, off = wgid / 8; wgid = (xcd < r ? xcd * (q + 1) : r * (q + 1) + (xcd - r) * q) + off; }
;         const int nig = 8 * nN, gid = wgid / nig, fm = gid * 8, gsz = (nM - fm) < 8 ? (nM - fm) : 8;
;         u.pm = fm + ((wgid % nig) % gsz); u.pn = (wgid % nig) / gsz; u.pb = pb;
;         u.a = A + (size_t)pb * sA + (size_t)u.pm * 256 * lda * 2; u.b = B + (size_t)pb * sB + (size_t)u.pn * 256 * ldb * 2; return true;
;     const int tid = opaque_tid(), wid = __builtin_amdgcn_readfirstlane(tid >> 6), lane = tid & 63, wr = wid >> 2, wc = wid & 3, fr = lane & 15, fq = lane >> 4;
;     const int K = g.K, nt = K / BK;
;     unsigned voffA[2], voffB[2]; int gR[2], gCc[2];
; #pragma unroll
;     for (int i = 0; i < 2; ++i) { int R, C; stage_rc(tid * 16 + i * 8192, R, C); const int Rb = Epi::PERM ? ((R & ~31) + perm32(R & 31)) : R;
;         voffA[i] = (unsigned)(R * g.lda + C) * 2u; voffB[i] = (unsigned)(Rb * g.ldb + C) * 2u; gR[i] = R; gCc[i] = C; }
;     unsigned gC[2][2], gN[2][2];
;     ...
;     const size_t kstep = (size_t)(BK * 2);
;     const size_t hstepA = (size_t)HALF * g.lda * 2, hstepB = (size_t)HALF * g.ldb * 2;
;     const unsigned ldsw = (unsigned)wid * 1024u;
;     const int aoff = lds_byte(wr * 64 + fr, fq * 8), boff = lds_byte(wc * 32 + fr, fq * 8);
;     ...
;     Unit cur, nxt; int ui = 0;
;     if (!S.next(0, cur)) return;
;     f32x4 acc[2][2][4][2];
; #pragma unroll
;     for (int a = 0; a < 2; ++a)
; #pragma unroll
;         for (int b = 0; b < 2; ++b)
; #pragma unroll
;             for (int m = 0; m < 4; ++m)
; #pragma unroll
;                 for (int n = 0; n < 2; ++n) acc[a][b][m][n] = (f32x4){0.f, 0.f, 0.f, 0.f};
;     bf16x8 At[4][2], B0[2][2], B1[2][2];
;     const char* cA = cur.a; const char* cB = cur.b;
;     if constexpr (GATHER) { PG8_GOFF(cur, gC); }
;     if constexpr (SP2) {
;         PG8_STAGE(PG8_SB(0, 0), cB, voffB); PG8_STAGE(PG8_SB(0, 1), cB + hstepB, voffB); PG8_STAGE_A(PG8_SA(0, 0), cA, 0, gC); PG8_STAGE_A(PG8_SA(0, 1), cA, 1, gC);
;         if (wr == 1) PG8_BAR;
;         PG8_WAIT_V(2); PG8_BAR;
.LBB0_1430:
	s_andn2_b64 vcc, exec, s[0:1]
	s_cbranch_vccnz .LBB0_1451
	v_readlane_b32 s0, v252, 20
	v_readlane_b32 s1, v252, 21
	s_and_b64 s[0:1], s[0:1], exec
	s_cselect_b32 s56, 36, 32
	s_lshl_b32 s2, s56, 1
	s_waitcnt vmcnt(0)
	v_mov_b32_e32 v10, v0
	v_readlane_b32 s0, v252, 12
	s_cmp_le_i32 s2, s0
	v_readfirstlane_b32 s12, v10
	s_cbranch_scc1 .LBB0_1451
	v_lshlrev_b32_e32 v2, 4, v10
	v_add_u32_e32 v3, 0x2000, v2
	v_ashrrev_i32_e32 v4, 31, v3
	v_lshrrev_b32_e32 v4, 22, v4
	v_add_u32_e32 v4, v3, v4
	v_ashrrev_i32_e32 v11, 10, v4
	v_mul_i32_i24_e32 v4, 0x400, v11
	v_sub_u32_e32 v3, v3, v4
	v_lshrrev_b32_e32 v4, 4, v3
	v_bitop3_b32 v3, v4, v3, 32 bitop3:0x6c
	v_ashrrev_i32_e32 v4, 31, v3
	v_readlane_b32 s0, v252, 5
	v_lshrrev_b32_e32 v4, 26, v4
	s_ashr_i32 s14, s12, 6
	v_readlane_b32 s1, v252, 6
	v_add_u32_e32 v4, v3, v4
	v_lshlrev_b32_e32 v5, 3, v11
	s_ashr_i32 s13, s12, 8
	s_lshl_b32 s57, s14, 10
	s_lshl_b64 s[0:1], s[0:1], 19
	v_readlane_b32 s3, v253, 45
	v_ashrrev_i32_e32 v12, 6, v4
	v_and_b32_e32 v5, -16, v5
	s_add_u32 s58, s3, s0
	v_readlane_b32 s0, v253, 46
	v_add_u32_e32 v5, v12, v5
	s_addc_u32 s59, s0, s1
	v_and_b32_e32 v6, 3, v12
	s_mov_b32 s0, 0x3fffe0
	v_lshrrev_b32_e32 v7, 2, v5
	v_lshlrev_b32_e32 v8, 1, v5
	v_and_b32_e32 v4, 0xc0, v4
	v_and_or_b32 v6, v5, s0, v6
	v_and_b32_e32 v7, 4, v7
	v_and_b32_e32 v8, 24, v8
	v_sub_u32_e32 v3, v3, v4
	v_or3_b32 v6, v6, v7, v8
	v_lshlrev_b32_e32 v7, 5, v11
	v_ashrrev_i16_sdwa v3, v245, sext(v3) dst_sel:DWORD dst_unused:UNUSED_PAD src0_sel:DWORD src1_sel:BYTE_0
	v_and_b32_e32 v7, 32, v7
	v_bfe_i32 v13, v3, 0, 16
	v_add_lshl_u32 v3, v7, v13, 1
	v_lshl_add_u32 v174, v6, 10, v3
	v_lshl_add_u32 v176, v5, 10, v3
	v_bfe_i32 v3, v10, 27, 1
	v_lshrrev_b32_e32 v3, 22, v3
	v_add_u32_e32 v3, v2, v3
	v_and_b32_e32 v3, 0xfffffc00, v3
	v_sub_u32_e32 v2, v2, v3
	v_lshrrev_b32_e32 v3, 4, v2
	v_bitop3_b32 v3, v3, v2, 32 bitop3:0x6c
	v_ashrrev_i32_e32 v2, 31, v2
	v_lshrrev_b32_e32 v2, 26, v2
	v_add_u32_e32 v2, v3, v2
	v_ashrrev_i32_e32 v14, 6, v2
	v_ashrrev_i32_e32 v2, 31, v10
	v_lshrrev_b32_e32 v2, 26, v2
	v_add_u32_e32 v2, v10, v2
	v_ashrrev_i32_e32 v15, 6, v2
	v_lshlrev_b32_e32 v2, 3, v15
	v_and_b32_e32 v2, -16, v2
	v_add_u32_e32 v2, v14, v2
	v_and_b32_e32 v4, 3, v14
	v_lshrrev_b32_e32 v5, 2, v2
	v_lshlrev_b32_e32 v6, 1, v2
	v_cvt_f32_ubyte0_e32 v7, s2
	v_and_or_b32 v4, v2, s0, v4
	v_and_b32_e32 v5, 4, v5
	v_and_b32_e32 v6, 24, v6
	v_rcp_iflag_f32_e32 v7, v7
	v_or3_b32 v4, v4, v5, v6
	v_mul_i32_i24_e32 v6, 64, v14
	v_sub_u32_e32 v3, v3, v6
	v_ashrrev_i16_sdwa v3, v245, sext(v3) dst_sel:DWORD dst_unused:UNUSED_PAD src0_sel:DWORD src1_sel:BYTE_0
	v_bfe_i32 v16, v3, 0, 16
	v_mul_f32_e32 v3, 0x4f7ffffe, v7
	v_cvt_u32_f32_e32 v3, v3
	s_sub_i32 s62, 0, s2
	s_lshr_b32 s60, s56, 2
	s_add_i32 s61, s60, 1
	v_readfirstlane_b32 s0, v3
	s_mul_i32 s1, s62, s0
	s_mul_hi_u32 s1, s0, s1
	s_add_i32 s0, s0, s1
	v_readlane_b32 s1, v254, 47
	s_mul_hi_u32 s0, s1, s0
	s_mul_i32 s0, s0, s2
	s_sub_i32 s0, s1, s0
	s_sub_i32 s1, s0, s2
	s_cmp_ge_u32 s0, s2
	s_cselect_b32 s0, s1, s0
	s_sub_i32 s1, s0, s2
	s_cmp_ge_u32 s0, s2
	s_cselect_b32 s0, s1, s0
	v_readlane_b32 s1, v252, 7
	s_xor_b32 s0, s0, s1
	s_sub_i32 s0, s0, s1
	s_bfe_i32 s1, s0, 0x80000
	s_bfe_u32 s1, s1, 0x3000c
	s_add_i32 s1, s0, s1
	s_bfe_i32 s3, s1, 0x80000
	s_and_b32 s1, s1, 0xfff8
	s_sub_i32 s0, s0, s1
	s_sext_i32_i16 s3, s3
	s_bfe_i32 s1, s0, 0x80000
	s_ashr_i32 s3, s3, 3
	s_sext_i32_i16 s1, s1
	s_cmp_lt_i32 s1, 0
	s_cselect_b32 s1, s61, s60
	s_mul_i32 s0, s1, s0
	s_add_i32 s0, s0, s3
	s_bfe_i32 s1, s0, 0x80000
	s_bfe_u32 s1, s1, 0x4000b
	s_add_i32 s1, s0, s1
	s_bfe_i32 s3, s1, 0x80000
	s_sext_i32_i16 s3, s3
	s_ashr_i32 s3, s3, 4
	v_lshlrev_b32_e32 v5, 5, v15
	s_lshl_b32 s3, s3, 3
	v_and_b32_e32 v5, 32, v5
	s_sub_i32 s15, s56, s3
	s_and_b32 s1, s1, 0xfff0
	v_add_lshl_u32 v5, v5, v16, 1
	s_min_u32 s15, s15, 8
	s_sub_i32 s16, s0, s1
	v_lshl_add_u32 v206, v4, 10, v5
	s_sext_i32_i8 s0, s16
	v_cvt_f32_ubyte0_e32 v4, s15
	v_cvt_f32_i32_e32 v3, s0
	v_rcp_iflag_f32_e32 v6, v4
	v_lshl_add_u32 v178, v2, 10, v5
	s_ashr_i32 s0, s0, 30
	s_or_b32 s17, s0, 1
	v_mul_f32_e32 v2, v3, v6
	v_trunc_f32_e32 v2, v2
	v_fma_f32 v3, -v2, v4, v3
	v_cvt_i32_f32_e32 v2, v2
	v_cmp_ge_f32_e64 s[0:1], |v3|, v4
	s_and_b64 s[0:1], s[0:1], exec
	s_cselect_b32 s0, s17, 0
	v_readfirstlane_b32 s1, v2
	s_add_i32 s24, s1, s0
	s_mul_i32 s0, s24, s15
	s_sub_i32 s0, s16, s0
	s_sext_i32_i8 s0, s0
	s_add_i32 s54, s3, s0
	s_ashr_i32 s55, s54, 31
	s_lshl_b64 s[0:1], s[54:55], 18
	v_readlane_b32 s16, v252, 2
	v_readlane_b32 s17, v252, 3
	s_add_u32 s0, s16, s0
	s_addc_u32 s1, s17, s1
	s_bfe_i64 s[16:17], s[24:25], 0x80000
	s_lshl_b64 s[16:17], s[16:17], 18
	s_add_u32 s30, s58, s16
	s_addc_u32 s31, s59, s17
	s_add_i32 s55, s57, 0
	s_add_i32 m0, s55, 0x10000
	v_mov_b32_e32 v175, v207
	global_load_lds_dwordx4 v206, s[30:31]
	s_add_i32 m0, s55, 0x12000
	s_add_u32 s16, s30, 0x20000
	global_load_lds_dwordx4 v174, s[30:31]
	s_addc_u32 s17, s31, 0
	s_add_i32 m0, s55, 0x14000
	s_add_i32 s63, s55, 0x2000
	global_load_lds_dwordx4 v206, s[16:17]
	s_add_i32 m0, s55, 0x16000
	v_mov_b32_e32 v179, v207
	global_load_lds_dwordx4 v174, s[16:17]
	s_mov_b32 m0, s55
	s_add_u32 s16, s0, 0x20000
	global_load_lds_dwordx4 v178, s[0:1]
	s_mov_b32 m0, s63
	s_addc_u32 s17, s1, 0
	s_add_i32 s64, s55, 0x4000
	global_load_lds_dwordx4 v176, s[0:1]
	s_mov_b32 m0, s64
	s_add_i32 s65, s55, 0x6000
	global_load_lds_dwordx4 v178, s[16:17]
	s_mov_b32 m0, s65
	v_mov_b32_e32 v177, v207
	global_load_lds_dwordx4 v176, s[16:17]
	s_cmp_eq_u32 s13, 1
	s_mov_b32 s3, s5
	v_lshl_add_u64 v[8:9], s[30:31], 0, v[206:207]
	v_lshl_add_u64 v[6:7], s[30:31], 0, v[174:175]
	v_lshl_add_u64 v[2:3], s[0:1], 0, v[178:179]
	s_cselect_b64 s[34:35], -1, 0
	s_cmp_lg_u32 s13, 1
	v_lshl_add_u64 v[4:5], s[0:1], 0, v[176:177]
	s_cbranch_scc1 .LBB0_1434
	s_barrier
	s_setprio 1

; #define PG8_STAGE(bufoff, gbase, voff) do { _Pragma("unroll") for (int _i = 0; _i < 2; ++_i) \
;         __builtin_amdgcn_global_load_lds((const unsigned*)((const char*)(gbase) + (voff)[_i]), (LAS unsigned*)(lds + (bufoff) + ldsw + _i * 8192), 16, 0, 0); } while (0)
; #define PG8_STAGE_A(bufoff, kptr, half, VO) do { if constexpr (GATHER) { _Pragma("unroll") for (int _i = 0; _i < 2; ++_i) \
;         __builtin_amdgcn_global_load_lds((const unsigned*)((const char*)(kptr) + (VO)[half][_i]), (LAS unsigned*)(lds + (bufoff) + ldsw + _i * 8192), 16, 0, 0); } \
;         else { PG8_STAGE(bufoff, (kptr) + (half) * hstepA, voffA); } } while (0)
; #define PG8_WAIT_V(n) asm volatile("s_waitcnt vmcnt(" #n ")" ::: "memory")
;     ...
;         for (int t = 0; t < nt; t += 2) {
;             const bool last = (t == nt - 2);
;             const char* a1 = cA + (size_t)(t + 1) * kstep;
;             const char* a2 = last ? nA : cA + (size_t)(t + 2) * kstep; const char* b2 = last ? nB : cB + (size_t)(t + 2) * kstep;
;             const char* a3 = a2 + kstep; const char* b3 = b2 + kstep;
;             unsigned g2[2][2];
;             if constexpr (GATHER) {
; #pragma unroll
;                 for (int _h = 0; _h < 2; ++_h)
; #pragma unroll
;                     for (int _i = 0; _i < 2; ++_i) g2[_h][_i] = last ? gN[_h][_i] : gC[_h][_i]; }
;             if constexpr (SP2) {
;             PG8_LDB(B0, 0, 0); PG8_LDB(B1, 0, 1); PG8_SCHED; PG8_LDA(At, 0, 0); PG8_STAGE_A(PG8_SA(1, 1), a1, 1, gC);
;             PG8_WAIT_V(8); PG8_WAIT_L(0); PG8_BAR; PG8_MMA(0, 0, At, B0); PG8_MMA(0, 1, At, B1); PG8_BAR; PG8_SCHED;
;             PG8_LDA(At, 0, 1); PG8_STAGE(PG8_SB(0, 0), b2, voffB); PG8_STAGE(PG8_SB(0, 1), b2 + hstepB, voffB); PG8_STAGE_A(PG8_SA(0, 0), a2, 0, g2);
;             PG8_WAIT_V(8); PG8_WAIT_L(0); PG8_BAR; PG8_MMA(1, 0, At, B0); PG8_MMA(1, 1, At, B1); PG8_BAR; PG8_SCHED;
;             PG8_LDB(B0, 1, 0); PG8_LDB(B1, 1, 1); PG8_SCHED; PG8_LDA(At, 1, 0); PG8_STAGE_A(PG8_SA(0, 1), a2, 1, g2);
;             PG8_WAIT_V(8); PG8_WAIT_L(0); PG8_BAR; PG8_MMA(0, 0, At, B0); PG8_MMA(0, 1, At, B1); PG8_BAR; PG8_SCHED;
;             PG8_LDA(At, 1, 1); PG8_STAGE(PG8_SB(1, 0), b3, voffB); PG8_STAGE(PG8_SB(1, 1), b3 + hstepB, voffB); PG8_STAGE_A(PG8_SA(1, 0), a3, 0, g2);
;             PG8_WAIT_V(8); PG8_WAIT_L(0); PG8_BAR; PG8_MMA(1, 0, At, B0); PG8_MMA(1, 1, At, B1); PG8_BAR; PG8_SCHED;
.LBB0_1443:
	s_add_u32 s0, s24, 0xfffe0080
	s_addc_u32 s1, s25, -1
	s_add_i32 s15, 0, 0x10000
	s_cmp_eq_u32 s14, 4
	s_cselect_b32 s31, s49, s1
	s_cselect_b32 s30, s48, s0
	s_cselect_b32 s1, s51, s13
	s_cselect_b32 s0, s50, s12
	s_add_i32 s18, 0, 0x14000
	v_add_u32_e32 v62, s15, v199
	v_add_u32_e32 v150, s18, v199
	ds_read_b128 v[38:41], v62
	ds_read_b128 v[46:49], v62 offset:1024
	ds_read_b128 v[54:57], v62 offset:2048
	ds_read_b128 v[62:65], v62 offset:3072
	ds_read_b128 v[122:125], v150
	ds_read_b128 v[130:133], v150 offset:1024
	ds_read_b128 v[142:145], v150 offset:2048
	ds_read_b128 v[150:153], v150 offset:3072
	v_lshl_add_u64 v[196:197], s[24:25], 0, v[180:181]
	s_add_i32 m0, s55, 0xc000
	ds_read_b128 v[154:157], v201
	ds_read_b128 v[158:161], v201 offset:1024
	ds_read_b128 v[166:169], v201 offset:2048
	ds_read_b128 v[184:187], v201 offset:3072
	ds_read_b128 v[188:191], v201 offset:4096
	ds_read_b128 v[192:195], v201 offset:5120
	ds_read_b128 v[202:205], v201 offset:6144
	ds_read_b128 v[216:219], v201 offset:7168
	global_load_lds_dwordx4 v[196:197], off
	v_lshl_add_u64 v[196:197], s[24:25], 0, v[182:183]
	s_add_i32 m0, s55, 0xe000
	s_nop 0
	global_load_lds_dwordx4 v[196:197], off
	s_waitcnt vmcnt(8)
	s_waitcnt lgkmcnt(0)
	s_barrier
	s_waitcnt lgkmcnt(0)
	v_mfma_f32_16x16x32_bf16 v[170:173], v[38:41], v[154:157], v[170:173]
	v_mfma_f32_16x16x32_bf16 v[162:165], v[54:57], v[154:157], v[162:165]
	v_mfma_f32_16x16x32_bf16 v[134:137], v[38:41], v[166:169], v[134:137]
	v_mfma_f32_16x16x32_bf16 v[126:129], v[54:57], v[166:169], v[126:129]
	v_mfma_f32_16x16x32_bf16 v[110:113], v[38:41], v[188:191], v[110:113]
	v_mfma_f32_16x16x32_bf16 v[106:109], v[54:57], v[188:191], v[106:109]
	v_mfma_f32_16x16x32_bf16 v[94:97], v[38:41], v[202:205], v[94:97]
	v_mfma_f32_16x16x32_bf16 v[90:93], v[54:57], v[202:205], v[90:93]
	v_mfma_f32_16x16x32_bf16 v[170:173], v[46:49], v[158:161], v[170:173]
	v_mfma_f32_16x16x32_bf16 v[162:165], v[62:65], v[158:161], v[162:165]
	v_mfma_f32_16x16x32_bf16 v[134:137], v[46:49], v[184:187], v[134:137]
	v_mfma_f32_16x16x32_bf16 v[126:129], v[62:65], v[184:187], v[126:129]
	v_mfma_f32_16x16x32_bf16 v[110:113], v[46:49], v[192:195], v[110:113]
	v_mfma_f32_16x16x32_bf16 v[106:109], v[62:65], v[192:195], v[106:109]
	v_mfma_f32_16x16x32_bf16 v[94:97], v[46:49], v[216:219], v[94:97]
	v_mfma_f32_16x16x32_bf16 v[90:93], v[62:65], v[216:219], v[90:93]
	v_mfma_f32_16x16x32_bf16 v[146:149], v[122:125], v[154:157], v[146:149]
	v_mfma_f32_16x16x32_bf16 v[138:141], v[142:145], v[154:157], v[138:141]
	v_mfma_f32_16x16x32_bf16 v[118:121], v[122:125], v[166:169], v[118:121]
	v_mfma_f32_16x16x32_bf16 v[114:117], v[142:145], v[166:169], v[114:117]
	v_mfma_f32_16x16x32_bf16 v[102:105], v[122:125], v[188:191], v[102:105]
	v_mfma_f32_16x16x32_bf16 v[98:101], v[142:145], v[188:191], v[98:101]
	v_mfma_f32_16x16x32_bf16 v[86:89], v[122:125], v[202:205], v[86:89]
	v_mfma_f32_16x16x32_bf16 v[82:85], v[142:145], v[202:205], v[82:85]
	v_mfma_f32_16x16x32_bf16 v[146:149], v[130:133], v[158:161], v[146:149]
	v_mfma_f32_16x16x32_bf16 v[138:141], v[150:153], v[158:161], v[138:141]
	v_mfma_f32_16x16x32_bf16 v[118:121], v[130:133], v[184:187], v[118:121]
	v_mfma_f32_16x16x32_bf16 v[114:117], v[150:153], v[184:187], v[114:117]
	v_mfma_f32_16x16x32_bf16 v[102:105], v[130:133], v[192:195], v[102:105]
	v_mfma_f32_16x16x32_bf16 v[98:101], v[150:153], v[192:195], v[98:101]
	v_mfma_f32_16x16x32_bf16 v[86:89], v[130:133], v[216:219], v[86:89]
	v_mfma_f32_16x16x32_bf16 v[82:85], v[150:153], v[216:219], v[82:85]
	s_barrier
	s_add_i32 s15, s15, s57
	v_lshl_add_u64 v[196:197], s[0:1], 0, v[206:207]
	s_mov_b32 m0, s15
	ds_read_b128 v[154:157], v201 offset:16384
	ds_read_b128 v[158:161], v201 offset:17408
	ds_read_b128 v[166:169], v201 offset:18432
	ds_read_b128 v[184:187], v201 offset:19456
	ds_read_b128 v[188:191], v201 offset:20480
	ds_read_b128 v[192:195], v201 offset:21504
	ds_read_b128 v[202:205], v201 offset:22528
	ds_read_b128 v[216:219], v201 offset:23552
	global_load_lds_dwordx4 v[196:197], off
	s_add_i32 m0, s15, 0x2000
	s_add_u32 s16, s0, 0x20000
	v_lshl_add_u64 v[208:209], s[0:1], 0, v[174:175]
	s_addc_u32 s17, s1, 0
	s_add_i32 s15, s18, s57
	global_load_lds_dwordx4 v[208:209], off
	v_lshl_add_u64 v[210:211], s[16:17], 0, v[206:207]
	s_mov_b32 m0, s15
	v_lshl_add_u64 v[212:213], s[30:31], 0, v[176:177]
	global_load_lds_dwordx4 v[210:211], off
	v_lshl_add_u64 v[210:211], s[16:17], 0, v[174:175]
	s_add_i32 m0, s15, 0x2000
	s_nop 0
	global_load_lds_dwordx4 v[210:211], off
	v_lshl_add_u64 v[210:211], s[30:31], 0, v[178:179]
	s_mov_b32 m0, s55
	s_nop 0
	global_load_lds_dwordx4 v[210:211], off
	s_mov_b32 m0, s63
	s_nop 0
	global_load_lds_dwordx4 v[212:213], off
	s_waitcnt vmcnt(8)
	s_waitcnt lgkmcnt(0)
	s_barrier
; #define PG8_STAGE(bufoff, gbase, voff) do { _Pragma("unroll") for (int _i = 0; _i < 2; ++_i) \
;         __builtin_amdgcn_global_load_lds((const unsigned*)((const char*)(gbase) + (voff)[_i]), (LAS unsigned*)(lds + (bufoff) + ldsw + _i * 8192), 16, 0, 0); } while (0)
; #define PG8_STAGE_A(bufoff, kptr, half, VO) do { if constexpr (GATHER) { _Pragma("unroll") for (int _i = 0; _i < 2; ++_i) \
;         __builtin_amdgcn_global_load_lds((const unsigned*)((const char*)(kptr) + (VO)[half][_i]), (LAS unsigned*)(lds + (bufoff) + ldsw + _i * 8192), 16, 0, 0); } \
;         else { PG8_STAGE(bufoff, (kptr) + (half) * hstepA, voffA); } } while (0)
; #define PG8_WAIT_V(n) asm volatile("s_waitcnt vmcnt(" #n ")" ::: "memory")
;     ...
;         for (int t = 0; t < nt; t += 2) {
;             const bool last = (t == nt - 2);
;             const char* a1 = cA + (size_t)(t + 1) * kstep;
;             const char* a2 = last ? nA : cA + (size_t)(t + 2) * kstep; const char* b2 = last ? nB : cB + (size_t)(t + 2) * kstep;
;             const char* a3 = a2 + kstep; const char* b3 = b2 + kstep;
;             unsigned g2[2][2];
;             if constexpr (GATHER) {
; #pragma unroll
;                 for (int _h = 0; _h < 2; ++_h)
; #pragma unroll
;                     for (int _i = 0; _i < 2; ++_i) g2[_h][_i] = last ? gN[_h][_i] : gC[_h][_i]; }
;             if constexpr (SP2) {
;             PG8_LDB(B0, 0, 0); PG8_LDB(B1, 0, 1); PG8_SCHED; PG8_LDA(At, 0, 0); PG8_STAGE_A(PG8_SA(1, 1), a1, 1, gC);
;             PG8_WAIT_V(8); PG8_WAIT_L(0); PG8_BAR; PG8_MMA(0, 0, At, B0); PG8_MMA(0, 1, At, B1); PG8_BAR; PG8_SCHED;
;             PG8_LDA(At, 0, 1); PG8_STAGE(PG8_SB(0, 0), b2, voffB); PG8_STAGE(PG8_SB(0, 1), b2 + hstepB, voffB); PG8_STAGE_A(PG8_SA(0, 0), a2, 0, g2);
;             PG8_WAIT_V(8); PG8_WAIT_L(0); PG8_BAR; PG8_MMA(1, 0, At, B0); PG8_MMA(1, 1, At, B1); PG8_BAR; PG8_SCHED;
;             PG8_LDB(B0, 1, 0); PG8_LDB(B1, 1, 1); PG8_SCHED; PG8_LDA(At, 1, 0); PG8_STAGE_A(PG8_SA(0, 1), a2, 1, g2);
;             PG8_WAIT_V(8); PG8_WAIT_L(0); PG8_BAR; PG8_MMA(0, 0, At, B0); PG8_MMA(0, 1, At, B1); PG8_BAR; PG8_SCHED;
;             PG8_LDA(At, 1, 1); PG8_STAGE(PG8_SB(1, 0), b3, voffB); PG8_STAGE(PG8_SB(1, 1), b3 + hstepB, voffB); PG8_STAGE_A(PG8_SA(1, 0), a3, 0, g2);
;             PG8_WAIT_V(8); PG8_WAIT_L(0); PG8_BAR; PG8_MMA(1, 0, At, B0); PG8_MMA(1, 1, At, B1); PG8_BAR; PG8_SCHED;
	s_waitcnt lgkmcnt(0)
	v_mfma_f32_16x16x32_bf16 v[78:81], v[38:41], v[154:157], v[78:81]
	v_mfma_f32_16x16x32_bf16 v[74:77], v[54:57], v[154:157], v[74:77]
	v_mfma_f32_16x16x32_bf16 v[58:61], v[38:41], v[166:169], v[58:61]
	v_mfma_f32_16x16x32_bf16 v[50:53], v[54:57], v[166:169], v[50:53]
	v_mfma_f32_16x16x32_bf16 v[30:33], v[38:41], v[188:191], v[30:33]
	v_mfma_f32_16x16x32_bf16 v[26:29], v[54:57], v[188:191], v[26:29]
	v_mfma_f32_16x16x32_bf16 v[14:17], v[38:41], v[202:205], v[14:17]
	v_mfma_f32_16x16x32_bf16 v[10:13], v[54:57], v[202:205], v[10:13]
	v_mfma_f32_16x16x32_bf16 v[78:81], v[46:49], v[158:161], v[78:81]
	v_mfma_f32_16x16x32_bf16 v[74:77], v[62:65], v[158:161], v[74:77]
	v_mfma_f32_16x16x32_bf16 v[58:61], v[46:49], v[184:187], v[58:61]
	v_mfma_f32_16x16x32_bf16 v[50:53], v[62:65], v[184:187], v[50:53]
	v_mfma_f32_16x16x32_bf16 v[30:33], v[46:49], v[192:195], v[30:33]
	v_mfma_f32_16x16x32_bf16 v[26:29], v[62:65], v[192:195], v[26:29]
	v_mfma_f32_16x16x32_bf16 v[14:17], v[46:49], v[216:219], v[14:17]
	v_mfma_f32_16x16x32_bf16 v[10:13], v[62:65], v[216:219], v[10:13]
	v_mfma_f32_16x16x32_bf16 v[42:45], v[122:125], v[166:169], v[42:45]
	v_mfma_f32_16x16x32_bf16 v[34:37], v[142:145], v[166:169], v[34:37]
	v_mfma_f32_16x16x32_bf16 v[22:25], v[122:125], v[188:191], v[22:25]
	v_mfma_f32_16x16x32_bf16 v[18:21], v[142:145], v[188:191], v[18:21]
	v_mfma_f32_16x16x32_bf16 v[6:9], v[122:125], v[202:205], v[6:9]
	v_mfma_f32_16x16x32_bf16 v[2:5], v[142:145], v[202:205], v[2:5]
	v_mfma_f32_16x16x32_bf16 v[38:41], v[122:125], v[154:157], v[70:73]
	v_mfma_f32_16x16x32_bf16 v[46:49], v[142:145], v[154:157], v[66:69]
	v_mfma_f32_16x16x32_bf16 v[42:45], v[130:133], v[184:187], v[42:45]
	v_mfma_f32_16x16x32_bf16 v[34:37], v[150:153], v[184:187], v[34:37]
	v_mfma_f32_16x16x32_bf16 v[22:25], v[130:133], v[192:195], v[22:25]
	v_mfma_f32_16x16x32_bf16 v[18:21], v[150:153], v[192:195], v[18:21]
	v_mfma_f32_16x16x32_bf16 v[6:9], v[130:133], v[216:219], v[6:9]
	v_mfma_f32_16x16x32_bf16 v[2:5], v[150:153], v[216:219], v[2:5]
	v_mfma_f32_16x16x32_bf16 v[38:41], v[130:133], v[158:161], v[38:41]
	v_mfma_f32_16x16x32_bf16 v[46:49], v[150:153], v[158:161], v[46:49]
	s_barrier
	s_add_i32 s15, 0, 0x18000
	s_add_i32 s18, 0, 0x1c000
	v_add_u32_e32 v70, s15, v199
	v_add_u32_e32 v150, s18, v199
	ds_read_b128 v[54:57], v70
	ds_read_b128 v[62:65], v70 offset:1024
	ds_read_b128 v[66:69], v70 offset:2048
	ds_read_b128 v[70:73], v70 offset:3072
	ds_read_b128 v[122:125], v150
	ds_read_b128 v[130:133], v150 offset:1024
	ds_read_b128 v[142:145], v150 offset:2048
	ds_read_b128 v[150:153], v150 offset:3072
	s_add_u32 s16, s30, 0x20000
	s_addc_u32 s17, s31, 0
	s_mov_b32 m0, s64
	v_lshl_add_u64 v[220:221], s[16:17], 0, v[178:179]
	ds_read_b128 v[154:157], v201 offset:32768
	ds_read_b128 v[158:161], v201 offset:33792
	ds_read_b128 v[166:169], v201 offset:34816
	ds_read_b128 v[184:187], v201 offset:35840
	ds_read_b128 v[188:191], v201 offset:36864
	ds_read_b128 v[192:195], v201 offset:37888
	ds_read_b128 v[202:205], v201 offset:38912
	ds_read_b128 v[216:219], v201 offset:39936
	global_load_lds_dwordx4 v[220:221], off
	v_lshl_add_u64 v[220:221], s[16:17], 0, v[176:177]
	s_mov_b32 m0, s65
	s_nop 0
	global_load_lds_dwordx4 v[220:221], off
	s_waitcnt vmcnt(8)
	s_waitcnt lgkmcnt(0)
	s_barrier
	s_waitcnt lgkmcnt(0)
	v_mfma_f32_16x16x32_bf16 v[170:173], v[54:57], v[154:157], v[170:173]
	v_mfma_f32_16x16x32_bf16 v[162:165], v[66:69], v[154:157], v[162:165]
	v_mfma_f32_16x16x32_bf16 v[134:137], v[54:57], v[166:169], v[134:137]
	v_mfma_f32_16x16x32_bf16 v[126:129], v[66:69], v[166:169], v[126:129]
	v_mfma_f32_16x16x32_bf16 v[110:113], v[54:57], v[188:191], v[110:113]
	v_mfma_f32_16x16x32_bf16 v[106:109], v[66:69], v[188:191], v[106:109]
	v_mfma_f32_16x16x32_bf16 v[94:97], v[54:57], v[202:205], v[94:97]
	v_mfma_f32_16x16x32_bf16 v[90:93], v[66:69], v[202:205], v[90:93]
	v_mfma_f32_16x16x32_bf16 v[170:173], v[62:65], v[158:161], v[170:173]
	v_mfma_f32_16x16x32_bf16 v[162:165], v[70:73], v[158:161], v[162:165]
	v_mfma_f32_16x16x32_bf16 v[134:137], v[62:65], v[184:187], v[134:137]
	v_mfma_f32_16x16x32_bf16 v[126:129], v[70:73], v[184:187], v[126:129]
	v_mfma_f32_16x16x32_bf16 v[110:113], v[62:65], v[192:195], v[110:113]
	v_mfma_f32_16x16x32_bf16 v[106:109], v[70:73], v[192:195], v[106:109]
	v_mfma_f32_16x16x32_bf16 v[94:97], v[62:65], v[216:219], v[94:97]
	v_mfma_f32_16x16x32_bf16 v[90:93], v[70:73], v[216:219], v[90:93]
	v_mfma_f32_16x16x32_bf16 v[146:149], v[122:125], v[154:157], v[146:149]
	v_mfma_f32_16x16x32_bf16 v[138:141], v[142:145], v[154:157], v[138:141]
	v_mfma_f32_16x16x32_bf16 v[118:121], v[122:125], v[166:169], v[118:121]
	v_mfma_f32_16x16x32_bf16 v[114:117], v[142:145], v[166:169], v[114:117]
	v_mfma_f32_16x16x32_bf16 v[102:105], v[122:125], v[188:191], v[102:105]
	v_mfma_f32_16x16x32_bf16 v[98:101], v[142:145], v[188:191], v[98:101]
	v_mfma_f32_16x16x32_bf16 v[86:89], v[122:125], v[202:205], v[86:89]
	v_mfma_f32_16x16x32_bf16 v[82:85], v[142:145], v[202:205], v[82:85]
	v_mfma_f32_16x16x32_bf16 v[146:149], v[130:133], v[158:161], v[146:149]
	v_mfma_f32_16x16x32_bf16 v[138:141], v[150:153], v[158:161], v[138:141]
	v_mfma_f32_16x16x32_bf16 v[118:121], v[130:133], v[184:187], v[118:121]
	v_mfma_f32_16x16x32_bf16 v[114:117], v[150:153], v[184:187], v[114:117]
	v_mfma_f32_16x16x32_bf16 v[102:105], v[130:133], v[192:195], v[102:105]
	v_mfma_f32_16x16x32_bf16 v[98:101], v[150:153], v[192:195], v[98:101]
	v_mfma_f32_16x16x32_bf16 v[86:89], v[130:133], v[216:219], v[86:89]
	v_mfma_f32_16x16x32_bf16 v[82:85], v[150:153], v[216:219], v[82:85]
	s_barrier
; #define PG8_STAGE(bufoff, gbase, voff) do { _Pragma("unroll") for (int _i = 0; _i < 2; ++_i) \
;         __builtin_amdgcn_global_load_lds((const unsigned*)((const char*)(gbase) + (voff)[_i]), (LAS unsigned*)(lds + (bufoff) + ldsw + _i * 8192), 16, 0, 0); } while (0)
; #define PG8_STAGE_A(bufoff, kptr, half, VO) do { if constexpr (GATHER) { _Pragma("unroll") for (int _i = 0; _i < 2; ++_i) \
;         __builtin_amdgcn_global_load_lds((const unsigned*)((const char*)(kptr) + (VO)[half][_i]), (LAS unsigned*)(lds + (bufoff) + ldsw + _i * 8192), 16, 0, 0); } \
;         else { PG8_STAGE(bufoff, (kptr) + (half) * hstepA, voffA); } } while (0)
; #define PG8_WAIT_V(n) asm volatile("s_waitcnt vmcnt(" #n ")" ::: "memory")
;     ...
;         for (int t = 0; t < nt; t += 2) {
;             const bool last = (t == nt - 2);
;             const char* a1 = cA + (size_t)(t + 1) * kstep;
;             const char* a2 = last ? nA : cA + (size_t)(t + 2) * kstep; const char* b2 = last ? nB : cB + (size_t)(t + 2) * kstep;
;             const char* a3 = a2 + kstep; const char* b3 = b2 + kstep;
;             unsigned g2[2][2];
;             if constexpr (GATHER) {
; #pragma unroll
;                 for (int _h = 0; _h < 2; ++_h)
; #pragma unroll
;                     for (int _i = 0; _i < 2; ++_i) g2[_h][_i] = last ? gN[_h][_i] : gC[_h][_i]; }
;             if constexpr (SP2) {
;             PG8_LDB(B0, 0, 0); PG8_LDB(B1, 0, 1); PG8_SCHED; PG8_LDA(At, 0, 0); PG8_STAGE_A(PG8_SA(1, 1), a1, 1, gC);
;             PG8_WAIT_V(8); PG8_WAIT_L(0); PG8_BAR; PG8_MMA(0, 0, At, B0); PG8_MMA(0, 1, At, B1); PG8_BAR; PG8_SCHED;
;             PG8_LDA(At, 0, 1); PG8_STAGE(PG8_SB(0, 0), b2, voffB); PG8_STAGE(PG8_SB(0, 1), b2 + hstepB, voffB); PG8_STAGE_A(PG8_SA(0, 0), a2, 0, g2);
;             PG8_WAIT_V(8); PG8_WAIT_L(0); PG8_BAR; PG8_MMA(1, 0, At, B0); PG8_MMA(1, 1, At, B1); PG8_BAR; PG8_SCHED;
;             PG8_LDB(B0, 1, 0); PG8_LDB(B1, 1, 1); PG8_SCHED; PG8_LDA(At, 1, 0); PG8_STAGE_A(PG8_SA(0, 1), a2, 1, g2);
;             PG8_WAIT_V(8); PG8_WAIT_L(0); PG8_BAR; PG8_MMA(0, 0, At, B0); PG8_MMA(0, 1, At, B1); PG8_BAR; PG8_SCHED;
;             PG8_LDA(At, 1, 1); PG8_STAGE(PG8_SB(1, 0), b3, voffB); PG8_STAGE(PG8_SB(1, 1), b3 + hstepB, voffB); PG8_STAGE_A(PG8_SA(1, 0), a3, 0, g2);
;             PG8_WAIT_V(8); PG8_WAIT_L(0); PG8_BAR; PG8_MMA(1, 0, At, B0); PG8_MMA(1, 1, At, B1); PG8_BAR; PG8_SCHED;
	s_add_i32 s15, s15, s57
	v_lshl_add_u64 v[196:197], v[196:197], 0, s[8:9]
	s_mov_b32 m0, s15
	ds_read_b128 v[154:157], v201 offset:49152
	ds_read_b128 v[158:161], v201 offset:50176
	ds_read_b128 v[166:169], v201 offset:51200
	ds_read_b128 v[184:187], v201 offset:52224
	ds_read_b128 v[188:191], v201 offset:53248
	ds_read_b128 v[192:195], v201 offset:54272
	ds_read_b128 v[202:205], v201 offset:55296
	ds_read_b128 v[216:219], v201 offset:56320
	global_load_lds_dwordx4 v[196:197], off
	s_add_i32 m0, s15, 0x2000
	s_add_u32 s0, s0, 0x20080
	v_lshl_add_u64 v[196:197], v[208:209], 0, s[8:9]
	s_addc_u32 s1, s1, 0
	s_add_i32 s15, s18, s57
	global_load_lds_dwordx4 v[196:197], off
	v_lshl_add_u64 v[196:197], s[0:1], 0, v[206:207]
	s_mov_b32 m0, s15
	s_nop 0
	global_load_lds_dwordx4 v[196:197], off
	v_lshl_add_u64 v[196:197], s[0:1], 0, v[174:175]
	s_add_i32 m0, s15, 0x2000
	s_nop 0
	global_load_lds_dwordx4 v[196:197], off
	v_lshl_add_u64 v[196:197], v[210:211], 0, s[8:9]
	s_mov_b32 m0, s4
	s_nop 0
	global_load_lds_dwordx4 v[196:197], off
	v_lshl_add_u64 v[196:197], v[212:213], 0, s[8:9]
	s_mov_b32 m0, s66
	s_nop 0
	global_load_lds_dwordx4 v[196:197], off
	s_waitcnt vmcnt(8)
	s_waitcnt lgkmcnt(0)
	s_barrier
	s_waitcnt lgkmcnt(0)
	v_mfma_f32_16x16x32_bf16 v[78:81], v[54:57], v[154:157], v[78:81]
	v_mfma_f32_16x16x32_bf16 v[74:77], v[66:69], v[154:157], v[74:77]
	v_mfma_f32_16x16x32_bf16 v[58:61], v[54:57], v[166:169], v[58:61]
	v_mfma_f32_16x16x32_bf16 v[50:53], v[66:69], v[166:169], v[50:53]
	v_mfma_f32_16x16x32_bf16 v[30:33], v[54:57], v[188:191], v[30:33]
	v_mfma_f32_16x16x32_bf16 v[26:29], v[66:69], v[188:191], v[26:29]
	v_mfma_f32_16x16x32_bf16 v[14:17], v[54:57], v[202:205], v[14:17]
	v_mfma_f32_16x16x32_bf16 v[10:13], v[66:69], v[202:205], v[10:13]
	v_mfma_f32_16x16x32_bf16 v[78:81], v[62:65], v[158:161], v[78:81]
	v_mfma_f32_16x16x32_bf16 v[74:77], v[70:73], v[158:161], v[74:77]
	v_mfma_f32_16x16x32_bf16 v[58:61], v[62:65], v[184:187], v[58:61]
	v_mfma_f32_16x16x32_bf16 v[50:53], v[70:73], v[184:187], v[50:53]
	v_mfma_f32_16x16x32_bf16 v[30:33], v[62:65], v[192:195], v[30:33]
	v_mfma_f32_16x16x32_bf16 v[26:29], v[70:73], v[192:195], v[26:29]
	v_mfma_f32_16x16x32_bf16 v[14:17], v[62:65], v[216:219], v[14:17]
	v_mfma_f32_16x16x32_bf16 v[10:13], v[70:73], v[216:219], v[10:13]
	v_mfma_f32_16x16x32_bf16 v[38:41], v[122:125], v[154:157], v[38:41]
	v_mfma_f32_16x16x32_bf16 v[70:73], v[130:133], v[158:161], v[38:41]
	v_mfma_f32_16x16x32_bf16 v[38:41], v[142:145], v[154:157], v[46:49]
	v_mfma_f32_16x16x32_bf16 v[66:69], v[150:153], v[158:161], v[38:41]
	v_mfma_f32_16x16x32_bf16 v[38:41], v[122:125], v[166:169], v[42:45]
	v_mfma_f32_16x16x32_bf16 v[34:37], v[142:145], v[166:169], v[34:37]
	v_mfma_f32_16x16x32_bf16 v[22:25], v[122:125], v[188:191], v[22:25]
	v_mfma_f32_16x16x32_bf16 v[18:21], v[142:145], v[188:191], v[18:21]
	v_mfma_f32_16x16x32_bf16 v[6:9], v[122:125], v[202:205], v[6:9]
	v_mfma_f32_16x16x32_bf16 v[2:5], v[142:145], v[202:205], v[2:5]
	v_mfma_f32_16x16x32_bf16 v[42:45], v[130:133], v[184:187], v[38:41]
	v_mfma_f32_16x16x32_bf16 v[34:37], v[150:153], v[184:187], v[34:37]
	v_mfma_f32_16x16x32_bf16 v[22:25], v[130:133], v[192:195], v[22:25]
	v_mfma_f32_16x16x32_bf16 v[18:21], v[150:153], v[192:195], v[18:21]
	v_mfma_f32_16x16x32_bf16 v[6:9], v[130:133], v[216:219], v[6:9]
	v_mfma_f32_16x16x32_bf16 v[2:5], v[150:153], v[216:219], v[2:5]
	s_barrier
	s_add_i32 s14, s14, 2
	s_add_u32 s24, s24, 0x100
	s_addc_u32 s25, s25, 0
	s_add_u32 s12, s12, 0x100
	s_addc_u32 s13, s13, 0
	s_cmp_gt_u32 s14, 5
	s_cbranch_scc0 .LBB0_1443
	s_and_b64 vcc, exec, s[42:43]
	s_cbranch_vccz .LBB0_1446
	s_barrier

;     __device__ __forceinline__ void init(const void* A_, const void* B_, int G_, int c_) { T.init(A_, B_, DM, DM, NLAT / 256, INP / 256, 1, 0, 0, G_, c_, 0); }
; __device__ __forceinline__ void moe_fill(const Params& p, LAS unsigned char* lds, int ph) { if (FILL_ON) moe_pump(p, lds, ph, Q_TOTAL, 0); }
; __device__ __forceinline__ void moe_convert_while(const Params& p, LAS unsigned char* lds, int ph, unsigned ngemm) { moe_pump(p, lds, ph, Q_TOTAL, 0, ngemm, false); }
; #define REPLOOP(id) for (int rep_ = 0; rep_ < NREP(id); ++rep_)
; #define REPBAR(id) do { if (rep_ + 1 < NREP(id)) xcd_barrier(bar); } while (0)
; #define SEAM(k) do { if (IN(k) && IN((k) + 1)) xcd_barrier(bar); } while (0)
; __global__ void __launch_bounds__(512, 2) fwd(Params p) {
;     ...
;             moe_fill(p, lds, pb + 5);
;          REPBAR(7); }
;         SEAM(pb + 5);
;         if (PSEL(8) && IN(pb + 6)) REPLOOP(8) {
;             pg8::TileSched S; S.init(ws + WS_CAT, (bf16_t*)(ws + WS_WTOUT) + (size_t)l * DM * DM, DM, DM, (l == 0 ? MT : NLAT) / 256, DM / 256, 1, 0, 0, l == 0 ? GgG : G, c, 0);
;             pg8::EpiOut E{p.in[I_X], p.in[I_CTX], l == 0 ? (const bf16_t*)nullptr : (const bf16_t*)(ws + WS_XA), mod + 2 * DM, (bf16_t*)(ws + WS_XB)};
;             if (l == 0 && c >= GgG) moe_convert_while(p, lds, pb + 6, GgG);
.LBB0_1501:
	s_setprio 0
	s_cmp_le_i32 s86, s4
	s_cselect_b64 s[0:1], -1, 0
	s_cmp_lt_i32 s4, s87
	s_cselect_b64 s[2:3], -1, 0
	s_and_b64 s[2:3], s[0:1], s[2:3]
	s_mov_b64 s[0:1], -1
	s_and_b64 vcc, exec, s[2:3]
	s_cbranch_vccnz .LBB0_1503
	v_readlane_b32 s0, v255, 56
	s_add_i32 s4, s0, 9
	s_mov_b64 s[0:1], 0

;     const int tid = opaque_tid(), wid = __builtin_amdgcn_readfirstlane(tid >> 6), lane = tid & 63, wr = wid >> 2, wc = wid & 3, fr = lane & 15, fq = lane >> 4;
;     const int K = g.K, nt = K / BK;
;     unsigned voffA[2], voffB[2]; int gR[2], gCc[2];
; #pragma unroll
;     for (int i = 0; i < 2; ++i) { int R, C; stage_rc(tid * 16 + i * 8192, R, C); const int Rb = Epi::PERM ? ((R & ~31) + perm32(R & 31)) : R;
;         voffA[i] = (unsigned)(R * g.lda + C) * 2u; voffB[i] = (unsigned)(Rb * g.ldb + C) * 2u; gR[i] = R; gCc[i] = C; }
;     unsigned gC[2][2], gN[2][2];
;     ...
;     const size_t kstep = (size_t)(BK * 2);
;     const size_t hstepA = (size_t)HALF * g.lda * 2, hstepB = (size_t)HALF * g.ldb * 2;
;     const unsigned ldsw = (unsigned)wid * 1024u;
;     const int aoff = lds_byte(wr * 64 + fr, fq * 8), boff = lds_byte(wc * 32 + fr, fq * 8);
;     ...
;     Unit cur, nxt; int ui = 0;
;     if (!S.next(0, cur)) return;
;     f32x4 acc[2][2][4][2];
; #pragma unroll
;     for (int a = 0; a < 2; ++a)
; #pragma unroll
;         for (int b = 0; b < 2; ++b)
; #pragma unroll
;             for (int m = 0; m < 4; ++m)
; #pragma unroll
;                 for (int n = 0; n < 2; ++n) acc[a][b][m][n] = (f32x4){0.f, 0.f, 0.f, 0.f};
;     bf16x8 At[4][2], B0[2][2], B1[2][2];
;     const char* cA = cur.a; const char* cB = cur.b;
;     if constexpr (GATHER) { PG8_GOFF(cur, gC); }
;     if constexpr (SP2) {
;         PG8_STAGE(PG8_SB(0, 0), cB, voffB); PG8_STAGE(PG8_SB(0, 1), cB + hstepB, voffB); PG8_STAGE_A(PG8_SA(0, 0), cA, 0, gC); PG8_STAGE_A(PG8_SA(0, 1), cA, 1, gC);
;         if (wr == 1) PG8_BAR;
;         PG8_WAIT_V(2); PG8_BAR;
; __global__ void __launch_bounds__(512, 2) fwd(Params p) {
;     ...
;             pg8::TileSched S; S.init(ws + WS_CAT, (bf16_t*)(ws + WS_WTOUT) + (size_t)l * DM * DM, DM, DM, (l == 0 ? MT : NLAT) / 256, DM / 256, 1, 0, 0, l == 0 ? GgG : G, c, 0);
;             pg8::EpiOut E{p.in[I_X], p.in[I_CTX], l == 0 ? (const bf16_t*)nullptr : (const bf16_t*)(ws + WS_XA), mod + 2 * DM, (bf16_t*)(ws + WS_XB)};
;             if (l == 0 && c >= GgG) moe_convert_while(p, lds, pb + 6, GgG);
;             else if (l == 0) { pg8::gemm_phase(lds, pg8::Desc{DM, DM, DM}, S, E); if (nconv) moe_mark_done(p, pb + 6); }
;             else { pg8::EpiOutBf Eb{(const bf16_t*)(ws + WS_XA), mod + 2 * DM, (bf16_t*)(ws + WS_XB)}; pg8::gemm_phase(lds, pg8::Desc{DM, DM, DM}, S, Eb); }
.LBB0_1658:
	s_and_b64 vcc, exec, s[0:1]
	s_cbranch_vccz .LBB0_1702
	v_readlane_b32 s0, v252, 5
	s_add_u32 s2, s84, s22
	v_readlane_b32 s1, v252, 6
	s_addc_u32 s3, s85, 0
	s_lshl_b64 s[0:1], s[0:1], 23
	v_readlane_b32 s4, v253, 49
	s_add_u32 s26, s4, s0
	v_readlane_b32 s0, v253, 50
	s_addc_u32 s27, s0, s1
	v_readlane_b32 s0, v255, 54
	v_readlane_b32 s1, v255, 55
	s_and_b64 s[0:1], s[0:1], exec
	v_readlane_b32 s0, v253, 57
	s_cselect_b32 s51, s94, s0
	s_cselect_b32 s50, 32, 36
	s_abs_i32 s0, s51
	s_waitcnt vmcnt(0)
	v_cvt_f32_u32_e32 v2, s0
	s_sub_i32 s12, 0, s0
	s_add_i32 s1, s51, s92
	s_ashr_i32 s4, s1, 31
	v_rcp_iflag_f32_e32 v2, v2
	s_abs_i32 s1, s1
	v_mul_f32_e32 v2, 0x4f7ffffe, v2
	v_cvt_u32_f32_e32 v2, v2
	s_nop 0
	v_readfirstlane_b32 s13, v2
	s_mul_i32 s12, s12, s13
	s_mul_hi_u32 s12, s13, s12
	s_add_i32 s13, s13, s12
	s_mul_hi_u32 s12, s1, s13
	s_mul_i32 s12, s12, s0
	s_sub_i32 s1, s1, s12
	s_sub_i32 s12, s1, s0
	s_cmp_ge_u32 s1, s0
	s_cselect_b32 s1, s12, s1
	s_sub_i32 s12, s1, s0
	s_cmp_ge_u32 s1, s0
	s_cselect_b32 s0, s12, s1
	s_xor_b32 s0, s0, s4
	s_sub_i32 s54, s0, s4
	s_add_u32 s55, s2, 0x14000
	s_addc_u32 s56, s3, 0
	s_ashr_i32 s57, s54, 31
	s_ashr_i32 s58, s51, 31
	s_andn2_b64 vcc, exec, s[76:77]
	s_mov_b64 s[0:1], -1
	s_cbranch_vccnz .LBB0_1683
	v_mov_b32_e32 v13, v0
	s_cmpk_gt_i32 s54, 0x11f
	s_nop 0
	v_readfirstlane_b32 s12, v13
	s_cbranch_scc1 .LBB0_1679
	v_lshlrev_b32_e32 v2, 4, v13
	v_add_u32_e32 v3, 0x2000, v2
	v_ashrrev_i32_e32 v4, 31, v3
	v_lshrrev_b32_e32 v4, 22, v4
	s_mul_hi_i32 s0, s54, 0x38e38e39
	v_add_u32_e32 v4, v3, v4
	s_lshr_b32 s1, s0, 31
	s_lshr_b32 s0, s0, 6
	v_ashrrev_i32_e32 v10, 10, v4
	s_add_i32 s0, s0, s1
	v_mul_i32_i24_e32 v4, 0x400, v10
	s_mulk_i32 s0, 0x120
	v_sub_u32_e32 v3, v3, v4
	s_sub_i32 s0, s54, s0
	v_lshrrev_b32_e32 v4, 4, v3
	s_sext_i32_i16 s1, s0
	v_bitop3_b32 v3, v4, v3, 32 bitop3:0x6c
	s_bfe_u32 s1, s1, 0x3001c
	v_ashrrev_i32_e32 v4, 31, v3
	s_add_i32 s1, s0, s1
	v_lshrrev_b32_e32 v4, 26, v4
	s_sext_i32_i16 s2, s1
	s_and_b32 s1, s1, 0xfff8
	v_add_u32_e32 v4, v3, v4
	v_lshlrev_b32_e32 v5, 3, v10
	s_ashr_i32 s14, s12, 6
	s_sub_i32 s0, s0, s1
	v_ashrrev_i32_e32 v11, 6, v4
	v_and_b32_e32 v5, -16, v5
	s_ashr_i32 s13, s12, 8
	s_lshl_b32 s52, s14, 10
	s_ashr_i32 s2, s2, 3
	s_sext_i32_i16 s1, s0
	v_add_u32_e32 v5, v11, v5
	s_cmp_lt_i32 s1, 0
	v_and_b32_e32 v6, 3, v11
	s_mov_b32 s1, 0xfffe0
	v_lshrrev_b32_e32 v7, 2, v5
	v_lshlrev_b32_e32 v8, 1, v5
	v_and_b32_e32 v4, 0xc0, v4
	v_and_or_b32 v6, v5, s1, v6
	v_and_b32_e32 v7, 4, v7
	v_and_b32_e32 v8, 24, v8
	v_sub_u32_e32 v3, v3, v4
	v_or3_b32 v6, v6, v7, v8
	v_lshlrev_b32_e32 v7, 5, v10
	v_ashrrev_i16_sdwa v3, v245, sext(v3) dst_sel:DWORD dst_unused:UNUSED_PAD src0_sel:DWORD src1_sel:BYTE_0
	v_and_b32_e32 v7, 32, v7
	v_bfe_i32 v12, v3, 0, 16
	v_add_lshl_u32 v3, v7, v12, 1
	v_lshl_add_u32 v130, v6, 12, v3
	v_lshl_add_u32 v132, v5, 12, v3
	v_bfe_i32 v3, v13, 27, 1
	v_lshrrev_b32_e32 v3, 22, v3
	v_add_u32_e32 v3, v2, v3
	v_and_b32_e32 v3, 0xfffffc00, v3
	v_sub_u32_e32 v2, v2, v3
	v_lshrrev_b32_e32 v3, 4, v2
	v_bitop3_b32 v3, v3, v2, 32 bitop3:0x6c
	v_ashrrev_i32_e32 v2, 31, v2
	v_lshrrev_b32_e32 v2, 26, v2
	v_add_u32_e32 v2, v3, v2
	v_ashrrev_i32_e32 v14, 6, v2
	v_ashrrev_i32_e32 v2, 31, v13
	v_lshrrev_b32_e32 v2, 26, v2
	v_add_u32_e32 v2, v13, v2
	v_ashrrev_i32_e32 v15, 6, v2
	v_lshlrev_b32_e32 v2, 3, v15
	v_and_b32_e32 v2, -16, v2
	v_add_u32_e32 v2, v14, v2
	v_and_b32_e32 v4, 3, v14
	v_and_or_b32 v4, v2, s1, v4
	s_cselect_b32 s1, 37, 36
	s_mul_i32 s0, s1, s0
	s_add_i32 s0, s0, s2
	s_sext_i32_i16 s1, s0
	s_bfe_u32 s1, s1, 0x60019
	v_lshrrev_b32_e32 v5, 2, v2
	v_lshlrev_b32_e32 v6, 1, v2
	s_add_i32 s1, s0, s1
	v_and_b32_e32 v5, 4, v5
	v_and_b32_e32 v6, 24, v6
	s_sext_i32_i16 s2, s1
	v_or3_b32 v4, v4, v5, v6
	v_mul_i32_i24_e32 v6, 64, v14
	s_ashr_i32 s2, s2, 6
	v_sub_u32_e32 v3, v3, v6
	s_lshl_b32 s2, s2, 3
	v_lshlrev_b32_e32 v5, 5, v15
	v_ashrrev_i16_sdwa v3, v245, sext(v3) dst_sel:DWORD dst_unused:UNUSED_PAD src0_sel:DWORD src1_sel:BYTE_0
	s_sub_i32 s3, 36, s2
	s_and_b32 s1, s1, 0xffc0
	v_and_b32_e32 v5, 32, v5
	v_bfe_i32 v16, v3, 0, 16
	s_min_u32 s3, s3, 8
	s_sub_i32 s15, s0, s1
	v_add_lshl_u32 v3, v5, v16, 1
	s_sext_i32_i16 s0, s15
	v_cvt_f32_ubyte0_e32 v5, s3
	v_lshl_add_u32 v206, v4, 12, v3
	v_cvt_f32_i32_e32 v4, s0
	v_rcp_iflag_f32_e32 v6, v5
	v_lshl_add_u32 v134, v2, 12, v3
	s_ashr_i32 s0, s0, 30
	s_or_b32 s4, s0, 1
	v_mul_f32_e32 v2, v4, v6
	v_trunc_f32_e32 v2, v2
	v_fma_f32 v3, -v2, v5, v4
	v_cvt_i32_f32_e32 v2, v2
	v_cmp_ge_f32_e64 s[0:1], |v3|, v5
	s_and_b64 s[0:1], s[0:1], exec
	s_cselect_b32 s0, s4, 0
	v_readfirstlane_b32 s1, v2
	s_add_i32 s4, s1, s0
	s_mul_i32 s0, s4, s3
	s_sub_i32 s0, s15, s0
	s_sext_i32_i8 s0, s0
	s_add_i32 s48, s2, s0
	s_ashr_i32 s49, s48, 31
	s_lshl_b64 s[0:1], s[48:49], 20
	v_readlane_b32 s2, v253, 47
	v_readlane_b32 s3, v253, 48
	s_add_u32 s0, s2, s0
	s_addc_u32 s1, s3, s1
	s_bfe_i64 s[2:3], s[4:5], 0x80000
	s_lshl_b64 s[2:3], s[2:3], 20
	s_add_u32 s30, s26, s2
	s_addc_u32 s31, s27, s3
	s_add_i32 s49, s52, 0
	s_add_i32 m0, s49, 0x10000
	v_mov_b32_e32 v131, v207
	global_load_lds_dwordx4 v206, s[30:31]
	s_add_i32 m0, s49, 0x12000
	s_add_u32 s2, s30, 0x80000
	global_load_lds_dwordx4 v130, s[30:31]
	s_addc_u32 s3, s31, 0
	s_add_i32 m0, s49, 0x14000
	s_add_i32 s53, s49, 0x2000
	global_load_lds_dwordx4 v206, s[2:3]
	s_add_i32 m0, s49, 0x16000
	v_mov_b32_e32 v135, v207
	global_load_lds_dwordx4 v130, s[2:3]
	s_mov_b32 m0, s49
	s_add_u32 s2, s0, 0x80000
	global_load_lds_dwordx4 v134, s[0:1]
	s_mov_b32 m0, s53
	s_addc_u32 s3, s1, 0
	s_add_i32 s59, s49, 0x4000
	global_load_lds_dwordx4 v132, s[0:1]
	s_mov_b32 m0, s59
	s_add_i32 s60, s49, 0x6000
	global_load_lds_dwordx4 v134, s[2:3]
	s_mov_b32 m0, s60
	v_mov_b32_e32 v133, v207
	global_load_lds_dwordx4 v132, s[2:3]
	s_cmp_eq_u32 s13, 1
	v_lshl_add_u64 v[8:9], s[30:31], 0, v[206:207]
	v_lshl_add_u64 v[6:7], s[30:31], 0, v[130:131]
	v_lshl_add_u64 v[2:3], s[0:1], 0, v[134:135]
	s_cselect_b64 s[2:3], -1, 0
	s_cmp_lg_u32 s13, 1
	v_lshl_add_u64 v[4:5], s[0:1], 0, v[132:133]
	s_cbranch_scc1 .LBB0_1663
	s_barrier
	s_setprio 1

; #define PG8_STAGE(bufoff, gbase, voff) do { _Pragma("unroll") for (int _i = 0; _i < 2; ++_i) \
;         __builtin_amdgcn_global_load_lds((const unsigned*)((const char*)(gbase) + (voff)[_i]), (LAS unsigned*)(lds + (bufoff) + ldsw + _i * 8192), 16, 0, 0); } while (0)
; #define PG8_STAGE_A(bufoff, kptr, half, VO) do { if constexpr (GATHER) { _Pragma("unroll") for (int _i = 0; _i < 2; ++_i) \
;         __builtin_amdgcn_global_load_lds((const unsigned*)((const char*)(kptr) + (VO)[half][_i]), (LAS unsigned*)(lds + (bufoff) + ldsw + _i * 8192), 16, 0, 0); } \
;         else { PG8_STAGE(bufoff, (kptr) + (half) * hstepA, voffA); } } while (0)
; #define PG8_WAIT_V(n) asm volatile("s_waitcnt vmcnt(" #n ")" ::: "memory")
;     ...
;         for (int t = 0; t < nt; t += 2) {
;             const bool last = (t == nt - 2);
;             const char* a1 = cA + (size_t)(t + 1) * kstep;
;             const char* a2 = last ? nA : cA + (size_t)(t + 2) * kstep; const char* b2 = last ? nB : cB + (size_t)(t + 2) * kstep;
;             const char* a3 = a2 + kstep; const char* b3 = b2 + kstep;
;             unsigned g2[2][2];
;             if constexpr (GATHER) {
; #pragma unroll
;                 for (int _h = 0; _h < 2; ++_h)
; #pragma unroll
;                     for (int _i = 0; _i < 2; ++_i) g2[_h][_i] = last ? gN[_h][_i] : gC[_h][_i]; }
;             if constexpr (SP2) {
;             PG8_LDB(B0, 0, 0); PG8_LDB(B1, 0, 1); PG8_SCHED; PG8_LDA(At, 0, 0); PG8_STAGE_A(PG8_SA(1, 1), a1, 1, gC);
;             PG8_WAIT_V(8); PG8_WAIT_L(0); PG8_BAR; PG8_MMA(0, 0, At, B0); PG8_MMA(0, 1, At, B1); PG8_BAR; PG8_SCHED;
;             PG8_LDA(At, 0, 1); PG8_STAGE(PG8_SB(0, 0), b2, voffB); PG8_STAGE(PG8_SB(0, 1), b2 + hstepB, voffB); PG8_STAGE_A(PG8_SA(0, 0), a2, 0, g2);
;             PG8_WAIT_V(8); PG8_WAIT_L(0); PG8_BAR; PG8_MMA(1, 0, At, B0); PG8_MMA(1, 1, At, B1); PG8_BAR; PG8_SCHED;
;             PG8_LDB(B0, 1, 0); PG8_LDB(B1, 1, 1); PG8_SCHED; PG8_LDA(At, 1, 0); PG8_STAGE_A(PG8_SA(0, 1), a2, 1, g2);
;             PG8_WAIT_V(8); PG8_WAIT_L(0); PG8_BAR; PG8_MMA(0, 0, At, B0); PG8_MMA(0, 1, At, B1); PG8_BAR; PG8_SCHED;
;             PG8_LDA(At, 1, 1); PG8_STAGE(PG8_SB(1, 0), b3, voffB); PG8_STAGE(PG8_SB(1, 1), b3 + hstepB, voffB); PG8_STAGE_A(PG8_SA(1, 0), a3, 0, g2);
;             PG8_WAIT_V(8); PG8_WAIT_L(0); PG8_BAR; PG8_MMA(1, 0, At, B0); PG8_MMA(1, 1, At, B1); PG8_BAR; PG8_SCHED;
.LBB0_1669:
	s_add_u32 s0, s24, 0xfff80080
	s_addc_u32 s1, s25, -1
	s_add_i32 s15, 0, 0x10000
	s_cmp_eq_u32 s14, 28
	s_cselect_b32 s31, s45, s1
	s_cselect_b32 s30, s44, s0
	v_add_u32_e32 v158, s15, v161
	s_cselect_b32 s1, s47, s13
	s_cselect_b32 s0, s46, s12
	s_add_i32 s18, 0, 0x14000
	ds_read_b128 v[164:167], v158
	ds_read_b128 v[168:171], v158 offset:1024
	ds_read_b128 v[172:175], v158 offset:2048
	ds_read_b128 v[176:179], v158 offset:3072
	v_add_u32_e32 v158, s18, v161
	ds_read_b128 v[180:183], v158
	ds_read_b128 v[184:187], v158 offset:1024
	ds_read_b128 v[188:191], v158 offset:2048
	ds_read_b128 v[192:195], v158 offset:3072
	v_lshl_add_u64 v[158:159], s[24:25], 0, v[154:155]
	s_add_i32 m0, s49, 0xc000
	ds_read_b128 v[196:199], v163
	ds_read_b128 v[200:203], v163 offset:1024
	ds_read_b128 v[216:219], v163 offset:2048
	ds_read_b128 v[220:223], v163 offset:3072
	ds_read_b128 v[224:227], v163 offset:4096
	ds_read_b128 v[228:231], v163 offset:5120
	ds_read_b128 v[232:235], v163 offset:6144
	ds_read_b128 v[236:239], v163 offset:7168
	global_load_lds_dwordx4 v[158:159], off
	v_lshl_add_u64 v[158:159], s[24:25], 0, v[156:157]
	s_add_i32 m0, s49, 0xe000
	s_nop 0
	global_load_lds_dwordx4 v[158:159], off
	s_waitcnt vmcnt(8)
	s_waitcnt lgkmcnt(0)
	s_barrier
	s_waitcnt lgkmcnt(0)
	v_mfma_f32_16x16x32_bf16 v[126:129], v[164:167], v[196:199], v[126:129]
	v_mfma_f32_16x16x32_bf16 v[122:125], v[172:175], v[196:199], v[122:125]
	v_mfma_f32_16x16x32_bf16 v[118:121], v[164:167], v[216:219], v[118:121]
	v_mfma_f32_16x16x32_bf16 v[114:117], v[172:175], v[216:219], v[114:117]
	v_mfma_f32_16x16x32_bf16 v[102:105], v[164:167], v[224:227], v[102:105]
	v_mfma_f32_16x16x32_bf16 v[98:101], v[172:175], v[224:227], v[98:101]
	v_mfma_f32_16x16x32_bf16 v[86:89], v[164:167], v[232:235], v[86:89]
	v_mfma_f32_16x16x32_bf16 v[82:85], v[172:175], v[232:235], v[82:85]
	v_mfma_f32_16x16x32_bf16 v[126:129], v[168:171], v[200:203], v[126:129]
	v_mfma_f32_16x16x32_bf16 v[122:125], v[176:179], v[200:203], v[122:125]
	v_mfma_f32_16x16x32_bf16 v[118:121], v[168:171], v[220:223], v[118:121]
	v_mfma_f32_16x16x32_bf16 v[114:117], v[176:179], v[220:223], v[114:117]
	v_mfma_f32_16x16x32_bf16 v[102:105], v[168:171], v[228:231], v[102:105]
	v_mfma_f32_16x16x32_bf16 v[98:101], v[176:179], v[228:231], v[98:101]
	v_mfma_f32_16x16x32_bf16 v[86:89], v[168:171], v[236:239], v[86:89]
	v_mfma_f32_16x16x32_bf16 v[82:85], v[176:179], v[236:239], v[82:85]
	v_mfma_f32_16x16x32_bf16 v[110:113], v[180:183], v[196:199], v[110:113]
	v_mfma_f32_16x16x32_bf16 v[106:109], v[188:191], v[196:199], v[106:109]
	v_mfma_f32_16x16x32_bf16 v[94:97], v[180:183], v[216:219], v[94:97]
	v_mfma_f32_16x16x32_bf16 v[90:93], v[188:191], v[216:219], v[90:93]
	v_mfma_f32_16x16x32_bf16 v[78:81], v[180:183], v[224:227], v[78:81]
	v_mfma_f32_16x16x32_bf16 v[74:77], v[188:191], v[224:227], v[74:77]
	v_mfma_f32_16x16x32_bf16 v[70:73], v[180:183], v[232:235], v[70:73]
	v_mfma_f32_16x16x32_bf16 v[66:69], v[188:191], v[232:235], v[66:69]
	v_mfma_f32_16x16x32_bf16 v[110:113], v[184:187], v[200:203], v[110:113]
	v_mfma_f32_16x16x32_bf16 v[106:109], v[192:195], v[200:203], v[106:109]
	v_mfma_f32_16x16x32_bf16 v[94:97], v[184:187], v[220:223], v[94:97]
	v_mfma_f32_16x16x32_bf16 v[90:93], v[192:195], v[220:223], v[90:93]
	v_mfma_f32_16x16x32_bf16 v[78:81], v[184:187], v[228:231], v[78:81]
	v_mfma_f32_16x16x32_bf16 v[74:77], v[192:195], v[228:231], v[74:77]
	v_mfma_f32_16x16x32_bf16 v[70:73], v[184:187], v[236:239], v[70:73]
	v_mfma_f32_16x16x32_bf16 v[66:69], v[192:195], v[236:239], v[66:69]
	s_barrier
	s_add_i32 s15, s15, s52
	v_lshl_add_u64 v[158:159], s[0:1], 0, v[206:207]
	s_mov_b32 m0, s15
	ds_read_b128 v[196:199], v163 offset:16384
	ds_read_b128 v[200:203], v163 offset:17408
	ds_read_b128 v[216:219], v163 offset:18432
	ds_read_b128 v[220:223], v163 offset:19456
	ds_read_b128 v[224:227], v163 offset:20480
	ds_read_b128 v[228:231], v163 offset:21504
	ds_read_b128 v[232:235], v163 offset:22528
	ds_read_b128 v[236:239], v163 offset:23552
	global_load_lds_dwordx4 v[158:159], off
	s_add_i32 m0, s15, 0x2000
	s_add_u32 s16, s0, 0x80000
	v_lshl_add_u64 v[204:205], s[0:1], 0, v[130:131]
	s_addc_u32 s17, s1, 0
	s_add_i32 s15, s18, s52
	global_load_lds_dwordx4 v[204:205], off
	v_lshl_add_u64 v[208:209], s[16:17], 0, v[206:207]
	s_mov_b32 m0, s15
	v_lshl_add_u64 v[210:211], s[30:31], 0, v[132:133]
	global_load_lds_dwordx4 v[208:209], off
	v_lshl_add_u64 v[208:209], s[16:17], 0, v[130:131]
	s_add_i32 m0, s15, 0x2000
	s_nop 0
	global_load_lds_dwordx4 v[208:209], off
	v_lshl_add_u64 v[208:209], s[30:31], 0, v[134:135]
	s_mov_b32 m0, s49
	s_nop 0
	global_load_lds_dwordx4 v[208:209], off
	s_mov_b32 m0, s53
	s_nop 0
	global_load_lds_dwordx4 v[210:211], off
	s_waitcnt vmcnt(8)
	s_waitcnt lgkmcnt(0)
	s_barrier
; #define PG8_STAGE(bufoff, gbase, voff) do { _Pragma("unroll") for (int _i = 0; _i < 2; ++_i) \
;         __builtin_amdgcn_global_load_lds((const unsigned*)((const char*)(gbase) + (voff)[_i]), (LAS unsigned*)(lds + (bufoff) + ldsw + _i * 8192), 16, 0, 0); } while (0)
; #define PG8_STAGE_A(bufoff, kptr, half, VO) do { if constexpr (GATHER) { _Pragma("unroll") for (int _i = 0; _i < 2; ++_i) \
;         __builtin_amdgcn_global_load_lds((const unsigned*)((const char*)(kptr) + (VO)[half][_i]), (LAS unsigned*)(lds + (bufoff) + ldsw + _i * 8192), 16, 0, 0); } \
;         else { PG8_STAGE(bufoff, (kptr) + (half) * hstepA, voffA); } } while (0)
; #define PG8_WAIT_V(n) asm volatile("s_waitcnt vmcnt(" #n ")" ::: "memory")
;     ...
;         for (int t = 0; t < nt; t += 2) {
;             const bool last = (t == nt - 2);
;             const char* a1 = cA + (size_t)(t + 1) * kstep;
;             const char* a2 = last ? nA : cA + (size_t)(t + 2) * kstep; const char* b2 = last ? nB : cB + (size_t)(t + 2) * kstep;
;             const char* a3 = a2 + kstep; const char* b3 = b2 + kstep;
;             unsigned g2[2][2];
;             if constexpr (GATHER) {
; #pragma unroll
;                 for (int _h = 0; _h < 2; ++_h)
; #pragma unroll
;                     for (int _i = 0; _i < 2; ++_i) g2[_h][_i] = last ? gN[_h][_i] : gC[_h][_i]; }
;             if constexpr (SP2) {
;             PG8_LDB(B0, 0, 0); PG8_LDB(B1, 0, 1); PG8_SCHED; PG8_LDA(At, 0, 0); PG8_STAGE_A(PG8_SA(1, 1), a1, 1, gC);
;             PG8_WAIT_V(8); PG8_WAIT_L(0); PG8_BAR; PG8_MMA(0, 0, At, B0); PG8_MMA(0, 1, At, B1); PG8_BAR; PG8_SCHED;
;             PG8_LDA(At, 0, 1); PG8_STAGE(PG8_SB(0, 0), b2, voffB); PG8_STAGE(PG8_SB(0, 1), b2 + hstepB, voffB); PG8_STAGE_A(PG8_SA(0, 0), a2, 0, g2);
;             PG8_WAIT_V(8); PG8_WAIT_L(0); PG8_BAR; PG8_MMA(1, 0, At, B0); PG8_MMA(1, 1, At, B1); PG8_BAR; PG8_SCHED;
;             PG8_LDB(B0, 1, 0); PG8_LDB(B1, 1, 1); PG8_SCHED; PG8_LDA(At, 1, 0); PG8_STAGE_A(PG8_SA(0, 1), a2, 1, g2);
;             PG8_WAIT_V(8); PG8_WAIT_L(0); PG8_BAR; PG8_MMA(0, 0, At, B0); PG8_MMA(0, 1, At, B1); PG8_BAR; PG8_SCHED;
;             PG8_LDA(At, 1, 1); PG8_STAGE(PG8_SB(1, 0), b3, voffB); PG8_STAGE(PG8_SB(1, 1), b3 + hstepB, voffB); PG8_STAGE_A(PG8_SA(1, 0), a3, 0, g2);
;             PG8_WAIT_V(8); PG8_WAIT_L(0); PG8_BAR; PG8_MMA(1, 0, At, B0); PG8_MMA(1, 1, At, B1); PG8_BAR; PG8_SCHED;
	s_waitcnt lgkmcnt(0)
	v_mfma_f32_16x16x32_bf16 v[62:65], v[164:167], v[196:199], v[62:65]
	v_mfma_f32_16x16x32_bf16 v[58:61], v[172:175], v[196:199], v[58:61]
	v_mfma_f32_16x16x32_bf16 v[54:57], v[164:167], v[216:219], v[54:57]
	v_mfma_f32_16x16x32_bf16 v[50:53], v[172:175], v[216:219], v[50:53]
	v_mfma_f32_16x16x32_bf16 v[38:41], v[164:167], v[224:227], v[38:41]
	v_mfma_f32_16x16x32_bf16 v[34:37], v[172:175], v[224:227], v[34:37]
	v_mfma_f32_16x16x32_bf16 v[22:25], v[164:167], v[232:235], v[22:25]
	v_mfma_f32_16x16x32_bf16 v[18:21], v[172:175], v[232:235], v[18:21]
	v_mfma_f32_16x16x32_bf16 v[62:65], v[168:171], v[200:203], v[62:65]
	v_mfma_f32_16x16x32_bf16 v[58:61], v[176:179], v[200:203], v[58:61]
	v_mfma_f32_16x16x32_bf16 v[54:57], v[168:171], v[220:223], v[54:57]
	v_mfma_f32_16x16x32_bf16 v[50:53], v[176:179], v[220:223], v[50:53]
	v_mfma_f32_16x16x32_bf16 v[38:41], v[168:171], v[228:231], v[38:41]
	v_mfma_f32_16x16x32_bf16 v[34:37], v[176:179], v[228:231], v[34:37]
	v_mfma_f32_16x16x32_bf16 v[22:25], v[168:171], v[236:239], v[22:25]
	v_mfma_f32_16x16x32_bf16 v[18:21], v[176:179], v[236:239], v[18:21]
	v_mfma_f32_16x16x32_bf16 v[46:49], v[180:183], v[196:199], v[46:49]
	v_mfma_f32_16x16x32_bf16 v[42:45], v[188:191], v[196:199], v[42:45]
	v_mfma_f32_16x16x32_bf16 v[30:33], v[180:183], v[216:219], v[30:33]
	v_mfma_f32_16x16x32_bf16 v[26:29], v[188:191], v[216:219], v[26:29]
	v_mfma_f32_16x16x32_bf16 v[14:17], v[180:183], v[224:227], v[14:17]
	v_mfma_f32_16x16x32_bf16 v[10:13], v[188:191], v[224:227], v[10:13]
	v_mfma_f32_16x16x32_bf16 v[6:9], v[180:183], v[232:235], v[6:9]
	v_mfma_f32_16x16x32_bf16 v[2:5], v[188:191], v[232:235], v[2:5]
	v_mfma_f32_16x16x32_bf16 v[46:49], v[184:187], v[200:203], v[46:49]
	v_mfma_f32_16x16x32_bf16 v[42:45], v[192:195], v[200:203], v[42:45]
	v_mfma_f32_16x16x32_bf16 v[30:33], v[184:187], v[220:223], v[30:33]
	v_mfma_f32_16x16x32_bf16 v[26:29], v[192:195], v[220:223], v[26:29]
	v_mfma_f32_16x16x32_bf16 v[14:17], v[184:187], v[228:231], v[14:17]
	v_mfma_f32_16x16x32_bf16 v[10:13], v[192:195], v[228:231], v[10:13]
	v_mfma_f32_16x16x32_bf16 v[6:9], v[184:187], v[236:239], v[6:9]
	v_mfma_f32_16x16x32_bf16 v[2:5], v[192:195], v[236:239], v[2:5]
	s_barrier
	s_add_i32 s15, 0, 0x18000
	s_add_i32 s18, 0, 0x1c000
	v_add_u32_e32 v176, s15, v161
	v_add_u32_e32 v192, s18, v161
	ds_read_b128 v[164:167], v176
	ds_read_b128 v[168:171], v176 offset:1024
	ds_read_b128 v[172:175], v176 offset:2048
	ds_read_b128 v[176:179], v176 offset:3072
	ds_read_b128 v[180:183], v192
	ds_read_b128 v[184:187], v192 offset:1024
	ds_read_b128 v[188:191], v192 offset:2048
	ds_read_b128 v[192:195], v192 offset:3072
	s_add_u32 s16, s30, 0x80000
	s_addc_u32 s17, s31, 0
	s_mov_b32 m0, s59
	v_lshl_add_u64 v[212:213], s[16:17], 0, v[134:135]
	ds_read_b128 v[196:199], v163 offset:32768
	ds_read_b128 v[200:203], v163 offset:33792
	ds_read_b128 v[216:219], v163 offset:34816
	ds_read_b128 v[220:223], v163 offset:35840
	ds_read_b128 v[224:227], v163 offset:36864
	ds_read_b128 v[228:231], v163 offset:37888
	ds_read_b128 v[232:235], v163 offset:38912
	ds_read_b128 v[236:239], v163 offset:39936
	global_load_lds_dwordx4 v[212:213], off
	v_lshl_add_u64 v[212:213], s[16:17], 0, v[132:133]
	s_mov_b32 m0, s60
	s_nop 0
	global_load_lds_dwordx4 v[212:213], off
	s_waitcnt vmcnt(8)
	s_waitcnt lgkmcnt(0)
	s_barrier
	s_waitcnt lgkmcnt(0)
	v_mfma_f32_16x16x32_bf16 v[126:129], v[164:167], v[196:199], v[126:129]
	v_mfma_f32_16x16x32_bf16 v[122:125], v[172:175], v[196:199], v[122:125]
	v_mfma_f32_16x16x32_bf16 v[118:121], v[164:167], v[216:219], v[118:121]
	v_mfma_f32_16x16x32_bf16 v[114:117], v[172:175], v[216:219], v[114:117]
	v_mfma_f32_16x16x32_bf16 v[102:105], v[164:167], v[224:227], v[102:105]
	v_mfma_f32_16x16x32_bf16 v[98:101], v[172:175], v[224:227], v[98:101]
	v_mfma_f32_16x16x32_bf16 v[86:89], v[164:167], v[232:235], v[86:89]
	v_mfma_f32_16x16x32_bf16 v[82:85], v[172:175], v[232:235], v[82:85]
	v_mfma_f32_16x16x32_bf16 v[126:129], v[168:171], v[200:203], v[126:129]
	v_mfma_f32_16x16x32_bf16 v[122:125], v[176:179], v[200:203], v[122:125]
	v_mfma_f32_16x16x32_bf16 v[118:121], v[168:171], v[220:223], v[118:121]
	v_mfma_f32_16x16x32_bf16 v[114:117], v[176:179], v[220:223], v[114:117]
	v_mfma_f32_16x16x32_bf16 v[102:105], v[168:171], v[228:231], v[102:105]
	v_mfma_f32_16x16x32_bf16 v[98:101], v[176:179], v[228:231], v[98:101]
	v_mfma_f32_16x16x32_bf16 v[86:89], v[168:171], v[236:239], v[86:89]
	v_mfma_f32_16x16x32_bf16 v[82:85], v[176:179], v[236:239], v[82:85]
	v_mfma_f32_16x16x32_bf16 v[110:113], v[180:183], v[196:199], v[110:113]
	v_mfma_f32_16x16x32_bf16 v[106:109], v[188:191], v[196:199], v[106:109]
	v_mfma_f32_16x16x32_bf16 v[94:97], v[180:183], v[216:219], v[94:97]
	v_mfma_f32_16x16x32_bf16 v[90:93], v[188:191], v[216:219], v[90:93]
	v_mfma_f32_16x16x32_bf16 v[78:81], v[180:183], v[224:227], v[78:81]
	v_mfma_f32_16x16x32_bf16 v[74:77], v[188:191], v[224:227], v[74:77]
	v_mfma_f32_16x16x32_bf16 v[70:73], v[180:183], v[232:235], v[70:73]
	v_mfma_f32_16x16x32_bf16 v[66:69], v[188:191], v[232:235], v[66:69]
	v_mfma_f32_16x16x32_bf16 v[110:113], v[184:187], v[200:203], v[110:113]
	v_mfma_f32_16x16x32_bf16 v[106:109], v[192:195], v[200:203], v[106:109]
	v_mfma_f32_16x16x32_bf16 v[94:97], v[184:187], v[220:223], v[94:97]
	v_mfma_f32_16x16x32_bf16 v[90:93], v[192:195], v[220:223], v[90:93]
	v_mfma_f32_16x16x32_bf16 v[78:81], v[184:187], v[228:231], v[78:81]
	v_mfma_f32_16x16x32_bf16 v[74:77], v[192:195], v[228:231], v[74:77]
	v_mfma_f32_16x16x32_bf16 v[70:73], v[184:187], v[236:239], v[70:73]
	v_mfma_f32_16x16x32_bf16 v[66:69], v[192:195], v[236:239], v[66:69]
	s_barrier
; #define PG8_STAGE(bufoff, gbase, voff) do { _Pragma("unroll") for (int _i = 0; _i < 2; ++_i) \
;         __builtin_amdgcn_global_load_lds((const unsigned*)((const char*)(gbase) + (voff)[_i]), (LAS unsigned*)(lds + (bufoff) + ldsw + _i * 8192), 16, 0, 0); } while (0)
; #define PG8_STAGE_A(bufoff, kptr, half, VO) do { if constexpr (GATHER) { _Pragma("unroll") for (int _i = 0; _i < 2; ++_i) \
;         __builtin_amdgcn_global_load_lds((const unsigned*)((const char*)(kptr) + (VO)[half][_i]), (LAS unsigned*)(lds + (bufoff) + ldsw + _i * 8192), 16, 0, 0); } \
;         else { PG8_STAGE(bufoff, (kptr) + (half) * hstepA, voffA); } } while (0)
; #define PG8_WAIT_V(n) asm volatile("s_waitcnt vmcnt(" #n ")" ::: "memory")
;     ...
;         for (int t = 0; t < nt; t += 2) {
;             const bool last = (t == nt - 2);
;             const char* a1 = cA + (size_t)(t + 1) * kstep;
;             const char* a2 = last ? nA : cA + (size_t)(t + 2) * kstep; const char* b2 = last ? nB : cB + (size_t)(t + 2) * kstep;
;             const char* a3 = a2 + kstep; const char* b3 = b2 + kstep;
;             unsigned g2[2][2];
;             if constexpr (GATHER) {
; #pragma unroll
;                 for (int _h = 0; _h < 2; ++_h)
; #pragma unroll
;                     for (int _i = 0; _i < 2; ++_i) g2[_h][_i] = last ? gN[_h][_i] : gC[_h][_i]; }
;             if constexpr (SP2) {
;             PG8_LDB(B0, 0, 0); PG8_LDB(B1, 0, 1); PG8_SCHED; PG8_LDA(At, 0, 0); PG8_STAGE_A(PG8_SA(1, 1), a1, 1, gC);
;             PG8_WAIT_V(8); PG8_WAIT_L(0); PG8_BAR; PG8_MMA(0, 0, At, B0); PG8_MMA(0, 1, At, B1); PG8_BAR; PG8_SCHED;
;             PG8_LDA(At, 0, 1); PG8_STAGE(PG8_SB(0, 0), b2, voffB); PG8_STAGE(PG8_SB(0, 1), b2 + hstepB, voffB); PG8_STAGE_A(PG8_SA(0, 0), a2, 0, g2);
;             PG8_WAIT_V(8); PG8_WAIT_L(0); PG8_BAR; PG8_MMA(1, 0, At, B0); PG8_MMA(1, 1, At, B1); PG8_BAR; PG8_SCHED;
;             PG8_LDB(B0, 1, 0); PG8_LDB(B1, 1, 1); PG8_SCHED; PG8_LDA(At, 1, 0); PG8_STAGE_A(PG8_SA(0, 1), a2, 1, g2);
;             PG8_WAIT_V(8); PG8_WAIT_L(0); PG8_BAR; PG8_MMA(0, 0, At, B0); PG8_MMA(0, 1, At, B1); PG8_BAR; PG8_SCHED;
;             PG8_LDA(At, 1, 1); PG8_STAGE(PG8_SB(1, 0), b3, voffB); PG8_STAGE(PG8_SB(1, 1), b3 + hstepB, voffB); PG8_STAGE_A(PG8_SA(1, 0), a3, 0, g2);
;             PG8_WAIT_V(8); PG8_WAIT_L(0); PG8_BAR; PG8_MMA(1, 0, At, B0); PG8_MMA(1, 1, At, B1); PG8_BAR; PG8_SCHED;
	s_add_i32 s15, s15, s52
	v_lshl_add_u64 v[158:159], v[158:159], 0, s[8:9]
	s_mov_b32 m0, s15
	ds_read_b128 v[196:199], v163 offset:49152
	ds_read_b128 v[200:203], v163 offset:50176
	ds_read_b128 v[216:219], v163 offset:51200
	ds_read_b128 v[220:223], v163 offset:52224
	ds_read_b128 v[224:227], v163 offset:53248
	ds_read_b128 v[228:231], v163 offset:54272
	ds_read_b128 v[232:235], v163 offset:55296
	ds_read_b128 v[236:239], v163 offset:56320
	global_load_lds_dwordx4 v[158:159], off
	s_add_i32 m0, s15, 0x2000
	s_add_u32 s0, s0, 0x80080
	v_lshl_add_u64 v[158:159], v[204:205], 0, s[8:9]
	s_addc_u32 s1, s1, 0
	s_add_i32 s15, s18, s52
	global_load_lds_dwordx4 v[158:159], off
	v_lshl_add_u64 v[158:159], s[0:1], 0, v[206:207]
	s_mov_b32 m0, s15
	s_nop 0
	global_load_lds_dwordx4 v[158:159], off
	v_lshl_add_u64 v[158:159], s[0:1], 0, v[130:131]
	s_add_i32 m0, s15, 0x2000
	s_nop 0
	global_load_lds_dwordx4 v[158:159], off
	v_lshl_add_u64 v[158:159], v[208:209], 0, s[8:9]
	s_mov_b32 m0, s61
	s_nop 0
	global_load_lds_dwordx4 v[158:159], off
	v_lshl_add_u64 v[158:159], v[210:211], 0, s[8:9]
	s_mov_b32 m0, s62
	s_nop 0
	global_load_lds_dwordx4 v[158:159], off
	s_waitcnt vmcnt(8)
	s_waitcnt lgkmcnt(0)
	s_barrier
	s_waitcnt lgkmcnt(0)
	v_mfma_f32_16x16x32_bf16 v[62:65], v[164:167], v[196:199], v[62:65]
	v_mfma_f32_16x16x32_bf16 v[58:61], v[172:175], v[196:199], v[58:61]
	v_mfma_f32_16x16x32_bf16 v[54:57], v[164:167], v[216:219], v[54:57]
	v_mfma_f32_16x16x32_bf16 v[50:53], v[172:175], v[216:219], v[50:53]
	v_mfma_f32_16x16x32_bf16 v[38:41], v[164:167], v[224:227], v[38:41]
	v_mfma_f32_16x16x32_bf16 v[34:37], v[172:175], v[224:227], v[34:37]
	v_mfma_f32_16x16x32_bf16 v[22:25], v[164:167], v[232:235], v[22:25]
	v_mfma_f32_16x16x32_bf16 v[18:21], v[172:175], v[232:235], v[18:21]
	v_mfma_f32_16x16x32_bf16 v[62:65], v[168:171], v[200:203], v[62:65]
	v_mfma_f32_16x16x32_bf16 v[58:61], v[176:179], v[200:203], v[58:61]
	v_mfma_f32_16x16x32_bf16 v[54:57], v[168:171], v[220:223], v[54:57]
	v_mfma_f32_16x16x32_bf16 v[50:53], v[176:179], v[220:223], v[50:53]
	v_mfma_f32_16x16x32_bf16 v[38:41], v[168:171], v[228:231], v[38:41]
	v_mfma_f32_16x16x32_bf16 v[34:37], v[176:179], v[228:231], v[34:37]
	v_mfma_f32_16x16x32_bf16 v[22:25], v[168:171], v[236:239], v[22:25]
	v_mfma_f32_16x16x32_bf16 v[18:21], v[176:179], v[236:239], v[18:21]
	v_mfma_f32_16x16x32_bf16 v[46:49], v[180:183], v[196:199], v[46:49]
	v_mfma_f32_16x16x32_bf16 v[42:45], v[188:191], v[196:199], v[42:45]
	v_mfma_f32_16x16x32_bf16 v[30:33], v[180:183], v[216:219], v[30:33]
	v_mfma_f32_16x16x32_bf16 v[26:29], v[188:191], v[216:219], v[26:29]
	v_mfma_f32_16x16x32_bf16 v[14:17], v[180:183], v[224:227], v[14:17]
	v_mfma_f32_16x16x32_bf16 v[10:13], v[188:191], v[224:227], v[10:13]
	v_mfma_f32_16x16x32_bf16 v[6:9], v[180:183], v[232:235], v[6:9]
	v_mfma_f32_16x16x32_bf16 v[2:5], v[188:191], v[232:235], v[2:5]
	v_mfma_f32_16x16x32_bf16 v[46:49], v[184:187], v[200:203], v[46:49]
	v_mfma_f32_16x16x32_bf16 v[42:45], v[192:195], v[200:203], v[42:45]
	v_mfma_f32_16x16x32_bf16 v[30:33], v[184:187], v[220:223], v[30:33]
	v_mfma_f32_16x16x32_bf16 v[26:29], v[192:195], v[220:223], v[26:29]
	v_mfma_f32_16x16x32_bf16 v[14:17], v[184:187], v[228:231], v[14:17]
	v_mfma_f32_16x16x32_bf16 v[10:13], v[192:195], v[228:231], v[10:13]
	v_mfma_f32_16x16x32_bf16 v[6:9], v[184:187], v[236:239], v[6:9]
	v_mfma_f32_16x16x32_bf16 v[2:5], v[192:195], v[236:239], v[2:5]
	s_barrier
	s_add_i32 s14, s14, 2
	s_add_u32 s24, s24, 0x100
	s_addc_u32 s25, s25, 0
	s_add_u32 s12, s12, 0x100
	s_addc_u32 s13, s13, 0
	s_cmp_gt_u32 s14, 29
	s_cbranch_scc0 .LBB0_1669
	s_and_b64 vcc, exec, s[38:39]
	s_cbranch_vccz .LBB0_1672
	s_barrier

; __device__ __forceinline__ int opaque_tid() { int t = threadIdx.x; asm volatile("" : "+v"(t)); return t; }
; #define PG8_GOFF(u, o) do { _Pragma("unroll") for (int _h = 0; _h < 2; ++_h) _Pragma("unroll") for (int _i = 0; _i < 2; ++_i) { const int _r = (u).pm * 256 + _h * 128 + gR[_i]; \
;         const int _tok = _r < nvalid ? rowtok[(u).pb * EROWS + _r] : 0; (o)[_h][_i] = (unsigned)(_tok * g.lda + gCc[_i]) * 2u; } } while (0)
; #define PG8_WAIT_V(n) asm volatile("s_waitcnt vmcnt(" #n ")" ::: "memory")
;     const int tid = opaque_tid(), wid = __builtin_amdgcn_readfirstlane(tid >> 6), lane = tid & 63, wr = wid >> 2, wc = wid & 3, fr = lane & 15, fq = lane >> 4;
;     const int K = g.K, nt = K / BK;
;     unsigned voffA[2], voffB[2]; int gR[2], gCc[2];
; #pragma unroll
;     for (int i = 0; i < 2; ++i) { int R, C; stage_rc(tid * 16 + i * 8192, R, C); const int Rb = Epi::PERM ? ((R & ~31) + perm32(R & 31)) : R;
;         voffA[i] = (unsigned)(R * g.lda + C) * 2u; voffB[i] = (unsigned)(Rb * g.ldb + C) * 2u; gR[i] = R; gCc[i] = C; }
;     unsigned gC[2][2], gN[2][2];
;     ...
;     const size_t kstep = (size_t)(BK * 2);
;     const size_t hstepA = (size_t)HALF * g.lda * 2, hstepB = (size_t)HALF * g.ldb * 2;
;     const unsigned ldsw = (unsigned)wid * 1024u;
;     const int aoff = lds_byte(wr * 64 + fr, fq * 8), boff = lds_byte(wc * 32 + fr, fq * 8);
;     ...
;     Unit cur, nxt; int ui = 0;
;     if (!S.next(0, cur)) return;
;     f32x4 acc[2][2][4][2];
; #pragma unroll
;     for (int a = 0; a < 2; ++a)
; #pragma unroll
;         for (int b = 0; b < 2; ++b)
; #pragma unroll
;             for (int m = 0; m < 4; ++m)
; #pragma unroll
;                 for (int n = 0; n < 2; ++n) acc[a][b][m][n] = (f32x4){0.f, 0.f, 0.f, 0.f};
;     bf16x8 At[4][2], B0[2][2], B1[2][2];
;     const char* cA = cur.a; const char* cB = cur.b;
;     if constexpr (GATHER) { PG8_GOFF(cur, gC); }
;     if constexpr (SP2) {
;         PG8_STAGE(PG8_SB(0, 0), cB, voffB); PG8_STAGE(PG8_SB(0, 1), cB + hstepB, voffB); PG8_STAGE_A(PG8_SA(0, 0), cA, 0, gC); PG8_STAGE_A(PG8_SA(0, 1), cA, 1, gC);
;         if (wr == 1) PG8_BAR;
;         PG8_WAIT_V(2); PG8_BAR;
; __global__ void __launch_bounds__(512, 2) fwd(Params p) {
;     ...
;             else { pg8::EpiOutBf Eb{(const bf16_t*)(ws + WS_XA), mod + 2 * DM, (bf16_t*)(ws + WS_XB)}; pg8::gemm_phase(lds, pg8::Desc{DM, DM, DM}, S, Eb); }
.LBB0_1683:
	s_and_b64 vcc, exec, s[0:1]
	s_cbranch_vccz .LBB0_1702
	v_mov_b32_e32 v2, v0
	s_cmpk_gt_i32 s54, 0xff
	s_nop 0
	v_readfirstlane_b32 s12, v2
	s_cbranch_scc1 .LBB0_1702
	v_lshlrev_b32_e32 v6, 4, v2
	v_add_u32_e32 v4, 0x2000, v6
	v_ashrrev_i32_e32 v3, 31, v4
	v_lshrrev_b32_e32 v3, 22, v3
	v_add_u32_e32 v3, v4, v3
	s_lshr_b32 s0, s57, 24
	v_ashrrev_i32_e32 v3, 10, v3
	s_add_i32 s0, s54, s0
	v_mul_i32_i24_e32 v5, 0x400, v3
	s_and_b32 s0, s0, 0xff00
	v_sub_u32_e32 v4, v4, v5
	s_sub_i32 s0, s54, s0
	v_lshrrev_b32_e32 v5, 4, v4
	s_sext_i32_i16 s1, s0
	v_bitop3_b32 v5, v5, v4, 32 bitop3:0x6c
	s_bfe_u32 s1, s1, 0x3001c
	v_ashrrev_i32_e32 v4, 31, v5
	s_add_i32 s1, s0, s1
	v_lshrrev_b32_e32 v4, 26, v4
	s_sext_i32_i16 s2, s1
	s_and_b32 s1, s1, 0xfff8
	v_add_u32_e32 v7, v5, v4
	v_lshlrev_b32_e32 v8, 3, v3
	s_ashr_i32 s14, s12, 6
	s_sub_i32 s0, s0, s1
	v_ashrrev_i32_e32 v4, 6, v7
	v_and_b32_e32 v8, -16, v8
	s_ashr_i32 s13, s12, 8
	s_lshl_b32 s52, s14, 10
	s_ashr_i32 s2, s2, 3
	s_sext_i32_i16 s1, s0
	s_lshl_b32 s3, s0, 5
	v_add_u32_e32 v8, v4, v8
	s_cmp_lt_i32 s1, 0
	v_and_b32_e32 v9, 3, v4
	s_mov_b32 s1, 0xfffe0
	v_lshrrev_b32_e32 v10, 2, v8
	v_lshlrev_b32_e32 v11, 1, v8
	v_and_b32_e32 v7, 0xc0, v7
	v_and_or_b32 v9, v8, s1, v9
	v_and_b32_e32 v10, 4, v10
	v_and_b32_e32 v11, 24, v11
	v_sub_u32_e32 v5, v5, v7
	v_or3_b32 v9, v9, v10, v11
	v_lshlrev_b32_e32 v10, 5, v3
	v_ashrrev_i16_sdwa v5, v245, sext(v5) dst_sel:DWORD dst_unused:UNUSED_PAD src0_sel:DWORD src1_sel:BYTE_0
	v_and_b32_e32 v10, 32, v10
	v_bfe_i32 v5, v5, 0, 16
	v_add_lshl_u32 v7, v10, v5, 1
	v_lshl_add_u32 v216, v9, 12, v7
	v_lshl_add_u32 v218, v8, 12, v7
	v_bfe_i32 v7, v2, 27, 1
	v_lshrrev_b32_e32 v7, 22, v7
	v_add_u32_e32 v7, v6, v7
	v_and_b32_e32 v7, 0xfffffc00, v7
	v_sub_u32_e32 v6, v6, v7
	v_lshrrev_b32_e32 v7, 4, v6
	v_bitop3_b32 v8, v7, v6, 32 bitop3:0x6c
	v_ashrrev_i32_e32 v7, 31, v2
	v_lshrrev_b32_e32 v7, 26, v7
	v_ashrrev_i32_e32 v6, 31, v6
	v_add_u32_e32 v7, v2, v7
	v_lshrrev_b32_e32 v6, 26, v6
	v_ashrrev_i32_e32 v7, 6, v7
	s_mul_i32 s0, s0, 33
	v_add_u32_e32 v6, v8, v6
	v_lshlrev_b32_e32 v9, 3, v7
	v_ashrrev_i32_e32 v6, 6, v6
	v_and_b32_e32 v9, -16, v9
	s_cselect_b32 s0, s0, s3
	v_add_u32_e32 v9, v6, v9
	v_and_b32_e32 v10, 3, v6
	s_add_i32 s0, s0, s2
	v_and_or_b32 v10, v9, s1, v10
	s_sext_i32_i16 s1, s0
	s_bfe_u32 s1, s1, 0x60019
	s_add_i32 s1, s0, s1
	s_sext_i32_i16 s2, s1
	s_and_b32 s1, s1, 0xffc0
	s_sub_i32 s0, s0, s1
	s_bfe_i32 s1, s0, 0x80000
	s_bfe_u32 s1, s1, 0x3000c
	s_add_i32 s1, s0, s1
	s_bfe_i32 s3, s1, 0x80000
	s_and_b32 s1, s1, 0xf8
	s_ashr_i32 s2, s2, 6
	s_sub_i32 s0, s0, s1
	s_lshl_b32 s2, s2, 3
	s_sext_i32_i8 s0, s0
	s_add_i32 s48, s2, s0
	v_lshrrev_b32_e32 v11, 2, v9
	v_lshlrev_b32_e32 v12, 1, v9
	s_sext_i32_i16 s3, s3
	s_ashr_i32 s49, s48, 31
	v_and_b32_e32 v11, 4, v11
	v_and_b32_e32 v12, 24, v12
	s_lshr_b32 s4, s3, 3
	s_lshl_b64 s[0:1], s[48:49], 20
	v_readlane_b32 s2, v253, 47
	v_or3_b32 v10, v10, v11, v12
	v_mul_i32_i24_e32 v12, 64, v6
	v_readlane_b32 s3, v253, 48
	s_add_u32 s0, s2, s0
	v_sub_u32_e32 v8, v8, v12
	s_addc_u32 s1, s3, s1
	s_bfe_i64 s[2:3], s[4:5], 0x100000
	v_lshlrev_b32_e32 v11, 5, v7
	v_ashrrev_i16_sdwa v8, v245, sext(v8) dst_sel:DWORD dst_unused:UNUSED_PAD src0_sel:DWORD src1_sel:BYTE_0
	s_lshl_b64 s[2:3], s[2:3], 20
	v_and_b32_e32 v11, 32, v11
	v_bfe_i32 v8, v8, 0, 16
	s_add_u32 s30, s26, s2
	v_add_lshl_u32 v11, v11, v8, 1
	s_addc_u32 s31, s27, s3
	s_add_i32 s49, s52, 0
	v_lshl_add_u32 v206, v10, 12, v11
	s_add_i32 m0, s49, 0x10000
	v_lshl_add_u32 v220, v9, 12, v11
	global_load_lds_dwordx4 v206, s[30:31]
	s_add_i32 m0, s49, 0x12000
	s_add_u32 s2, s30, 0x80000
	global_load_lds_dwordx4 v216, s[30:31]
	s_addc_u32 s3, s31, 0
	s_add_i32 m0, s49, 0x14000
	s_add_i32 s53, s49, 0x2000
	global_load_lds_dwordx4 v206, s[2:3]
	s_add_i32 m0, s49, 0x16000
	s_nop 0
	global_load_lds_dwordx4 v216, s[2:3]
	s_mov_b32 m0, s49
	s_add_u32 s2, s0, 0x80000
	global_load_lds_dwordx4 v220, s[0:1]
	s_mov_b32 m0, s53
	s_addc_u32 s3, s1, 0
	s_add_i32 s59, s49, 0x4000
	global_load_lds_dwordx4 v218, s[0:1]
	s_mov_b32 m0, s59
	s_add_i32 s60, s49, 0x6000
	global_load_lds_dwordx4 v220, s[2:3]
	s_mov_b32 m0, s60
	s_cmp_eq_u32 s13, 1
	global_load_lds_dwordx4 v218, s[2:3]
	s_cselect_b64 s[2:3], -1, 0
	s_cmp_lg_u32 s13, 1
	s_cbranch_scc1 .LBB0_1687
	s_barrier
	s_setprio 1

; #define PG8_STAGE(bufoff, gbase, voff) do { _Pragma("unroll") for (int _i = 0; _i < 2; ++_i) \
;         __builtin_amdgcn_global_load_lds((const unsigned*)((const char*)(gbase) + (voff)[_i]), (LAS unsigned*)(lds + (bufoff) + ldsw + _i * 8192), 16, 0, 0); } while (0)
; #define PG8_STAGE_A(bufoff, kptr, half, VO) do { if constexpr (GATHER) { _Pragma("unroll") for (int _i = 0; _i < 2; ++_i) \
;         __builtin_amdgcn_global_load_lds((const unsigned*)((const char*)(kptr) + (VO)[half][_i]), (LAS unsigned*)(lds + (bufoff) + ldsw + _i * 8192), 16, 0, 0); } \
;         else { PG8_STAGE(bufoff, (kptr) + (half) * hstepA, voffA); } } while (0)
; #define PG8_WAIT_V(n) asm volatile("s_waitcnt vmcnt(" #n ")" ::: "memory")
;     ...
;         for (int t = 0; t < nt; t += 2) {
;             const bool last = (t == nt - 2);
;             const char* a1 = cA + (size_t)(t + 1) * kstep;
;             const char* a2 = last ? nA : cA + (size_t)(t + 2) * kstep; const char* b2 = last ? nB : cB + (size_t)(t + 2) * kstep;
;             const char* a3 = a2 + kstep; const char* b3 = b2 + kstep;
;             unsigned g2[2][2];
;             if constexpr (GATHER) {
; #pragma unroll
;                 for (int _h = 0; _h < 2; ++_h)
; #pragma unroll
;                     for (int _i = 0; _i < 2; ++_i) g2[_h][_i] = last ? gN[_h][_i] : gC[_h][_i]; }
;             if constexpr (SP2) {
;             PG8_LDB(B0, 0, 0); PG8_LDB(B1, 0, 1); PG8_SCHED; PG8_LDA(At, 0, 0); PG8_STAGE_A(PG8_SA(1, 1), a1, 1, gC);
;             PG8_WAIT_V(8); PG8_WAIT_L(0); PG8_BAR; PG8_MMA(0, 0, At, B0); PG8_MMA(0, 1, At, B1); PG8_BAR; PG8_SCHED;
;             PG8_LDA(At, 0, 1); PG8_STAGE(PG8_SB(0, 0), b2, voffB); PG8_STAGE(PG8_SB(0, 1), b2 + hstepB, voffB); PG8_STAGE_A(PG8_SA(0, 0), a2, 0, g2);
;             PG8_WAIT_V(8); PG8_WAIT_L(0); PG8_BAR; PG8_MMA(1, 0, At, B0); PG8_MMA(1, 1, At, B1); PG8_BAR; PG8_SCHED;
;             PG8_LDB(B0, 1, 0); PG8_LDB(B1, 1, 1); PG8_SCHED; PG8_LDA(At, 1, 0); PG8_STAGE_A(PG8_SA(0, 1), a2, 1, g2);
;             PG8_WAIT_V(8); PG8_WAIT_L(0); PG8_BAR; PG8_MMA(0, 0, At, B0); PG8_MMA(0, 1, At, B1); PG8_BAR; PG8_SCHED;
;             PG8_LDA(At, 1, 1); PG8_STAGE(PG8_SB(1, 0), b3, voffB); PG8_STAGE(PG8_SB(1, 1), b3 + hstepB, voffB); PG8_STAGE_A(PG8_SA(1, 0), a3, 0, g2);
;             PG8_WAIT_V(8); PG8_WAIT_L(0); PG8_BAR; PG8_MMA(1, 0, At, B0); PG8_MMA(1, 1, At, B1); PG8_BAR; PG8_SCHED;
.LBB0_1693:
	s_add_u32 s0, s24, 0xfff80080
	s_addc_u32 s1, s25, -1
	s_add_i32 s15, 0, 0x10000
	s_cmp_eq_u32 s14, 28
	s_cselect_b32 s31, s45, s1
	s_cselect_b32 s30, s44, s0
	s_cselect_b32 s1, s47, s13
	s_cselect_b32 s0, s46, s12
	s_add_i32 s18, 0, 0x14000
	v_add_u32_e32 v142, s15, v244
	v_add_u32_e32 v158, s18, v244
	ds_read_b128 v[122:125], v142
	ds_read_b128 v[126:129], v142 offset:1024
	ds_read_b128 v[134:137], v142 offset:2048
	ds_read_b128 v[142:145], v142 offset:3072
	ds_read_b128 v[146:149], v158
	ds_read_b128 v[150:153], v158 offset:1024
	ds_read_b128 v[154:157], v158 offset:2048
	ds_read_b128 v[158:161], v158 offset:3072
	v_lshl_add_u64 v[194:195], s[24:25], 0, v[222:223]
	s_add_i32 m0, s49, 0xc000
	ds_read_b128 v[162:165], v209
	ds_read_b128 v[166:169], v209 offset:1024
	ds_read_b128 v[170:173], v209 offset:2048
	ds_read_b128 v[174:177], v209 offset:3072
	ds_read_b128 v[178:181], v209 offset:4096
	ds_read_b128 v[182:185], v209 offset:5120
	ds_read_b128 v[186:189], v209 offset:6144
	ds_read_b128 v[190:193], v209 offset:7168
	global_load_lds_dwordx4 v[194:195], off
	v_lshl_add_u64 v[194:195], s[24:25], 0, v[224:225]
	s_add_i32 m0, s49, 0xe000
	s_nop 0
	global_load_lds_dwordx4 v[194:195], off
	s_waitcnt vmcnt(8)
	s_waitcnt lgkmcnt(0)
	s_barrier
	s_waitcnt lgkmcnt(0)
	v_mfma_f32_16x16x32_bf16 v[138:141], v[122:125], v[162:165], v[138:141]
	v_mfma_f32_16x16x32_bf16 v[130:133], v[134:137], v[162:165], v[130:133]
	v_mfma_f32_16x16x32_bf16 v[114:117], v[122:125], v[170:173], v[114:117]
	v_mfma_f32_16x16x32_bf16 v[106:109], v[134:137], v[170:173], v[106:109]
	v_mfma_f32_16x16x32_bf16 v[98:101], v[122:125], v[178:181], v[98:101]
	v_mfma_f32_16x16x32_bf16 v[90:93], v[134:137], v[178:181], v[90:93]
	v_mfma_f32_16x16x32_bf16 v[82:85], v[122:125], v[186:189], v[82:85]
	v_mfma_f32_16x16x32_bf16 v[74:77], v[134:137], v[186:189], v[74:77]
	v_mfma_f32_16x16x32_bf16 v[138:141], v[126:129], v[166:169], v[138:141]
	v_mfma_f32_16x16x32_bf16 v[130:133], v[142:145], v[166:169], v[130:133]
	v_mfma_f32_16x16x32_bf16 v[114:117], v[126:129], v[174:177], v[114:117]
	v_mfma_f32_16x16x32_bf16 v[106:109], v[142:145], v[174:177], v[106:109]
	v_mfma_f32_16x16x32_bf16 v[98:101], v[126:129], v[182:185], v[98:101]
	v_mfma_f32_16x16x32_bf16 v[90:93], v[142:145], v[182:185], v[90:93]
	v_mfma_f32_16x16x32_bf16 v[82:85], v[126:129], v[190:193], v[82:85]
	v_mfma_f32_16x16x32_bf16 v[74:77], v[142:145], v[190:193], v[74:77]
	v_mfma_f32_16x16x32_bf16 v[118:121], v[146:149], v[162:165], v[118:121]
	v_mfma_f32_16x16x32_bf16 v[110:113], v[154:157], v[162:165], v[110:113]
	v_mfma_f32_16x16x32_bf16 v[102:105], v[146:149], v[170:173], v[102:105]
	v_mfma_f32_16x16x32_bf16 v[94:97], v[154:157], v[170:173], v[94:97]
	v_mfma_f32_16x16x32_bf16 v[86:89], v[146:149], v[178:181], v[86:89]
	v_mfma_f32_16x16x32_bf16 v[78:81], v[154:157], v[178:181], v[78:81]
	v_mfma_f32_16x16x32_bf16 v[70:73], v[146:149], v[186:189], v[70:73]
	v_mfma_f32_16x16x32_bf16 v[66:69], v[154:157], v[186:189], v[66:69]
	v_mfma_f32_16x16x32_bf16 v[118:121], v[150:153], v[166:169], v[118:121]
	v_mfma_f32_16x16x32_bf16 v[110:113], v[158:161], v[166:169], v[110:113]
	v_mfma_f32_16x16x32_bf16 v[102:105], v[150:153], v[174:177], v[102:105]
	v_mfma_f32_16x16x32_bf16 v[94:97], v[158:161], v[174:177], v[94:97]
	v_mfma_f32_16x16x32_bf16 v[86:89], v[150:153], v[182:185], v[86:89]
	v_mfma_f32_16x16x32_bf16 v[78:81], v[158:161], v[182:185], v[78:81]
	v_mfma_f32_16x16x32_bf16 v[70:73], v[150:153], v[190:193], v[70:73]
	v_mfma_f32_16x16x32_bf16 v[66:69], v[158:161], v[190:193], v[66:69]
	s_barrier
	s_add_i32 s15, s15, s52
	v_lshl_add_u64 v[194:195], s[0:1], 0, v[206:207]
	s_mov_b32 m0, s15
	ds_read_b128 v[162:165], v209 offset:16384
	ds_read_b128 v[166:169], v209 offset:17408
	ds_read_b128 v[170:173], v209 offset:18432
	ds_read_b128 v[174:177], v209 offset:19456
	ds_read_b128 v[178:181], v209 offset:20480
	ds_read_b128 v[182:185], v209 offset:21504
	ds_read_b128 v[186:189], v209 offset:22528
	ds_read_b128 v[190:193], v209 offset:23552
	global_load_lds_dwordx4 v[194:195], off
	s_add_i32 m0, s15, 0x2000
	s_add_u32 s16, s0, 0x80000
	v_lshl_add_u64 v[196:197], s[0:1], 0, v[216:217]
	s_addc_u32 s17, s1, 0
	s_add_i32 s15, s18, s52
	global_load_lds_dwordx4 v[196:197], off
	v_lshl_add_u64 v[198:199], s[16:17], 0, v[206:207]
	s_mov_b32 m0, s15
	v_lshl_add_u64 v[200:201], s[30:31], 0, v[218:219]
	global_load_lds_dwordx4 v[198:199], off
	v_lshl_add_u64 v[198:199], s[16:17], 0, v[216:217]
	s_add_i32 m0, s15, 0x2000
	s_nop 0
	global_load_lds_dwordx4 v[198:199], off
	v_lshl_add_u64 v[198:199], s[30:31], 0, v[220:221]
	s_mov_b32 m0, s49
	s_nop 0
	global_load_lds_dwordx4 v[198:199], off
	s_mov_b32 m0, s53
	s_nop 0
	global_load_lds_dwordx4 v[200:201], off
	s_waitcnt vmcnt(8)
	s_waitcnt lgkmcnt(0)
	s_barrier
; #define PG8_STAGE(bufoff, gbase, voff) do { _Pragma("unroll") for (int _i = 0; _i < 2; ++_i) \
;         __builtin_amdgcn_global_load_lds((const unsigned*)((const char*)(gbase) + (voff)[_i]), (LAS unsigned*)(lds + (bufoff) + ldsw + _i * 8192), 16, 0, 0); } while (0)
; #define PG8_STAGE_A(bufoff, kptr, half, VO) do { if constexpr (GATHER) { _Pragma("unroll") for (int _i = 0; _i < 2; ++_i) \
;         __builtin_amdgcn_global_load_lds((const unsigned*)((const char*)(kptr) + (VO)[half][_i]), (LAS unsigned*)(lds + (bufoff) + ldsw + _i * 8192), 16, 0, 0); } \
;         else { PG8_STAGE(bufoff, (kptr) + (half) * hstepA, voffA); } } while (0)
; #define PG8_WAIT_V(n) asm volatile("s_waitcnt vmcnt(" #n ")" ::: "memory")
;     ...
;         for (int t = 0; t < nt; t += 2) {
;             const bool last = (t == nt - 2);
;             const char* a1 = cA + (size_t)(t + 1) * kstep;
;             const char* a2 = last ? nA : cA + (size_t)(t + 2) * kstep; const char* b2 = last ? nB : cB + (size_t)(t + 2) * kstep;
;             const char* a3 = a2 + kstep; const char* b3 = b2 + kstep;
;             unsigned g2[2][2];
;             if constexpr (GATHER) {
; #pragma unroll
;                 for (int _h = 0; _h < 2; ++_h)
; #pragma unroll
;                     for (int _i = 0; _i < 2; ++_i) g2[_h][_i] = last ? gN[_h][_i] : gC[_h][_i]; }
;             if constexpr (SP2) {
;             PG8_LDB(B0, 0, 0); PG8_LDB(B1, 0, 1); PG8_SCHED; PG8_LDA(At, 0, 0); PG8_STAGE_A(PG8_SA(1, 1), a1, 1, gC);
;             PG8_WAIT_V(8); PG8_WAIT_L(0); PG8_BAR; PG8_MMA(0, 0, At, B0); PG8_MMA(0, 1, At, B1); PG8_BAR; PG8_SCHED;
;             PG8_LDA(At, 0, 1); PG8_STAGE(PG8_SB(0, 0), b2, voffB); PG8_STAGE(PG8_SB(0, 1), b2 + hstepB, voffB); PG8_STAGE_A(PG8_SA(0, 0), a2, 0, g2);
;             PG8_WAIT_V(8); PG8_WAIT_L(0); PG8_BAR; PG8_MMA(1, 0, At, B0); PG8_MMA(1, 1, At, B1); PG8_BAR; PG8_SCHED;
;             PG8_LDB(B0, 1, 0); PG8_LDB(B1, 1, 1); PG8_SCHED; PG8_LDA(At, 1, 0); PG8_STAGE_A(PG8_SA(0, 1), a2, 1, g2);
;             PG8_WAIT_V(8); PG8_WAIT_L(0); PG8_BAR; PG8_MMA(0, 0, At, B0); PG8_MMA(0, 1, At, B1); PG8_BAR; PG8_SCHED;
;             PG8_LDA(At, 1, 1); PG8_STAGE(PG8_SB(1, 0), b3, voffB); PG8_STAGE(PG8_SB(1, 1), b3 + hstepB, voffB); PG8_STAGE_A(PG8_SA(1, 0), a3, 0, g2);
;             PG8_WAIT_V(8); PG8_WAIT_L(0); PG8_BAR; PG8_MMA(1, 0, At, B0); PG8_MMA(1, 1, At, B1); PG8_BAR; PG8_SCHED;
	s_waitcnt lgkmcnt(0)
	v_mfma_f32_16x16x32_bf16 v[62:65], v[122:125], v[162:165], v[62:65]
	v_mfma_f32_16x16x32_bf16 v[58:61], v[134:137], v[162:165], v[58:61]
	v_mfma_f32_16x16x32_bf16 v[50:53], v[122:125], v[170:173], v[50:53]
	v_mfma_f32_16x16x32_bf16 v[42:45], v[134:137], v[170:173], v[42:45]
	v_mfma_f32_16x16x32_bf16 v[34:37], v[122:125], v[178:181], v[34:37]
	v_mfma_f32_16x16x32_bf16 v[26:29], v[134:137], v[178:181], v[26:29]
	v_mfma_f32_16x16x32_bf16 v[18:21], v[122:125], v[186:189], v[18:21]
	v_mfma_f32_16x16x32_bf16 v[10:13], v[134:137], v[186:189], v[10:13]
	v_mfma_f32_16x16x32_bf16 v[62:65], v[126:129], v[166:169], v[62:65]
	v_mfma_f32_16x16x32_bf16 v[58:61], v[142:145], v[166:169], v[58:61]
	v_mfma_f32_16x16x32_bf16 v[50:53], v[126:129], v[174:177], v[50:53]
	v_mfma_f32_16x16x32_bf16 v[42:45], v[142:145], v[174:177], v[42:45]
	v_mfma_f32_16x16x32_bf16 v[34:37], v[126:129], v[182:185], v[34:37]
	v_mfma_f32_16x16x32_bf16 v[26:29], v[142:145], v[182:185], v[26:29]
	v_mfma_f32_16x16x32_bf16 v[18:21], v[126:129], v[190:193], v[18:21]
	v_mfma_f32_16x16x32_bf16 v[10:13], v[142:145], v[190:193], v[10:13]
	v_mfma_f32_16x16x32_bf16 v[54:57], v[146:149], v[162:165], v[54:57]
	v_mfma_f32_16x16x32_bf16 v[46:49], v[154:157], v[162:165], v[46:49]
	v_mfma_f32_16x16x32_bf16 v[38:41], v[146:149], v[170:173], v[38:41]
	v_mfma_f32_16x16x32_bf16 v[30:33], v[154:157], v[170:173], v[30:33]
	v_mfma_f32_16x16x32_bf16 v[22:25], v[146:149], v[178:181], v[22:25]
	v_mfma_f32_16x16x32_bf16 v[14:17], v[154:157], v[178:181], v[14:17]
	v_mfma_f32_16x16x32_bf16 v[6:9], v[146:149], v[186:189], v[6:9]
	v_mfma_f32_16x16x32_bf16 v[2:5], v[154:157], v[186:189], v[2:5]
	v_mfma_f32_16x16x32_bf16 v[54:57], v[150:153], v[166:169], v[54:57]
	v_mfma_f32_16x16x32_bf16 v[46:49], v[158:161], v[166:169], v[46:49]
	v_mfma_f32_16x16x32_bf16 v[38:41], v[150:153], v[174:177], v[38:41]
	v_mfma_f32_16x16x32_bf16 v[30:33], v[158:161], v[174:177], v[30:33]
	v_mfma_f32_16x16x32_bf16 v[22:25], v[150:153], v[182:185], v[22:25]
	v_mfma_f32_16x16x32_bf16 v[14:17], v[158:161], v[182:185], v[14:17]
	v_mfma_f32_16x16x32_bf16 v[6:9], v[150:153], v[190:193], v[6:9]
	v_mfma_f32_16x16x32_bf16 v[2:5], v[158:161], v[190:193], v[2:5]
	s_barrier
	s_add_i32 s15, 0, 0x18000
	s_add_i32 s18, 0, 0x1c000
	v_add_u32_e32 v142, s15, v244
	v_add_u32_e32 v158, s18, v244
	ds_read_b128 v[122:125], v142
	ds_read_b128 v[126:129], v142 offset:1024
	ds_read_b128 v[134:137], v142 offset:2048
	ds_read_b128 v[142:145], v142 offset:3072
	ds_read_b128 v[146:149], v158
	ds_read_b128 v[150:153], v158 offset:1024
	ds_read_b128 v[154:157], v158 offset:2048
	ds_read_b128 v[158:161], v158 offset:3072
	s_add_u32 s16, s30, 0x80000
	s_addc_u32 s17, s31, 0
	s_mov_b32 m0, s59
	v_lshl_add_u64 v[202:203], s[16:17], 0, v[220:221]
	ds_read_b128 v[162:165], v209 offset:32768
	ds_read_b128 v[166:169], v209 offset:33792
	ds_read_b128 v[170:173], v209 offset:34816
	ds_read_b128 v[174:177], v209 offset:35840
	ds_read_b128 v[178:181], v209 offset:36864
	ds_read_b128 v[182:185], v209 offset:37888
	ds_read_b128 v[186:189], v209 offset:38912
	ds_read_b128 v[190:193], v209 offset:39936
	global_load_lds_dwordx4 v[202:203], off
	v_lshl_add_u64 v[202:203], s[16:17], 0, v[218:219]
	s_mov_b32 m0, s60
	s_nop 0
	global_load_lds_dwordx4 v[202:203], off
	s_waitcnt vmcnt(8)
	s_waitcnt lgkmcnt(0)
	s_barrier
	s_waitcnt lgkmcnt(0)
	v_mfma_f32_16x16x32_bf16 v[138:141], v[122:125], v[162:165], v[138:141]
	v_mfma_f32_16x16x32_bf16 v[130:133], v[134:137], v[162:165], v[130:133]
	v_mfma_f32_16x16x32_bf16 v[114:117], v[122:125], v[170:173], v[114:117]
	v_mfma_f32_16x16x32_bf16 v[106:109], v[134:137], v[170:173], v[106:109]
	v_mfma_f32_16x16x32_bf16 v[98:101], v[122:125], v[178:181], v[98:101]
	v_mfma_f32_16x16x32_bf16 v[90:93], v[134:137], v[178:181], v[90:93]
	v_mfma_f32_16x16x32_bf16 v[82:85], v[122:125], v[186:189], v[82:85]
	v_mfma_f32_16x16x32_bf16 v[74:77], v[134:137], v[186:189], v[74:77]
	v_mfma_f32_16x16x32_bf16 v[138:141], v[126:129], v[166:169], v[138:141]
	v_mfma_f32_16x16x32_bf16 v[130:133], v[142:145], v[166:169], v[130:133]
	v_mfma_f32_16x16x32_bf16 v[114:117], v[126:129], v[174:177], v[114:117]
	v_mfma_f32_16x16x32_bf16 v[106:109], v[142:145], v[174:177], v[106:109]
	v_mfma_f32_16x16x32_bf16 v[98:101], v[126:129], v[182:185], v[98:101]
	v_mfma_f32_16x16x32_bf16 v[90:93], v[142:145], v[182:185], v[90:93]
	v_mfma_f32_16x16x32_bf16 v[82:85], v[126:129], v[190:193], v[82:85]
	v_mfma_f32_16x16x32_bf16 v[74:77], v[142:145], v[190:193], v[74:77]
	v_mfma_f32_16x16x32_bf16 v[118:121], v[146:149], v[162:165], v[118:121]
	v_mfma_f32_16x16x32_bf16 v[110:113], v[154:157], v[162:165], v[110:113]
	v_mfma_f32_16x16x32_bf16 v[102:105], v[146:149], v[170:173], v[102:105]
	v_mfma_f32_16x16x32_bf16 v[94:97], v[154:157], v[170:173], v[94:97]
	v_mfma_f32_16x16x32_bf16 v[86:89], v[146:149], v[178:181], v[86:89]
	v_mfma_f32_16x16x32_bf16 v[78:81], v[154:157], v[178:181], v[78:81]
	v_mfma_f32_16x16x32_bf16 v[70:73], v[146:149], v[186:189], v[70:73]
	v_mfma_f32_16x16x32_bf16 v[66:69], v[154:157], v[186:189], v[66:69]
	v_mfma_f32_16x16x32_bf16 v[118:121], v[150:153], v[166:169], v[118:121]
	v_mfma_f32_16x16x32_bf16 v[110:113], v[158:161], v[166:169], v[110:113]
	v_mfma_f32_16x16x32_bf16 v[102:105], v[150:153], v[174:177], v[102:105]
	v_mfma_f32_16x16x32_bf16 v[94:97], v[158:161], v[174:177], v[94:97]
	v_mfma_f32_16x16x32_bf16 v[86:89], v[150:153], v[182:185], v[86:89]
	v_mfma_f32_16x16x32_bf16 v[78:81], v[158:161], v[182:185], v[78:81]
	v_mfma_f32_16x16x32_bf16 v[70:73], v[150:153], v[190:193], v[70:73]
	v_mfma_f32_16x16x32_bf16 v[66:69], v[158:161], v[190:193], v[66:69]
	s_barrier
; #define PG8_STAGE(bufoff, gbase, voff) do { _Pragma("unroll") for (int _i = 0; _i < 2; ++_i) \
;         __builtin_amdgcn_global_load_lds((const unsigned*)((const char*)(gbase) + (voff)[_i]), (LAS unsigned*)(lds + (bufoff) + ldsw + _i * 8192), 16, 0, 0); } while (0)
; #define PG8_STAGE_A(bufoff, kptr, half, VO) do { if constexpr (GATHER) { _Pragma("unroll") for (int _i = 0; _i < 2; ++_i) \
;         __builtin_amdgcn_global_load_lds((const unsigned*)((const char*)(kptr) + (VO)[half][_i]), (LAS unsigned*)(lds + (bufoff) + ldsw + _i * 8192), 16, 0, 0); } \
;         else { PG8_STAGE(bufoff, (kptr) + (half) * hstepA, voffA); } } while (0)
; #define PG8_WAIT_V(n) asm volatile("s_waitcnt vmcnt(" #n ")" ::: "memory")
;     ...
;         for (int t = 0; t < nt; t += 2) {
;             const bool last = (t == nt - 2);
;             const char* a1 = cA + (size_t)(t + 1) * kstep;
;             const char* a2 = last ? nA : cA + (size_t)(t + 2) * kstep; const char* b2 = last ? nB : cB + (size_t)(t + 2) * kstep;
;             const char* a3 = a2 + kstep; const char* b3 = b2 + kstep;
;             unsigned g2[2][2];
;             if constexpr (GATHER) {
; #pragma unroll
;                 for (int _h = 0; _h < 2; ++_h)
; #pragma unroll
;                     for (int _i = 0; _i < 2; ++_i) g2[_h][_i] = last ? gN[_h][_i] : gC[_h][_i]; }
;             if constexpr (SP2) {
;             PG8_LDB(B0, 0, 0); PG8_LDB(B1, 0, 1); PG8_SCHED; PG8_LDA(At, 0, 0); PG8_STAGE_A(PG8_SA(1, 1), a1, 1, gC);
;             PG8_WAIT_V(8); PG8_WAIT_L(0); PG8_BAR; PG8_MMA(0, 0, At, B0); PG8_MMA(0, 1, At, B1); PG8_BAR; PG8_SCHED;
;             PG8_LDA(At, 0, 1); PG8_STAGE(PG8_SB(0, 0), b2, voffB); PG8_STAGE(PG8_SB(0, 1), b2 + hstepB, voffB); PG8_STAGE_A(PG8_SA(0, 0), a2, 0, g2);
;             PG8_WAIT_V(8); PG8_WAIT_L(0); PG8_BAR; PG8_MMA(1, 0, At, B0); PG8_MMA(1, 1, At, B1); PG8_BAR; PG8_SCHED;
;             PG8_LDB(B0, 1, 0); PG8_LDB(B1, 1, 1); PG8_SCHED; PG8_LDA(At, 1, 0); PG8_STAGE_A(PG8_SA(0, 1), a2, 1, g2);
;             PG8_WAIT_V(8); PG8_WAIT_L(0); PG8_BAR; PG8_MMA(0, 0, At, B0); PG8_MMA(0, 1, At, B1); PG8_BAR; PG8_SCHED;
;             PG8_LDA(At, 1, 1); PG8_STAGE(PG8_SB(1, 0), b3, voffB); PG8_STAGE(PG8_SB(1, 1), b3 + hstepB, voffB); PG8_STAGE_A(PG8_SA(1, 0), a3, 0, g2);
;             PG8_WAIT_V(8); PG8_WAIT_L(0); PG8_BAR; PG8_MMA(1, 0, At, B0); PG8_MMA(1, 1, At, B1); PG8_BAR; PG8_SCHED;
	s_add_i32 s15, s15, s52
	v_lshl_add_u64 v[194:195], v[194:195], 0, s[8:9]
	s_mov_b32 m0, s15
	ds_read_b128 v[162:165], v209 offset:49152
	ds_read_b128 v[166:169], v209 offset:50176
	ds_read_b128 v[170:173], v209 offset:51200
	ds_read_b128 v[174:177], v209 offset:52224
	ds_read_b128 v[178:181], v209 offset:53248
	ds_read_b128 v[182:185], v209 offset:54272
	ds_read_b128 v[186:189], v209 offset:55296
	ds_read_b128 v[190:193], v209 offset:56320
	global_load_lds_dwordx4 v[194:195], off
	s_add_i32 m0, s15, 0x2000
	s_add_u32 s0, s0, 0x80080
	v_lshl_add_u64 v[194:195], v[196:197], 0, s[8:9]
	s_addc_u32 s1, s1, 0
	s_add_i32 s15, s18, s52
	global_load_lds_dwordx4 v[194:195], off
	v_lshl_add_u64 v[194:195], s[0:1], 0, v[206:207]
	s_mov_b32 m0, s15
	s_nop 0
	global_load_lds_dwordx4 v[194:195], off
	v_lshl_add_u64 v[194:195], s[0:1], 0, v[216:217]
	s_add_i32 m0, s15, 0x2000
	s_nop 0
	global_load_lds_dwordx4 v[194:195], off
	v_lshl_add_u64 v[194:195], v[198:199], 0, s[8:9]
	s_mov_b32 m0, s61
	s_nop 0
	global_load_lds_dwordx4 v[194:195], off
	v_lshl_add_u64 v[194:195], v[200:201], 0, s[8:9]
	s_mov_b32 m0, s62
	s_nop 0
	global_load_lds_dwordx4 v[194:195], off
	s_waitcnt vmcnt(8)
	s_waitcnt lgkmcnt(0)
	s_barrier
	s_waitcnt lgkmcnt(0)
	v_mfma_f32_16x16x32_bf16 v[62:65], v[122:125], v[162:165], v[62:65]
	v_mfma_f32_16x16x32_bf16 v[58:61], v[134:137], v[162:165], v[58:61]
	v_mfma_f32_16x16x32_bf16 v[50:53], v[122:125], v[170:173], v[50:53]
	v_mfma_f32_16x16x32_bf16 v[42:45], v[134:137], v[170:173], v[42:45]
	v_mfma_f32_16x16x32_bf16 v[34:37], v[122:125], v[178:181], v[34:37]
	v_mfma_f32_16x16x32_bf16 v[26:29], v[134:137], v[178:181], v[26:29]
	v_mfma_f32_16x16x32_bf16 v[18:21], v[122:125], v[186:189], v[18:21]
	v_mfma_f32_16x16x32_bf16 v[10:13], v[134:137], v[186:189], v[10:13]
	v_mfma_f32_16x16x32_bf16 v[62:65], v[126:129], v[166:169], v[62:65]
	v_mfma_f32_16x16x32_bf16 v[58:61], v[142:145], v[166:169], v[58:61]
	v_mfma_f32_16x16x32_bf16 v[50:53], v[126:129], v[174:177], v[50:53]
	v_mfma_f32_16x16x32_bf16 v[42:45], v[142:145], v[174:177], v[42:45]
	v_mfma_f32_16x16x32_bf16 v[34:37], v[126:129], v[182:185], v[34:37]
	v_mfma_f32_16x16x32_bf16 v[26:29], v[142:145], v[182:185], v[26:29]
	v_mfma_f32_16x16x32_bf16 v[18:21], v[126:129], v[190:193], v[18:21]
	v_mfma_f32_16x16x32_bf16 v[10:13], v[142:145], v[190:193], v[10:13]
	v_mfma_f32_16x16x32_bf16 v[54:57], v[146:149], v[162:165], v[54:57]
	v_mfma_f32_16x16x32_bf16 v[46:49], v[154:157], v[162:165], v[46:49]
	v_mfma_f32_16x16x32_bf16 v[38:41], v[146:149], v[170:173], v[38:41]
	v_mfma_f32_16x16x32_bf16 v[30:33], v[154:157], v[170:173], v[30:33]
	v_mfma_f32_16x16x32_bf16 v[22:25], v[146:149], v[178:181], v[22:25]
	v_mfma_f32_16x16x32_bf16 v[14:17], v[154:157], v[178:181], v[14:17]
	v_mfma_f32_16x16x32_bf16 v[6:9], v[146:149], v[186:189], v[6:9]
	v_mfma_f32_16x16x32_bf16 v[2:5], v[154:157], v[186:189], v[2:5]
	v_mfma_f32_16x16x32_bf16 v[54:57], v[150:153], v[166:169], v[54:57]
	v_mfma_f32_16x16x32_bf16 v[46:49], v[158:161], v[166:169], v[46:49]
	v_mfma_f32_16x16x32_bf16 v[38:41], v[150:153], v[174:177], v[38:41]
	v_mfma_f32_16x16x32_bf16 v[30:33], v[158:161], v[174:177], v[30:33]
	v_mfma_f32_16x16x32_bf16 v[22:25], v[150:153], v[182:185], v[22:25]
	v_mfma_f32_16x16x32_bf16 v[14:17], v[158:161], v[182:185], v[14:17]
	v_mfma_f32_16x16x32_bf16 v[6:9], v[150:153], v[190:193], v[6:9]
	v_mfma_f32_16x16x32_bf16 v[2:5], v[158:161], v[190:193], v[2:5]
	s_barrier
	s_add_i32 s14, s14, 2
	s_add_u32 s24, s24, 0x100
	s_addc_u32 s25, s25, 0
	s_add_u32 s12, s12, 0x100
	s_addc_u32 s13, s13, 0
	s_cmp_gt_u32 s14, 29
	s_cbranch_scc0 .LBB0_1693
	s_and_b64 vcc, exec, s[38:39]
	s_cbranch_vccz .LBB0_1696
	s_barrier

; __device__ __forceinline__ void moe_fill(const Params& p, LAS unsigned char* lds, int ph) { if (FILL_ON) moe_pump(p, lds, ph, Q_TOTAL, 0); }
; #define REPLOOP(id) for (int rep_ = 0; rep_ < NREP(id); ++rep_)
; #define REPBAR(id) do { if (rep_ + 1 < NREP(id)) xcd_barrier(bar); } while (0)
; #define SEAM(k) do { if (IN(k) && IN((k) + 1)) xcd_barrier(bar); } while (0)
; __global__ void __launch_bounds__(512, 2) fwd(Params p) {
;     ...
;             moe_fill(p, lds, pb + 6);
;          REPBAR(8); }
;         SEAM(pb + 6);
;         if (PSEL(9) && IN(pb + 7)) REPLOOP(9) { ph_norm2_router(p, l, lds); __syncthreads(); REPBAR(9); }
.LBB0_1752:
	s_setprio 0
	s_cmp_le_i32 s86, s4
	s_cselect_b64 s[0:1], -1, 0
	s_cmp_lt_i32 s4, s87
	s_cselect_b64 s[2:3], -1, 0
	s_and_b64 s[2:3], s[0:1], s[2:3]
	s_mov_b64 s[0:1], -1
	s_and_b64 vcc, exec, s[2:3]
	s_cbranch_vccnz .LBB0_1754
	v_readlane_b32 s0, v255, 56
	s_add_i32 s4, s0, 10
	s_mov_b64 s[0:1], 0

; __device__ __forceinline__ void ph_topk(const Params& p, int l, LAS unsigned char* lds) {
;     const int tid = opaque_tid(), lane = tid & 63, wave = tid >> 6;
;     unsigned char* ws = opaque_ptr(p.ws); const float* AFF = (const float*)(ws + WS_AFF);
;     int* ROWTOK = (int*)(ws + WS_ROWTOK); float* ROWAFF = (float*)(ws + WS_ROWAFF); int* INV = (int*)(ws + WS_INV);
;     LAS int* hist = (LAS int*)lds;
;     LAS int* ctl = (LAS int*)(lds + 1024);
;     LAS int* wsum = (LAS int*)(lds + 1280);
;     const int nunits = (l == 0) ? 128 : 64;
;     for (int it = blockIdx.x; it < nunits; it += gridDim.x) {
;         const bool lat = it < 64; const int u = lat ? it : it - 64; const int b = u >> 4, e = u & 15;
;         const int n = lat ? SEQ : CTX, cap = lat ? CAPL : CAPC;
;         const int tok0 = lat ? b * SEQ : NLAT + b * CTX; const int rowbase = lat ? b * CAPL : 1024 + b * CAPC;
;         unsigned key[4];
; #pragma unroll
;         for (int j = 0; j < 4; ++j) { const int t = tid * 4 + j; key[j] = t < n ? __float_as_uint(AFF[(size_t)(tok0 + t) * 16 + e]) : 0u; }
;         unsigned prefix = 0u; int remaining = cap;
;     ...
;             if (tid < 256) hist[tid] = 0;
;             __syncthreads();
; #pragma unroll
;             for (int j = 0; j < 4; ++j) { const int t = tid * 4 + j; if (t < n) { const bool match = (pass == 3) || ((key[j] >> (8 * (pass + 1))) == (prefix >> (8 * (pass + 1)))); if (match) atomicAdd((int*)&hist[(key[j] >> (8 * pass)) & 255u], 1); } }
;             __syncthreads();
;             if (wave == 0) {
;                 const int b0 = hist[4 * lane], b1 = hist[4 * lane + 1], b2 = hist[4 * lane + 2], b3 = hist[4 * lane + 3];
;                 const int s = b0 + b1 + b2 + b3; int suf = s;
; #pragma unroll
;                 for (int off = 1; off < 64; off <<= 1) { const int t = __shfl_down(suf, off); if (lane + off < 64) suf += t; }
;                 const int above = suf - s; const int c3 = above + b3, c2 = c3 + b2, c1 = c2 + b1, c0 = c1 + b0;
;                 if (above < remaining && c0 >= remaining) { int dg, nr;
;                     if (c3 >= remaining) { dg = 4 * lane + 3; nr = remaining - above; } else if (c2 >= remaining) { dg = 4 * lane + 2; nr = remaining - c3; }
;                     else if (c1 >= remaining) { dg = 4 * lane + 1; nr = remaining - c2; } else { dg = 4 * lane; nr = remaining - c1; }
.LBB0_1812:
	s_setprio 0
	s_cmp_gt_i32 s86, s4
	s_cselect_b64 s[0:1], -1, 0
	s_cmp_ge_i32 s4, s87
	s_cselect_b64 s[2:3], -1, 0
	s_or_b64 s[0:1], s[0:1], s[2:3]
	s_and_b64 vcc, exec, s[0:1]
	v_readlane_b32 s0, v252, 5
	s_mulk_i32 s0, 0x1800
	v_readlane_b32 s1, v252, 6
	v_writelane_b32 v255, s0, 59
	s_cbranch_vccnz .LBB0_2011
	v_readlane_b32 s0, v252, 20
	v_readlane_b32 s1, v252, 21
	s_and_b64 s[0:1], s[0:1], exec
	s_cselect_b32 s4, 0x80, 64
	s_cmp_ge_i32 s92, s4
	s_waitcnt vmcnt(0)
	v_mov_b32_e32 v2, v0
	s_mov_b64 s[0:1], 0
	s_cbranch_scc1 .LBB0_1910
	v_and_b32_e32 v6, 63, v249
	v_cmp_ne_u32_e32 vcc, 63, v6
	v_and_b32_e32 v5, 64, v249
	v_readlane_b32 s12, v251, 55
	v_addc_co_u32_e32 v7, vcc, 0, v249, vcc
	v_cmp_gt_u32_e32 vcc, 62, v6
	v_lshlrev_b32_e32 v20, 2, v7
	v_readlane_b32 s16, v251, 59
	v_cndmask_b32_e64 v7, 0, 2, vcc
	v_cmp_gt_u32_e32 vcc, 60, v6
	v_add_lshl_u32 v21, v7, v249, 2
	v_readlane_b32 s17, v251, 60
	v_cndmask_b32_e64 v7, 0, 4, vcc
	v_cmp_gt_u32_e32 vcc, 56, v6
	v_add_lshl_u32 v22, v7, v249, 2
	s_add_u32 s0, s16, s0
	v_cndmask_b32_e64 v7, 0, 8, vcc
	v_cmp_gt_u32_e32 vcc, 48, v6
	s_addc_u32 s1, s17, s1
	s_add_u32 s34, s0, 0x35df8000
	v_cndmask_b32_e64 v6, 0, 16, vcc
	v_add_lshl_u32 v24, v6, v249, 2
	v_mov_b32_e32 v6, 0x80
	v_lshl_or_b32 v25, v249, 2, v6
	v_add_u32_e32 v6, -1, v249
	v_cmp_lt_i32_e32 vcc, v6, v5
	s_addc_u32 s35, s1, 0
	s_add_u32 s30, s0, 0x35e88000
	v_cndmask_b32_e32 v6, v6, v249, vcc
	v_lshlrev_b32_e32 v26, 2, v6
	v_add_u32_e32 v6, -2, v249
	v_cmp_lt_i32_e32 vcc, v6, v5
	s_addc_u32 s31, s1, 0
	s_add_u32 s24, s0, 0x35e9c000
	v_cndmask_b32_e32 v6, v6, v249, vcc
	v_lshlrev_b32_e32 v27, 2, v6
	v_add_u32_e32 v6, -4, v249
	v_cmp_lt_i32_e32 vcc, v6, v5
	v_and_b32_e32 v4, 63, v2
	v_readlane_b32 s14, v251, 57
	v_cndmask_b32_e32 v6, v6, v249, vcc
	v_lshlrev_b32_e32 v28, 2, v6
	v_add_u32_e32 v6, -8, v249
	v_cmp_lt_i32_e32 vcc, v6, v5
	s_addc_u32 s25, s1, 0
	v_cmp_eq_u32_e64 s[38:39], 63, v4
	v_cndmask_b32_e32 v6, v6, v249, vcc
	v_lshlrev_b32_e32 v29, 2, v6
	v_add_u32_e32 v6, -16, v249
	v_cmp_gt_u32_e64 s[40:41], 62, v4
	v_cmp_gt_u32_e64 s[42:43], 60, v4
	v_cmp_gt_u32_e64 s[44:45], 56, v4
	v_cmp_gt_u32_e64 s[46:47], 48, v4
	v_cmp_gt_u32_e64 s[48:49], 32, v4
	v_cmp_eq_u32_e64 s[50:51], 0, v4
	v_cmp_gt_u32_e64 s[52:53], 2, v4
	v_cmp_gt_u32_e64 s[54:55], 4, v4
	v_cmp_gt_u32_e64 s[56:57], 8, v4
	v_cmp_lt_i32_e32 vcc, v6, v5
	v_cmp_gt_u32_e64 s[58:59], 16, v4
	v_subrev_u32_e32 v4, 32, v249
	s_add_u32 s14, s0, 0x35eb0000
	v_lshlrev_b32_e32 v14, 2, v2
	s_movk_i32 s0, 0x100
	v_cndmask_b32_e32 v6, v6, v249, vcc
	v_cmp_lt_i32_e32 vcc, v4, v5
	v_readlane_b32 s15, v251, 58
	v_ashrrev_i32_e32 v3, 6, v2
	v_cmp_gt_i32_e64 s[2:3], s0, v2
	v_cmp_gt_u32_e64 s[36:37], 64, v2
	v_add_u32_e32 v15, 0, v14
	v_mul_lo_u32 v2, v2, 12
	v_cndmask_b32_e32 v4, v4, v249, vcc
	s_addc_u32 s15, s1, 0
	v_or_b32_e32 v16, 1, v14
	v_or_b32_e32 v17, 2, v14
	v_or_b32_e32 v18, 3, v14
	v_lshl_add_u32 v19, v3, 2, 0
	v_add_lshl_u32 v23, v7, v249, 2
	v_lshlrev_b32_e32 v30, 2, v6
	v_lshlrev_b32_e32 v31, 2, v4
	v_cmp_lt_i32_e64 s[60:61], 0, v3
	v_cmp_lt_i32_e64 s[62:63], 1, v3
	v_cmp_lt_i32_e64 s[64:65], 2, v3
	v_cmp_lt_i32_e64 s[66:67], 3, v3
	v_cmp_lt_i32_e64 s[68:69], 4, v3
	v_cmp_lt_i32_e64 s[70:71], 5, v3
	v_cmp_lt_i32_e64 s[72:73], 6, v3
	v_cmp_lt_i32_e64 s[74:75], 7, v3
	v_add_u32_e32 v32, v15, v2
	v_readlane_b32 s16, v251, 54
	v_readlane_b32 s13, v251, 56
	v_readlane_b32 s18, v251, 61
	v_readlane_b32 s19, v251, 62
	s_branch .LBB0_1817

;     __device__ __forceinline__ void init(const void* A_, const void* B_, int G_, int c_) { T.init(A_, B_, DM, DM, NLAT / 256, INP / 256, 1, 0, 0, G_, c_, 0); }
; __device__ __forceinline__ void moe_mark_done(const Params& p, int ph) { if (threadIdx.x == 0) (void)__hip_atomic_fetch_add((unsigned*)(p.ws + WS_CTL) + CW_DONE + 64 * ph, 1u, __ATOMIC_RELAXED, __HIP_MEMORY_SCOPE_AGENT); }
; __device__ __forceinline__ void moe_convert_while(const Params& p, LAS unsigned char* lds, int ph, unsigned ngemm) { moe_pump(p, lds, ph, Q_TOTAL, 0, ngemm, false); }
; __device__ __forceinline__ void moe_require(const Params& p, LAS unsigned char* lds, int upto) { moe_pump(p, lds, 0, upto, 1); }
; #define REPLOOP(id) for (int rep_ = 0; rep_ < NREP(id); ++rep_)
; #define REPBAR(id) do { if (rep_ + 1 < NREP(id)) xcd_barrier(bar); } while (0)
; #define SEAM(k) do { if (IN(k) && IN((k) + 1)) xcd_barrier(bar); } while (0)
; __global__ void __launch_bounds__(512, 2) fwd(Params p) {
;     ...
;         if (PSEL(10) && IN(pb + 8)) REPLOOP(10) { ph_topk(p, l, lds); __syncthreads(); moe_require(p, lds, l * Q_LAYER + Q_GU);  REPBAR(10); }
;         if (PSEL(11) && IN(pb + 9)) REPLOOP(11) { }
;         SEAM(pb + 9);
;         if (PSEL(12) && IN(pb + 10)) REPLOOP(12) {
;             pg8::MoeSched S; S.init(ws + WS_H, (bf16_t*)(ws + WS_WTGU) + (size_t)l * NE * 2048 * DM, DM, DM, l == 0 ? 5 : 4, 8, 0, (size_t)2048 * DM * 2, l == 0 ? GgK : G, c);
;             pg8::EpiGU E{(bf16_t*)(ws + WS_HID)};
;             if (l == 0 && c >= GgK) moe_convert_while(p, lds, pb + 10, GgK); else { pg8::gemm_phase<pg8::EpiGU, pg8::MoeSched, true>(lds, pg8::Desc{DM, DM, DM}, S, E, (const int*)(ws + WS_ROWTOK), l == 0 ? 1152 : 1024); if (l == 0 && nconv) moe_mark_done(p, pb + 10); }
.LBB0_2061:
	s_setprio 0
	s_cmp_le_i32 s86, s4
	s_cselect_b64 s[2:3], -1, 0
	s_and_b64 s[2:3], s[2:3], s[0:1]
	s_mov_b64 s[0:1], -1
	s_and_b64 vcc, exec, s[2:3]
	s_cbranch_vccnz .LBB0_2063
	v_readlane_b32 s0, v255, 56
	s_add_i32 s4, s0, 13
	s_mov_b64 s[0:1], 0

; #define PG8_GOFF(u, o) do { _Pragma("unroll") for (int _h = 0; _h < 2; ++_h) _Pragma("unroll") for (int _i = 0; _i < 2; ++_i) { const int _r = (u).pm * 256 + _h * 128 + gR[_i]; \
;         const int _tok = _r < nvalid ? rowtok[(u).pb * EROWS + _r] : 0; (o)[_h][_i] = (unsigned)(_tok * g.lda + gCc[_i]) * 2u; } } while (0)
; #define PG8_STAGE(bufoff, gbase, voff) do { _Pragma("unroll") for (int _i = 0; _i < 2; ++_i) \
;         __builtin_amdgcn_global_load_lds((const unsigned*)((const char*)(gbase) + (voff)[_i]), (LAS unsigned*)(lds + (bufoff) + ldsw + _i * 8192), 16, 0, 0); } while (0)
; #define PG8_STAGE_A(bufoff, kptr, half, VO) do { if constexpr (GATHER) { _Pragma("unroll") for (int _i = 0; _i < 2; ++_i) \
;         __builtin_amdgcn_global_load_lds((const unsigned*)((const char*)(kptr) + (VO)[half][_i]), (LAS unsigned*)(lds + (bufoff) + ldsw + _i * 8192), 16, 0, 0); } \
;         else { PG8_STAGE(bufoff, (kptr) + (half) * hstepA, voffA); } } while (0)
; #define PG8_WAIT_V(n) asm volatile("s_waitcnt vmcnt(" #n ")" ::: "memory")
; #define PG8_BAR __builtin_amdgcn_s_barrier()
;     ...
;     const size_t kstep = (size_t)(BK * 2);
;     const size_t hstepA = (size_t)HALF * g.lda * 2, hstepB = (size_t)HALF * g.ldb * 2;
;     const unsigned ldsw = (unsigned)wid * 1024u;
;     const int aoff = lds_byte(wr * 64 + fr, fq * 8), boff = lds_byte(wc * 32 + fr, fq * 8);
;     ...
;     Unit cur, nxt; int ui = 0;
;     if (!S.next(0, cur)) return;
;     f32x4 acc[2][2][4][2];
; #pragma unroll
;     for (int a = 0; a < 2; ++a)
; #pragma unroll
;         for (int b = 0; b < 2; ++b)
; #pragma unroll
;             for (int m = 0; m < 4; ++m)
; #pragma unroll
;                 for (int n = 0; n < 2; ++n) acc[a][b][m][n] = (f32x4){0.f, 0.f, 0.f, 0.f};
;     bf16x8 At[4][2], B0[2][2], B1[2][2];
;     const char* cA = cur.a; const char* cB = cur.b;
;     if constexpr (GATHER) { PG8_GOFF(cur, gC); }
;     if constexpr (SP2) {
;         PG8_STAGE(PG8_SB(0, 0), cB, voffB); PG8_STAGE(PG8_SB(0, 1), cB + hstepB, voffB); PG8_STAGE_A(PG8_SA(0, 0), cA, 0, gC); PG8_STAGE_A(PG8_SA(0, 1), cA, 1, gC);
;         if (wr == 1) PG8_BAR;
;         PG8_WAIT_V(2); PG8_BAR;
.LBB0_2236:
	s_or_b64 exec, exec, s[0:1]
	v_mul_i32_i24_e32 v14, 64, v2
	v_lshlrev_b32_e32 v3, 5, v3
	v_sub_u32_e32 v4, v4, v14
	v_and_b32_e32 v3, 32, v3
	v_ashrrev_i16_sdwa v4, v245, sext(v4) dst_sel:DWORD dst_unused:UNUSED_PAD src0_sel:DWORD src1_sel:BYTE_0
	v_add_u32_sdwa v148, v3, sext(v4) dst_sel:DWORD dst_unused:UNUSED_PAD src0_sel:DWORD src1_sel:WORD_0
	v_lshlrev_b32_e32 v4, 6, v7
	v_lshlrev_b32_e32 v3, 5, v8
	v_sub_u32_e32 v4, v9, v4
	v_and_b32_e32 v3, 32, v3
	v_ashrrev_i16_sdwa v4, v245, sext(v4) dst_sel:DWORD dst_unused:UNUSED_PAD src0_sel:DWORD src1_sel:BYTE_0
	v_add_u32_sdwa v149, v3, sext(v4) dst_sel:DWORD dst_unused:UNUSED_PAD src0_sel:DWORD src1_sel:WORD_0
	v_lshlrev_b32_e32 v3, 1, v146
	v_lshrrev_b32_e32 v4, 2, v146
	v_and_b32_e32 v2, 3, v2
	s_mov_b32 s1, 0xfffe0
	v_and_b32_e32 v3, 24, v3
	v_and_b32_e32 v4, 4, v4
	v_and_or_b32 v2, v146, s1, v2
	v_or3_b32 v2, v2, v4, v3
	v_and_b32_e32 v4, 3, v7
	v_and_or_b32 v4, v147, s1, v4
	s_ashr_i32 s1, s14, 6
	v_lshlrev_b32_e32 v3, 1, v148
	s_lshl_b32 s56, s1, 10
	v_lshl_add_u32 v130, v2, 12, v3
	v_lshlrev_b32_e32 v2, 1, v147
	v_lshrrev_b32_e32 v3, 2, v147
	s_add_i32 s57, s56, 0
	v_and_b32_e32 v2, 24, v2
	v_and_b32_e32 v3, 4, v3
	s_add_i32 m0, s57, 0x10000
	s_ashr_i32 s0, s14, 8
	v_or3_b32 v2, v4, v3, v2
	v_lshlrev_b32_e32 v3, 1, v149
	global_load_lds_dwordx4 v130, s[24:25]
	s_add_i32 m0, s57, 0x12000
	v_lshl_add_u32 v132, v2, 12, v3
	s_add_u32 s12, s24, 0x80000
	global_load_lds_dwordx4 v132, s[24:25]
	s_addc_u32 s13, s25, 0
	s_add_i32 m0, s57, 0x14000
	v_add_lshl_u32 v138, v5, v148, 1
	global_load_lds_dwordx4 v130, s[12:13]
	s_add_i32 m0, s57, 0x16000
	s_add_i32 s58, s57, 0x2000
	global_load_lds_dwordx4 v132, s[12:13]
	v_readlane_b32 s12, v252, 24
	s_mov_b32 m0, s57
	v_readlane_b32 s13, v252, 25
	v_add_lshl_u32 v136, v6, v149, 1
	s_add_i32 s59, s57, 0x4000
	v_add_lshl_u32 v134, v13, v148, 1
	s_add_i32 s60, s57, 0x6000
	v_add_lshl_u32 v140, v12, v149, 1
	global_load_lds_dwordx4 v138, s[12:13]
	s_mov_b32 m0, s58
	v_mov_b32_e32 v131, v207
	global_load_lds_dwordx4 v136, s[12:13]
	s_mov_b32 m0, s59
	v_mov_b32_e32 v133, v207
	global_load_lds_dwordx4 v134, s[12:13]
	s_mov_b32 m0, s60
	v_mov_b32_e32 v139, v207
	global_load_lds_dwordx4 v140, s[12:13]
	v_mov_b32_e32 v137, v207
	s_cmp_eq_u32 s0, 1
	v_lshl_add_u64 v[8:9], s[24:25], 0, v[130:131]
	v_lshl_add_u64 v[4:5], s[24:25], 0, v[132:133]
	v_lshl_add_u64 v[2:3], s[12:13], 0, v[138:139]
	s_cselect_b64 s[40:41], -1, 0
	s_cmp_lg_u32 s0, 1
	v_lshl_add_u64 v[6:7], s[12:13], 0, v[136:137]
	s_cbranch_scc1 .LBB0_2238
	s_barrier
	s_setprio 1

; #define PG8_GOFF(u, o) do { _Pragma("unroll") for (int _h = 0; _h < 2; ++_h) _Pragma("unroll") for (int _i = 0; _i < 2; ++_i) { const int _r = (u).pm * 256 + _h * 128 + gR[_i]; \
;         const int _tok = _r < nvalid ? rowtok[(u).pb * EROWS + _r] : 0; (o)[_h][_i] = (unsigned)(_tok * g.lda + gCc[_i]) * 2u; } } while (0)
; #define PG8_WAIT_V(n) asm volatile("s_waitcnt vmcnt(" #n ")" ::: "memory")
; #define PG8_WAIT_L(n) asm volatile("s_waitcnt lgkmcnt(" #n ")" ::: "memory")
;     ...
;         if constexpr (GATHER) { if (has_next) { PG8_GOFF(nxt, gN); } else {
; #pragma unroll
;             for (int _h = 0; _h < 2; ++_h)
; #pragma unroll
;                 for (int _i = 0; _i < 2; ++_i) gN[_h][_i] = gC[_h][_i]; } }
; #pragma nounroll
;         for (int t = 0; t < nt; t += 2) {
;             const bool last = (t == nt - 2);
;             const char* a1 = cA + (size_t)(t + 1) * kstep;
;             const char* a2 = last ? nA : cA + (size_t)(t + 2) * kstep; const char* b2 = last ? nB : cB + (size_t)(t + 2) * kstep;
;             const char* a3 = a2 + kstep; const char* b3 = b2 + kstep;
;             unsigned g2[2][2];
;             if constexpr (GATHER) {
; #pragma unroll
;                 for (int _h = 0; _h < 2; ++_h)
; #pragma unroll
;                     for (int _i = 0; _i < 2; ++_i) g2[_h][_i] = last ? gN[_h][_i] : gC[_h][_i]; }
;             if constexpr (SP2) {
;             PG8_LDB(B0, 0, 0); PG8_LDB(B1, 0, 1); PG8_SCHED; PG8_LDA(At, 0, 0); PG8_STAGE_A(PG8_SA(1, 1), a1, 1, gC);
;             PG8_WAIT_V(8); PG8_WAIT_L(0); PG8_BAR; PG8_MMA(0, 0, At, B0); PG8_MMA(0, 1, At, B1); PG8_BAR; PG8_SCHED;
;             PG8_LDA(At, 0, 1); PG8_STAGE(PG8_SB(0, 0), b2, voffB); PG8_STAGE(PG8_SB(0, 1), b2 + hstepB, voffB); PG8_STAGE_A(PG8_SA(0, 0), a2, 0, g2);
;             PG8_WAIT_V(8); PG8_WAIT_L(0); PG8_BAR; PG8_MMA(1, 0, At, B0); PG8_MMA(1, 1, At, B1); PG8_BAR; PG8_SCHED;
;             PG8_LDB(B0, 1, 0); PG8_LDB(B1, 1, 1); PG8_SCHED; PG8_LDA(At, 1, 0); PG8_STAGE_A(PG8_SA(0, 1), a2, 1, g2);
;             PG8_WAIT_V(8); PG8_WAIT_L(0); PG8_BAR; PG8_MMA(0, 0, At, B0); PG8_MMA(0, 1, At, B1); PG8_BAR; PG8_SCHED;
;             PG8_LDA(At, 1, 1); PG8_STAGE(PG8_SB(1, 0), b3, voffB); PG8_STAGE(PG8_SB(1, 1), b3 + hstepB, voffB); PG8_STAGE_A(PG8_SA(1, 0), a3, 0, g2);
;             PG8_WAIT_V(8); PG8_WAIT_L(0); PG8_BAR; PG8_MMA(1, 0, At, B0); PG8_MMA(1, 1, At, B1); PG8_BAR; PG8_SCHED;
.LBB0_2265:
	s_add_u32 s0, s34, s24
	s_addc_u32 s1, s35, s25
	s_add_u32 s19, s0, 0x100
	s_addc_u32 s20, s1, 0
	s_add_u32 s21, s16, s24
	s_addc_u32 s22, s17, s25
	s_cmpk_eq_i32 s24, 0xf00
	s_cselect_b64 vcc, -1, 0
	s_and_b64 s[0:1], vcc, exec
	s_cselect_b32 s31, s12, s20
	s_cselect_b32 s30, s13, s19
	s_cselect_b32 s1, s14, s22
	s_cselect_b32 s0, s15, s21
	s_add_i32 s19, 0, 0x10000
	v_add_u32_e32 v161, s19, v139
	s_add_i32 s22, 0, 0x14000
	ds_read_b128 v[162:165], v161
	ds_read_b128 v[166:169], v161 offset:1024
	ds_read_b128 v[170:173], v161 offset:2048
	ds_read_b128 v[174:177], v161 offset:3072
	v_add_u32_e32 v161, s22, v139
	ds_read_b128 v[178:181], v161
	ds_read_b128 v[182:185], v161 offset:1024
	ds_read_b128 v[186:189], v161 offset:2048
	ds_read_b128 v[190:193], v161 offset:3072
	v_cndmask_b32_e32 v206, v138, v160, vcc
	v_cndmask_b32_e32 v212, v136, v159, vcc
	v_cndmask_b32_e32 v135, v134, v157, vcc
	v_cndmask_b32_e32 v141, v140, v158, vcc
	v_lshl_add_u64 v[214:215], v[144:145], 0, s[24:25]
	s_add_i32 m0, s57, 0xc000
	ds_read_b128 v[194:197], v156
	ds_read_b128 v[198:201], v156 offset:1024
	ds_read_b128 v[202:205], v156 offset:2048
	ds_read_b128 v[208:211], v156 offset:3072
	ds_read_b128 v[216:219], v156 offset:4096
	ds_read_b128 v[220:223], v156 offset:5120
	ds_read_b128 v[224:227], v156 offset:6144
	ds_read_b128 v[228:231], v156 offset:7168
	global_load_lds_dwordx4 v[214:215], off
	v_lshl_add_u64 v[214:215], v[142:143], 0, s[24:25]
	s_add_i32 m0, s57, 0xe000
	s_nop 0
	global_load_lds_dwordx4 v[214:215], off
	s_waitcnt vmcnt(8)
	s_waitcnt lgkmcnt(0)
	s_barrier
	s_waitcnt lgkmcnt(0)
	v_mfma_f32_16x16x32_bf16 v[126:129], v[162:165], v[194:197], v[126:129]
	v_mfma_f32_16x16x32_bf16 v[122:125], v[170:173], v[194:197], v[122:125]
	v_mfma_f32_16x16x32_bf16 v[110:113], v[162:165], v[202:205], v[110:113]
	v_mfma_f32_16x16x32_bf16 v[106:109], v[170:173], v[202:205], v[106:109]
	v_mfma_f32_16x16x32_bf16 v[94:97], v[162:165], v[216:219], v[94:97]
	v_mfma_f32_16x16x32_bf16 v[90:93], v[170:173], v[216:219], v[90:93]
	v_mfma_f32_16x16x32_bf16 v[78:81], v[162:165], v[224:227], v[78:81]
	v_mfma_f32_16x16x32_bf16 v[74:77], v[170:173], v[224:227], v[74:77]
	v_mfma_f32_16x16x32_bf16 v[126:129], v[166:169], v[198:201], v[126:129]
	v_mfma_f32_16x16x32_bf16 v[122:125], v[174:177], v[198:201], v[122:125]
	v_mfma_f32_16x16x32_bf16 v[110:113], v[166:169], v[208:211], v[110:113]
	v_mfma_f32_16x16x32_bf16 v[106:109], v[174:177], v[208:211], v[106:109]
	v_mfma_f32_16x16x32_bf16 v[94:97], v[166:169], v[220:223], v[94:97]
	v_mfma_f32_16x16x32_bf16 v[90:93], v[174:177], v[220:223], v[90:93]
	v_mfma_f32_16x16x32_bf16 v[78:81], v[166:169], v[228:231], v[78:81]
	v_mfma_f32_16x16x32_bf16 v[74:77], v[174:177], v[228:231], v[74:77]
	v_mfma_f32_16x16x32_bf16 v[118:121], v[178:181], v[194:197], v[118:121]
	v_mfma_f32_16x16x32_bf16 v[114:117], v[186:189], v[194:197], v[114:117]
	v_mfma_f32_16x16x32_bf16 v[102:105], v[178:181], v[202:205], v[102:105]
	v_mfma_f32_16x16x32_bf16 v[98:101], v[186:189], v[202:205], v[98:101]
	v_mfma_f32_16x16x32_bf16 v[86:89], v[178:181], v[216:219], v[86:89]
	v_mfma_f32_16x16x32_bf16 v[82:85], v[186:189], v[216:219], v[82:85]
	v_mfma_f32_16x16x32_bf16 v[70:73], v[178:181], v[224:227], v[70:73]
	v_mfma_f32_16x16x32_bf16 v[66:69], v[186:189], v[224:227], v[66:69]
	v_mfma_f32_16x16x32_bf16 v[118:121], v[182:185], v[198:201], v[118:121]
	v_mfma_f32_16x16x32_bf16 v[114:117], v[190:193], v[198:201], v[114:117]
	v_mfma_f32_16x16x32_bf16 v[102:105], v[182:185], v[208:211], v[102:105]
	v_mfma_f32_16x16x32_bf16 v[98:101], v[190:193], v[208:211], v[98:101]
	v_mfma_f32_16x16x32_bf16 v[86:89], v[182:185], v[220:223], v[86:89]
	v_mfma_f32_16x16x32_bf16 v[82:85], v[190:193], v[220:223], v[82:85]
	v_mfma_f32_16x16x32_bf16 v[70:73], v[182:185], v[228:231], v[70:73]
	v_mfma_f32_16x16x32_bf16 v[66:69], v[190:193], v[228:231], v[66:69]
	s_barrier
	s_add_i32 s19, s19, s56
	v_lshl_add_u64 v[214:215], s[0:1], 0, v[130:131]
	s_mov_b32 m0, s19
	ds_read_b128 v[194:197], v156 offset:16384
	ds_read_b128 v[198:201], v156 offset:17408
	ds_read_b128 v[202:205], v156 offset:18432
	ds_read_b128 v[208:211], v156 offset:19456
	ds_read_b128 v[216:219], v156 offset:20480
	ds_read_b128 v[220:223], v156 offset:21504
	ds_read_b128 v[224:227], v156 offset:22528
	ds_read_b128 v[228:231], v156 offset:23552
	global_load_lds_dwordx4 v[214:215], off
	s_add_i32 m0, s19, 0x2000
	s_add_u32 s20, s0, 0x80000
	v_lshl_add_u64 v[232:233], s[0:1], 0, v[132:133]
	s_addc_u32 s21, s1, 0
	s_add_i32 s19, s22, s56
	global_load_lds_dwordx4 v[232:233], off
	v_lshl_add_u64 v[234:235], s[20:21], 0, v[130:131]
	s_mov_b32 m0, s19
	v_mov_b32_e32 v213, v207
	global_load_lds_dwordx4 v[234:235], off
	v_lshl_add_u64 v[234:235], s[20:21], 0, v[132:133]
	s_add_i32 m0, s19, 0x2000
	s_nop 0
	global_load_lds_dwordx4 v[234:235], off
	s_mov_b32 m0, s57
	v_lshl_add_u64 v[234:235], s[30:31], 0, v[206:207]
	global_load_lds_dwordx4 v206, s[30:31]
	s_mov_b32 m0, s58
	s_nop 0
	global_load_lds_dwordx4 v212, s[30:31]
	s_waitcnt vmcnt(8)
	s_waitcnt lgkmcnt(0)
	v_lshl_add_u64 v[212:213], s[30:31], 0, v[212:213]
	s_barrier
; #define PG8_STAGE(bufoff, gbase, voff) do { _Pragma("unroll") for (int _i = 0; _i < 2; ++_i) \
;         __builtin_amdgcn_global_load_lds((const unsigned*)((const char*)(gbase) + (voff)[_i]), (LAS unsigned*)(lds + (bufoff) + ldsw + _i * 8192), 16, 0, 0); } while (0)
; #define PG8_STAGE_A(bufoff, kptr, half, VO) do { if constexpr (GATHER) { _Pragma("unroll") for (int _i = 0; _i < 2; ++_i) \
;         __builtin_amdgcn_global_load_lds((const unsigned*)((const char*)(kptr) + (VO)[half][_i]), (LAS unsigned*)(lds + (bufoff) + ldsw + _i * 8192), 16, 0, 0); } \
;         else { PG8_STAGE(bufoff, (kptr) + (half) * hstepA, voffA); } } while (0)
; #define PG8_WAIT_V(n) asm volatile("s_waitcnt vmcnt(" #n ")" ::: "memory")
;     ...
;         for (int t = 0; t < nt; t += 2) {
;             const bool last = (t == nt - 2);
;             const char* a1 = cA + (size_t)(t + 1) * kstep;
;             const char* a2 = last ? nA : cA + (size_t)(t + 2) * kstep; const char* b2 = last ? nB : cB + (size_t)(t + 2) * kstep;
;             const char* a3 = a2 + kstep; const char* b3 = b2 + kstep;
;             unsigned g2[2][2];
;             if constexpr (GATHER) {
; #pragma unroll
;                 for (int _h = 0; _h < 2; ++_h)
; #pragma unroll
;                     for (int _i = 0; _i < 2; ++_i) g2[_h][_i] = last ? gN[_h][_i] : gC[_h][_i]; }
;             if constexpr (SP2) {
;             PG8_LDB(B0, 0, 0); PG8_LDB(B1, 0, 1); PG8_SCHED; PG8_LDA(At, 0, 0); PG8_STAGE_A(PG8_SA(1, 1), a1, 1, gC);
;             PG8_WAIT_V(8); PG8_WAIT_L(0); PG8_BAR; PG8_MMA(0, 0, At, B0); PG8_MMA(0, 1, At, B1); PG8_BAR; PG8_SCHED;
;             PG8_LDA(At, 0, 1); PG8_STAGE(PG8_SB(0, 0), b2, voffB); PG8_STAGE(PG8_SB(0, 1), b2 + hstepB, voffB); PG8_STAGE_A(PG8_SA(0, 0), a2, 0, g2);
;             PG8_WAIT_V(8); PG8_WAIT_L(0); PG8_BAR; PG8_MMA(1, 0, At, B0); PG8_MMA(1, 1, At, B1); PG8_BAR; PG8_SCHED;
;             PG8_LDB(B0, 1, 0); PG8_LDB(B1, 1, 1); PG8_SCHED; PG8_LDA(At, 1, 0); PG8_STAGE_A(PG8_SA(0, 1), a2, 1, g2);
;             PG8_WAIT_V(8); PG8_WAIT_L(0); PG8_BAR; PG8_MMA(0, 0, At, B0); PG8_MMA(0, 1, At, B1); PG8_BAR; PG8_SCHED;
;             PG8_LDA(At, 1, 1); PG8_STAGE(PG8_SB(1, 0), b3, voffB); PG8_STAGE(PG8_SB(1, 1), b3 + hstepB, voffB); PG8_STAGE_A(PG8_SA(1, 0), a3, 0, g2);
;             PG8_WAIT_V(8); PG8_WAIT_L(0); PG8_BAR; PG8_MMA(1, 0, At, B0); PG8_MMA(1, 1, At, B1); PG8_BAR; PG8_SCHED;
	s_waitcnt lgkmcnt(0)
	v_mfma_f32_16x16x32_bf16 v[62:65], v[162:165], v[194:197], v[62:65]
	v_mfma_f32_16x16x32_bf16 v[58:61], v[170:173], v[194:197], v[58:61]
	v_mfma_f32_16x16x32_bf16 v[46:49], v[162:165], v[202:205], v[46:49]
	v_mfma_f32_16x16x32_bf16 v[42:45], v[170:173], v[202:205], v[42:45]
	v_mfma_f32_16x16x32_bf16 v[30:33], v[162:165], v[216:219], v[30:33]
	v_mfma_f32_16x16x32_bf16 v[26:29], v[170:173], v[216:219], v[26:29]
	v_mfma_f32_16x16x32_bf16 v[14:17], v[162:165], v[224:227], v[14:17]
	v_mfma_f32_16x16x32_bf16 v[10:13], v[170:173], v[224:227], v[10:13]
	v_mfma_f32_16x16x32_bf16 v[62:65], v[166:169], v[198:201], v[62:65]
	v_mfma_f32_16x16x32_bf16 v[58:61], v[174:177], v[198:201], v[58:61]
	v_mfma_f32_16x16x32_bf16 v[46:49], v[166:169], v[208:211], v[46:49]
	v_mfma_f32_16x16x32_bf16 v[42:45], v[174:177], v[208:211], v[42:45]
	v_mfma_f32_16x16x32_bf16 v[30:33], v[166:169], v[220:223], v[30:33]
	v_mfma_f32_16x16x32_bf16 v[26:29], v[174:177], v[220:223], v[26:29]
	v_mfma_f32_16x16x32_bf16 v[14:17], v[166:169], v[228:231], v[14:17]
	v_mfma_f32_16x16x32_bf16 v[10:13], v[174:177], v[228:231], v[10:13]
	v_mfma_f32_16x16x32_bf16 v[54:57], v[178:181], v[194:197], v[54:57]
	v_mfma_f32_16x16x32_bf16 v[50:53], v[186:189], v[194:197], v[50:53]
	v_mfma_f32_16x16x32_bf16 v[38:41], v[178:181], v[202:205], v[38:41]
	v_mfma_f32_16x16x32_bf16 v[34:37], v[186:189], v[202:205], v[34:37]
	v_mfma_f32_16x16x32_bf16 v[22:25], v[178:181], v[216:219], v[22:25]
	v_mfma_f32_16x16x32_bf16 v[18:21], v[186:189], v[216:219], v[18:21]
	v_mfma_f32_16x16x32_bf16 v[6:9], v[178:181], v[224:227], v[6:9]
	v_mfma_f32_16x16x32_bf16 v[2:5], v[186:189], v[224:227], v[2:5]
	v_mfma_f32_16x16x32_bf16 v[54:57], v[182:185], v[198:201], v[54:57]
	v_mfma_f32_16x16x32_bf16 v[50:53], v[190:193], v[198:201], v[50:53]
	v_mfma_f32_16x16x32_bf16 v[38:41], v[182:185], v[208:211], v[38:41]
	v_mfma_f32_16x16x32_bf16 v[34:37], v[190:193], v[208:211], v[34:37]
	v_mfma_f32_16x16x32_bf16 v[22:25], v[182:185], v[220:223], v[22:25]
	v_mfma_f32_16x16x32_bf16 v[18:21], v[190:193], v[220:223], v[18:21]
	v_mfma_f32_16x16x32_bf16 v[6:9], v[182:185], v[228:231], v[6:9]
	v_mfma_f32_16x16x32_bf16 v[2:5], v[190:193], v[228:231], v[2:5]
	s_barrier
	s_add_i32 s19, 0, 0x18000
	v_add_u32_e32 v161, s19, v139
	s_add_i32 s20, 0, 0x1c000
	ds_read_b128 v[162:165], v161
	ds_read_b128 v[166:169], v161 offset:1024
	ds_read_b128 v[170:173], v161 offset:2048
	ds_read_b128 v[174:177], v161 offset:3072
	v_add_u32_e32 v161, s20, v139
	ds_read_b128 v[178:181], v161
	ds_read_b128 v[182:185], v161 offset:1024
	ds_read_b128 v[186:189], v161 offset:2048
	ds_read_b128 v[190:193], v161 offset:3072
	s_mov_b32 m0, s59
	ds_read_b128 v[194:197], v156 offset:32768
	ds_read_b128 v[198:201], v156 offset:33792
	ds_read_b128 v[202:205], v156 offset:34816
	ds_read_b128 v[208:211], v156 offset:35840
	ds_read_b128 v[216:219], v156 offset:36864
	ds_read_b128 v[220:223], v156 offset:37888
	ds_read_b128 v[224:227], v156 offset:38912
	ds_read_b128 v[228:231], v156 offset:39936
	global_load_lds_dwordx4 v135, s[30:31]
	s_mov_b32 m0, s60
	s_nop 0
	global_load_lds_dwordx4 v141, s[30:31]
	s_waitcnt vmcnt(8)
	s_waitcnt lgkmcnt(0)
	s_barrier
	s_waitcnt lgkmcnt(0)
	v_mfma_f32_16x16x32_bf16 v[126:129], v[162:165], v[194:197], v[126:129]
	v_mfma_f32_16x16x32_bf16 v[122:125], v[170:173], v[194:197], v[122:125]
	v_mfma_f32_16x16x32_bf16 v[110:113], v[162:165], v[202:205], v[110:113]
	v_mfma_f32_16x16x32_bf16 v[106:109], v[170:173], v[202:205], v[106:109]
	v_mfma_f32_16x16x32_bf16 v[94:97], v[162:165], v[216:219], v[94:97]
	v_mfma_f32_16x16x32_bf16 v[90:93], v[170:173], v[216:219], v[90:93]
	v_mfma_f32_16x16x32_bf16 v[78:81], v[162:165], v[224:227], v[78:81]
	v_mfma_f32_16x16x32_bf16 v[74:77], v[170:173], v[224:227], v[74:77]
	v_mfma_f32_16x16x32_bf16 v[126:129], v[166:169], v[198:201], v[126:129]
	v_mfma_f32_16x16x32_bf16 v[122:125], v[174:177], v[198:201], v[122:125]
	v_mfma_f32_16x16x32_bf16 v[110:113], v[166:169], v[208:211], v[110:113]
	v_mfma_f32_16x16x32_bf16 v[106:109], v[174:177], v[208:211], v[106:109]
	v_mfma_f32_16x16x32_bf16 v[94:97], v[166:169], v[220:223], v[94:97]
	v_mfma_f32_16x16x32_bf16 v[90:93], v[174:177], v[220:223], v[90:93]
	v_mfma_f32_16x16x32_bf16 v[78:81], v[166:169], v[228:231], v[78:81]
	v_mfma_f32_16x16x32_bf16 v[74:77], v[174:177], v[228:231], v[74:77]
	v_mfma_f32_16x16x32_bf16 v[118:121], v[178:181], v[194:197], v[118:121]
	v_mfma_f32_16x16x32_bf16 v[114:117], v[186:189], v[194:197], v[114:117]
	v_mfma_f32_16x16x32_bf16 v[102:105], v[178:181], v[202:205], v[102:105]
	v_mfma_f32_16x16x32_bf16 v[98:101], v[186:189], v[202:205], v[98:101]
	v_mfma_f32_16x16x32_bf16 v[86:89], v[178:181], v[216:219], v[86:89]
	v_mfma_f32_16x16x32_bf16 v[82:85], v[186:189], v[216:219], v[82:85]
	v_mfma_f32_16x16x32_bf16 v[70:73], v[178:181], v[224:227], v[70:73]
	v_mfma_f32_16x16x32_bf16 v[66:69], v[186:189], v[224:227], v[66:69]
	v_mfma_f32_16x16x32_bf16 v[118:121], v[182:185], v[198:201], v[118:121]
	v_mfma_f32_16x16x32_bf16 v[114:117], v[190:193], v[198:201], v[114:117]
	v_mfma_f32_16x16x32_bf16 v[102:105], v[182:185], v[208:211], v[102:105]
	v_mfma_f32_16x16x32_bf16 v[98:101], v[190:193], v[208:211], v[98:101]
	v_mfma_f32_16x16x32_bf16 v[86:89], v[182:185], v[220:223], v[86:89]
	v_mfma_f32_16x16x32_bf16 v[82:85], v[190:193], v[220:223], v[82:85]
	v_mfma_f32_16x16x32_bf16 v[70:73], v[182:185], v[228:231], v[70:73]
	v_mfma_f32_16x16x32_bf16 v[66:69], v[190:193], v[228:231], v[66:69]
	s_barrier
; #define PG8_STAGE(bufoff, gbase, voff) do { _Pragma("unroll") for (int _i = 0; _i < 2; ++_i) \
;         __builtin_amdgcn_global_load_lds((const unsigned*)((const char*)(gbase) + (voff)[_i]), (LAS unsigned*)(lds + (bufoff) + ldsw + _i * 8192), 16, 0, 0); } while (0)
; #define PG8_STAGE_A(bufoff, kptr, half, VO) do { if constexpr (GATHER) { _Pragma("unroll") for (int _i = 0; _i < 2; ++_i) \
;         __builtin_amdgcn_global_load_lds((const unsigned*)((const char*)(kptr) + (VO)[half][_i]), (LAS unsigned*)(lds + (bufoff) + ldsw + _i * 8192), 16, 0, 0); } \
;         else { PG8_STAGE(bufoff, (kptr) + (half) * hstepA, voffA); } } while (0)
; #define PG8_WAIT_V(n) asm volatile("s_waitcnt vmcnt(" #n ")" ::: "memory")
;     ...
;         for (int t = 0; t < nt; t += 2) {
;             const bool last = (t == nt - 2);
;             const char* a1 = cA + (size_t)(t + 1) * kstep;
;             const char* a2 = last ? nA : cA + (size_t)(t + 2) * kstep; const char* b2 = last ? nB : cB + (size_t)(t + 2) * kstep;
;             const char* a3 = a2 + kstep; const char* b3 = b2 + kstep;
;             unsigned g2[2][2];
;             if constexpr (GATHER) {
; #pragma unroll
;                 for (int _h = 0; _h < 2; ++_h)
; #pragma unroll
;                     for (int _i = 0; _i < 2; ++_i) g2[_h][_i] = last ? gN[_h][_i] : gC[_h][_i]; }
;             if constexpr (SP2) {
;             PG8_LDB(B0, 0, 0); PG8_LDB(B1, 0, 1); PG8_SCHED; PG8_LDA(At, 0, 0); PG8_STAGE_A(PG8_SA(1, 1), a1, 1, gC);
;             PG8_WAIT_V(8); PG8_WAIT_L(0); PG8_BAR; PG8_MMA(0, 0, At, B0); PG8_MMA(0, 1, At, B1); PG8_BAR; PG8_SCHED;
;             PG8_LDA(At, 0, 1); PG8_STAGE(PG8_SB(0, 0), b2, voffB); PG8_STAGE(PG8_SB(0, 1), b2 + hstepB, voffB); PG8_STAGE_A(PG8_SA(0, 0), a2, 0, g2);
;             PG8_WAIT_V(8); PG8_WAIT_L(0); PG8_BAR; PG8_MMA(1, 0, At, B0); PG8_MMA(1, 1, At, B1); PG8_BAR; PG8_SCHED;
;             PG8_LDB(B0, 1, 0); PG8_LDB(B1, 1, 1); PG8_SCHED; PG8_LDA(At, 1, 0); PG8_STAGE_A(PG8_SA(0, 1), a2, 1, g2);
;             PG8_WAIT_V(8); PG8_WAIT_L(0); PG8_BAR; PG8_MMA(0, 0, At, B0); PG8_MMA(0, 1, At, B1); PG8_BAR; PG8_SCHED;
;             PG8_LDA(At, 1, 1); PG8_STAGE(PG8_SB(1, 0), b3, voffB); PG8_STAGE(PG8_SB(1, 1), b3 + hstepB, voffB); PG8_STAGE_A(PG8_SA(1, 0), a3, 0, g2);
;             PG8_WAIT_V(8); PG8_WAIT_L(0); PG8_BAR; PG8_MMA(1, 0, At, B0); PG8_MMA(1, 1, At, B1); PG8_BAR; PG8_SCHED;
	s_add_i32 s19, s19, s56
	v_lshl_add_u64 v[214:215], v[214:215], 0, s[8:9]
	s_mov_b32 m0, s19
	ds_read_b128 v[194:197], v156 offset:49152
	ds_read_b128 v[198:201], v156 offset:50176
	ds_read_b128 v[202:205], v156 offset:51200
	ds_read_b128 v[208:211], v156 offset:52224
	ds_read_b128 v[216:219], v156 offset:53248
	ds_read_b128 v[220:223], v156 offset:54272
	ds_read_b128 v[224:227], v156 offset:55296
	ds_read_b128 v[228:231], v156 offset:56320
	global_load_lds_dwordx4 v[214:215], off
	s_add_i32 m0, s19, 0x2000
	s_add_u32 s0, s0, 0x80080
	v_lshl_add_u64 v[214:215], v[232:233], 0, s[8:9]
	s_addc_u32 s1, s1, 0
	s_add_i32 s19, s20, s56
	global_load_lds_dwordx4 v[214:215], off
	v_lshl_add_u64 v[214:215], s[0:1], 0, v[130:131]
	s_mov_b32 m0, s19
	v_lshl_add_u64 v[212:213], v[212:213], 0, s[8:9]
	global_load_lds_dwordx4 v[214:215], off
	v_lshl_add_u64 v[214:215], s[0:1], 0, v[132:133]
	s_add_i32 m0, s19, 0x2000
	s_nop 0
	global_load_lds_dwordx4 v[214:215], off
	v_lshl_add_u64 v[214:215], v[234:235], 0, s[8:9]
	s_mov_b32 m0, s63
	s_nop 0
	global_load_lds_dwordx4 v[214:215], off
	s_mov_b32 m0, s64
	s_nop 0
	global_load_lds_dwordx4 v[212:213], off
	s_waitcnt vmcnt(8)
	s_waitcnt lgkmcnt(0)
	s_barrier
	s_waitcnt lgkmcnt(0)
	v_mfma_f32_16x16x32_bf16 v[62:65], v[162:165], v[194:197], v[62:65]
	v_mfma_f32_16x16x32_bf16 v[58:61], v[170:173], v[194:197], v[58:61]
	v_mfma_f32_16x16x32_bf16 v[46:49], v[162:165], v[202:205], v[46:49]
	v_mfma_f32_16x16x32_bf16 v[42:45], v[170:173], v[202:205], v[42:45]
	v_mfma_f32_16x16x32_bf16 v[30:33], v[162:165], v[216:219], v[30:33]
	v_mfma_f32_16x16x32_bf16 v[26:29], v[170:173], v[216:219], v[26:29]
	v_mfma_f32_16x16x32_bf16 v[14:17], v[162:165], v[224:227], v[14:17]
	v_mfma_f32_16x16x32_bf16 v[10:13], v[170:173], v[224:227], v[10:13]
	v_mfma_f32_16x16x32_bf16 v[62:65], v[166:169], v[198:201], v[62:65]
	v_mfma_f32_16x16x32_bf16 v[58:61], v[174:177], v[198:201], v[58:61]
	v_mfma_f32_16x16x32_bf16 v[46:49], v[166:169], v[208:211], v[46:49]
	v_mfma_f32_16x16x32_bf16 v[42:45], v[174:177], v[208:211], v[42:45]
	v_mfma_f32_16x16x32_bf16 v[30:33], v[166:169], v[220:223], v[30:33]
	v_mfma_f32_16x16x32_bf16 v[26:29], v[174:177], v[220:223], v[26:29]
	v_mfma_f32_16x16x32_bf16 v[14:17], v[166:169], v[228:231], v[14:17]
	v_mfma_f32_16x16x32_bf16 v[10:13], v[174:177], v[228:231], v[10:13]
	v_mfma_f32_16x16x32_bf16 v[54:57], v[178:181], v[194:197], v[54:57]
	v_mfma_f32_16x16x32_bf16 v[50:53], v[186:189], v[194:197], v[50:53]
	v_mfma_f32_16x16x32_bf16 v[38:41], v[178:181], v[202:205], v[38:41]
	v_mfma_f32_16x16x32_bf16 v[34:37], v[186:189], v[202:205], v[34:37]
	v_mfma_f32_16x16x32_bf16 v[22:25], v[178:181], v[216:219], v[22:25]
	v_mfma_f32_16x16x32_bf16 v[18:21], v[186:189], v[216:219], v[18:21]
	v_mfma_f32_16x16x32_bf16 v[6:9], v[178:181], v[224:227], v[6:9]
	v_mfma_f32_16x16x32_bf16 v[2:5], v[186:189], v[224:227], v[2:5]
	v_mfma_f32_16x16x32_bf16 v[54:57], v[182:185], v[198:201], v[54:57]
	v_mfma_f32_16x16x32_bf16 v[50:53], v[190:193], v[198:201], v[50:53]
	v_mfma_f32_16x16x32_bf16 v[38:41], v[182:185], v[208:211], v[38:41]
	v_mfma_f32_16x16x32_bf16 v[34:37], v[190:193], v[208:211], v[34:37]
	v_mfma_f32_16x16x32_bf16 v[22:25], v[182:185], v[220:223], v[22:25]
	v_mfma_f32_16x16x32_bf16 v[18:21], v[190:193], v[220:223], v[18:21]
	v_mfma_f32_16x16x32_bf16 v[6:9], v[182:185], v[228:231], v[6:9]
	v_mfma_f32_16x16x32_bf16 v[2:5], v[190:193], v[228:231], v[2:5]
	s_barrier
	s_add_i32 s18, s18, 2
	s_add_u32 s24, s24, 0x100
	s_addc_u32 s25, s25, 0
	s_cmp_gt_u32 s18, 29
	s_cbranch_scc0 .LBB0_2265
	s_and_b64 vcc, exec, s[42:43]
	s_cbranch_vccz .LBB0_2268
	s_barrier

;     __device__ __forceinline__ void init(const void* A_, const void* B_, int G_, int c_) { T.init(A_, B_, DM, DM, NLAT / 256, INP / 256, 1, 0, 0, G_, c_, 0); }
; __device__ __forceinline__ void moe_fill(const Params& p, LAS unsigned char* lds, int ph) { if (FILL_ON) moe_pump(p, lds, ph, Q_TOTAL, 0); }
; __device__ __forceinline__ void moe_mark_done(const Params& p, int ph) { if (threadIdx.x == 0) (void)__hip_atomic_fetch_add((unsigned*)(p.ws + WS_CTL) + CW_DONE + 64 * ph, 1u, __ATOMIC_RELAXED, __HIP_MEMORY_SCOPE_AGENT); }
; __device__ __forceinline__ void moe_convert_while(const Params& p, LAS unsigned char* lds, int ph, unsigned ngemm) { moe_pump(p, lds, ph, Q_TOTAL, 0, ngemm, false); }
; __device__ __forceinline__ void moe_require(const Params& p, LAS unsigned char* lds, int upto) { moe_pump(p, lds, 0, upto, 1); }
; #define REPLOOP(id) for (int rep_ = 0; rep_ < NREP(id); ++rep_)
; #define REPBAR(id) do { if (rep_ + 1 < NREP(id)) xcd_barrier(bar); } while (0)
; #define SEAM(k) do { if (IN(k) && IN((k) + 1)) xcd_barrier(bar); } while (0)
; __global__ void __launch_bounds__(512, 2) fwd(Params p) {
;     ...
;             moe_require(p, lds, (l + 1) * Q_LAYER); moe_fill(p, lds, pb + 10);
;          REPBAR(12); }
;         SEAM(pb + 10);
;         if (PSEL(13) && IN(pb + 11)) REPLOOP(13) {
;             pg8::MoeSched S; S.init(ws + WS_HID, (bf16_t*)(ws + WS_WTDN) + (size_t)l * NE * DM * FF, FF, FF, l == 0 ? 5 : 4, 8, (size_t)EROWS * FF * 2, (size_t)DM * FF * 2, l == 0 ? GgK : G, c);
;             pg8::EpiDown E{(bf16_t*)(ws + WS_YS), (const float*)(ws + WS_ROWAFF)};
;             if (l == 0 && c >= GgK) moe_convert_while(p, lds, pb + 11, GgK); else { pg8::gemm_phase(lds, pg8::Desc{FF, FF, FF}, S, E); if (l == 0 && nconv) moe_mark_done(p, pb + 11); }
.LBB0_2427:
	s_setprio 0
	s_cmp_le_i32 s86, s4
	s_cselect_b64 s[0:1], -1, 0
	s_cmp_lt_i32 s4, s87
	s_cselect_b64 s[2:3], -1, 0
	s_and_b64 s[2:3], s[0:1], s[2:3]
	s_mov_b64 s[0:1], -1
	s_and_b64 vcc, exec, s[2:3]
	s_cbranch_vccnz .LBB0_2429
	v_readlane_b32 s0, v255, 56
	s_add_i32 s4, s0, 14
	s_mov_b64 s[0:1], 0

; __device__ __forceinline__ int opaque_tid() { int t = threadIdx.x; asm volatile("" : "+v"(t)); return t; }
;     __device__ __forceinline__ bool next(int i, Unit& u) const {
;         int e, rem; const int per = nM * nN;
;         if ((G & 7) == 0) { const int x = c & 7, j = c >> 3, w = G >> 3; const int L = i * w + j; if (L >= 2 * per) return false; e = 2 * x + L / per; rem = L % per; }
;         else { const long L = (long)i * G + c; if (L >= (long)NE * per) return false; e = (int)(L / per); rem = (int)(L % per); }
;         u.pn = rem / nM; u.pm = rem % nM; u.pb = e;
;         u.a = sA == 0 ? A : A + (size_t)e * sA + (size_t)u.pm * 256 * lda * 2; u.b = B + (size_t)e * sB + (size_t)u.pn * 256 * ldb * 2; return true;
;     const int tid = opaque_tid(), wid = __builtin_amdgcn_readfirstlane(tid >> 6), lane = tid & 63, wr = wid >> 2, wc = wid & 3, fr = lane & 15, fq = lane >> 4;
;     const int K = g.K, nt = K / BK;
;     unsigned voffA[2], voffB[2]; int gR[2], gCc[2];
; #pragma unroll
;     for (int i = 0; i < 2; ++i) { int R, C; stage_rc(tid * 16 + i * 8192, R, C); const int Rb = Epi::PERM ? ((R & ~31) + perm32(R & 31)) : R;
;         voffA[i] = (unsigned)(R * g.lda + C) * 2u; voffB[i] = (unsigned)(Rb * g.ldb + C) * 2u; gR[i] = R; gCc[i] = C; }
;     unsigned gC[2][2], gN[2][2];
;     ...
;     const size_t kstep = (size_t)(BK * 2);
;     const size_t hstepA = (size_t)HALF * g.lda * 2, hstepB = (size_t)HALF * g.ldb * 2;
;     const unsigned ldsw = (unsigned)wid * 1024u;
;     const int aoff = lds_byte(wr * 64 + fr, fq * 8), boff = lds_byte(wc * 32 + fr, fq * 8);
;     ...
;     Unit cur, nxt; int ui = 0;
;     if (!S.next(0, cur)) return;
;     f32x4 acc[2][2][4][2];
; #pragma unroll
;     for (int a = 0; a < 2; ++a)
; #pragma unroll
;         for (int b = 0; b < 2; ++b)
; #pragma unroll
;             for (int m = 0; m < 4; ++m)
; #pragma unroll
;                 for (int n = 0; n < 2; ++n) acc[a][b][m][n] = (f32x4){0.f, 0.f, 0.f, 0.f};
;     bf16x8 At[4][2], B0[2][2], B1[2][2];
;     const char* cA = cur.a; const char* cB = cur.b;
;     if constexpr (GATHER) { PG8_GOFF(cur, gC); }
;     if constexpr (SP2) {
;         PG8_STAGE(PG8_SB(0, 0), cB, voffB); PG8_STAGE(PG8_SB(0, 1), cB + hstepB, voffB); PG8_STAGE_A(PG8_SA(0, 0), cA, 0, gC); PG8_STAGE_A(PG8_SA(0, 1), cA, 1, gC);
;         if (wr == 1) PG8_BAR;
;         PG8_WAIT_V(2); PG8_BAR;
.LBB0_2438:
	s_and_b64 vcc, exec, s[0:1]
	s_cbranch_vccz .LBB0_2466
	v_ashrrev_i32_e32 v3, 31, v10
	v_lshrrev_b32_e32 v3, 26, v3
	v_add_u32_e32 v3, v10, v3
	v_ashrrev_i32_e32 v11, 6, v3
	v_bfe_i32 v3, v10, 27, 1
	v_lshlrev_b32_e32 v2, 4, v10
	v_lshrrev_b32_e32 v3, 22, v3
	v_add_u32_e32 v3, v2, v3
	v_and_b32_e32 v3, 0xfffffc00, v3
	v_sub_u32_e32 v3, v2, v3
	v_lshrrev_b32_e32 v4, 4, v3
	v_bitop3_b32 v4, v4, v3, 32 bitop3:0x6c
	v_ashrrev_i32_e32 v3, 31, v3
	v_lshrrev_b32_e32 v3, 26, v3
	v_add_u32_e32 v3, v4, v3
	v_ashrrev_i32_e32 v12, 6, v3
	v_lshlrev_b32_e32 v5, 3, v11
	v_mul_i32_i24_e32 v6, 64, v12
	v_and_b32_e32 v5, -16, v5
	v_sub_u32_e32 v4, v4, v6
	v_add_u32_e32 v3, v12, v5
	v_lshlrev_b32_e32 v5, 5, v11
	v_ashrrev_i16_sdwa v4, v245, sext(v4) dst_sel:DWORD dst_unused:UNUSED_PAD src0_sel:DWORD src1_sel:BYTE_0
	v_and_b32_e32 v5, 32, v5
	v_bfe_i32 v13, v4, 0, 16
	v_and_b32_e32 v7, 3, v12
	s_mov_b32 s0, 0x1fffe0
	v_add_lshl_u32 v5, v5, v13, 1
	v_add_u32_e32 v2, 0x2000, v2
	v_lshlrev_b32_e32 v4, 1, v3
	v_lshrrev_b32_e32 v6, 2, v3
	v_and_or_b32 v7, v3, s0, v7
	v_lshl_add_u32 v130, v3, 11, v5
	v_ashrrev_i32_e32 v3, 31, v2
	v_lshrrev_b32_e32 v3, 22, v3
	v_add_u32_e32 v3, v2, v3
	v_ashrrev_i32_e32 v14, 10, v3
	v_mul_i32_i24_e32 v3, 0x400, v14
	v_sub_u32_e32 v2, v2, v3
	v_and_b32_e32 v4, 24, v4
	v_and_b32_e32 v6, 4, v6
	v_lshrrev_b32_e32 v3, 4, v2
	v_or3_b32 v4, v7, v6, v4
	v_bitop3_b32 v2, v3, v2, 32 bitop3:0x6c
	v_lshl_add_u32 v206, v4, 11, v5
	v_ashrrev_i32_e32 v4, 31, v2
	v_lshrrev_b32_e32 v4, 26, v4
	v_lshlrev_b32_e32 v3, 3, v14
	v_add_u32_e32 v4, v2, v4
	v_and_b32_e32 v3, -16, v3
	v_ashrrev_i32_e32 v15, 6, v4
	v_add_u32_e32 v3, v15, v3
	v_and_b32_e32 v6, 3, v15
	v_and_or_b32 v6, v3, s0, v6
	v_readlane_b32 s0, v252, 5
	s_ashr_i32 s4, s12, 6
	v_readlane_b32 s1, v252, 6
	s_ashr_i32 s14, s12, 8
	s_lshl_b32 s62, s4, 10
	s_lshl_b64 s[0:1], s[0:1], 26
	v_readlane_b32 s15, v254, 11
	v_and_b32_e32 v4, 0xc0, v4
	s_add_u32 s63, s15, s0
	v_readlane_b32 s0, v254, 12
	v_sub_u32_e32 v2, v2, v4
	s_addc_u32 s64, s0, s1
	s_sub_i32 s0, s13, s60
	v_ashrrev_i16_sdwa v2, v245, sext(v2) dst_sel:DWORD dst_unused:UNUSED_PAD src0_sel:DWORD src1_sel:BYTE_0
	s_cmp_ge_u32 s13, s60
	v_lshlrev_b32_e32 v5, 5, v14
	v_bfe_i32 v16, v2, 0, 16
	v_lshlrev_b32_e32 v2, 1, v3
	v_lshrrev_b32_e32 v4, 2, v3
	s_cselect_b32 s0, s0, s13
	v_readlane_b32 s1, v254, 8
	v_and_b32_e32 v5, 32, v5
	v_and_b32_e32 v2, 24, v2
	v_and_b32_e32 v4, 4, v4
	s_xor_b32 s0, s0, s1
	v_or3_b32 v2, v6, v4, v2
	v_add_lshl_u32 v4, v5, v16, 1
	s_sub_i32 s13, s0, s1
	v_cvt_f32_ubyte0_e32 v5, s26
	v_lshl_add_u32 v132, v3, 11, v4
	v_cvt_f32_i32_e32 v3, s13
	v_rcp_iflag_f32_e32 v17, v5
	v_lshl_add_u32 v134, v2, 11, v4
	s_ashr_i32 s0, s13, 30
	s_or_b32 s15, s0, 1
	v_mul_f32_e32 v2, v3, v17
	v_trunc_f32_e32 v2, v2
	v_fma_f32 v3, -v2, v5, v3
	v_cvt_i32_f32_e32 v2, v2
	v_cmp_ge_f32_e64 s[0:1], |v3|, v5
	s_and_b64 s[0:1], s[0:1], exec
	s_cselect_b32 s0, s15, 0
	v_readfirstlane_b32 s1, v2
	s_add_i32 s24, s1, s0
	s_mul_i32 s0, s24, s26
	s_sub_i32 s42, s13, s0
	s_ashr_i32 s37, s36, 31
	s_mul_i32 s1, s36, 0x280000
	v_readlane_b32 s16, v254, 0
	s_mul_hi_i32 s0, s36, 0x280000
	v_readlane_b32 s17, v254, 1
	s_add_u32 s13, s16, s1
	s_addc_u32 s15, s17, s0
	s_bfe_i64 s[0:1], s[42:43], 0x80000
	s_lshl_b64 s[0:1], s[0:1], 19
	s_add_u32 s0, s13, s0
	s_addc_u32 s1, s15, s1
	s_lshl_b64 s[16:17], s[36:37], 22
	s_add_u32 s13, s63, s16
	s_addc_u32 s15, s64, s17
	s_bfe_i64 s[16:17], s[24:25], 0x80000
	s_lshl_b64 s[16:17], s[16:17], 19
	s_add_u32 s30, s13, s16
	s_addc_u32 s31, s15, s17
	s_add_i32 s37, s62, 0
	s_add_i32 m0, s37, 0x10000
	v_mov_b32_e32 v135, v207
	global_load_lds_dwordx4 v206, s[30:31]
	s_add_i32 m0, s37, 0x12000
	s_add_u32 s16, s30, 0x40000
	global_load_lds_dwordx4 v134, s[30:31]
	s_addc_u32 s17, s31, 0
	s_add_i32 m0, s37, 0x14000
	s_add_i32 s65, s37, 0x2000
	global_load_lds_dwordx4 v206, s[16:17]
	s_add_i32 m0, s37, 0x16000
	v_mov_b32_e32 v131, v207
	global_load_lds_dwordx4 v134, s[16:17]
	s_mov_b32 m0, s37
	s_add_u32 s16, s0, 0x40000
	global_load_lds_dwordx4 v130, s[0:1]
	s_mov_b32 m0, s65
	s_addc_u32 s17, s1, 0
	s_add_i32 s66, s37, 0x4000
	global_load_lds_dwordx4 v132, s[0:1]
	s_mov_b32 m0, s66
	s_add_i32 s67, s37, 0x6000
	global_load_lds_dwordx4 v130, s[16:17]
	s_mov_b32 m0, s67
	v_mov_b32_e32 v133, v207
	global_load_lds_dwordx4 v132, s[16:17]
	s_cmp_eq_u32 s14, 1
	v_lshl_add_u64 v[8:9], s[30:31], 0, v[206:207]
	v_lshl_add_u64 v[6:7], s[30:31], 0, v[134:135]
	v_lshl_add_u64 v[2:3], s[0:1], 0, v[130:131]
	s_cselect_b64 s[40:41], -1, 0
	s_cmp_lg_u32 s14, 1
	v_lshl_add_u64 v[4:5], s[0:1], 0, v[132:133]
	s_cbranch_scc1 .LBB0_2441
	s_barrier
	s_setprio 1

; #define PG8_STAGE(bufoff, gbase, voff) do { _Pragma("unroll") for (int _i = 0; _i < 2; ++_i) \
;         __builtin_amdgcn_global_load_lds((const unsigned*)((const char*)(gbase) + (voff)[_i]), (LAS unsigned*)(lds + (bufoff) + ldsw + _i * 8192), 16, 0, 0); } while (0)
; #define PG8_STAGE_A(bufoff, kptr, half, VO) do { if constexpr (GATHER) { _Pragma("unroll") for (int _i = 0; _i < 2; ++_i) \
;         __builtin_amdgcn_global_load_lds((const unsigned*)((const char*)(kptr) + (VO)[half][_i]), (LAS unsigned*)(lds + (bufoff) + ldsw + _i * 8192), 16, 0, 0); } \
;         else { PG8_STAGE(bufoff, (kptr) + (half) * hstepA, voffA); } } while (0)
; #define PG8_WAIT_V(n) asm volatile("s_waitcnt vmcnt(" #n ")" ::: "memory")
;     ...
;         for (int t = 0; t < nt; t += 2) {
;             const bool last = (t == nt - 2);
;             const char* a1 = cA + (size_t)(t + 1) * kstep;
;             const char* a2 = last ? nA : cA + (size_t)(t + 2) * kstep; const char* b2 = last ? nB : cB + (size_t)(t + 2) * kstep;
;             const char* a3 = a2 + kstep; const char* b3 = b2 + kstep;
;             unsigned g2[2][2];
;             if constexpr (GATHER) {
; #pragma unroll
;                 for (int _h = 0; _h < 2; ++_h)
; #pragma unroll
;                     for (int _i = 0; _i < 2; ++_i) g2[_h][_i] = last ? gN[_h][_i] : gC[_h][_i]; }
;             if constexpr (SP2) {
;             PG8_LDB(B0, 0, 0); PG8_LDB(B1, 0, 1); PG8_SCHED; PG8_LDA(At, 0, 0); PG8_STAGE_A(PG8_SA(1, 1), a1, 1, gC);
;             PG8_WAIT_V(8); PG8_WAIT_L(0); PG8_BAR; PG8_MMA(0, 0, At, B0); PG8_MMA(0, 1, At, B1); PG8_BAR; PG8_SCHED;
;             PG8_LDA(At, 0, 1); PG8_STAGE(PG8_SB(0, 0), b2, voffB); PG8_STAGE(PG8_SB(0, 1), b2 + hstepB, voffB); PG8_STAGE_A(PG8_SA(0, 0), a2, 0, g2);
;             PG8_WAIT_V(8); PG8_WAIT_L(0); PG8_BAR; PG8_MMA(1, 0, At, B0); PG8_MMA(1, 1, At, B1); PG8_BAR; PG8_SCHED;
;             PG8_LDB(B0, 1, 0); PG8_LDB(B1, 1, 1); PG8_SCHED; PG8_LDA(At, 1, 0); PG8_STAGE_A(PG8_SA(0, 1), a2, 1, g2);
;             PG8_WAIT_V(8); PG8_WAIT_L(0); PG8_BAR; PG8_MMA(0, 0, At, B0); PG8_MMA(0, 1, At, B1); PG8_BAR; PG8_SCHED;
;             PG8_LDA(At, 1, 1); PG8_STAGE(PG8_SB(1, 0), b3, voffB); PG8_STAGE(PG8_SB(1, 1), b3 + hstepB, voffB); PG8_STAGE_A(PG8_SA(1, 0), a3, 0, g2);
;             PG8_WAIT_V(8); PG8_WAIT_L(0); PG8_BAR; PG8_MMA(1, 0, At, B0); PG8_MMA(1, 1, At, B1); PG8_BAR; PG8_SCHED;
.LBB0_2458:
	s_add_u32 s0, s24, 0xfffc0080
	s_addc_u32 s1, s25, -1
	s_add_i32 s19, 0, 0x10000
	s_cmp_eq_u32 s18, 12
	s_cselect_b32 s31, s12, s1
	s_cselect_b32 s30, s13, s0
	v_add_u32_e32 v140, s19, v145
	s_cselect_b32 s1, s14, s17
	s_cselect_b32 s0, s15, s16
	s_add_i32 s22, 0, 0x14000
	ds_read_b128 v[156:159], v140
	ds_read_b128 v[160:163], v140 offset:1024
	ds_read_b128 v[164:167], v140 offset:2048
	ds_read_b128 v[168:171], v140 offset:3072
	v_add_u32_e32 v140, s22, v145
	ds_read_b128 v[172:175], v140
	ds_read_b128 v[176:179], v140 offset:1024
	ds_read_b128 v[180:183], v140 offset:2048
	ds_read_b128 v[184:187], v140 offset:3072
	v_lshl_add_u64 v[142:143], s[24:25], 0, v[136:137]
	s_add_i32 m0, s37, 0xc000
	ds_read_b128 v[188:191], v155
	ds_read_b128 v[192:195], v155 offset:1024
	ds_read_b128 v[196:199], v155 offset:2048
	ds_read_b128 v[200:203], v155 offset:3072
	ds_read_b128 v[208:211], v155 offset:4096
	ds_read_b128 v[216:219], v155 offset:5120
	ds_read_b128 v[220:223], v155 offset:6144
	ds_read_b128 v[224:227], v155 offset:7168
	global_load_lds_dwordx4 v[142:143], off
	v_lshl_add_u64 v[142:143], s[24:25], 0, v[138:139]
	s_add_i32 m0, s37, 0xe000
	s_nop 0
	global_load_lds_dwordx4 v[142:143], off
	s_waitcnt vmcnt(8)
	s_waitcnt lgkmcnt(0)
	s_barrier
	s_waitcnt lgkmcnt(0)
	v_mfma_f32_16x16x32_bf16 v[126:129], v[156:159], v[188:191], v[126:129]
	v_mfma_f32_16x16x32_bf16 v[122:125], v[164:167], v[188:191], v[122:125]
	v_mfma_f32_16x16x32_bf16 v[110:113], v[156:159], v[196:199], v[110:113]
	v_mfma_f32_16x16x32_bf16 v[106:109], v[164:167], v[196:199], v[106:109]
	v_mfma_f32_16x16x32_bf16 v[94:97], v[156:159], v[208:211], v[94:97]
	v_mfma_f32_16x16x32_bf16 v[90:93], v[164:167], v[208:211], v[90:93]
	v_mfma_f32_16x16x32_bf16 v[86:89], v[156:159], v[220:223], v[86:89]
	v_mfma_f32_16x16x32_bf16 v[78:81], v[164:167], v[220:223], v[78:81]
	v_mfma_f32_16x16x32_bf16 v[126:129], v[160:163], v[192:195], v[126:129]
	v_mfma_f32_16x16x32_bf16 v[122:125], v[168:171], v[192:195], v[122:125]
	v_mfma_f32_16x16x32_bf16 v[110:113], v[160:163], v[200:203], v[110:113]
	v_mfma_f32_16x16x32_bf16 v[106:109], v[168:171], v[200:203], v[106:109]
	v_mfma_f32_16x16x32_bf16 v[94:97], v[160:163], v[216:219], v[94:97]
	v_mfma_f32_16x16x32_bf16 v[90:93], v[168:171], v[216:219], v[90:93]
	v_mfma_f32_16x16x32_bf16 v[86:89], v[160:163], v[224:227], v[86:89]
	v_mfma_f32_16x16x32_bf16 v[78:81], v[168:171], v[224:227], v[78:81]
	v_mfma_f32_16x16x32_bf16 v[118:121], v[172:175], v[188:191], v[118:121]
	v_mfma_f32_16x16x32_bf16 v[114:117], v[180:183], v[188:191], v[114:117]
	v_mfma_f32_16x16x32_bf16 v[102:105], v[172:175], v[196:199], v[102:105]
	v_mfma_f32_16x16x32_bf16 v[98:101], v[180:183], v[196:199], v[98:101]
	v_mfma_f32_16x16x32_bf16 v[82:85], v[172:175], v[208:211], v[82:85]
	v_mfma_f32_16x16x32_bf16 v[74:77], v[180:183], v[208:211], v[74:77]
	v_mfma_f32_16x16x32_bf16 v[70:73], v[172:175], v[220:223], v[70:73]
	v_mfma_f32_16x16x32_bf16 v[66:69], v[180:183], v[220:223], v[66:69]
	v_mfma_f32_16x16x32_bf16 v[118:121], v[176:179], v[192:195], v[118:121]
	v_mfma_f32_16x16x32_bf16 v[114:117], v[184:187], v[192:195], v[114:117]
	v_mfma_f32_16x16x32_bf16 v[102:105], v[176:179], v[200:203], v[102:105]
	v_mfma_f32_16x16x32_bf16 v[98:101], v[184:187], v[200:203], v[98:101]
	v_mfma_f32_16x16x32_bf16 v[82:85], v[176:179], v[216:219], v[82:85]
	v_mfma_f32_16x16x32_bf16 v[74:77], v[184:187], v[216:219], v[74:77]
	v_mfma_f32_16x16x32_bf16 v[70:73], v[176:179], v[224:227], v[70:73]
	v_mfma_f32_16x16x32_bf16 v[66:69], v[184:187], v[224:227], v[66:69]
	s_barrier
	s_add_i32 s19, s19, s62
	v_lshl_add_u64 v[142:143], s[0:1], 0, v[206:207]
	s_mov_b32 m0, s19
	ds_read_b128 v[188:191], v155 offset:16384
	ds_read_b128 v[192:195], v155 offset:17408
	ds_read_b128 v[196:199], v155 offset:18432
	ds_read_b128 v[200:203], v155 offset:19456
	ds_read_b128 v[208:211], v155 offset:20480
	ds_read_b128 v[216:219], v155 offset:21504
	ds_read_b128 v[220:223], v155 offset:22528
	ds_read_b128 v[224:227], v155 offset:23552
	global_load_lds_dwordx4 v[142:143], off
	s_add_i32 m0, s19, 0x2000
	s_add_u32 s20, s0, 0x40000
	v_lshl_add_u64 v[204:205], s[0:1], 0, v[134:135]
	s_addc_u32 s21, s1, 0
	s_add_i32 s19, s22, s62
	global_load_lds_dwordx4 v[204:205], off
	v_lshl_add_u64 v[212:213], s[20:21], 0, v[206:207]
	s_mov_b32 m0, s19
	v_lshl_add_u64 v[214:215], s[30:31], 0, v[132:133]
	global_load_lds_dwordx4 v[212:213], off
	v_lshl_add_u64 v[212:213], s[20:21], 0, v[134:135]
	s_add_i32 m0, s19, 0x2000
	s_nop 0
	global_load_lds_dwordx4 v[212:213], off
	v_lshl_add_u64 v[212:213], s[30:31], 0, v[130:131]
	s_mov_b32 m0, s37
	s_nop 0
	global_load_lds_dwordx4 v[212:213], off
	s_mov_b32 m0, s65
	s_nop 0
	global_load_lds_dwordx4 v[214:215], off
	s_waitcnt vmcnt(8)
	s_waitcnt lgkmcnt(0)
	s_barrier
; #define PG8_STAGE(bufoff, gbase, voff) do { _Pragma("unroll") for (int _i = 0; _i < 2; ++_i) \
;         __builtin_amdgcn_global_load_lds((const unsigned*)((const char*)(gbase) + (voff)[_i]), (LAS unsigned*)(lds + (bufoff) + ldsw + _i * 8192), 16, 0, 0); } while (0)
; #define PG8_STAGE_A(bufoff, kptr, half, VO) do { if constexpr (GATHER) { _Pragma("unroll") for (int _i = 0; _i < 2; ++_i) \
;         __builtin_amdgcn_global_load_lds((const unsigned*)((const char*)(kptr) + (VO)[half][_i]), (LAS unsigned*)(lds + (bufoff) + ldsw + _i * 8192), 16, 0, 0); } \
;         else { PG8_STAGE(bufoff, (kptr) + (half) * hstepA, voffA); } } while (0)
; #define PG8_WAIT_V(n) asm volatile("s_waitcnt vmcnt(" #n ")" ::: "memory")
;     ...
;         for (int t = 0; t < nt; t += 2) {
;             const bool last = (t == nt - 2);
;             const char* a1 = cA + (size_t)(t + 1) * kstep;
;             const char* a2 = last ? nA : cA + (size_t)(t + 2) * kstep; const char* b2 = last ? nB : cB + (size_t)(t + 2) * kstep;
;             const char* a3 = a2 + kstep; const char* b3 = b2 + kstep;
;             unsigned g2[2][2];
;             if constexpr (GATHER) {
; #pragma unroll
;                 for (int _h = 0; _h < 2; ++_h)
; #pragma unroll
;                     for (int _i = 0; _i < 2; ++_i) g2[_h][_i] = last ? gN[_h][_i] : gC[_h][_i]; }
;             if constexpr (SP2) {
;             PG8_LDB(B0, 0, 0); PG8_LDB(B1, 0, 1); PG8_SCHED; PG8_LDA(At, 0, 0); PG8_STAGE_A(PG8_SA(1, 1), a1, 1, gC);
;             PG8_WAIT_V(8); PG8_WAIT_L(0); PG8_BAR; PG8_MMA(0, 0, At, B0); PG8_MMA(0, 1, At, B1); PG8_BAR; PG8_SCHED;
;             PG8_LDA(At, 0, 1); PG8_STAGE(PG8_SB(0, 0), b2, voffB); PG8_STAGE(PG8_SB(0, 1), b2 + hstepB, voffB); PG8_STAGE_A(PG8_SA(0, 0), a2, 0, g2);
;             PG8_WAIT_V(8); PG8_WAIT_L(0); PG8_BAR; PG8_MMA(1, 0, At, B0); PG8_MMA(1, 1, At, B1); PG8_BAR; PG8_SCHED;
;             PG8_LDB(B0, 1, 0); PG8_LDB(B1, 1, 1); PG8_SCHED; PG8_LDA(At, 1, 0); PG8_STAGE_A(PG8_SA(0, 1), a2, 1, g2);
;             PG8_WAIT_V(8); PG8_WAIT_L(0); PG8_BAR; PG8_MMA(0, 0, At, B0); PG8_MMA(0, 1, At, B1); PG8_BAR; PG8_SCHED;
;             PG8_LDA(At, 1, 1); PG8_STAGE(PG8_SB(1, 0), b3, voffB); PG8_STAGE(PG8_SB(1, 1), b3 + hstepB, voffB); PG8_STAGE_A(PG8_SA(1, 0), a3, 0, g2);
;             PG8_WAIT_V(8); PG8_WAIT_L(0); PG8_BAR; PG8_MMA(1, 0, At, B0); PG8_MMA(1, 1, At, B1); PG8_BAR; PG8_SCHED;
	s_waitcnt lgkmcnt(0)
	v_mfma_f32_16x16x32_bf16 v[62:65], v[156:159], v[188:191], v[62:65]
	v_mfma_f32_16x16x32_bf16 v[58:61], v[164:167], v[188:191], v[58:61]
	v_mfma_f32_16x16x32_bf16 v[54:57], v[156:159], v[196:199], v[54:57]
	v_mfma_f32_16x16x32_bf16 v[46:49], v[164:167], v[196:199], v[46:49]
	v_mfma_f32_16x16x32_bf16 v[38:41], v[156:159], v[208:211], v[38:41]
	v_mfma_f32_16x16x32_bf16 v[30:33], v[164:167], v[208:211], v[30:33]
	v_mfma_f32_16x16x32_bf16 v[22:25], v[156:159], v[220:223], v[22:25]
	v_mfma_f32_16x16x32_bf16 v[14:17], v[164:167], v[220:223], v[14:17]
	v_mfma_f32_16x16x32_bf16 v[62:65], v[160:163], v[192:195], v[62:65]
	v_mfma_f32_16x16x32_bf16 v[58:61], v[168:171], v[192:195], v[58:61]
	v_mfma_f32_16x16x32_bf16 v[54:57], v[160:163], v[200:203], v[54:57]
	v_mfma_f32_16x16x32_bf16 v[46:49], v[168:171], v[200:203], v[46:49]
	v_mfma_f32_16x16x32_bf16 v[38:41], v[160:163], v[216:219], v[38:41]
	v_mfma_f32_16x16x32_bf16 v[30:33], v[168:171], v[216:219], v[30:33]
	v_mfma_f32_16x16x32_bf16 v[22:25], v[160:163], v[224:227], v[22:25]
	v_mfma_f32_16x16x32_bf16 v[14:17], v[168:171], v[224:227], v[14:17]
	v_mfma_f32_16x16x32_bf16 v[50:53], v[172:175], v[188:191], v[50:53]
	v_mfma_f32_16x16x32_bf16 v[42:45], v[180:183], v[188:191], v[42:45]
	v_mfma_f32_16x16x32_bf16 v[34:37], v[172:175], v[196:199], v[34:37]
	v_mfma_f32_16x16x32_bf16 v[26:29], v[180:183], v[196:199], v[26:29]
	v_mfma_f32_16x16x32_bf16 v[18:21], v[172:175], v[208:211], v[18:21]
	v_mfma_f32_16x16x32_bf16 v[10:13], v[180:183], v[208:211], v[10:13]
	v_mfma_f32_16x16x32_bf16 v[6:9], v[172:175], v[220:223], v[6:9]
	v_mfma_f32_16x16x32_bf16 v[2:5], v[180:183], v[220:223], v[2:5]
	v_mfma_f32_16x16x32_bf16 v[50:53], v[176:179], v[192:195], v[50:53]
	v_mfma_f32_16x16x32_bf16 v[42:45], v[184:187], v[192:195], v[42:45]
	v_mfma_f32_16x16x32_bf16 v[34:37], v[176:179], v[200:203], v[34:37]
	v_mfma_f32_16x16x32_bf16 v[26:29], v[184:187], v[200:203], v[26:29]
	v_mfma_f32_16x16x32_bf16 v[18:21], v[176:179], v[216:219], v[18:21]
	v_mfma_f32_16x16x32_bf16 v[10:13], v[184:187], v[216:219], v[10:13]
	v_mfma_f32_16x16x32_bf16 v[6:9], v[176:179], v[224:227], v[6:9]
	v_mfma_f32_16x16x32_bf16 v[2:5], v[184:187], v[224:227], v[2:5]
	s_barrier
	s_add_i32 s19, 0, 0x18000
	v_add_u32_e32 v140, s19, v145
	s_add_i32 s22, 0, 0x1c000
	ds_read_b128 v[156:159], v140
	ds_read_b128 v[160:163], v140 offset:1024
	ds_read_b128 v[164:167], v140 offset:2048
	ds_read_b128 v[168:171], v140 offset:3072
	v_add_u32_e32 v140, s22, v145
	ds_read_b128 v[172:175], v140
	ds_read_b128 v[176:179], v140 offset:1024
	ds_read_b128 v[180:183], v140 offset:2048
	ds_read_b128 v[184:187], v140 offset:3072
	s_add_u32 s20, s30, 0x40000
	s_addc_u32 s21, s31, 0
	s_mov_b32 m0, s66
	v_lshl_add_u64 v[228:229], s[20:21], 0, v[130:131]
	ds_read_b128 v[188:191], v155 offset:32768
	ds_read_b128 v[192:195], v155 offset:33792
	ds_read_b128 v[196:199], v155 offset:34816
	ds_read_b128 v[200:203], v155 offset:35840
	ds_read_b128 v[208:211], v155 offset:36864
	ds_read_b128 v[216:219], v155 offset:37888
	ds_read_b128 v[220:223], v155 offset:38912
	ds_read_b128 v[224:227], v155 offset:39936
	global_load_lds_dwordx4 v[228:229], off
	v_lshl_add_u64 v[228:229], s[20:21], 0, v[132:133]
	s_mov_b32 m0, s67
	s_nop 0
	global_load_lds_dwordx4 v[228:229], off
	s_waitcnt vmcnt(8)
	s_waitcnt lgkmcnt(0)
	s_barrier
	s_waitcnt lgkmcnt(0)
	v_mfma_f32_16x16x32_bf16 v[126:129], v[156:159], v[188:191], v[126:129]
	v_mfma_f32_16x16x32_bf16 v[122:125], v[164:167], v[188:191], v[122:125]
	v_mfma_f32_16x16x32_bf16 v[110:113], v[156:159], v[196:199], v[110:113]
	v_mfma_f32_16x16x32_bf16 v[106:109], v[164:167], v[196:199], v[106:109]
	v_mfma_f32_16x16x32_bf16 v[94:97], v[156:159], v[208:211], v[94:97]
	v_mfma_f32_16x16x32_bf16 v[90:93], v[164:167], v[208:211], v[90:93]
	v_mfma_f32_16x16x32_bf16 v[86:89], v[156:159], v[220:223], v[86:89]
	v_mfma_f32_16x16x32_bf16 v[78:81], v[164:167], v[220:223], v[78:81]
	v_mfma_f32_16x16x32_bf16 v[126:129], v[160:163], v[192:195], v[126:129]
	v_mfma_f32_16x16x32_bf16 v[122:125], v[168:171], v[192:195], v[122:125]
	v_mfma_f32_16x16x32_bf16 v[110:113], v[160:163], v[200:203], v[110:113]
	v_mfma_f32_16x16x32_bf16 v[106:109], v[168:171], v[200:203], v[106:109]
	v_mfma_f32_16x16x32_bf16 v[94:97], v[160:163], v[216:219], v[94:97]
	v_mfma_f32_16x16x32_bf16 v[90:93], v[168:171], v[216:219], v[90:93]
	v_mfma_f32_16x16x32_bf16 v[86:89], v[160:163], v[224:227], v[86:89]
	v_mfma_f32_16x16x32_bf16 v[78:81], v[168:171], v[224:227], v[78:81]
	v_mfma_f32_16x16x32_bf16 v[118:121], v[172:175], v[188:191], v[118:121]
	v_mfma_f32_16x16x32_bf16 v[114:117], v[180:183], v[188:191], v[114:117]
	v_mfma_f32_16x16x32_bf16 v[102:105], v[172:175], v[196:199], v[102:105]
	v_mfma_f32_16x16x32_bf16 v[98:101], v[180:183], v[196:199], v[98:101]
	v_mfma_f32_16x16x32_bf16 v[82:85], v[172:175], v[208:211], v[82:85]
	v_mfma_f32_16x16x32_bf16 v[74:77], v[180:183], v[208:211], v[74:77]
	v_mfma_f32_16x16x32_bf16 v[70:73], v[172:175], v[220:223], v[70:73]
	v_mfma_f32_16x16x32_bf16 v[66:69], v[180:183], v[220:223], v[66:69]
	v_mfma_f32_16x16x32_bf16 v[118:121], v[176:179], v[192:195], v[118:121]
	v_mfma_f32_16x16x32_bf16 v[114:117], v[184:187], v[192:195], v[114:117]
	v_mfma_f32_16x16x32_bf16 v[102:105], v[176:179], v[200:203], v[102:105]
	v_mfma_f32_16x16x32_bf16 v[98:101], v[184:187], v[200:203], v[98:101]
	v_mfma_f32_16x16x32_bf16 v[82:85], v[176:179], v[216:219], v[82:85]
	v_mfma_f32_16x16x32_bf16 v[74:77], v[184:187], v[216:219], v[74:77]
	v_mfma_f32_16x16x32_bf16 v[70:73], v[176:179], v[224:227], v[70:73]
	v_mfma_f32_16x16x32_bf16 v[66:69], v[184:187], v[224:227], v[66:69]
	s_barrier
; #define PG8_STAGE(bufoff, gbase, voff) do { _Pragma("unroll") for (int _i = 0; _i < 2; ++_i) \
;         __builtin_amdgcn_global_load_lds((const unsigned*)((const char*)(gbase) + (voff)[_i]), (LAS unsigned*)(lds + (bufoff) + ldsw + _i * 8192), 16, 0, 0); } while (0)
; #define PG8_STAGE_A(bufoff, kptr, half, VO) do { if constexpr (GATHER) { _Pragma("unroll") for (int _i = 0; _i < 2; ++_i) \
;         __builtin_amdgcn_global_load_lds((const unsigned*)((const char*)(kptr) + (VO)[half][_i]), (LAS unsigned*)(lds + (bufoff) + ldsw + _i * 8192), 16, 0, 0); } \
;         else { PG8_STAGE(bufoff, (kptr) + (half) * hstepA, voffA); } } while (0)
; #define PG8_WAIT_V(n) asm volatile("s_waitcnt vmcnt(" #n ")" ::: "memory")
;     ...
;         for (int t = 0; t < nt; t += 2) {
;             const bool last = (t == nt - 2);
;             const char* a1 = cA + (size_t)(t + 1) * kstep;
;             const char* a2 = last ? nA : cA + (size_t)(t + 2) * kstep; const char* b2 = last ? nB : cB + (size_t)(t + 2) * kstep;
;             const char* a3 = a2 + kstep; const char* b3 = b2 + kstep;
;             unsigned g2[2][2];
;             if constexpr (GATHER) {
; #pragma unroll
;                 for (int _h = 0; _h < 2; ++_h)
; #pragma unroll
;                     for (int _i = 0; _i < 2; ++_i) g2[_h][_i] = last ? gN[_h][_i] : gC[_h][_i]; }
;             if constexpr (SP2) {
;             PG8_LDB(B0, 0, 0); PG8_LDB(B1, 0, 1); PG8_SCHED; PG8_LDA(At, 0, 0); PG8_STAGE_A(PG8_SA(1, 1), a1, 1, gC);
;             PG8_WAIT_V(8); PG8_WAIT_L(0); PG8_BAR; PG8_MMA(0, 0, At, B0); PG8_MMA(0, 1, At, B1); PG8_BAR; PG8_SCHED;
;             PG8_LDA(At, 0, 1); PG8_STAGE(PG8_SB(0, 0), b2, voffB); PG8_STAGE(PG8_SB(0, 1), b2 + hstepB, voffB); PG8_STAGE_A(PG8_SA(0, 0), a2, 0, g2);
;             PG8_WAIT_V(8); PG8_WAIT_L(0); PG8_BAR; PG8_MMA(1, 0, At, B0); PG8_MMA(1, 1, At, B1); PG8_BAR; PG8_SCHED;
;             PG8_LDB(B0, 1, 0); PG8_LDB(B1, 1, 1); PG8_SCHED; PG8_LDA(At, 1, 0); PG8_STAGE_A(PG8_SA(0, 1), a2, 1, g2);
;             PG8_WAIT_V(8); PG8_WAIT_L(0); PG8_BAR; PG8_MMA(0, 0, At, B0); PG8_MMA(0, 1, At, B1); PG8_BAR; PG8_SCHED;
;             PG8_LDA(At, 1, 1); PG8_STAGE(PG8_SB(1, 0), b3, voffB); PG8_STAGE(PG8_SB(1, 1), b3 + hstepB, voffB); PG8_STAGE_A(PG8_SA(1, 0), a3, 0, g2);
;             PG8_WAIT_V(8); PG8_WAIT_L(0); PG8_BAR; PG8_MMA(1, 0, At, B0); PG8_MMA(1, 1, At, B1); PG8_BAR; PG8_SCHED;
	s_add_i32 s19, s19, s62
	v_lshl_add_u64 v[142:143], v[142:143], 0, s[8:9]
	s_mov_b32 m0, s19
	ds_read_b128 v[188:191], v155 offset:49152
	ds_read_b128 v[192:195], v155 offset:50176
	ds_read_b128 v[196:199], v155 offset:51200
	ds_read_b128 v[200:203], v155 offset:52224
	ds_read_b128 v[208:211], v155 offset:53248
	ds_read_b128 v[216:219], v155 offset:54272
	ds_read_b128 v[220:223], v155 offset:55296
	ds_read_b128 v[224:227], v155 offset:56320
	global_load_lds_dwordx4 v[142:143], off
	s_add_i32 m0, s19, 0x2000
	s_add_u32 s0, s0, 0x40080
	v_lshl_add_u64 v[142:143], v[204:205], 0, s[8:9]
	s_addc_u32 s1, s1, 0
	s_add_i32 s19, s22, s62
	global_load_lds_dwordx4 v[142:143], off
	v_lshl_add_u64 v[142:143], s[0:1], 0, v[206:207]
	s_mov_b32 m0, s19
	s_nop 0
	global_load_lds_dwordx4 v[142:143], off
	v_lshl_add_u64 v[142:143], s[0:1], 0, v[134:135]
	s_add_i32 m0, s19, 0x2000
	s_nop 0
	global_load_lds_dwordx4 v[142:143], off
	v_lshl_add_u64 v[142:143], v[212:213], 0, s[8:9]
	s_mov_b32 m0, s70
	s_nop 0
	global_load_lds_dwordx4 v[142:143], off
	v_lshl_add_u64 v[142:143], v[214:215], 0, s[8:9]
	s_mov_b32 m0, s71
	s_nop 0
	global_load_lds_dwordx4 v[142:143], off
	s_waitcnt vmcnt(8)
	s_waitcnt lgkmcnt(0)
	s_barrier
	s_waitcnt lgkmcnt(0)
	v_mfma_f32_16x16x32_bf16 v[62:65], v[156:159], v[188:191], v[62:65]
	v_mfma_f32_16x16x32_bf16 v[58:61], v[164:167], v[188:191], v[58:61]
	v_mfma_f32_16x16x32_bf16 v[54:57], v[156:159], v[196:199], v[54:57]
	v_mfma_f32_16x16x32_bf16 v[46:49], v[164:167], v[196:199], v[46:49]
	v_mfma_f32_16x16x32_bf16 v[38:41], v[156:159], v[208:211], v[38:41]
	v_mfma_f32_16x16x32_bf16 v[30:33], v[164:167], v[208:211], v[30:33]
	v_mfma_f32_16x16x32_bf16 v[22:25], v[156:159], v[220:223], v[22:25]
	v_mfma_f32_16x16x32_bf16 v[14:17], v[164:167], v[220:223], v[14:17]
	v_mfma_f32_16x16x32_bf16 v[62:65], v[160:163], v[192:195], v[62:65]
	v_mfma_f32_16x16x32_bf16 v[58:61], v[168:171], v[192:195], v[58:61]
	v_mfma_f32_16x16x32_bf16 v[54:57], v[160:163], v[200:203], v[54:57]
	v_mfma_f32_16x16x32_bf16 v[46:49], v[168:171], v[200:203], v[46:49]
	v_mfma_f32_16x16x32_bf16 v[38:41], v[160:163], v[216:219], v[38:41]
	v_mfma_f32_16x16x32_bf16 v[30:33], v[168:171], v[216:219], v[30:33]
	v_mfma_f32_16x16x32_bf16 v[22:25], v[160:163], v[224:227], v[22:25]
	v_mfma_f32_16x16x32_bf16 v[14:17], v[168:171], v[224:227], v[14:17]
	v_mfma_f32_16x16x32_bf16 v[50:53], v[172:175], v[188:191], v[50:53]
	v_mfma_f32_16x16x32_bf16 v[42:45], v[180:183], v[188:191], v[42:45]
	v_mfma_f32_16x16x32_bf16 v[34:37], v[172:175], v[196:199], v[34:37]
	v_mfma_f32_16x16x32_bf16 v[26:29], v[180:183], v[196:199], v[26:29]
	v_mfma_f32_16x16x32_bf16 v[18:21], v[172:175], v[208:211], v[18:21]
	v_mfma_f32_16x16x32_bf16 v[10:13], v[180:183], v[208:211], v[10:13]
	v_mfma_f32_16x16x32_bf16 v[6:9], v[172:175], v[220:223], v[6:9]
	v_mfma_f32_16x16x32_bf16 v[2:5], v[180:183], v[220:223], v[2:5]
	v_mfma_f32_16x16x32_bf16 v[50:53], v[176:179], v[192:195], v[50:53]
	v_mfma_f32_16x16x32_bf16 v[42:45], v[184:187], v[192:195], v[42:45]
	v_mfma_f32_16x16x32_bf16 v[34:37], v[176:179], v[200:203], v[34:37]
	v_mfma_f32_16x16x32_bf16 v[26:29], v[184:187], v[200:203], v[26:29]
	v_mfma_f32_16x16x32_bf16 v[18:21], v[176:179], v[216:219], v[18:21]
	v_mfma_f32_16x16x32_bf16 v[10:13], v[184:187], v[216:219], v[10:13]
	v_mfma_f32_16x16x32_bf16 v[6:9], v[176:179], v[224:227], v[6:9]
	v_mfma_f32_16x16x32_bf16 v[2:5], v[184:187], v[224:227], v[2:5]
	s_barrier
	s_add_i32 s18, s18, 2
	s_add_u32 s24, s24, 0x100
	s_addc_u32 s25, s25, 0
	s_add_u32 s16, s16, 0x100
	s_addc_u32 s17, s17, 0
	s_cmp_gt_u32 s18, 13
	s_cbranch_scc0 .LBB0_2458
	s_and_b64 vcc, exec, s[42:43]
	s_cbranch_vccz .LBB0_2461
	s_barrier

; __device__ __forceinline__ void moe_fill(const Params& p, LAS unsigned char* lds, int ph) { if (FILL_ON) moe_pump(p, lds, ph, Q_TOTAL, 0); }
; #define REPLOOP(id) for (int rep_ = 0; rep_ < NREP(id); ++rep_)
; #define REPBAR(id) do { if (rep_ + 1 < NREP(id)) xcd_barrier(bar); } while (0)
; #define SEAM(k) do { if (IN(k) && IN((k) + 1)) xcd_barrier(bar); } while (0)
; __global__ void __launch_bounds__(512, 2) fwd(Params p) {
;     ...
;             moe_fill(p, lds, pb + 11);
;          REPBAR(13); }
;         SEAM(pb + 11);
;         if (PSEL(14) && IN(pb + 12)) REPLOOP(14) { ph_combine(p, l);  REPBAR(14); }
.LBB0_2673:
	s_setprio 0
	s_cmp_gt_i32 s86, s4
	s_cselect_b64 s[0:1], -1, 0
	s_cmp_ge_i32 s4, s87
	s_cselect_b64 s[2:3], -1, 0
	s_or_b64 s[0:1], s[0:1], s[2:3]
	s_and_b64 vcc, exec, s[0:1]
	s_cbranch_vccz .LBB0_2674
	s_getpc_b64 s[98:99]
